# GEMM K-loops: the mid-segment s_setprio 0 / s_setprio 1 pair between the two MFMA groups of every compute segment removed (no inserted issue slots inside the MFMA run)
# baseline (speedup 1.0000x reference)
; #define PG8_STAGE(bufoff, gbase, o0, o1) do { \
;         __builtin_amdgcn_global_load_lds((const unsigned*)((const char*)(gbase) + (o0)), (LAS unsigned*)(lds + (bufoff) + ldsw), 16, 0, 0); \
;         __builtin_amdgcn_global_load_lds((const unsigned*)((const char*)(gbase) + (o1)), (LAS unsigned*)(lds + (bufoff) + ldsw + 8192), 16, 0, 0); } while (0)
; #define PG8_LDA(dst, b, h) do { _Pragma("unroll") for (int m = 0; m < 4; ++m) _Pragma("unroll") for (int k = 0; k < 2; ++k) dst[m][k] = *(const LAS bf16x8*)(lds + PG8_SA(b, h) + aoff + m * 2048 + k * 1024); } while (0)
; #define PG8_LDB(dst, b, h) do { _Pragma("unroll") for (int n = 0; n < 2; ++n) _Pragma("unroll") for (int k = 0; k < 2; ++k) dst[n][k] = *(const LAS bf16x8*)(lds + PG8_SB(b, h) + boff + n * 2048 + k * 1024); } while (0)
; #define PG8_WAIT_V(n) asm volatile("s_waitcnt vmcnt(" #n ")" ::: "memory")
; #define PG8_WAIT_L(n) asm volatile("s_waitcnt lgkmcnt(" #n ")" ::: "memory")
; #define PG8_BAR __builtin_amdgcn_s_barrier()
; #define PG8_SCHED __builtin_amdgcn_sched_barrier(0)
; template <class Epi, class Sched, class Prob>
; __device__ __forceinline__ void gemm_phase(LAS unsigned char* lds, LAS unsigned char* lds_epi, const Prob g, const Sched& S, const Epi& E, int wid) {
;     ...
;         const bool has_next = S.next(ui + 1, nxt);
;         const char* nA = has_next ? g.a_base(nxt) : cA; const char* nB = has_next ? g.b_base(nxt) : cB;
; _Pragma("clang loop unroll(disable)")
;         for (int t = 0; t < nt; t += 2) {
;             const bool last = (t == nt - 2);
;             const char* a1 = cA + (size_t)(t + 1) * kstep;
;             const char* a2 = last ? nA : cA + (size_t)(t + 2) * kstep; const char* b2 = last ? nB : cB + (size_t)(t + 2) * kstep;
;             const char* a3 = a2 + kstep; const char* b3 = b2 + kstep;
;             PG8_LDB(B0, 0, 0); PG8_LDB(B1, 0, 1); PG8_SCHED; PG8_LDA(At, 0, 0); PG8_STAGE(PG8_SA(1, 1), a1, cA10, cA11);
;             PG8_WAIT_V(8); PG8_WAIT_L(0); PG8_BAR; PG8_MMA(0, 0, At, B0); PG8_MMA(0, 1, At, B1); PG8_BAR; PG8_SCHED;
;             PG8_LDA(At, 0, 1); PG8_STAGE(PG8_SB(0, 0), b2, vB0, vB1); PG8_STAGE(PG8_SB(0, 1), b2 + hstepB, vB0, vB1); PG8_STAGE(PG8_SA(0, 0), a2, cA00, cA01);
;             PG8_WAIT_V(8); PG8_WAIT_L(0); PG8_BAR; PG8_MMA(1, 0, At, B0); PG8_MMA(1, 1, At, B1); PG8_BAR; PG8_SCHED;
.LBB0_261:
	s_ashr_i32 s3, s2, 31
	s_lshl_b64 s[48:49], s[2:3], 20
	s_add_u32 s48, s33, s48
	s_addc_u32 s49, s39, s49
	s_and_b64 s[50:51], s[46:47], exec
	s_cselect_b32 s3, s49, s15
	s_cselect_b32 s77, s48, s14
	s_ashr_i32 s45, s44, 31
	s_lshl_b64 s[50:51], s[44:45], 20
	s_add_u32 s50, s56, s50
	s_addc_u32 s51, s57, s51
	s_and_b64 s[54:55], s[46:47], exec
	s_cselect_b32 s45, s51, s53
	s_cselect_b32 s78, s50, s52
	s_add_u32 s14, s14, 0x80
	s_addc_u32 s15, s15, 0
	s_add_u32 s79, s52, 0x100
	v_mov_b32_e32 v44, 0
	s_addc_u32 s80, s53, 0
	s_mov_b32 s81, -2
	v_add_u32_e32 v140, s72, v194
	v_add_u32_e32 v156, s73, v194
	ds_read_b128 v[128:131], v140
	ds_read_b128 v[132:135], v140 offset:1024
	ds_read_b128 v[136:139], v140 offset:2048
	ds_read_b128 v[140:143], v140 offset:3072
	ds_read_b128 v[174:177], v156
	ds_read_b128 v[178:181], v156 offset:1024
	ds_read_b128 v[182:185], v156 offset:2048
	ds_read_b128 v[186:189], v156 offset:3072
	s_add_u32 s52, s14, 0x80
	s_addc_u32 s53, s15, 0
	s_cmp_eq_u32 s81, 28
	s_cselect_b32 s55, s3, s53
	s_cselect_b32 s54, s77, s52
	s_cselect_b32 s53, s45, s80
	s_cselect_b32 s52, s78, s79
	v_lshl_add_u64 v[190:191], s[14:15], 0, v[170:171]
	s_add_i32 m0, s25, 0xc000
	ds_read_b128 v[208:211], v204
	ds_read_b128 v[212:215], v204 offset:1024
	ds_read_b128 v[216:219], v204 offset:2048
	ds_read_b128 v[220:223], v204 offset:3072
	ds_read_b128 v[224:227], v204 offset:4096
	ds_read_b128 v[228:231], v204 offset:5120
	ds_read_b128 v[232:235], v204 offset:6144
	ds_read_b128 v[238:241], v204 offset:7168
	global_load_lds_dwordx4 v[190:191], off
	v_lshl_add_u64 v[190:191], s[14:15], 0, v[168:169]
	s_add_i32 m0, s25, 0xe000
	s_nop 0
	global_load_lds_dwordx4 v[190:191], off
	s_waitcnt vmcnt(8)
	s_waitcnt lgkmcnt(0)
	s_barrier
	s_setprio 1
	s_waitcnt lgkmcnt(0)
	v_mfma_f32_16x16x32_bf16 v[80:83], v[128:131], v[208:211], 0
	v_mfma_f32_16x16x32_bf16 v[92:95], v[136:139], v[208:211], 0
	v_mfma_f32_16x16x32_bf16 v[52:55], v[128:131], v[216:219], 0
	v_mfma_f32_16x16x32_bf16 v[68:71], v[136:139], v[216:219], 0
	v_mfma_f32_16x16x32_bf16 v[28:31], v[128:131], v[224:227], 0
	v_mfma_f32_16x16x32_bf16 v[36:39], v[136:139], v[224:227], 0
	v_mfma_f32_16x16x32_bf16 v[8:11], v[128:131], v[232:235], 0
	v_mfma_f32_16x16x32_bf16 v[16:19], v[136:139], v[232:235], 0
	v_mfma_f32_16x16x32_bf16 v[80:83], v[132:135], v[212:215], v[80:83]
	v_mfma_f32_16x16x32_bf16 v[92:95], v[140:143], v[212:215], v[92:95]
	v_mfma_f32_16x16x32_bf16 v[52:55], v[132:135], v[220:223], v[52:55]
	v_mfma_f32_16x16x32_bf16 v[68:71], v[140:143], v[220:223], v[68:71]
	v_mfma_f32_16x16x32_bf16 v[28:31], v[132:135], v[228:231], v[28:31]
	v_mfma_f32_16x16x32_bf16 v[36:39], v[140:143], v[228:231], v[36:39]
	v_mfma_f32_16x16x32_bf16 v[8:11], v[132:135], v[238:241], v[8:11]
	v_mfma_f32_16x16x32_bf16 v[16:19], v[140:143], v[238:241], v[16:19]
	v_mfma_f32_16x16x32_bf16 v[120:123], v[174:177], v[208:211], 0
	v_mfma_f32_16x16x32_bf16 v[124:127], v[182:185], v[208:211], 0
	v_mfma_f32_16x16x32_bf16 v[104:107], v[174:177], v[216:219], 0
	v_mfma_f32_16x16x32_bf16 v[112:115], v[182:185], v[216:219], 0
	v_mfma_f32_16x16x32_bf16 v[84:87], v[174:177], v[224:227], 0
	v_mfma_f32_16x16x32_bf16 v[96:99], v[182:185], v[224:227], 0
	v_mfma_f32_16x16x32_bf16 v[48:51], v[174:177], v[232:235], 0
	v_mfma_f32_16x16x32_bf16 v[64:67], v[182:185], v[232:235], 0
	v_mfma_f32_16x16x32_bf16 v[120:123], v[178:181], v[212:215], v[120:123]
	v_mfma_f32_16x16x32_bf16 v[124:127], v[186:189], v[212:215], v[124:127]
	v_mfma_f32_16x16x32_bf16 v[104:107], v[178:181], v[220:223], v[104:107]
	v_mfma_f32_16x16x32_bf16 v[112:115], v[186:189], v[220:223], v[112:115]
	v_mfma_f32_16x16x32_bf16 v[84:87], v[178:181], v[228:231], v[84:87]
	v_mfma_f32_16x16x32_bf16 v[96:99], v[186:189], v[228:231], v[96:99]
	v_mfma_f32_16x16x32_bf16 v[48:51], v[178:181], v[238:241], v[48:51]
	v_mfma_f32_16x16x32_bf16 v[64:67], v[186:189], v[238:241], v[64:67]
	s_setprio 0
	s_barrier
	s_add_i32 s82, s72, s97
	v_lshl_add_u64 v[190:191], s[52:53], 0, v[144:145]
	s_mov_b32 m0, s82
	ds_read_b128 v[208:211], v204 offset:16384
	ds_read_b128 v[212:215], v204 offset:17408
	ds_read_b128 v[216:219], v204 offset:18432
	ds_read_b128 v[220:223], v204 offset:19456
	ds_read_b128 v[224:227], v204 offset:20480
	ds_read_b128 v[228:231], v204 offset:21504
	ds_read_b128 v[232:235], v204 offset:22528
	ds_read_b128 v[238:241], v204 offset:23552
	global_load_lds_dwordx4 v[190:191], off
	s_add_i32 m0, s82, 0x2000
	s_add_u32 s82, s52, 0x80000
	v_lshl_add_u64 v[236:237], s[52:53], 0, v[146:147]
	s_addc_u32 s83, s53, 0
	s_add_i32 s84, s73, s97
	global_load_lds_dwordx4 v[236:237], off
	v_lshl_add_u64 v[242:243], s[82:83], 0, v[144:145]
	s_mov_b32 m0, s84
	v_lshl_add_u64 v[244:245], s[54:55], 0, v[152:153]
	global_load_lds_dwordx4 v[242:243], off
	v_lshl_add_u64 v[242:243], s[82:83], 0, v[146:147]
	s_add_i32 m0, s84, 0x2000
	s_nop 0
	global_load_lds_dwordx4 v[242:243], off
	v_lshl_add_u64 v[242:243], s[54:55], 0, v[148:149]
	s_mov_b32 m0, s25
	s_nop 0
	global_load_lds_dwordx4 v[242:243], off
	s_mov_b32 m0, s58
	s_nop 0
	global_load_lds_dwordx4 v[244:245], off
	s_waitcnt vmcnt(8)
	s_waitcnt lgkmcnt(0)
	s_barrier
; #define PG8_STAGE(bufoff, gbase, o0, o1) do { \
;         __builtin_amdgcn_global_load_lds((const unsigned*)((const char*)(gbase) + (o0)), (LAS unsigned*)(lds + (bufoff) + ldsw), 16, 0, 0); \
;         __builtin_amdgcn_global_load_lds((const unsigned*)((const char*)(gbase) + (o1)), (LAS unsigned*)(lds + (bufoff) + ldsw + 8192), 16, 0, 0); } while (0)
; #define PG8_LDA(dst, b, h) do { _Pragma("unroll") for (int m = 0; m < 4; ++m) _Pragma("unroll") for (int k = 0; k < 2; ++k) dst[m][k] = *(const LAS bf16x8*)(lds + PG8_SA(b, h) + aoff + m * 2048 + k * 1024); } while (0)
; #define PG8_LDB(dst, b, h) do { _Pragma("unroll") for (int n = 0; n < 2; ++n) _Pragma("unroll") for (int k = 0; k < 2; ++k) dst[n][k] = *(const LAS bf16x8*)(lds + PG8_SB(b, h) + boff + n * 2048 + k * 1024); } while (0)
; #define PG8_WAIT_V(n) asm volatile("s_waitcnt vmcnt(" #n ")" ::: "memory")
; #define PG8_WAIT_L(n) asm volatile("s_waitcnt lgkmcnt(" #n ")" ::: "memory")
; #define PG8_BAR __builtin_amdgcn_s_barrier()
; #define PG8_SCHED __builtin_amdgcn_sched_barrier(0)
; template <class Epi, class Sched, class Prob>
; __device__ __forceinline__ void gemm_phase(LAS unsigned char* lds, LAS unsigned char* lds_epi, const Prob g, const Sched& S, const Epi& E, int wid) {
;     ...
;             PG8_WAIT_V(8); PG8_WAIT_L(0); PG8_BAR; PG8_MMA(1, 0, At, B0); PG8_MMA(1, 1, At, B1); PG8_BAR; PG8_SCHED;
;             PG8_LDB(B0, 1, 0); PG8_LDB(B1, 1, 1); PG8_SCHED; PG8_LDA(At, 1, 0); PG8_STAGE(PG8_SA(0, 1), a2, cA10, cA11);
;             PG8_WAIT_V(8); PG8_WAIT_L(0); PG8_BAR; PG8_MMA(0, 0, At, B0); PG8_MMA(0, 1, At, B1); PG8_BAR; PG8_SCHED;
	s_setprio 1
	s_waitcnt lgkmcnt(0)
	v_mfma_f32_16x16x32_bf16 v[56:59], v[128:131], v[208:211], 0
	v_mfma_f32_16x16x32_bf16 v[72:75], v[136:139], v[208:211], 0
	v_mfma_f32_16x16x32_bf16 v[32:35], v[128:131], v[216:219], 0
	v_mfma_f32_16x16x32_bf16 v[40:43], v[136:139], v[216:219], 0
	v_mfma_f32_16x16x32_bf16 v[12:15], v[128:131], v[224:227], 0
	v_mfma_f32_16x16x32_bf16 v[20:23], v[136:139], v[224:227], 0
	v_mfma_f32_16x16x32_bf16 v[0:3], v[128:131], v[232:235], 0
	v_mfma_f32_16x16x32_bf16 v[4:7], v[136:139], v[232:235], 0
	v_mfma_f32_16x16x32_bf16 v[56:59], v[132:135], v[212:215], v[56:59]
	v_mfma_f32_16x16x32_bf16 v[72:75], v[140:143], v[212:215], v[72:75]
	v_mfma_f32_16x16x32_bf16 v[32:35], v[132:135], v[220:223], v[32:35]
	v_mfma_f32_16x16x32_bf16 v[40:43], v[140:143], v[220:223], v[40:43]
	v_mfma_f32_16x16x32_bf16 v[12:15], v[132:135], v[228:231], v[12:15]
	v_mfma_f32_16x16x32_bf16 v[20:23], v[140:143], v[228:231], v[20:23]
	v_mfma_f32_16x16x32_bf16 v[0:3], v[132:135], v[238:241], v[0:3]
	v_mfma_f32_16x16x32_bf16 v[4:7], v[140:143], v[238:241], v[4:7]
	v_mfma_f32_16x16x32_bf16 v[108:111], v[174:177], v[208:211], 0
	v_mfma_f32_16x16x32_bf16 v[116:119], v[182:185], v[208:211], 0
	v_mfma_f32_16x16x32_bf16 v[88:91], v[174:177], v[216:219], 0
	v_mfma_f32_16x16x32_bf16 v[100:103], v[182:185], v[216:219], 0
	v_mfma_f32_16x16x32_bf16 v[60:63], v[174:177], v[224:227], 0
	v_mfma_f32_16x16x32_bf16 v[76:79], v[182:185], v[224:227], 0
	v_mfma_f32_16x16x32_bf16 v[24:27], v[174:177], v[232:235], 0
	v_mfma_f32_16x16x32_bf16 v[44:47], v[182:185], v[232:235], 0
	v_mfma_f32_16x16x32_bf16 v[108:111], v[178:181], v[212:215], v[108:111]
	v_mfma_f32_16x16x32_bf16 v[116:119], v[186:189], v[212:215], v[116:119]
	v_mfma_f32_16x16x32_bf16 v[88:91], v[178:181], v[220:223], v[88:91]
	v_mfma_f32_16x16x32_bf16 v[100:103], v[186:189], v[220:223], v[100:103]
	v_mfma_f32_16x16x32_bf16 v[60:63], v[178:181], v[228:231], v[60:63]
	v_mfma_f32_16x16x32_bf16 v[76:79], v[186:189], v[228:231], v[76:79]
	v_mfma_f32_16x16x32_bf16 v[24:27], v[178:181], v[238:241], v[24:27]
	v_mfma_f32_16x16x32_bf16 v[44:47], v[186:189], v[238:241], v[44:47]
	s_setprio 0
	s_barrier
	s_add_i32 s82, 0, 0x18000
	s_add_i32 s83, 0, 0x1c000
	v_add_u32_e32 v140, s82, v194
	v_add_u32_e32 v156, s83, v194
	ds_read_b128 v[128:131], v140
	ds_read_b128 v[132:135], v140 offset:1024
	ds_read_b128 v[136:139], v140 offset:2048
	ds_read_b128 v[140:143], v140 offset:3072
	ds_read_b128 v[174:177], v156
	ds_read_b128 v[178:181], v156 offset:1024
	ds_read_b128 v[182:185], v156 offset:2048
	ds_read_b128 v[186:189], v156 offset:3072
	s_mov_b32 m0, s59
	v_lshl_add_u64 v[246:247], s[54:55], 0, v[150:151]
	ds_read_b128 v[208:211], v204 offset:32768
	ds_read_b128 v[212:215], v204 offset:33792
	ds_read_b128 v[216:219], v204 offset:34816
	ds_read_b128 v[220:223], v204 offset:35840
	ds_read_b128 v[224:227], v204 offset:36864
	ds_read_b128 v[228:231], v204 offset:37888
	ds_read_b128 v[232:235], v204 offset:38912
	ds_read_b128 v[238:241], v204 offset:39936
	global_load_lds_dwordx4 v[246:247], off
	v_lshl_add_u64 v[246:247], s[54:55], 0, v[154:155]
	s_mov_b32 m0, s60
	s_nop 0
	global_load_lds_dwordx4 v[246:247], off
	s_waitcnt vmcnt(8)
	s_waitcnt lgkmcnt(0)
	s_barrier
	s_setprio 1
	s_waitcnt lgkmcnt(0)
	v_mfma_f32_16x16x32_bf16 v[80:83], v[128:131], v[208:211], v[80:83]
	v_mfma_f32_16x16x32_bf16 v[92:95], v[136:139], v[208:211], v[92:95]
	v_mfma_f32_16x16x32_bf16 v[52:55], v[128:131], v[216:219], v[52:55]
	v_mfma_f32_16x16x32_bf16 v[68:71], v[136:139], v[216:219], v[68:71]
	v_mfma_f32_16x16x32_bf16 v[28:31], v[128:131], v[224:227], v[28:31]
	v_mfma_f32_16x16x32_bf16 v[36:39], v[136:139], v[224:227], v[36:39]
	v_mfma_f32_16x16x32_bf16 v[8:11], v[128:131], v[232:235], v[8:11]
	v_mfma_f32_16x16x32_bf16 v[16:19], v[136:139], v[232:235], v[16:19]
	v_mfma_f32_16x16x32_bf16 v[80:83], v[132:135], v[212:215], v[80:83]
	v_mfma_f32_16x16x32_bf16 v[92:95], v[140:143], v[212:215], v[92:95]
	v_mfma_f32_16x16x32_bf16 v[52:55], v[132:135], v[220:223], v[52:55]
	v_mfma_f32_16x16x32_bf16 v[68:71], v[140:143], v[220:223], v[68:71]
	v_mfma_f32_16x16x32_bf16 v[28:31], v[132:135], v[228:231], v[28:31]
	v_mfma_f32_16x16x32_bf16 v[36:39], v[140:143], v[228:231], v[36:39]
	v_mfma_f32_16x16x32_bf16 v[8:11], v[132:135], v[238:241], v[8:11]
	v_mfma_f32_16x16x32_bf16 v[16:19], v[140:143], v[238:241], v[16:19]
	v_mfma_f32_16x16x32_bf16 v[120:123], v[174:177], v[208:211], v[120:123]
	v_mfma_f32_16x16x32_bf16 v[124:127], v[182:185], v[208:211], v[124:127]
	v_mfma_f32_16x16x32_bf16 v[104:107], v[174:177], v[216:219], v[104:107]
	v_mfma_f32_16x16x32_bf16 v[112:115], v[182:185], v[216:219], v[112:115]
	v_mfma_f32_16x16x32_bf16 v[84:87], v[174:177], v[224:227], v[84:87]
	v_mfma_f32_16x16x32_bf16 v[96:99], v[182:185], v[224:227], v[96:99]
	v_mfma_f32_16x16x32_bf16 v[48:51], v[174:177], v[232:235], v[48:51]
	v_mfma_f32_16x16x32_bf16 v[64:67], v[182:185], v[232:235], v[64:67]
	v_mfma_f32_16x16x32_bf16 v[120:123], v[178:181], v[212:215], v[120:123]
	v_mfma_f32_16x16x32_bf16 v[124:127], v[186:189], v[212:215], v[124:127]
	v_mfma_f32_16x16x32_bf16 v[104:107], v[178:181], v[220:223], v[104:107]
	v_mfma_f32_16x16x32_bf16 v[112:115], v[186:189], v[220:223], v[112:115]
	v_mfma_f32_16x16x32_bf16 v[84:87], v[178:181], v[228:231], v[84:87]
	v_mfma_f32_16x16x32_bf16 v[96:99], v[186:189], v[228:231], v[96:99]
	v_mfma_f32_16x16x32_bf16 v[48:51], v[178:181], v[238:241], v[48:51]
	v_mfma_f32_16x16x32_bf16 v[64:67], v[186:189], v[238:241], v[64:67]
	s_setprio 0
	s_barrier
; #define PG8_STAGE(bufoff, gbase, o0, o1) do { \
;         __builtin_amdgcn_global_load_lds((const unsigned*)((const char*)(gbase) + (o0)), (LAS unsigned*)(lds + (bufoff) + ldsw), 16, 0, 0); \
;         __builtin_amdgcn_global_load_lds((const unsigned*)((const char*)(gbase) + (o1)), (LAS unsigned*)(lds + (bufoff) + ldsw + 8192), 16, 0, 0); } while (0)
; #define PG8_LDA(dst, b, h) do { _Pragma("unroll") for (int m = 0; m < 4; ++m) _Pragma("unroll") for (int k = 0; k < 2; ++k) dst[m][k] = *(const LAS bf16x8*)(lds + PG8_SA(b, h) + aoff + m * 2048 + k * 1024); } while (0)
; #define PG8_LDB(dst, b, h) do { _Pragma("unroll") for (int n = 0; n < 2; ++n) _Pragma("unroll") for (int k = 0; k < 2; ++k) dst[n][k] = *(const LAS bf16x8*)(lds + PG8_SB(b, h) + boff + n * 2048 + k * 1024); } while (0)
; template <class Epi, class Sched, class Prob>
; __device__ __forceinline__ void gemm_phase(LAS unsigned char* lds, LAS unsigned char* lds_epi, const Prob g, const Sched& S, const Epi& E, int wid) {
;     ...
;         for (int t = 0; t < nt; t += 2) {
;             const bool last = (t == nt - 2);
;             const char* a1 = cA + (size_t)(t + 1) * kstep;
;             const char* a2 = last ? nA : cA + (size_t)(t + 2) * kstep; const char* b2 = last ? nB : cB + (size_t)(t + 2) * kstep;
;             const char* a3 = a2 + kstep; const char* b3 = b2 + kstep;
;             PG8_LDB(B0, 0, 0); PG8_LDB(B1, 0, 1); PG8_SCHED; PG8_LDA(At, 0, 0); PG8_STAGE(PG8_SA(1, 1), a1, cA10, cA11);
;             PG8_WAIT_V(8); PG8_WAIT_L(0); PG8_BAR; PG8_MMA(0, 0, At, B0); PG8_MMA(0, 1, At, B1); PG8_BAR; PG8_SCHED;
;             PG8_LDA(At, 0, 1); PG8_STAGE(PG8_SB(0, 0), b2, vB0, vB1); PG8_STAGE(PG8_SB(0, 1), b2 + hstepB, vB0, vB1); PG8_STAGE(PG8_SA(0, 0), a2, cA00, cA01);
;             PG8_WAIT_V(8); PG8_WAIT_L(0); PG8_BAR; PG8_MMA(1, 0, At, B0); PG8_MMA(1, 1, At, B1); PG8_BAR; PG8_SCHED;
;             PG8_LDB(B0, 1, 0); PG8_LDB(B1, 1, 1); PG8_SCHED; PG8_LDA(At, 1, 0); PG8_STAGE(PG8_SA(0, 1), a2, cA10, cA11);
;             PG8_WAIT_V(8); PG8_WAIT_L(0); PG8_BAR; PG8_MMA(0, 0, At, B0); PG8_MMA(0, 1, At, B1); PG8_BAR; PG8_SCHED;
;             PG8_LDA(At, 1, 1); PG8_STAGE(PG8_SB(1, 0), b3, vB0, vB1); PG8_STAGE(PG8_SB(1, 1), b3 + hstepB, vB0, vB1); PG8_STAGE(PG8_SA(1, 0), a3, cA00, cA01);
;             PG8_WAIT_V(8); PG8_WAIT_L(0); PG8_BAR; PG8_MMA(1, 0, At, B0); PG8_MMA(1, 1, At, B1); PG8_BAR; PG8_SCHED;
	s_add_i32 s54, s82, s97
	v_lshl_add_u64 v[190:191], v[190:191], 0, s[20:21]
	s_mov_b32 m0, s54
	ds_read_b128 v[208:211], v204 offset:49152
	ds_read_b128 v[212:215], v204 offset:50176
	ds_read_b128 v[216:219], v204 offset:51200
	ds_read_b128 v[220:223], v204 offset:52224
	ds_read_b128 v[224:227], v204 offset:53248
	ds_read_b128 v[228:231], v204 offset:54272
	ds_read_b128 v[232:235], v204 offset:55296
	ds_read_b128 v[238:241], v204 offset:56320
	global_load_lds_dwordx4 v[190:191], off
	s_add_i32 m0, s54, 0x2000
	s_add_u32 s52, s52, 0x80080
	v_lshl_add_u64 v[190:191], v[236:237], 0, s[20:21]
	s_addc_u32 s53, s53, 0
	s_add_i32 s54, s83, s97
	global_load_lds_dwordx4 v[190:191], off
	v_lshl_add_u64 v[190:191], s[52:53], 0, v[144:145]
	s_mov_b32 m0, s54
	s_nop 0
	global_load_lds_dwordx4 v[190:191], off
	v_lshl_add_u64 v[190:191], s[52:53], 0, v[146:147]
	s_add_i32 m0, s54, 0x2000
	s_nop 0
	global_load_lds_dwordx4 v[190:191], off
	v_lshl_add_u64 v[190:191], v[242:243], 0, s[20:21]
	s_mov_b32 m0, s70
	s_nop 0
	global_load_lds_dwordx4 v[190:191], off
	v_lshl_add_u64 v[190:191], v[244:245], 0, s[20:21]
	s_mov_b32 m0, s71
	s_nop 0
	global_load_lds_dwordx4 v[190:191], off
	s_waitcnt vmcnt(8)
	s_waitcnt lgkmcnt(0)
	s_barrier
	s_setprio 1
	s_waitcnt lgkmcnt(0)
	v_mfma_f32_16x16x32_bf16 v[56:59], v[128:131], v[208:211], v[56:59]
	v_mfma_f32_16x16x32_bf16 v[72:75], v[136:139], v[208:211], v[72:75]
	v_mfma_f32_16x16x32_bf16 v[32:35], v[128:131], v[216:219], v[32:35]
	v_mfma_f32_16x16x32_bf16 v[40:43], v[136:139], v[216:219], v[40:43]
	v_mfma_f32_16x16x32_bf16 v[12:15], v[128:131], v[224:227], v[12:15]
	v_mfma_f32_16x16x32_bf16 v[20:23], v[136:139], v[224:227], v[20:23]
	v_mfma_f32_16x16x32_bf16 v[0:3], v[128:131], v[232:235], v[0:3]
	v_mfma_f32_16x16x32_bf16 v[4:7], v[136:139], v[232:235], v[4:7]
	v_mfma_f32_16x16x32_bf16 v[56:59], v[132:135], v[212:215], v[56:59]
	v_mfma_f32_16x16x32_bf16 v[72:75], v[140:143], v[212:215], v[72:75]
	v_mfma_f32_16x16x32_bf16 v[32:35], v[132:135], v[220:223], v[32:35]
	v_mfma_f32_16x16x32_bf16 v[40:43], v[140:143], v[220:223], v[40:43]
	v_mfma_f32_16x16x32_bf16 v[12:15], v[132:135], v[228:231], v[12:15]
	v_mfma_f32_16x16x32_bf16 v[20:23], v[140:143], v[228:231], v[20:23]
	v_mfma_f32_16x16x32_bf16 v[0:3], v[132:135], v[238:241], v[0:3]
	v_mfma_f32_16x16x32_bf16 v[4:7], v[140:143], v[238:241], v[4:7]
	v_mfma_f32_16x16x32_bf16 v[108:111], v[174:177], v[208:211], v[108:111]
	v_mfma_f32_16x16x32_bf16 v[116:119], v[182:185], v[208:211], v[116:119]
	v_mfma_f32_16x16x32_bf16 v[88:91], v[174:177], v[216:219], v[88:91]
	v_mfma_f32_16x16x32_bf16 v[100:103], v[182:185], v[216:219], v[100:103]
	v_mfma_f32_16x16x32_bf16 v[60:63], v[174:177], v[224:227], v[60:63]
	v_mfma_f32_16x16x32_bf16 v[76:79], v[182:185], v[224:227], v[76:79]
	v_mfma_f32_16x16x32_bf16 v[24:27], v[174:177], v[232:235], v[24:27]
	v_mfma_f32_16x16x32_bf16 v[44:47], v[182:185], v[232:235], v[44:47]
	v_mfma_f32_16x16x32_bf16 v[108:111], v[178:181], v[212:215], v[108:111]
	v_mfma_f32_16x16x32_bf16 v[116:119], v[186:189], v[212:215], v[116:119]
	v_mfma_f32_16x16x32_bf16 v[88:91], v[178:181], v[220:223], v[88:91]
	v_mfma_f32_16x16x32_bf16 v[100:103], v[186:189], v[220:223], v[100:103]
	v_mfma_f32_16x16x32_bf16 v[60:63], v[178:181], v[228:231], v[60:63]
	v_mfma_f32_16x16x32_bf16 v[76:79], v[186:189], v[228:231], v[76:79]
	v_mfma_f32_16x16x32_bf16 v[24:27], v[178:181], v[238:241], v[24:27]
	v_mfma_f32_16x16x32_bf16 v[44:47], v[186:189], v[238:241], v[44:47]
	s_setprio 0
	s_barrier
	s_add_i32 s81, s81, 2
	s_add_u32 s14, s14, 0x100
	s_addc_u32 s15, s15, 0
	s_add_u32 s79, s79, 0x100
	s_addc_u32 s80, s80, 0
	s_cmp_gt_u32 s81, 29
.LBB0_262:
	v_add_u32_e32 v140, s72, v194
	v_add_u32_e32 v156, s73, v194
	ds_read_b128 v[128:131], v140
	ds_read_b128 v[132:135], v140 offset:1024
	ds_read_b128 v[136:139], v140 offset:2048
	ds_read_b128 v[140:143], v140 offset:3072
	ds_read_b128 v[174:177], v156
	ds_read_b128 v[178:181], v156 offset:1024
	ds_read_b128 v[182:185], v156 offset:2048
	ds_read_b128 v[186:189], v156 offset:3072
	s_add_u32 s52, s14, 0x80
	s_addc_u32 s53, s15, 0
	s_cmp_eq_u32 s81, 28
	s_cselect_b32 s55, s3, s53
	s_cselect_b32 s54, s77, s52
	s_cselect_b32 s53, s45, s80
	s_cselect_b32 s52, s78, s79
	v_lshl_add_u64 v[190:191], s[14:15], 0, v[170:171]
	s_add_i32 m0, s25, 0xc000
	ds_read_b128 v[208:211], v204
	ds_read_b128 v[212:215], v204 offset:1024
	ds_read_b128 v[216:219], v204 offset:2048
	ds_read_b128 v[220:223], v204 offset:3072
	ds_read_b128 v[224:227], v204 offset:4096
	ds_read_b128 v[228:231], v204 offset:5120
	ds_read_b128 v[232:235], v204 offset:6144
	ds_read_b128 v[238:241], v204 offset:7168
	global_load_lds_dwordx4 v[190:191], off
	v_lshl_add_u64 v[190:191], s[14:15], 0, v[168:169]
	s_add_i32 m0, s25, 0xe000
	s_nop 0
	global_load_lds_dwordx4 v[190:191], off
	s_waitcnt vmcnt(8)
	s_waitcnt lgkmcnt(0)
	s_barrier
; #define PG8_STAGE(bufoff, gbase, o0, o1) do { \
;         __builtin_amdgcn_global_load_lds((const unsigned*)((const char*)(gbase) + (o0)), (LAS unsigned*)(lds + (bufoff) + ldsw), 16, 0, 0); \
;         __builtin_amdgcn_global_load_lds((const unsigned*)((const char*)(gbase) + (o1)), (LAS unsigned*)(lds + (bufoff) + ldsw + 8192), 16, 0, 0); } while (0)
; #define PG8_LDA(dst, b, h) do { _Pragma("unroll") for (int m = 0; m < 4; ++m) _Pragma("unroll") for (int k = 0; k < 2; ++k) dst[m][k] = *(const LAS bf16x8*)(lds + PG8_SA(b, h) + aoff + m * 2048 + k * 1024); } while (0)
; #define PG8_WAIT_V(n) asm volatile("s_waitcnt vmcnt(" #n ")" ::: "memory")
; #define PG8_WAIT_L(n) asm volatile("s_waitcnt lgkmcnt(" #n ")" ::: "memory")
; #define PG8_BAR __builtin_amdgcn_s_barrier()
; #define PG8_SCHED __builtin_amdgcn_sched_barrier(0)
; template <class Epi, class Sched, class Prob>
; __device__ __forceinline__ void gemm_phase(LAS unsigned char* lds, LAS unsigned char* lds_epi, const Prob g, const Sched& S, const Epi& E, int wid) {
;     ...
;             PG8_WAIT_V(8); PG8_WAIT_L(0); PG8_BAR; PG8_MMA(0, 0, At, B0); PG8_MMA(0, 1, At, B1); PG8_BAR; PG8_SCHED;
;             PG8_LDA(At, 0, 1); PG8_STAGE(PG8_SB(0, 0), b2, vB0, vB1); PG8_STAGE(PG8_SB(0, 1), b2 + hstepB, vB0, vB1); PG8_STAGE(PG8_SA(0, 0), a2, cA00, cA01);
;             PG8_WAIT_V(8); PG8_WAIT_L(0); PG8_BAR; PG8_MMA(1, 0, At, B0); PG8_MMA(1, 1, At, B1); PG8_BAR; PG8_SCHED;
	s_setprio 1
	s_waitcnt lgkmcnt(0)
	v_mfma_f32_16x16x32_bf16 v[80:83], v[128:131], v[208:211], v[80:83]
	v_mfma_f32_16x16x32_bf16 v[92:95], v[136:139], v[208:211], v[92:95]
	v_mfma_f32_16x16x32_bf16 v[52:55], v[128:131], v[216:219], v[52:55]
	v_mfma_f32_16x16x32_bf16 v[68:71], v[136:139], v[216:219], v[68:71]
	v_mfma_f32_16x16x32_bf16 v[28:31], v[128:131], v[224:227], v[28:31]
	v_mfma_f32_16x16x32_bf16 v[36:39], v[136:139], v[224:227], v[36:39]
	v_mfma_f32_16x16x32_bf16 v[8:11], v[128:131], v[232:235], v[8:11]
	v_mfma_f32_16x16x32_bf16 v[16:19], v[136:139], v[232:235], v[16:19]
	v_mfma_f32_16x16x32_bf16 v[80:83], v[132:135], v[212:215], v[80:83]
	v_mfma_f32_16x16x32_bf16 v[92:95], v[140:143], v[212:215], v[92:95]
	v_mfma_f32_16x16x32_bf16 v[52:55], v[132:135], v[220:223], v[52:55]
	v_mfma_f32_16x16x32_bf16 v[68:71], v[140:143], v[220:223], v[68:71]
	v_mfma_f32_16x16x32_bf16 v[28:31], v[132:135], v[228:231], v[28:31]
	v_mfma_f32_16x16x32_bf16 v[36:39], v[140:143], v[228:231], v[36:39]
	v_mfma_f32_16x16x32_bf16 v[8:11], v[132:135], v[238:241], v[8:11]
	v_mfma_f32_16x16x32_bf16 v[16:19], v[140:143], v[238:241], v[16:19]
	v_mfma_f32_16x16x32_bf16 v[120:123], v[174:177], v[208:211], v[120:123]
	v_mfma_f32_16x16x32_bf16 v[124:127], v[182:185], v[208:211], v[124:127]
	v_mfma_f32_16x16x32_bf16 v[104:107], v[174:177], v[216:219], v[104:107]
	v_mfma_f32_16x16x32_bf16 v[112:115], v[182:185], v[216:219], v[112:115]
	v_mfma_f32_16x16x32_bf16 v[84:87], v[174:177], v[224:227], v[84:87]
	v_mfma_f32_16x16x32_bf16 v[96:99], v[182:185], v[224:227], v[96:99]
	v_mfma_f32_16x16x32_bf16 v[48:51], v[174:177], v[232:235], v[48:51]
	v_mfma_f32_16x16x32_bf16 v[64:67], v[182:185], v[232:235], v[64:67]
	v_mfma_f32_16x16x32_bf16 v[120:123], v[178:181], v[212:215], v[120:123]
	v_mfma_f32_16x16x32_bf16 v[124:127], v[186:189], v[212:215], v[124:127]
	v_mfma_f32_16x16x32_bf16 v[104:107], v[178:181], v[220:223], v[104:107]
	v_mfma_f32_16x16x32_bf16 v[112:115], v[186:189], v[220:223], v[112:115]
	v_mfma_f32_16x16x32_bf16 v[84:87], v[178:181], v[228:231], v[84:87]
	v_mfma_f32_16x16x32_bf16 v[96:99], v[186:189], v[228:231], v[96:99]
	v_mfma_f32_16x16x32_bf16 v[48:51], v[178:181], v[238:241], v[48:51]
	v_mfma_f32_16x16x32_bf16 v[64:67], v[186:189], v[238:241], v[64:67]
	s_setprio 0
	s_barrier
	s_add_i32 s82, s72, s97
	v_lshl_add_u64 v[190:191], s[52:53], 0, v[144:145]
	s_mov_b32 m0, s82
	ds_read_b128 v[208:211], v204 offset:16384
	ds_read_b128 v[212:215], v204 offset:17408
	ds_read_b128 v[216:219], v204 offset:18432
	ds_read_b128 v[220:223], v204 offset:19456
	ds_read_b128 v[224:227], v204 offset:20480
	ds_read_b128 v[228:231], v204 offset:21504
	ds_read_b128 v[232:235], v204 offset:22528
	ds_read_b128 v[238:241], v204 offset:23552
	global_load_lds_dwordx4 v[190:191], off
	s_add_i32 m0, s82, 0x2000
	s_add_u32 s82, s52, 0x80000
	v_lshl_add_u64 v[236:237], s[52:53], 0, v[146:147]
	s_addc_u32 s83, s53, 0
	s_add_i32 s84, s73, s97
	global_load_lds_dwordx4 v[236:237], off
	v_lshl_add_u64 v[242:243], s[82:83], 0, v[144:145]
	s_mov_b32 m0, s84
	v_lshl_add_u64 v[244:245], s[54:55], 0, v[152:153]
	global_load_lds_dwordx4 v[242:243], off
	v_lshl_add_u64 v[242:243], s[82:83], 0, v[146:147]
	s_add_i32 m0, s84, 0x2000
	s_nop 0
	global_load_lds_dwordx4 v[242:243], off
	v_lshl_add_u64 v[242:243], s[54:55], 0, v[148:149]
	s_mov_b32 m0, s25
	s_nop 0
	global_load_lds_dwordx4 v[242:243], off
	s_mov_b32 m0, s58
	s_nop 0
	global_load_lds_dwordx4 v[244:245], off
	s_waitcnt vmcnt(8)
	s_waitcnt lgkmcnt(0)
	s_barrier
	s_setprio 1
	s_waitcnt lgkmcnt(0)
	v_mfma_f32_16x16x32_bf16 v[56:59], v[128:131], v[208:211], v[56:59]
	v_mfma_f32_16x16x32_bf16 v[72:75], v[136:139], v[208:211], v[72:75]
	v_mfma_f32_16x16x32_bf16 v[32:35], v[128:131], v[216:219], v[32:35]
	v_mfma_f32_16x16x32_bf16 v[40:43], v[136:139], v[216:219], v[40:43]
	v_mfma_f32_16x16x32_bf16 v[12:15], v[128:131], v[224:227], v[12:15]
	v_mfma_f32_16x16x32_bf16 v[20:23], v[136:139], v[224:227], v[20:23]
	v_mfma_f32_16x16x32_bf16 v[0:3], v[128:131], v[232:235], v[0:3]
	v_mfma_f32_16x16x32_bf16 v[4:7], v[136:139], v[232:235], v[4:7]
	v_mfma_f32_16x16x32_bf16 v[56:59], v[132:135], v[212:215], v[56:59]
	v_mfma_f32_16x16x32_bf16 v[72:75], v[140:143], v[212:215], v[72:75]
	v_mfma_f32_16x16x32_bf16 v[32:35], v[132:135], v[220:223], v[32:35]
	v_mfma_f32_16x16x32_bf16 v[40:43], v[140:143], v[220:223], v[40:43]
	v_mfma_f32_16x16x32_bf16 v[12:15], v[132:135], v[228:231], v[12:15]
	v_mfma_f32_16x16x32_bf16 v[20:23], v[140:143], v[228:231], v[20:23]
	v_mfma_f32_16x16x32_bf16 v[0:3], v[132:135], v[238:241], v[0:3]
	v_mfma_f32_16x16x32_bf16 v[4:7], v[140:143], v[238:241], v[4:7]
	v_mfma_f32_16x16x32_bf16 v[108:111], v[174:177], v[208:211], v[108:111]
	v_mfma_f32_16x16x32_bf16 v[116:119], v[182:185], v[208:211], v[116:119]
	v_mfma_f32_16x16x32_bf16 v[88:91], v[174:177], v[216:219], v[88:91]
	v_mfma_f32_16x16x32_bf16 v[100:103], v[182:185], v[216:219], v[100:103]
	v_mfma_f32_16x16x32_bf16 v[60:63], v[174:177], v[224:227], v[60:63]
	v_mfma_f32_16x16x32_bf16 v[76:79], v[182:185], v[224:227], v[76:79]
	v_mfma_f32_16x16x32_bf16 v[24:27], v[174:177], v[232:235], v[24:27]
	v_mfma_f32_16x16x32_bf16 v[44:47], v[182:185], v[232:235], v[44:47]
	v_mfma_f32_16x16x32_bf16 v[108:111], v[178:181], v[212:215], v[108:111]
	v_mfma_f32_16x16x32_bf16 v[116:119], v[186:189], v[212:215], v[116:119]
	v_mfma_f32_16x16x32_bf16 v[88:91], v[178:181], v[220:223], v[88:91]
	v_mfma_f32_16x16x32_bf16 v[100:103], v[186:189], v[220:223], v[100:103]
	v_mfma_f32_16x16x32_bf16 v[60:63], v[178:181], v[228:231], v[60:63]
	v_mfma_f32_16x16x32_bf16 v[76:79], v[186:189], v[228:231], v[76:79]
	v_mfma_f32_16x16x32_bf16 v[24:27], v[178:181], v[238:241], v[24:27]
	v_mfma_f32_16x16x32_bf16 v[44:47], v[186:189], v[238:241], v[44:47]
	s_setprio 0
	s_barrier
; #define PG8_STAGE(bufoff, gbase, o0, o1) do { \
;         __builtin_amdgcn_global_load_lds((const unsigned*)((const char*)(gbase) + (o0)), (LAS unsigned*)(lds + (bufoff) + ldsw), 16, 0, 0); \
;         __builtin_amdgcn_global_load_lds((const unsigned*)((const char*)(gbase) + (o1)), (LAS unsigned*)(lds + (bufoff) + ldsw + 8192), 16, 0, 0); } while (0)
; #define PG8_LDA(dst, b, h) do { _Pragma("unroll") for (int m = 0; m < 4; ++m) _Pragma("unroll") for (int k = 0; k < 2; ++k) dst[m][k] = *(const LAS bf16x8*)(lds + PG8_SA(b, h) + aoff + m * 2048 + k * 1024); } while (0)
; #define PG8_LDB(dst, b, h) do { _Pragma("unroll") for (int n = 0; n < 2; ++n) _Pragma("unroll") for (int k = 0; k < 2; ++k) dst[n][k] = *(const LAS bf16x8*)(lds + PG8_SB(b, h) + boff + n * 2048 + k * 1024); } while (0)
; #define PG8_WAIT_V(n) asm volatile("s_waitcnt vmcnt(" #n ")" ::: "memory")
; #define PG8_WAIT_L(n) asm volatile("s_waitcnt lgkmcnt(" #n ")" ::: "memory")
; #define PG8_BAR __builtin_amdgcn_s_barrier()
; #define PG8_SCHED __builtin_amdgcn_sched_barrier(0)
; template <class Epi, class Sched, class Prob>
; __device__ __forceinline__ void gemm_phase(LAS unsigned char* lds, LAS unsigned char* lds_epi, const Prob g, const Sched& S, const Epi& E, int wid) {
;     ...
;             PG8_LDB(B0, 1, 0); PG8_LDB(B1, 1, 1); PG8_SCHED; PG8_LDA(At, 1, 0); PG8_STAGE(PG8_SA(0, 1), a2, cA10, cA11);
;             PG8_WAIT_V(8); PG8_WAIT_L(0); PG8_BAR; PG8_MMA(0, 0, At, B0); PG8_MMA(0, 1, At, B1); PG8_BAR; PG8_SCHED;
	s_add_i32 s82, 0, 0x18000
	s_add_i32 s83, 0, 0x1c000
	v_add_u32_e32 v140, s82, v194
	v_add_u32_e32 v156, s83, v194
	ds_read_b128 v[128:131], v140
	ds_read_b128 v[132:135], v140 offset:1024
	ds_read_b128 v[136:139], v140 offset:2048
	ds_read_b128 v[140:143], v140 offset:3072
	ds_read_b128 v[174:177], v156
	ds_read_b128 v[178:181], v156 offset:1024
	ds_read_b128 v[182:185], v156 offset:2048
	ds_read_b128 v[186:189], v156 offset:3072
	s_mov_b32 m0, s59
	v_lshl_add_u64 v[246:247], s[54:55], 0, v[150:151]
	ds_read_b128 v[208:211], v204 offset:32768
	ds_read_b128 v[212:215], v204 offset:33792
	ds_read_b128 v[216:219], v204 offset:34816
	ds_read_b128 v[220:223], v204 offset:35840
	ds_read_b128 v[224:227], v204 offset:36864
	ds_read_b128 v[228:231], v204 offset:37888
	ds_read_b128 v[232:235], v204 offset:38912
	ds_read_b128 v[238:241], v204 offset:39936
	global_load_lds_dwordx4 v[246:247], off
	v_lshl_add_u64 v[246:247], s[54:55], 0, v[154:155]
	s_mov_b32 m0, s60
	s_nop 0
	global_load_lds_dwordx4 v[246:247], off
	s_waitcnt vmcnt(8)
	s_waitcnt lgkmcnt(0)
	s_barrier
	s_setprio 1
	s_waitcnt lgkmcnt(0)
	v_mfma_f32_16x16x32_bf16 v[80:83], v[128:131], v[208:211], v[80:83]
	v_mfma_f32_16x16x32_bf16 v[92:95], v[136:139], v[208:211], v[92:95]
	v_mfma_f32_16x16x32_bf16 v[52:55], v[128:131], v[216:219], v[52:55]
	v_mfma_f32_16x16x32_bf16 v[68:71], v[136:139], v[216:219], v[68:71]
	v_mfma_f32_16x16x32_bf16 v[28:31], v[128:131], v[224:227], v[28:31]
	v_mfma_f32_16x16x32_bf16 v[36:39], v[136:139], v[224:227], v[36:39]
	v_mfma_f32_16x16x32_bf16 v[8:11], v[128:131], v[232:235], v[8:11]
	v_mfma_f32_16x16x32_bf16 v[16:19], v[136:139], v[232:235], v[16:19]
	v_mfma_f32_16x16x32_bf16 v[80:83], v[132:135], v[212:215], v[80:83]
	v_mfma_f32_16x16x32_bf16 v[92:95], v[140:143], v[212:215], v[92:95]
	v_mfma_f32_16x16x32_bf16 v[52:55], v[132:135], v[220:223], v[52:55]
	v_mfma_f32_16x16x32_bf16 v[68:71], v[140:143], v[220:223], v[68:71]
	v_mfma_f32_16x16x32_bf16 v[28:31], v[132:135], v[228:231], v[28:31]
	v_mfma_f32_16x16x32_bf16 v[36:39], v[140:143], v[228:231], v[36:39]
	v_mfma_f32_16x16x32_bf16 v[8:11], v[132:135], v[238:241], v[8:11]
	v_mfma_f32_16x16x32_bf16 v[16:19], v[140:143], v[238:241], v[16:19]
	v_mfma_f32_16x16x32_bf16 v[120:123], v[174:177], v[208:211], v[120:123]
	v_mfma_f32_16x16x32_bf16 v[124:127], v[182:185], v[208:211], v[124:127]
	v_mfma_f32_16x16x32_bf16 v[104:107], v[174:177], v[216:219], v[104:107]
	v_mfma_f32_16x16x32_bf16 v[112:115], v[182:185], v[216:219], v[112:115]
	v_mfma_f32_16x16x32_bf16 v[84:87], v[174:177], v[224:227], v[84:87]
	v_mfma_f32_16x16x32_bf16 v[96:99], v[182:185], v[224:227], v[96:99]
	v_mfma_f32_16x16x32_bf16 v[48:51], v[174:177], v[232:235], v[48:51]
	v_mfma_f32_16x16x32_bf16 v[64:67], v[182:185], v[232:235], v[64:67]
	v_mfma_f32_16x16x32_bf16 v[120:123], v[178:181], v[212:215], v[120:123]
	v_mfma_f32_16x16x32_bf16 v[124:127], v[186:189], v[212:215], v[124:127]
	v_mfma_f32_16x16x32_bf16 v[104:107], v[178:181], v[220:223], v[104:107]
	v_mfma_f32_16x16x32_bf16 v[112:115], v[186:189], v[220:223], v[112:115]
	v_mfma_f32_16x16x32_bf16 v[84:87], v[178:181], v[228:231], v[84:87]
	v_mfma_f32_16x16x32_bf16 v[96:99], v[186:189], v[228:231], v[96:99]
	v_mfma_f32_16x16x32_bf16 v[48:51], v[178:181], v[238:241], v[48:51]
	v_mfma_f32_16x16x32_bf16 v[64:67], v[186:189], v[238:241], v[64:67]
	s_setprio 0
	s_barrier
; #define PG8_STAGE(bufoff, gbase, o0, o1) do { \
;         __builtin_amdgcn_global_load_lds((const unsigned*)((const char*)(gbase) + (o0)), (LAS unsigned*)(lds + (bufoff) + ldsw), 16, 0, 0); \
;         __builtin_amdgcn_global_load_lds((const unsigned*)((const char*)(gbase) + (o1)), (LAS unsigned*)(lds + (bufoff) + ldsw + 8192), 16, 0, 0); } while (0)
; #define PG8_LDA(dst, b, h) do { _Pragma("unroll") for (int m = 0; m < 4; ++m) _Pragma("unroll") for (int k = 0; k < 2; ++k) dst[m][k] = *(const LAS bf16x8*)(lds + PG8_SA(b, h) + aoff + m * 2048 + k * 1024); } while (0)
; #define PG8_WAIT_V(n) asm volatile("s_waitcnt vmcnt(" #n ")" ::: "memory")
; #define PG8_WAIT_L(n) asm volatile("s_waitcnt lgkmcnt(" #n ")" ::: "memory")
; #define PG8_BAR __builtin_amdgcn_s_barrier()
; #define PG8_SCHED __builtin_amdgcn_sched_barrier(0)
; template <class Epi, class Sched, class Prob>
; __device__ __forceinline__ void gemm_phase(LAS unsigned char* lds, LAS unsigned char* lds_epi, const Prob g, const Sched& S, const Epi& E, int wid) {
;     ...
;             PG8_LDA(At, 1, 1); PG8_STAGE(PG8_SB(1, 0), b3, vB0, vB1); PG8_STAGE(PG8_SB(1, 1), b3 + hstepB, vB0, vB1); PG8_STAGE(PG8_SA(1, 0), a3, cA00, cA01);
;             PG8_WAIT_V(8); PG8_WAIT_L(0); PG8_BAR; PG8_MMA(1, 0, At, B0); PG8_MMA(1, 1, At, B1); PG8_BAR; PG8_SCHED;
;         }
;         if constexpr (Prob::FP8) asm volatile("s_nop 7\n\ts_nop 7\n\ts_nop 7" ::: "memory");
;         if (wr == 0) PG8_BAR;
	s_add_i32 s54, s82, s97
	v_lshl_add_u64 v[190:191], v[190:191], 0, s[20:21]
	s_mov_b32 m0, s54
	ds_read_b128 v[208:211], v204 offset:49152
	ds_read_b128 v[212:215], v204 offset:50176
	ds_read_b128 v[216:219], v204 offset:51200
	ds_read_b128 v[220:223], v204 offset:52224
	ds_read_b128 v[224:227], v204 offset:53248
	ds_read_b128 v[228:231], v204 offset:54272
	ds_read_b128 v[232:235], v204 offset:55296
	ds_read_b128 v[238:241], v204 offset:56320
	global_load_lds_dwordx4 v[190:191], off
	s_add_i32 m0, s54, 0x2000
	s_add_u32 s52, s52, 0x80080
	v_lshl_add_u64 v[190:191], v[236:237], 0, s[20:21]
	s_addc_u32 s53, s53, 0
	s_add_i32 s54, s83, s97
	global_load_lds_dwordx4 v[190:191], off
	v_lshl_add_u64 v[190:191], s[52:53], 0, v[144:145]
	s_mov_b32 m0, s54
	s_nop 0
	global_load_lds_dwordx4 v[190:191], off
	v_lshl_add_u64 v[190:191], s[52:53], 0, v[146:147]
	s_add_i32 m0, s54, 0x2000
	s_nop 0
	global_load_lds_dwordx4 v[190:191], off
	v_lshl_add_u64 v[190:191], v[242:243], 0, s[20:21]
	s_mov_b32 m0, s70
	s_nop 0
	global_load_lds_dwordx4 v[190:191], off
	v_lshl_add_u64 v[190:191], v[244:245], 0, s[20:21]
	s_mov_b32 m0, s71
	s_nop 0
	global_load_lds_dwordx4 v[190:191], off
	s_waitcnt vmcnt(8)
	s_waitcnt lgkmcnt(0)
	s_barrier
	s_setprio 1
	s_waitcnt lgkmcnt(0)
	v_mfma_f32_16x16x32_bf16 v[56:59], v[128:131], v[208:211], v[56:59]
	v_mfma_f32_16x16x32_bf16 v[72:75], v[136:139], v[208:211], v[72:75]
	v_mfma_f32_16x16x32_bf16 v[32:35], v[128:131], v[216:219], v[32:35]
	v_mfma_f32_16x16x32_bf16 v[40:43], v[136:139], v[216:219], v[40:43]
	v_mfma_f32_16x16x32_bf16 v[12:15], v[128:131], v[224:227], v[12:15]
	v_mfma_f32_16x16x32_bf16 v[20:23], v[136:139], v[224:227], v[20:23]
	v_mfma_f32_16x16x32_bf16 v[0:3], v[128:131], v[232:235], v[0:3]
	v_mfma_f32_16x16x32_bf16 v[4:7], v[136:139], v[232:235], v[4:7]
	v_mfma_f32_16x16x32_bf16 v[56:59], v[132:135], v[212:215], v[56:59]
	v_mfma_f32_16x16x32_bf16 v[72:75], v[140:143], v[212:215], v[72:75]
	v_mfma_f32_16x16x32_bf16 v[32:35], v[132:135], v[220:223], v[32:35]
	v_mfma_f32_16x16x32_bf16 v[40:43], v[140:143], v[220:223], v[40:43]
	v_mfma_f32_16x16x32_bf16 v[12:15], v[132:135], v[228:231], v[12:15]
	v_mfma_f32_16x16x32_bf16 v[20:23], v[140:143], v[228:231], v[20:23]
	v_mfma_f32_16x16x32_bf16 v[0:3], v[132:135], v[238:241], v[0:3]
	v_mfma_f32_16x16x32_bf16 v[4:7], v[140:143], v[238:241], v[4:7]
	v_mfma_f32_16x16x32_bf16 v[108:111], v[174:177], v[208:211], v[108:111]
	v_mfma_f32_16x16x32_bf16 v[116:119], v[182:185], v[208:211], v[116:119]
	v_mfma_f32_16x16x32_bf16 v[88:91], v[174:177], v[216:219], v[88:91]
	v_mfma_f32_16x16x32_bf16 v[100:103], v[182:185], v[216:219], v[100:103]
	v_mfma_f32_16x16x32_bf16 v[60:63], v[174:177], v[224:227], v[60:63]
	v_mfma_f32_16x16x32_bf16 v[76:79], v[182:185], v[224:227], v[76:79]
	v_mfma_f32_16x16x32_bf16 v[24:27], v[174:177], v[232:235], v[24:27]
	v_mfma_f32_16x16x32_bf16 v[44:47], v[182:185], v[232:235], v[44:47]
	v_mfma_f32_16x16x32_bf16 v[108:111], v[178:181], v[212:215], v[108:111]
	v_mfma_f32_16x16x32_bf16 v[116:119], v[186:189], v[212:215], v[116:119]
	v_mfma_f32_16x16x32_bf16 v[88:91], v[178:181], v[220:223], v[88:91]
	v_mfma_f32_16x16x32_bf16 v[100:103], v[186:189], v[220:223], v[100:103]
	v_mfma_f32_16x16x32_bf16 v[60:63], v[178:181], v[228:231], v[60:63]
	v_mfma_f32_16x16x32_bf16 v[76:79], v[186:189], v[228:231], v[76:79]
	v_mfma_f32_16x16x32_bf16 v[24:27], v[178:181], v[238:241], v[24:27]
	v_mfma_f32_16x16x32_bf16 v[44:47], v[186:189], v[238:241], v[44:47]
	s_setprio 0
	s_barrier
	s_add_i32 s81, s81, 2
	s_add_u32 s14, s14, 0x100
	s_addc_u32 s15, s15, 0
	s_add_u32 s79, s79, 0x100
	s_addc_u32 s80, s80, 0
	s_cmp_gt_u32 s81, 29
	s_cbranch_scc0 .LBB0_262
	v_readlane_b32 s14, v254, 27
	v_readlane_b32 s15, v254, 28
	s_and_b64 vcc, exec, s[14:15]
	s_cbranch_vccz .LBB0_265
	s_barrier

; #define PG8_STAGE(bufoff, gbase, o0, o1) do { \
;         __builtin_amdgcn_global_load_lds((const unsigned*)((const char*)(gbase) + (o0)), (LAS unsigned*)(lds + (bufoff) + ldsw), 16, 0, 0); \
;         __builtin_amdgcn_global_load_lds((const unsigned*)((const char*)(gbase) + (o1)), (LAS unsigned*)(lds + (bufoff) + ldsw + 8192), 16, 0, 0); } while (0)
; #define PG8_LDA(dst, b, h) do { _Pragma("unroll") for (int m = 0; m < 4; ++m) _Pragma("unroll") for (int k = 0; k < 2; ++k) dst[m][k] = *(const LAS bf16x8*)(lds + PG8_SA(b, h) + aoff + m * 2048 + k * 1024); } while (0)
; #define PG8_LDB(dst, b, h) do { _Pragma("unroll") for (int n = 0; n < 2; ++n) _Pragma("unroll") for (int k = 0; k < 2; ++k) dst[n][k] = *(const LAS bf16x8*)(lds + PG8_SB(b, h) + boff + n * 2048 + k * 1024); } while (0)
; #define PG8_WAIT_V(n) asm volatile("s_waitcnt vmcnt(" #n ")" ::: "memory")
; #define PG8_WAIT_L(n) asm volatile("s_waitcnt lgkmcnt(" #n ")" ::: "memory")
; #define PG8_BAR __builtin_amdgcn_s_barrier()
; #define PG8_SCHED __builtin_amdgcn_sched_barrier(0)
; template <class Epi, class Sched, class Prob>
; __device__ __forceinline__ void gemm_phase(LAS unsigned char* lds, LAS unsigned char* lds_epi, const Prob g, const Sched& S, const Epi& E, int wid) {
;     ...
;             PG8_LDB(B0, 0, 0); PG8_LDB(B1, 0, 1); PG8_SCHED; PG8_LDA(At, 0, 0); PG8_STAGE(PG8_SA(1, 1), a1, cA10, cA11);
;             PG8_WAIT_V(8); PG8_WAIT_L(0); PG8_BAR; PG8_MMA(0, 0, At, B0); PG8_MMA(0, 1, At, B1); PG8_BAR; PG8_SCHED;
;             PG8_LDA(At, 0, 1); PG8_STAGE(PG8_SB(0, 0), b2, vB0, vB1); PG8_STAGE(PG8_SB(0, 1), b2 + hstepB, vB0, vB1); PG8_STAGE(PG8_SA(0, 0), a2, cA00, cA01);
;             PG8_WAIT_V(8); PG8_WAIT_L(0); PG8_BAR; PG8_MMA(1, 0, At, B0); PG8_MMA(1, 1, At, B1); PG8_BAR; PG8_SCHED;
.LBB0_1156:
	v_add_u32_e32 v146, s62, v149
	ds_read_b128 v[158:161], v146
	ds_read_b128 v[162:165], v146 offset:1024
	ds_read_b128 v[166:169], v146 offset:2048
	ds_read_b128 v[170:173], v146 offset:3072
	v_add_u32_e32 v146, s63, v149
	ds_read_b128 v[174:177], v146
	ds_read_b128 v[178:181], v146 offset:1024
	ds_read_b128 v[182:185], v146 offset:2048
	ds_read_b128 v[186:189], v146 offset:3072
	s_add_u32 s40, s38, 0x80
	s_addc_u32 s41, s39, 0
	s_cmp_eq_u32 s68, 28
	s_cselect_b32 s43, s25, s41
	s_cselect_b32 s42, s27, s40
	s_cselect_b32 s41, s23, s67
	s_cselect_b32 s40, s37, s66
	v_lshl_add_u64 v[146:147], s[38:39], 0, v[140:141]
	s_add_i32 m0, s53, 0xc000
	ds_read_b128 v[190:193], v153
	ds_read_b128 v[194:197], v153 offset:1024
	ds_read_b128 v[198:201], v153 offset:2048
	ds_read_b128 v[202:205], v153 offset:3072
	ds_read_b128 v[206:209], v153 offset:4096
	ds_read_b128 v[210:213], v153 offset:5120
	ds_read_b128 v[214:217], v153 offset:6144
	ds_read_b128 v[218:221], v153 offset:7168
	global_load_lds_dwordx4 v[146:147], off
	v_lshl_add_u64 v[146:147], s[38:39], 0, v[142:143]
	s_add_i32 m0, s53, 0xe000
	s_nop 0
	global_load_lds_dwordx4 v[146:147], off
	s_waitcnt vmcnt(8)
	s_waitcnt lgkmcnt(0)
	s_barrier
	s_setprio 1
	s_waitcnt lgkmcnt(0)
	v_mfma_f32_16x16x32_bf16 v[124:127], v[158:161], v[190:193], v[124:127]
	v_mfma_f32_16x16x32_bf16 v[120:123], v[166:169], v[190:193], v[120:123]
	v_mfma_f32_16x16x32_bf16 v[108:111], v[158:161], v[198:201], v[108:111]
	v_mfma_f32_16x16x32_bf16 v[104:107], v[166:169], v[198:201], v[104:107]
	v_mfma_f32_16x16x32_bf16 v[92:95], v[158:161], v[206:209], v[92:95]
	v_mfma_f32_16x16x32_bf16 v[88:91], v[166:169], v[206:209], v[88:91]
	v_mfma_f32_16x16x32_bf16 v[76:79], v[158:161], v[214:217], v[76:79]
	v_mfma_f32_16x16x32_bf16 v[72:75], v[166:169], v[214:217], v[72:75]
	v_mfma_f32_16x16x32_bf16 v[124:127], v[162:165], v[194:197], v[124:127]
	v_mfma_f32_16x16x32_bf16 v[120:123], v[170:173], v[194:197], v[120:123]
	v_mfma_f32_16x16x32_bf16 v[108:111], v[162:165], v[202:205], v[108:111]
	v_mfma_f32_16x16x32_bf16 v[104:107], v[170:173], v[202:205], v[104:107]
	v_mfma_f32_16x16x32_bf16 v[92:95], v[162:165], v[210:213], v[92:95]
	v_mfma_f32_16x16x32_bf16 v[88:91], v[170:173], v[210:213], v[88:91]
	v_mfma_f32_16x16x32_bf16 v[76:79], v[162:165], v[218:221], v[76:79]
	v_mfma_f32_16x16x32_bf16 v[72:75], v[170:173], v[218:221], v[72:75]
	v_mfma_f32_16x16x32_bf16 v[116:119], v[174:177], v[190:193], v[116:119]
	v_mfma_f32_16x16x32_bf16 v[112:115], v[182:185], v[190:193], v[112:115]
	v_mfma_f32_16x16x32_bf16 v[100:103], v[174:177], v[198:201], v[100:103]
	v_mfma_f32_16x16x32_bf16 v[96:99], v[182:185], v[198:201], v[96:99]
	v_mfma_f32_16x16x32_bf16 v[84:87], v[174:177], v[206:209], v[84:87]
	v_mfma_f32_16x16x32_bf16 v[80:83], v[182:185], v[206:209], v[80:83]
	v_mfma_f32_16x16x32_bf16 v[68:71], v[174:177], v[214:217], v[68:71]
	v_mfma_f32_16x16x32_bf16 v[64:67], v[182:185], v[214:217], v[64:67]
	v_mfma_f32_16x16x32_bf16 v[116:119], v[178:181], v[194:197], v[116:119]
	v_mfma_f32_16x16x32_bf16 v[112:115], v[186:189], v[194:197], v[112:115]
	v_mfma_f32_16x16x32_bf16 v[100:103], v[178:181], v[202:205], v[100:103]
	v_mfma_f32_16x16x32_bf16 v[96:99], v[186:189], v[202:205], v[96:99]
	v_mfma_f32_16x16x32_bf16 v[84:87], v[178:181], v[210:213], v[84:87]
	v_mfma_f32_16x16x32_bf16 v[80:83], v[186:189], v[210:213], v[80:83]
	v_mfma_f32_16x16x32_bf16 v[68:71], v[178:181], v[218:221], v[68:71]
	v_mfma_f32_16x16x32_bf16 v[64:67], v[186:189], v[218:221], v[64:67]
	s_setprio 0
	s_barrier
	s_add_i32 s69, s62, s97
	v_lshl_add_u64 v[146:147], s[40:41], 0, v[130:131]
	s_mov_b32 m0, s69
	ds_read_b128 v[190:193], v153 offset:16384
	ds_read_b128 v[194:197], v153 offset:17408
	ds_read_b128 v[198:201], v153 offset:18432
	ds_read_b128 v[202:205], v153 offset:19456
	ds_read_b128 v[206:209], v153 offset:20480
	ds_read_b128 v[210:213], v153 offset:21504
	ds_read_b128 v[214:217], v153 offset:22528
	ds_read_b128 v[218:221], v153 offset:23552
	global_load_lds_dwordx4 v[146:147], off
	s_add_i32 m0, s69, 0x2000
	s_add_u32 s70, s40, 0x80000
	v_lshl_add_u64 v[222:223], s[40:41], 0, v[128:129]
	s_addc_u32 s71, s41, 0
	s_add_i32 s69, s63, s97
	global_load_lds_dwordx4 v[222:223], off
	v_lshl_add_u64 v[224:225], s[70:71], 0, v[130:131]
	s_mov_b32 m0, s69
	v_lshl_add_u64 v[226:227], s[42:43], 0, v[128:129]
	global_load_lds_dwordx4 v[224:225], off
	v_lshl_add_u64 v[224:225], s[70:71], 0, v[128:129]
	s_add_i32 m0, s69, 0x2000
	s_nop 0
	global_load_lds_dwordx4 v[224:225], off
	v_lshl_add_u64 v[224:225], s[42:43], 0, v[130:131]
	s_mov_b32 m0, s53
	s_nop 0
	global_load_lds_dwordx4 v[224:225], off
	s_mov_b32 m0, s54
	s_nop 0
	global_load_lds_dwordx4 v[226:227], off
	s_waitcnt vmcnt(8)
	s_waitcnt lgkmcnt(0)
	s_barrier
; #define PG8_STAGE(bufoff, gbase, o0, o1) do { \
;         __builtin_amdgcn_global_load_lds((const unsigned*)((const char*)(gbase) + (o0)), (LAS unsigned*)(lds + (bufoff) + ldsw), 16, 0, 0); \
;         __builtin_amdgcn_global_load_lds((const unsigned*)((const char*)(gbase) + (o1)), (LAS unsigned*)(lds + (bufoff) + ldsw + 8192), 16, 0, 0); } while (0)
; #define PG8_LDA(dst, b, h) do { _Pragma("unroll") for (int m = 0; m < 4; ++m) _Pragma("unroll") for (int k = 0; k < 2; ++k) dst[m][k] = *(const LAS bf16x8*)(lds + PG8_SA(b, h) + aoff + m * 2048 + k * 1024); } while (0)
; #define PG8_LDB(dst, b, h) do { _Pragma("unroll") for (int n = 0; n < 2; ++n) _Pragma("unroll") for (int k = 0; k < 2; ++k) dst[n][k] = *(const LAS bf16x8*)(lds + PG8_SB(b, h) + boff + n * 2048 + k * 1024); } while (0)
; #define PG8_WAIT_V(n) asm volatile("s_waitcnt vmcnt(" #n ")" ::: "memory")
; #define PG8_WAIT_L(n) asm volatile("s_waitcnt lgkmcnt(" #n ")" ::: "memory")
; #define PG8_BAR __builtin_amdgcn_s_barrier()
; #define PG8_SCHED __builtin_amdgcn_sched_barrier(0)
; template <class Epi, class Sched, class Prob>
; __device__ __forceinline__ void gemm_phase(LAS unsigned char* lds, LAS unsigned char* lds_epi, const Prob g, const Sched& S, const Epi& E, int wid) {
;     ...
;             PG8_WAIT_V(8); PG8_WAIT_L(0); PG8_BAR; PG8_MMA(1, 0, At, B0); PG8_MMA(1, 1, At, B1); PG8_BAR; PG8_SCHED;
;             PG8_LDB(B0, 1, 0); PG8_LDB(B1, 1, 1); PG8_SCHED; PG8_LDA(At, 1, 0); PG8_STAGE(PG8_SA(0, 1), a2, cA10, cA11);
;             PG8_WAIT_V(8); PG8_WAIT_L(0); PG8_BAR; PG8_MMA(0, 0, At, B0); PG8_MMA(0, 1, At, B1); PG8_BAR; PG8_SCHED;
	s_setprio 1
	s_waitcnt lgkmcnt(0)
	v_mfma_f32_16x16x32_bf16 v[60:63], v[158:161], v[190:193], v[60:63]
	v_mfma_f32_16x16x32_bf16 v[56:59], v[166:169], v[190:193], v[56:59]
	v_mfma_f32_16x16x32_bf16 v[44:47], v[158:161], v[198:201], v[44:47]
	v_mfma_f32_16x16x32_bf16 v[40:43], v[166:169], v[198:201], v[40:43]
	v_mfma_f32_16x16x32_bf16 v[28:31], v[158:161], v[206:209], v[28:31]
	v_mfma_f32_16x16x32_bf16 v[24:27], v[166:169], v[206:209], v[24:27]
	v_mfma_f32_16x16x32_bf16 v[0:3], v[158:161], v[214:217], v[0:3]
	v_mfma_f32_16x16x32_bf16 v[12:15], v[166:169], v[214:217], v[12:15]
	v_mfma_f32_16x16x32_bf16 v[60:63], v[162:165], v[194:197], v[60:63]
	v_mfma_f32_16x16x32_bf16 v[56:59], v[170:173], v[194:197], v[56:59]
	v_mfma_f32_16x16x32_bf16 v[44:47], v[162:165], v[202:205], v[44:47]
	v_mfma_f32_16x16x32_bf16 v[40:43], v[170:173], v[202:205], v[40:43]
	v_mfma_f32_16x16x32_bf16 v[28:31], v[162:165], v[210:213], v[28:31]
	v_mfma_f32_16x16x32_bf16 v[24:27], v[170:173], v[210:213], v[24:27]
	v_mfma_f32_16x16x32_bf16 v[0:3], v[162:165], v[218:221], v[0:3]
	v_mfma_f32_16x16x32_bf16 v[12:15], v[170:173], v[218:221], v[12:15]
	v_mfma_f32_16x16x32_bf16 v[52:55], v[174:177], v[190:193], v[52:55]
	v_mfma_f32_16x16x32_bf16 v[48:51], v[182:185], v[190:193], v[48:51]
	v_mfma_f32_16x16x32_bf16 v[36:39], v[174:177], v[198:201], v[36:39]
	v_mfma_f32_16x16x32_bf16 v[32:35], v[182:185], v[198:201], v[32:35]
	v_mfma_f32_16x16x32_bf16 v[20:23], v[174:177], v[206:209], v[20:23]
	v_mfma_f32_16x16x32_bf16 v[16:19], v[182:185], v[206:209], v[16:19]
	v_mfma_f32_16x16x32_bf16 v[8:11], v[174:177], v[214:217], v[8:11]
	v_mfma_f32_16x16x32_bf16 v[4:7], v[182:185], v[214:217], v[4:7]
	v_mfma_f32_16x16x32_bf16 v[52:55], v[178:181], v[194:197], v[52:55]
	v_mfma_f32_16x16x32_bf16 v[48:51], v[186:189], v[194:197], v[48:51]
	v_mfma_f32_16x16x32_bf16 v[36:39], v[178:181], v[202:205], v[36:39]
	v_mfma_f32_16x16x32_bf16 v[32:35], v[186:189], v[202:205], v[32:35]
	v_mfma_f32_16x16x32_bf16 v[20:23], v[178:181], v[210:213], v[20:23]
	v_mfma_f32_16x16x32_bf16 v[16:19], v[186:189], v[210:213], v[16:19]
	v_mfma_f32_16x16x32_bf16 v[8:11], v[178:181], v[218:221], v[8:11]
	v_mfma_f32_16x16x32_bf16 v[4:7], v[186:189], v[218:221], v[4:7]
	s_setprio 0
	s_barrier
	s_add_i32 s69, 0, 0x18000
	v_add_u32_e32 v157, s69, v149
	s_add_i32 s70, 0, 0x1c000
	ds_read_b128 v[158:161], v157
	ds_read_b128 v[162:165], v157 offset:1024
	ds_read_b128 v[166:169], v157 offset:2048
	ds_read_b128 v[170:173], v157 offset:3072
	v_add_u32_e32 v157, s70, v149
	ds_read_b128 v[174:177], v157
	ds_read_b128 v[178:181], v157 offset:1024
	ds_read_b128 v[182:185], v157 offset:2048
	ds_read_b128 v[186:189], v157 offset:3072
	s_mov_b32 m0, s55
	v_lshl_add_u64 v[228:229], s[42:43], 0, v[132:133]
	ds_read_b128 v[190:193], v153 offset:32768
	ds_read_b128 v[194:197], v153 offset:33792
	ds_read_b128 v[198:201], v153 offset:34816
	ds_read_b128 v[202:205], v153 offset:35840
	ds_read_b128 v[206:209], v153 offset:36864
	ds_read_b128 v[210:213], v153 offset:37888
	ds_read_b128 v[214:217], v153 offset:38912
	ds_read_b128 v[218:221], v153 offset:39936
	global_load_lds_dwordx4 v[228:229], off
	v_lshl_add_u64 v[228:229], s[42:43], 0, v[134:135]
	s_mov_b32 m0, s56
	s_nop 0
	global_load_lds_dwordx4 v[228:229], off
	s_waitcnt vmcnt(8)
	s_waitcnt lgkmcnt(0)
	s_barrier
	s_setprio 1
	s_waitcnt lgkmcnt(0)
	v_mfma_f32_16x16x32_bf16 v[124:127], v[158:161], v[190:193], v[124:127]
	v_mfma_f32_16x16x32_bf16 v[120:123], v[166:169], v[190:193], v[120:123]
	v_mfma_f32_16x16x32_bf16 v[108:111], v[158:161], v[198:201], v[108:111]
	v_mfma_f32_16x16x32_bf16 v[104:107], v[166:169], v[198:201], v[104:107]
	v_mfma_f32_16x16x32_bf16 v[92:95], v[158:161], v[206:209], v[92:95]
	v_mfma_f32_16x16x32_bf16 v[88:91], v[166:169], v[206:209], v[88:91]
	v_mfma_f32_16x16x32_bf16 v[76:79], v[158:161], v[214:217], v[76:79]
	v_mfma_f32_16x16x32_bf16 v[72:75], v[166:169], v[214:217], v[72:75]
	v_mfma_f32_16x16x32_bf16 v[124:127], v[162:165], v[194:197], v[124:127]
	v_mfma_f32_16x16x32_bf16 v[120:123], v[170:173], v[194:197], v[120:123]
	v_mfma_f32_16x16x32_bf16 v[108:111], v[162:165], v[202:205], v[108:111]
	v_mfma_f32_16x16x32_bf16 v[104:107], v[170:173], v[202:205], v[104:107]
	v_mfma_f32_16x16x32_bf16 v[92:95], v[162:165], v[210:213], v[92:95]
	v_mfma_f32_16x16x32_bf16 v[88:91], v[170:173], v[210:213], v[88:91]
	v_mfma_f32_16x16x32_bf16 v[76:79], v[162:165], v[218:221], v[76:79]
	v_mfma_f32_16x16x32_bf16 v[72:75], v[170:173], v[218:221], v[72:75]
	v_mfma_f32_16x16x32_bf16 v[116:119], v[174:177], v[190:193], v[116:119]
	v_mfma_f32_16x16x32_bf16 v[112:115], v[182:185], v[190:193], v[112:115]
	v_mfma_f32_16x16x32_bf16 v[100:103], v[174:177], v[198:201], v[100:103]
	v_mfma_f32_16x16x32_bf16 v[96:99], v[182:185], v[198:201], v[96:99]
	v_mfma_f32_16x16x32_bf16 v[84:87], v[174:177], v[206:209], v[84:87]
	v_mfma_f32_16x16x32_bf16 v[80:83], v[182:185], v[206:209], v[80:83]
	v_mfma_f32_16x16x32_bf16 v[68:71], v[174:177], v[214:217], v[68:71]
	v_mfma_f32_16x16x32_bf16 v[64:67], v[182:185], v[214:217], v[64:67]
	v_mfma_f32_16x16x32_bf16 v[116:119], v[178:181], v[194:197], v[116:119]
	v_mfma_f32_16x16x32_bf16 v[112:115], v[186:189], v[194:197], v[112:115]
	v_mfma_f32_16x16x32_bf16 v[100:103], v[178:181], v[202:205], v[100:103]
	v_mfma_f32_16x16x32_bf16 v[96:99], v[186:189], v[202:205], v[96:99]
	v_mfma_f32_16x16x32_bf16 v[84:87], v[178:181], v[210:213], v[84:87]
	v_mfma_f32_16x16x32_bf16 v[80:83], v[186:189], v[210:213], v[80:83]
	v_mfma_f32_16x16x32_bf16 v[68:71], v[178:181], v[218:221], v[68:71]
	v_mfma_f32_16x16x32_bf16 v[64:67], v[186:189], v[218:221], v[64:67]
	s_setprio 0
	s_barrier
; #define PG8_STAGE(bufoff, gbase, o0, o1) do { \
;         __builtin_amdgcn_global_load_lds((const unsigned*)((const char*)(gbase) + (o0)), (LAS unsigned*)(lds + (bufoff) + ldsw), 16, 0, 0); \
;         __builtin_amdgcn_global_load_lds((const unsigned*)((const char*)(gbase) + (o1)), (LAS unsigned*)(lds + (bufoff) + ldsw + 8192), 16, 0, 0); } while (0)
; #define PG8_LDA(dst, b, h) do { _Pragma("unroll") for (int m = 0; m < 4; ++m) _Pragma("unroll") for (int k = 0; k < 2; ++k) dst[m][k] = *(const LAS bf16x8*)(lds + PG8_SA(b, h) + aoff + m * 2048 + k * 1024); } while (0)
; #define PG8_WAIT_V(n) asm volatile("s_waitcnt vmcnt(" #n ")" ::: "memory")
; #define PG8_WAIT_L(n) asm volatile("s_waitcnt lgkmcnt(" #n ")" ::: "memory")
; #define PG8_BAR __builtin_amdgcn_s_barrier()
; #define PG8_SCHED __builtin_amdgcn_sched_barrier(0)
; template <class Epi, class Sched, class Prob>
; __device__ __forceinline__ void gemm_phase(LAS unsigned char* lds, LAS unsigned char* lds_epi, const Prob g, const Sched& S, const Epi& E, int wid) {
;     ...
;             PG8_LDA(At, 1, 1); PG8_STAGE(PG8_SB(1, 0), b3, vB0, vB1); PG8_STAGE(PG8_SB(1, 1), b3 + hstepB, vB0, vB1); PG8_STAGE(PG8_SA(1, 0), a3, cA00, cA01);
;             PG8_WAIT_V(8); PG8_WAIT_L(0); PG8_BAR; PG8_MMA(1, 0, At, B0); PG8_MMA(1, 1, At, B1); PG8_BAR; PG8_SCHED;
;         }
;         if constexpr (Prob::FP8) asm volatile("s_nop 7\n\ts_nop 7\n\ts_nop 7" ::: "memory");
;         if (wr == 0) PG8_BAR;
	s_add_i32 s42, s69, s97
	v_lshl_add_u64 v[146:147], v[146:147], 0, s[16:17]
	s_mov_b32 m0, s42
	ds_read_b128 v[190:193], v153 offset:49152
	ds_read_b128 v[194:197], v153 offset:50176
	ds_read_b128 v[198:201], v153 offset:51200
	ds_read_b128 v[202:205], v153 offset:52224
	ds_read_b128 v[206:209], v153 offset:53248
	ds_read_b128 v[210:213], v153 offset:54272
	ds_read_b128 v[214:217], v153 offset:55296
	ds_read_b128 v[218:221], v153 offset:56320
	global_load_lds_dwordx4 v[146:147], off
	s_add_i32 m0, s42, 0x2000
	s_add_u32 s40, s40, 0x80080
	v_lshl_add_u64 v[146:147], v[222:223], 0, s[16:17]
	s_addc_u32 s41, s41, 0
	s_add_i32 s42, s70, s97
	global_load_lds_dwordx4 v[146:147], off
	v_lshl_add_u64 v[146:147], s[40:41], 0, v[130:131]
	s_mov_b32 m0, s42
	s_nop 0
	global_load_lds_dwordx4 v[146:147], off
	v_lshl_add_u64 v[146:147], s[40:41], 0, v[128:129]
	s_add_i32 m0, s42, 0x2000
	s_nop 0
	global_load_lds_dwordx4 v[146:147], off
	v_lshl_add_u64 v[146:147], v[224:225], 0, s[16:17]
	s_mov_b32 m0, s60
	s_nop 0
	global_load_lds_dwordx4 v[146:147], off
	v_lshl_add_u64 v[146:147], v[226:227], 0, s[16:17]
	s_mov_b32 m0, s61
	s_nop 0
	global_load_lds_dwordx4 v[146:147], off
	s_waitcnt vmcnt(8)
	s_waitcnt lgkmcnt(0)
	s_barrier
	s_setprio 1
	s_waitcnt lgkmcnt(0)
	v_mfma_f32_16x16x32_bf16 v[60:63], v[158:161], v[190:193], v[60:63]
	v_mfma_f32_16x16x32_bf16 v[56:59], v[166:169], v[190:193], v[56:59]
	v_mfma_f32_16x16x32_bf16 v[44:47], v[158:161], v[198:201], v[44:47]
	v_mfma_f32_16x16x32_bf16 v[40:43], v[166:169], v[198:201], v[40:43]
	v_mfma_f32_16x16x32_bf16 v[28:31], v[158:161], v[206:209], v[28:31]
	v_mfma_f32_16x16x32_bf16 v[24:27], v[166:169], v[206:209], v[24:27]
	v_mfma_f32_16x16x32_bf16 v[0:3], v[158:161], v[214:217], v[0:3]
	v_mfma_f32_16x16x32_bf16 v[12:15], v[166:169], v[214:217], v[12:15]
	v_mfma_f32_16x16x32_bf16 v[60:63], v[162:165], v[194:197], v[60:63]
	v_mfma_f32_16x16x32_bf16 v[56:59], v[170:173], v[194:197], v[56:59]
	v_mfma_f32_16x16x32_bf16 v[44:47], v[162:165], v[202:205], v[44:47]
	v_mfma_f32_16x16x32_bf16 v[40:43], v[170:173], v[202:205], v[40:43]
	v_mfma_f32_16x16x32_bf16 v[28:31], v[162:165], v[210:213], v[28:31]
	v_mfma_f32_16x16x32_bf16 v[24:27], v[170:173], v[210:213], v[24:27]
	v_mfma_f32_16x16x32_bf16 v[0:3], v[162:165], v[218:221], v[0:3]
	v_mfma_f32_16x16x32_bf16 v[12:15], v[170:173], v[218:221], v[12:15]
	v_mfma_f32_16x16x32_bf16 v[52:55], v[174:177], v[190:193], v[52:55]
	v_mfma_f32_16x16x32_bf16 v[48:51], v[182:185], v[190:193], v[48:51]
	v_mfma_f32_16x16x32_bf16 v[36:39], v[174:177], v[198:201], v[36:39]
	v_mfma_f32_16x16x32_bf16 v[32:35], v[182:185], v[198:201], v[32:35]
	v_mfma_f32_16x16x32_bf16 v[20:23], v[174:177], v[206:209], v[20:23]
	v_mfma_f32_16x16x32_bf16 v[16:19], v[182:185], v[206:209], v[16:19]
	v_mfma_f32_16x16x32_bf16 v[8:11], v[174:177], v[214:217], v[8:11]
	v_mfma_f32_16x16x32_bf16 v[4:7], v[182:185], v[214:217], v[4:7]
	v_mfma_f32_16x16x32_bf16 v[52:55], v[178:181], v[194:197], v[52:55]
	v_mfma_f32_16x16x32_bf16 v[48:51], v[186:189], v[194:197], v[48:51]
	v_mfma_f32_16x16x32_bf16 v[36:39], v[178:181], v[202:205], v[36:39]
	v_mfma_f32_16x16x32_bf16 v[32:35], v[186:189], v[202:205], v[32:35]
	v_mfma_f32_16x16x32_bf16 v[20:23], v[178:181], v[210:213], v[20:23]
	v_mfma_f32_16x16x32_bf16 v[16:19], v[186:189], v[210:213], v[16:19]
	v_mfma_f32_16x16x32_bf16 v[8:11], v[178:181], v[218:221], v[8:11]
	v_mfma_f32_16x16x32_bf16 v[4:7], v[186:189], v[218:221], v[4:7]
	s_setprio 0
	s_barrier
	s_add_i32 s68, s68, 2
	s_add_u32 s38, s38, 0x100
	s_addc_u32 s39, s39, 0
	s_add_u32 s66, s66, 0x100
	s_addc_u32 s67, s67, 0
	s_cmp_gt_u32 s68, 29
	s_cbranch_scc0 .LBB0_1156
	v_readlane_b32 s38, v254, 27
	v_readlane_b32 s39, v254, 28
	s_and_b64 vcc, exec, s[38:39]
	s_cbranch_vccz .LBB0_1159
	s_barrier

; #define PG8_STAGE(bufoff, gbase, o0, o1) do { \
;         __builtin_amdgcn_global_load_lds((const unsigned*)((const char*)(gbase) + (o0)), (LAS unsigned*)(lds + (bufoff) + ldsw), 16, 0, 0); \
;         __builtin_amdgcn_global_load_lds((const unsigned*)((const char*)(gbase) + (o1)), (LAS unsigned*)(lds + (bufoff) + ldsw + 8192), 16, 0, 0); } while (0)
; #define PG8_LDA(dst, b, h) do { _Pragma("unroll") for (int m = 0; m < 4; ++m) _Pragma("unroll") for (int k = 0; k < 2; ++k) dst[m][k] = *(const LAS bf16x8*)(lds + PG8_SA(b, h) + aoff + m * 2048 + k * 1024); } while (0)
; #define PG8_LDB(dst, b, h) do { _Pragma("unroll") for (int n = 0; n < 2; ++n) _Pragma("unroll") for (int k = 0; k < 2; ++k) dst[n][k] = *(const LAS bf16x8*)(lds + PG8_SB(b, h) + boff + n * 2048 + k * 1024); } while (0)
; #define PG8_WAIT_V(n) asm volatile("s_waitcnt vmcnt(" #n ")" ::: "memory")
; #define PG8_WAIT_L(n) asm volatile("s_waitcnt lgkmcnt(" #n ")" ::: "memory")
; #define PG8_BAR __builtin_amdgcn_s_barrier()
; #define PG8_SCHED __builtin_amdgcn_sched_barrier(0)
; template <class Epi, class Sched, class Prob>
; __device__ __forceinline__ void gemm_phase(LAS unsigned char* lds, LAS unsigned char* lds_epi, const Prob g, const Sched& S, const Epi& E, int wid) {
;     ...
;         const bool has_next = S.next(ui + 1, nxt);
;         const char* nA = has_next ? g.a_base(nxt) : cA; const char* nB = has_next ? g.b_base(nxt) : cB;
; _Pragma("clang loop unroll(disable)")
;         for (int t = 0; t < nt; t += 2) {
;             const bool last = (t == nt - 2);
;             const char* a1 = cA + (size_t)(t + 1) * kstep;
;             const char* a2 = last ? nA : cA + (size_t)(t + 2) * kstep; const char* b2 = last ? nB : cB + (size_t)(t + 2) * kstep;
;             const char* a3 = a2 + kstep; const char* b3 = b2 + kstep;
;             PG8_LDB(B0, 0, 0); PG8_LDB(B1, 0, 1); PG8_SCHED; PG8_LDA(At, 0, 0); PG8_STAGE(PG8_SA(1, 1), a1, cA10, cA11);
;             PG8_WAIT_V(8); PG8_WAIT_L(0); PG8_BAR; PG8_MMA(0, 0, At, B0); PG8_MMA(0, 1, At, B1); PG8_BAR; PG8_SCHED;
;             PG8_LDA(At, 0, 1); PG8_STAGE(PG8_SB(0, 0), b2, vB0, vB1); PG8_STAGE(PG8_SB(0, 1), b2 + hstepB, vB0, vB1); PG8_STAGE(PG8_SA(0, 0), a2, cA00, cA01);
;             PG8_WAIT_V(8); PG8_WAIT_L(0); PG8_BAR; PG8_MMA(1, 0, At, B0); PG8_MMA(1, 1, At, B1); PG8_BAR; PG8_SCHED;
.LBB0_1247:
	s_ashr_i32 s3, s2, 31
	s_lshl_b64 s[24:25], s[2:3], 19
	s_add_u32 s24, s36, s24
	s_addc_u32 s25, s37, s25
	s_and_b64 s[26:27], s[22:23], exec
	s_cselect_b32 s3, s25, s11
	s_cselect_b32 s54, s24, s10
	s_ashr_i32 s21, s20, 31
	s_lshl_b64 s[26:27], s[20:21], 19
	s_add_u32 s26, s40, s26
	s_addc_u32 s27, s41, s27
	s_and_b64 s[34:35], s[22:23], exec
	s_cselect_b32 s21, s27, s31
	s_cselect_b32 s55, s26, s30
	s_add_u32 s10, s10, 0x80
	s_addc_u32 s11, s11, 0
	s_add_u32 s56, s30, 0x100
	v_mov_b32_e32 v32, 0
	s_addc_u32 s58, s31, 0
	s_mov_b32 s59, -2
	ds_read_b128 v[24:27], v194
	ds_read_b128 v[28:31], v194 offset:1024
	ds_read_b128 v[16:19], v194 offset:2048
	ds_read_b128 v[20:23], v194 offset:3072
	ds_read_b128 v[8:11], v195
	ds_read_b128 v[12:15], v195 offset:1024
	ds_read_b128 v[0:3], v195 offset:2048
	ds_read_b128 v[4:7], v195 offset:3072
	s_add_u32 s30, s10, 0x80
	s_addc_u32 s31, s11, 0
	s_cmp_eq_u32 s59, 12
	s_cselect_b32 s35, s3, s31
	s_cselect_b32 s34, s54, s30
	s_cselect_b32 s31, s21, s58
	s_cselect_b32 s30, s55, s56
	v_lshl_add_u64 v[224:225], s[10:11], 0, v[178:179]
	s_add_i32 m0, s29, 0xc000
	ds_read_b128 v[182:185], v196
	ds_read_b128 v[186:189], v196 offset:1024
	ds_read_b128 v[200:203], v196 offset:2048
	ds_read_b128 v[204:207], v196 offset:3072
	ds_read_b128 v[208:211], v196 offset:4096
	ds_read_b128 v[212:215], v196 offset:5120
	ds_read_b128 v[216:219], v196 offset:6144
	ds_read_b128 v[220:223], v196 offset:7168
	global_load_lds_dwordx4 v[224:225], off
	v_lshl_add_u64 v[224:225], s[10:11], 0, v[176:177]
	s_add_i32 m0, s29, 0xe000
	s_nop 0
	global_load_lds_dwordx4 v[224:225], off
	s_waitcnt vmcnt(8)
	s_waitcnt lgkmcnt(0)
	s_barrier
	s_setprio 1
	s_waitcnt lgkmcnt(0)
	v_mfma_f32_16x16x128_f8f6f4 v[156:159], v[24:31], v[182:189], 0
	v_mfma_f32_16x16x128_f8f6f4 v[144:147], v[16:23], v[182:189], 0
	v_mfma_f32_16x16x128_f8f6f4 v[140:143], v[24:31], v[200:207], 0
	v_mfma_f32_16x16x128_f8f6f4 v[132:135], v[16:23], v[200:207], 0
	v_mfma_f32_16x16x128_f8f6f4 v[124:127], v[24:31], v[208:215], 0
	v_mfma_f32_16x16x128_f8f6f4 v[116:119], v[16:23], v[208:215], 0
	v_mfma_f32_16x16x128_f8f6f4 v[108:111], v[24:31], v[216:223], 0
	v_mfma_f32_16x16x128_f8f6f4 v[100:103], v[16:23], v[216:223], 0
	v_mfma_f32_16x16x128_f8f6f4 v[152:155], v[8:15], v[182:189], 0
	v_mfma_f32_16x16x128_f8f6f4 v[148:151], v[0:7], v[182:189], 0
	v_mfma_f32_16x16x128_f8f6f4 v[136:139], v[8:15], v[200:207], 0
	v_mfma_f32_16x16x128_f8f6f4 v[128:131], v[0:7], v[200:207], 0
	v_mfma_f32_16x16x128_f8f6f4 v[120:123], v[8:15], v[208:215], 0
	v_mfma_f32_16x16x128_f8f6f4 v[112:115], v[0:7], v[208:215], 0
	v_mfma_f32_16x16x128_f8f6f4 v[104:107], v[8:15], v[216:223], 0
	v_mfma_f32_16x16x128_f8f6f4 v[96:99], v[0:7], v[216:223], 0
	s_setprio 0
	s_barrier
	s_add_i32 s60, s50, s97
	v_lshl_add_u64 v[182:183], s[30:31], 0, v[162:163]
	s_mov_b32 m0, s60
	ds_read_b128 v[200:203], v196 offset:16384
	ds_read_b128 v[204:207], v196 offset:17408
	ds_read_b128 v[208:211], v196 offset:18432
	ds_read_b128 v[212:215], v196 offset:19456
	ds_read_b128 v[216:219], v196 offset:20480
	ds_read_b128 v[220:223], v196 offset:21504
	ds_read_b128 v[224:227], v196 offset:22528
	ds_read_b128 v[228:231], v196 offset:23552
	global_load_lds_dwordx4 v[182:183], off
	s_add_i32 m0, s60, 0x2000
	s_add_u32 s60, s30, 0x40000
	v_lshl_add_u64 v[184:185], s[30:31], 0, v[160:161]
	s_addc_u32 s61, s31, 0
	s_add_i32 s62, s51, s97
	global_load_lds_dwordx4 v[184:185], off
	v_lshl_add_u64 v[186:187], s[60:61], 0, v[162:163]
	s_mov_b32 m0, s62
	v_lshl_add_u64 v[188:189], s[34:35], 0, v[168:169]
	global_load_lds_dwordx4 v[186:187], off
	v_lshl_add_u64 v[186:187], s[60:61], 0, v[160:161]
	s_add_i32 m0, s62, 0x2000
	s_nop 0
	global_load_lds_dwordx4 v[186:187], off
	v_lshl_add_u64 v[186:187], s[34:35], 0, v[164:165]
	s_mov_b32 m0, s29
	s_nop 0
	global_load_lds_dwordx4 v[186:187], off
	s_mov_b32 m0, s43
	s_nop 0
	global_load_lds_dwordx4 v[188:189], off
	s_waitcnt vmcnt(8)
	s_waitcnt lgkmcnt(0)
	s_barrier
	s_setprio 1
	s_waitcnt lgkmcnt(0)
	v_mfma_f32_16x16x128_f8f6f4 v[92:95], v[24:31], v[200:207], 0
	v_mfma_f32_16x16x128_f8f6f4 v[84:87], v[16:23], v[200:207], 0
	v_mfma_f32_16x16x128_f8f6f4 v[76:79], v[24:31], v[208:215], 0
	v_mfma_f32_16x16x128_f8f6f4 v[68:71], v[16:23], v[208:215], 0
	v_mfma_f32_16x16x128_f8f6f4 v[60:63], v[24:31], v[216:223], 0
	v_mfma_f32_16x16x128_f8f6f4 v[52:55], v[16:23], v[216:223], 0
	v_mfma_f32_16x16x128_f8f6f4 v[44:47], v[24:31], v[224:231], 0
	v_mfma_f32_16x16x128_f8f6f4 v[36:39], v[16:23], v[224:231], 0
	v_mfma_f32_16x16x128_f8f6f4 v[88:91], v[8:15], v[200:207], 0
	v_mfma_f32_16x16x128_f8f6f4 v[80:83], v[0:7], v[200:207], 0
	v_mfma_f32_16x16x128_f8f6f4 v[72:75], v[8:15], v[208:215], 0
	v_mfma_f32_16x16x128_f8f6f4 v[64:67], v[0:7], v[208:215], 0
	v_mfma_f32_16x16x128_f8f6f4 v[56:59], v[8:15], v[216:223], 0
	v_mfma_f32_16x16x128_f8f6f4 v[48:51], v[0:7], v[216:223], 0
	v_mfma_f32_16x16x128_f8f6f4 v[40:43], v[8:15], v[224:231], 0
	v_mfma_f32_16x16x128_f8f6f4 v[32:35], v[0:7], v[224:231], 0
	s_setprio 0
	s_barrier
	s_add_i32 s60, 0, 0x18000
	s_add_i32 s61, 0, 0x1c000
	v_add_u32_e32 v12, s60, v191
	v_add_u32_e32 v28, s61, v191
	ds_read_b128 v[0:3], v12
	ds_read_b128 v[4:7], v12 offset:1024
	ds_read_b128 v[8:11], v12 offset:2048
	ds_read_b128 v[12:15], v12 offset:3072
	ds_read_b128 v[16:19], v28
	ds_read_b128 v[20:23], v28 offset:1024
	ds_read_b128 v[24:27], v28 offset:2048
	ds_read_b128 v[28:31], v28 offset:3072
	s_mov_b32 m0, s44
	v_lshl_add_u64 v[232:233], s[34:35], 0, v[166:167]
	ds_read_b128 v[200:203], v196 offset:32768
	ds_read_b128 v[204:207], v196 offset:33792
	ds_read_b128 v[208:211], v196 offset:34816
	ds_read_b128 v[212:215], v196 offset:35840
	ds_read_b128 v[216:219], v196 offset:36864
	ds_read_b128 v[220:223], v196 offset:37888
	ds_read_b128 v[224:227], v196 offset:38912
	ds_read_b128 v[228:231], v196 offset:39936
	global_load_lds_dwordx4 v[232:233], off
	v_lshl_add_u64 v[232:233], s[34:35], 0, v[170:171]
	s_mov_b32 m0, s45
	s_nop 0
	global_load_lds_dwordx4 v[232:233], off
	s_waitcnt vmcnt(8)
	s_waitcnt lgkmcnt(0)
	s_barrier
; #define PG8_STAGE(bufoff, gbase, o0, o1) do { \
;         __builtin_amdgcn_global_load_lds((const unsigned*)((const char*)(gbase) + (o0)), (LAS unsigned*)(lds + (bufoff) + ldsw), 16, 0, 0); \
;         __builtin_amdgcn_global_load_lds((const unsigned*)((const char*)(gbase) + (o1)), (LAS unsigned*)(lds + (bufoff) + ldsw + 8192), 16, 0, 0); } while (0)
; #define PG8_LDA(dst, b, h) do { _Pragma("unroll") for (int m = 0; m < 4; ++m) _Pragma("unroll") for (int k = 0; k < 2; ++k) dst[m][k] = *(const LAS bf16x8*)(lds + PG8_SA(b, h) + aoff + m * 2048 + k * 1024); } while (0)
; #define PG8_LDB(dst, b, h) do { _Pragma("unroll") for (int n = 0; n < 2; ++n) _Pragma("unroll") for (int k = 0; k < 2; ++k) dst[n][k] = *(const LAS bf16x8*)(lds + PG8_SB(b, h) + boff + n * 2048 + k * 1024); } while (0)
; template <class Epi, class Sched, class Prob>
; __device__ __forceinline__ void gemm_phase(LAS unsigned char* lds, LAS unsigned char* lds_epi, const Prob g, const Sched& S, const Epi& E, int wid) {
;     ...
;         for (int t = 0; t < nt; t += 2) {
;             const bool last = (t == nt - 2);
;             const char* a1 = cA + (size_t)(t + 1) * kstep;
;             const char* a2 = last ? nA : cA + (size_t)(t + 2) * kstep; const char* b2 = last ? nB : cB + (size_t)(t + 2) * kstep;
;             const char* a3 = a2 + kstep; const char* b3 = b2 + kstep;
;             PG8_LDB(B0, 0, 0); PG8_LDB(B1, 0, 1); PG8_SCHED; PG8_LDA(At, 0, 0); PG8_STAGE(PG8_SA(1, 1), a1, cA10, cA11);
;             PG8_WAIT_V(8); PG8_WAIT_L(0); PG8_BAR; PG8_MMA(0, 0, At, B0); PG8_MMA(0, 1, At, B1); PG8_BAR; PG8_SCHED;
;             PG8_LDA(At, 0, 1); PG8_STAGE(PG8_SB(0, 0), b2, vB0, vB1); PG8_STAGE(PG8_SB(0, 1), b2 + hstepB, vB0, vB1); PG8_STAGE(PG8_SA(0, 0), a2, cA00, cA01);
;             PG8_WAIT_V(8); PG8_WAIT_L(0); PG8_BAR; PG8_MMA(1, 0, At, B0); PG8_MMA(1, 1, At, B1); PG8_BAR; PG8_SCHED;
;             PG8_LDB(B0, 1, 0); PG8_LDB(B1, 1, 1); PG8_SCHED; PG8_LDA(At, 1, 0); PG8_STAGE(PG8_SA(0, 1), a2, cA10, cA11);
;             PG8_WAIT_V(8); PG8_WAIT_L(0); PG8_BAR; PG8_MMA(0, 0, At, B0); PG8_MMA(0, 1, At, B1); PG8_BAR; PG8_SCHED;
;             PG8_LDA(At, 1, 1); PG8_STAGE(PG8_SB(1, 0), b3, vB0, vB1); PG8_STAGE(PG8_SB(1, 1), b3 + hstepB, vB0, vB1); PG8_STAGE(PG8_SA(1, 0), a3, cA00, cA01);
;             PG8_WAIT_V(8); PG8_WAIT_L(0); PG8_BAR; PG8_MMA(1, 0, At, B0); PG8_MMA(1, 1, At, B1); PG8_BAR; PG8_SCHED;
	s_setprio 1
	s_waitcnt lgkmcnt(0)
	v_mfma_f32_16x16x128_f8f6f4 v[156:159], v[0:7], v[200:207], v[156:159]
	v_mfma_f32_16x16x128_f8f6f4 v[144:147], v[8:15], v[200:207], v[144:147]
	v_mfma_f32_16x16x128_f8f6f4 v[140:143], v[0:7], v[208:215], v[140:143]
	v_mfma_f32_16x16x128_f8f6f4 v[132:135], v[8:15], v[208:215], v[132:135]
	v_mfma_f32_16x16x128_f8f6f4 v[124:127], v[0:7], v[216:223], v[124:127]
	v_mfma_f32_16x16x128_f8f6f4 v[116:119], v[8:15], v[216:223], v[116:119]
	v_mfma_f32_16x16x128_f8f6f4 v[108:111], v[0:7], v[224:231], v[108:111]
	v_mfma_f32_16x16x128_f8f6f4 v[100:103], v[8:15], v[224:231], v[100:103]
	v_mfma_f32_16x16x128_f8f6f4 v[152:155], v[16:23], v[200:207], v[152:155]
	v_mfma_f32_16x16x128_f8f6f4 v[148:151], v[24:31], v[200:207], v[148:151]
	v_mfma_f32_16x16x128_f8f6f4 v[136:139], v[16:23], v[208:215], v[136:139]
	v_mfma_f32_16x16x128_f8f6f4 v[128:131], v[24:31], v[208:215], v[128:131]
	v_mfma_f32_16x16x128_f8f6f4 v[120:123], v[16:23], v[216:223], v[120:123]
	v_mfma_f32_16x16x128_f8f6f4 v[112:115], v[24:31], v[216:223], v[112:115]
	v_mfma_f32_16x16x128_f8f6f4 v[104:107], v[16:23], v[224:231], v[104:107]
	v_mfma_f32_16x16x128_f8f6f4 v[96:99], v[24:31], v[224:231], v[96:99]
	s_setprio 0
	s_barrier
	s_add_i32 s34, s60, s97
	v_lshl_add_u64 v[182:183], v[182:183], 0, s[14:15]
	s_mov_b32 m0, s34
	ds_read_b128 v[200:203], v196 offset:49152
	ds_read_b128 v[204:207], v196 offset:50176
	ds_read_b128 v[208:211], v196 offset:51200
	ds_read_b128 v[212:215], v196 offset:52224
	ds_read_b128 v[216:219], v196 offset:53248
	ds_read_b128 v[220:223], v196 offset:54272
	ds_read_b128 v[224:227], v196 offset:55296
	ds_read_b128 v[228:231], v196 offset:56320
	global_load_lds_dwordx4 v[182:183], off
	s_add_i32 m0, s34, 0x2000
	s_add_u32 s30, s30, 0x40080
	v_lshl_add_u64 v[182:183], v[184:185], 0, s[14:15]
	s_addc_u32 s31, s31, 0
	s_add_i32 s34, s61, s97
	global_load_lds_dwordx4 v[182:183], off
	v_lshl_add_u64 v[182:183], s[30:31], 0, v[162:163]
	s_mov_b32 m0, s34
	s_nop 0
	global_load_lds_dwordx4 v[182:183], off
	v_lshl_add_u64 v[182:183], s[30:31], 0, v[160:161]
	s_add_i32 m0, s34, 0x2000
	s_nop 0
	global_load_lds_dwordx4 v[182:183], off
	v_lshl_add_u64 v[182:183], v[186:187], 0, s[14:15]
	s_mov_b32 m0, s48
	s_nop 0
	global_load_lds_dwordx4 v[182:183], off
	v_lshl_add_u64 v[182:183], v[188:189], 0, s[14:15]
	s_mov_b32 m0, s49
	s_nop 0
	global_load_lds_dwordx4 v[182:183], off
	s_waitcnt vmcnt(8)
	s_waitcnt lgkmcnt(0)
	s_barrier
	s_setprio 1
	s_waitcnt lgkmcnt(0)
	v_mfma_f32_16x16x128_f8f6f4 v[92:95], v[0:7], v[200:207], v[92:95]
	v_mfma_f32_16x16x128_f8f6f4 v[84:87], v[8:15], v[200:207], v[84:87]
	v_mfma_f32_16x16x128_f8f6f4 v[76:79], v[0:7], v[208:215], v[76:79]
	v_mfma_f32_16x16x128_f8f6f4 v[68:71], v[8:15], v[208:215], v[68:71]
	v_mfma_f32_16x16x128_f8f6f4 v[60:63], v[0:7], v[216:223], v[60:63]
	v_mfma_f32_16x16x128_f8f6f4 v[52:55], v[8:15], v[216:223], v[52:55]
	v_mfma_f32_16x16x128_f8f6f4 v[44:47], v[0:7], v[224:231], v[44:47]
	v_mfma_f32_16x16x128_f8f6f4 v[36:39], v[8:15], v[224:231], v[36:39]
	v_mfma_f32_16x16x128_f8f6f4 v[88:91], v[16:23], v[200:207], v[88:91]
	v_mfma_f32_16x16x128_f8f6f4 v[80:83], v[24:31], v[200:207], v[80:83]
	v_mfma_f32_16x16x128_f8f6f4 v[72:75], v[16:23], v[208:215], v[72:75]
	v_mfma_f32_16x16x128_f8f6f4 v[64:67], v[24:31], v[208:215], v[64:67]
	v_mfma_f32_16x16x128_f8f6f4 v[56:59], v[16:23], v[216:223], v[56:59]
	v_mfma_f32_16x16x128_f8f6f4 v[48:51], v[24:31], v[216:223], v[48:51]
	v_mfma_f32_16x16x128_f8f6f4 v[40:43], v[16:23], v[224:231], v[40:43]
	v_mfma_f32_16x16x128_f8f6f4 v[32:35], v[24:31], v[224:231], v[32:35]
	s_setprio 0
	s_barrier
	s_add_i32 s59, s59, 2
	s_add_u32 s10, s10, 0x100
	s_addc_u32 s11, s11, 0
	s_add_u32 s56, s56, 0x100
	s_addc_u32 s58, s58, 0
	s_cmp_gt_u32 s59, 13
.LBB0_1248:
	ds_read_b128 v[24:27], v194
	ds_read_b128 v[28:31], v194 offset:1024
	ds_read_b128 v[16:19], v194 offset:2048
	ds_read_b128 v[20:23], v194 offset:3072
	ds_read_b128 v[8:11], v195
	ds_read_b128 v[12:15], v195 offset:1024
	ds_read_b128 v[0:3], v195 offset:2048
	ds_read_b128 v[4:7], v195 offset:3072
	s_add_u32 s30, s10, 0x80
	s_addc_u32 s31, s11, 0
	s_cmp_eq_u32 s59, 12
	s_cselect_b32 s35, s3, s31
	s_cselect_b32 s34, s54, s30
	s_cselect_b32 s31, s21, s58
	s_cselect_b32 s30, s55, s56
	v_lshl_add_u64 v[224:225], s[10:11], 0, v[178:179]
	s_add_i32 m0, s29, 0xc000
	ds_read_b128 v[182:185], v196
	ds_read_b128 v[186:189], v196 offset:1024
	ds_read_b128 v[200:203], v196 offset:2048
	ds_read_b128 v[204:207], v196 offset:3072
	ds_read_b128 v[208:211], v196 offset:4096
	ds_read_b128 v[212:215], v196 offset:5120
	ds_read_b128 v[216:219], v196 offset:6144
	ds_read_b128 v[220:223], v196 offset:7168
	global_load_lds_dwordx4 v[224:225], off
	v_lshl_add_u64 v[224:225], s[10:11], 0, v[176:177]
	s_add_i32 m0, s29, 0xe000
	s_nop 0
	global_load_lds_dwordx4 v[224:225], off
	s_waitcnt vmcnt(8)
	s_waitcnt lgkmcnt(0)
	s_barrier
	s_setprio 1
	s_waitcnt lgkmcnt(0)
	v_mfma_f32_16x16x128_f8f6f4 v[156:159], v[24:31], v[182:189], v[156:159]
	v_mfma_f32_16x16x128_f8f6f4 v[144:147], v[16:23], v[182:189], v[144:147]
	v_mfma_f32_16x16x128_f8f6f4 v[140:143], v[24:31], v[200:207], v[140:143]
	v_mfma_f32_16x16x128_f8f6f4 v[132:135], v[16:23], v[200:207], v[132:135]
	v_mfma_f32_16x16x128_f8f6f4 v[124:127], v[24:31], v[208:215], v[124:127]
	v_mfma_f32_16x16x128_f8f6f4 v[116:119], v[16:23], v[208:215], v[116:119]
	v_mfma_f32_16x16x128_f8f6f4 v[108:111], v[24:31], v[216:223], v[108:111]
	v_mfma_f32_16x16x128_f8f6f4 v[100:103], v[16:23], v[216:223], v[100:103]
	v_mfma_f32_16x16x128_f8f6f4 v[152:155], v[8:15], v[182:189], v[152:155]
	v_mfma_f32_16x16x128_f8f6f4 v[148:151], v[0:7], v[182:189], v[148:151]
	v_mfma_f32_16x16x128_f8f6f4 v[136:139], v[8:15], v[200:207], v[136:139]
	v_mfma_f32_16x16x128_f8f6f4 v[128:131], v[0:7], v[200:207], v[128:131]
	v_mfma_f32_16x16x128_f8f6f4 v[120:123], v[8:15], v[208:215], v[120:123]
	v_mfma_f32_16x16x128_f8f6f4 v[112:115], v[0:7], v[208:215], v[112:115]
	v_mfma_f32_16x16x128_f8f6f4 v[104:107], v[8:15], v[216:223], v[104:107]
	v_mfma_f32_16x16x128_f8f6f4 v[96:99], v[0:7], v[216:223], v[96:99]
	s_setprio 0
	s_barrier
; #define PG8_STAGE(bufoff, gbase, o0, o1) do { \
;         __builtin_amdgcn_global_load_lds((const unsigned*)((const char*)(gbase) + (o0)), (LAS unsigned*)(lds + (bufoff) + ldsw), 16, 0, 0); \
;         __builtin_amdgcn_global_load_lds((const unsigned*)((const char*)(gbase) + (o1)), (LAS unsigned*)(lds + (bufoff) + ldsw + 8192), 16, 0, 0); } while (0)
; #define PG8_LDA(dst, b, h) do { _Pragma("unroll") for (int m = 0; m < 4; ++m) _Pragma("unroll") for (int k = 0; k < 2; ++k) dst[m][k] = *(const LAS bf16x8*)(lds + PG8_SA(b, h) + aoff + m * 2048 + k * 1024); } while (0)
; #define PG8_LDB(dst, b, h) do { _Pragma("unroll") for (int n = 0; n < 2; ++n) _Pragma("unroll") for (int k = 0; k < 2; ++k) dst[n][k] = *(const LAS bf16x8*)(lds + PG8_SB(b, h) + boff + n * 2048 + k * 1024); } while (0)
; #define PG8_WAIT_V(n) asm volatile("s_waitcnt vmcnt(" #n ")" ::: "memory")
; #define PG8_WAIT_L(n) asm volatile("s_waitcnt lgkmcnt(" #n ")" ::: "memory")
; #define PG8_BAR __builtin_amdgcn_s_barrier()
; #define PG8_SCHED __builtin_amdgcn_sched_barrier(0)
; template <class Epi, class Sched, class Prob>
; __device__ __forceinline__ void gemm_phase(LAS unsigned char* lds, LAS unsigned char* lds_epi, const Prob g, const Sched& S, const Epi& E, int wid) {
;     ...
;             PG8_LDA(At, 0, 1); PG8_STAGE(PG8_SB(0, 0), b2, vB0, vB1); PG8_STAGE(PG8_SB(0, 1), b2 + hstepB, vB0, vB1); PG8_STAGE(PG8_SA(0, 0), a2, cA00, cA01);
;             PG8_WAIT_V(8); PG8_WAIT_L(0); PG8_BAR; PG8_MMA(1, 0, At, B0); PG8_MMA(1, 1, At, B1); PG8_BAR; PG8_SCHED;
;             PG8_LDB(B0, 1, 0); PG8_LDB(B1, 1, 1); PG8_SCHED; PG8_LDA(At, 1, 0); PG8_STAGE(PG8_SA(0, 1), a2, cA10, cA11);
;             PG8_WAIT_V(8); PG8_WAIT_L(0); PG8_BAR; PG8_MMA(0, 0, At, B0); PG8_MMA(0, 1, At, B1); PG8_BAR; PG8_SCHED;
	s_add_i32 s60, s50, s97
	v_lshl_add_u64 v[182:183], s[30:31], 0, v[162:163]
	s_mov_b32 m0, s60
	ds_read_b128 v[200:203], v196 offset:16384
	ds_read_b128 v[204:207], v196 offset:17408
	ds_read_b128 v[208:211], v196 offset:18432
	ds_read_b128 v[212:215], v196 offset:19456
	ds_read_b128 v[216:219], v196 offset:20480
	ds_read_b128 v[220:223], v196 offset:21504
	ds_read_b128 v[224:227], v196 offset:22528
	ds_read_b128 v[228:231], v196 offset:23552
	global_load_lds_dwordx4 v[182:183], off
	s_add_i32 m0, s60, 0x2000
	s_add_u32 s60, s30, 0x40000
	v_lshl_add_u64 v[184:185], s[30:31], 0, v[160:161]
	s_addc_u32 s61, s31, 0
	s_add_i32 s62, s51, s97
	global_load_lds_dwordx4 v[184:185], off
	v_lshl_add_u64 v[186:187], s[60:61], 0, v[162:163]
	s_mov_b32 m0, s62
	v_lshl_add_u64 v[188:189], s[34:35], 0, v[168:169]
	global_load_lds_dwordx4 v[186:187], off
	v_lshl_add_u64 v[186:187], s[60:61], 0, v[160:161]
	s_add_i32 m0, s62, 0x2000
	s_nop 0
	global_load_lds_dwordx4 v[186:187], off
	v_lshl_add_u64 v[186:187], s[34:35], 0, v[164:165]
	s_mov_b32 m0, s29
	s_nop 0
	global_load_lds_dwordx4 v[186:187], off
	s_mov_b32 m0, s43
	s_nop 0
	global_load_lds_dwordx4 v[188:189], off
	s_waitcnt vmcnt(8)
	s_waitcnt lgkmcnt(0)
	s_barrier
	s_setprio 1
	s_waitcnt lgkmcnt(0)
	v_mfma_f32_16x16x128_f8f6f4 v[92:95], v[24:31], v[200:207], v[92:95]
	v_mfma_f32_16x16x128_f8f6f4 v[84:87], v[16:23], v[200:207], v[84:87]
	v_mfma_f32_16x16x128_f8f6f4 v[76:79], v[24:31], v[208:215], v[76:79]
	v_mfma_f32_16x16x128_f8f6f4 v[68:71], v[16:23], v[208:215], v[68:71]
	v_mfma_f32_16x16x128_f8f6f4 v[60:63], v[24:31], v[216:223], v[60:63]
	v_mfma_f32_16x16x128_f8f6f4 v[52:55], v[16:23], v[216:223], v[52:55]
	v_mfma_f32_16x16x128_f8f6f4 v[44:47], v[24:31], v[224:231], v[44:47]
	v_mfma_f32_16x16x128_f8f6f4 v[36:39], v[16:23], v[224:231], v[36:39]
	v_mfma_f32_16x16x128_f8f6f4 v[88:91], v[8:15], v[200:207], v[88:91]
	v_mfma_f32_16x16x128_f8f6f4 v[80:83], v[0:7], v[200:207], v[80:83]
	v_mfma_f32_16x16x128_f8f6f4 v[72:75], v[8:15], v[208:215], v[72:75]
	v_mfma_f32_16x16x128_f8f6f4 v[64:67], v[0:7], v[208:215], v[64:67]
	v_mfma_f32_16x16x128_f8f6f4 v[56:59], v[8:15], v[216:223], v[56:59]
	v_mfma_f32_16x16x128_f8f6f4 v[48:51], v[0:7], v[216:223], v[48:51]
	v_mfma_f32_16x16x128_f8f6f4 v[40:43], v[8:15], v[224:231], v[40:43]
	v_mfma_f32_16x16x128_f8f6f4 v[32:35], v[0:7], v[224:231], v[32:35]
	s_setprio 0
	s_barrier
	s_add_i32 s60, 0, 0x18000
	s_add_i32 s61, 0, 0x1c000
	v_add_u32_e32 v12, s60, v191
	v_add_u32_e32 v28, s61, v191
	ds_read_b128 v[0:3], v12
	ds_read_b128 v[4:7], v12 offset:1024
	ds_read_b128 v[8:11], v12 offset:2048
	ds_read_b128 v[12:15], v12 offset:3072
	ds_read_b128 v[16:19], v28
	ds_read_b128 v[20:23], v28 offset:1024
	ds_read_b128 v[24:27], v28 offset:2048
	ds_read_b128 v[28:31], v28 offset:3072
	s_mov_b32 m0, s44
	v_lshl_add_u64 v[232:233], s[34:35], 0, v[166:167]
	ds_read_b128 v[200:203], v196 offset:32768
	ds_read_b128 v[204:207], v196 offset:33792
	ds_read_b128 v[208:211], v196 offset:34816
	ds_read_b128 v[212:215], v196 offset:35840
	ds_read_b128 v[216:219], v196 offset:36864
	ds_read_b128 v[220:223], v196 offset:37888
	ds_read_b128 v[224:227], v196 offset:38912
	ds_read_b128 v[228:231], v196 offset:39936
	global_load_lds_dwordx4 v[232:233], off
	v_lshl_add_u64 v[232:233], s[34:35], 0, v[170:171]
	s_mov_b32 m0, s45
	s_nop 0
	global_load_lds_dwordx4 v[232:233], off
	s_waitcnt vmcnt(8)
	s_waitcnt lgkmcnt(0)
	s_barrier
; #define PG8_STAGE(bufoff, gbase, o0, o1) do { \
;         __builtin_amdgcn_global_load_lds((const unsigned*)((const char*)(gbase) + (o0)), (LAS unsigned*)(lds + (bufoff) + ldsw), 16, 0, 0); \
;         __builtin_amdgcn_global_load_lds((const unsigned*)((const char*)(gbase) + (o1)), (LAS unsigned*)(lds + (bufoff) + ldsw + 8192), 16, 0, 0); } while (0)
; #define PG8_LDA(dst, b, h) do { _Pragma("unroll") for (int m = 0; m < 4; ++m) _Pragma("unroll") for (int k = 0; k < 2; ++k) dst[m][k] = *(const LAS bf16x8*)(lds + PG8_SA(b, h) + aoff + m * 2048 + k * 1024); } while (0)
; #define PG8_LDB(dst, b, h) do { _Pragma("unroll") for (int n = 0; n < 2; ++n) _Pragma("unroll") for (int k = 0; k < 2; ++k) dst[n][k] = *(const LAS bf16x8*)(lds + PG8_SB(b, h) + boff + n * 2048 + k * 1024); } while (0)
; #define PG8_WAIT_V(n) asm volatile("s_waitcnt vmcnt(" #n ")" ::: "memory")
; #define PG8_WAIT_L(n) asm volatile("s_waitcnt lgkmcnt(" #n ")" ::: "memory")
; #define PG8_BAR __builtin_amdgcn_s_barrier()
; #define PG8_SCHED __builtin_amdgcn_sched_barrier(0)
; template <class Epi, class Sched, class Prob>
; __device__ __forceinline__ void gemm_phase(LAS unsigned char* lds, LAS unsigned char* lds_epi, const Prob g, const Sched& S, const Epi& E, int wid) {
;     ...
;             PG8_LDB(B0, 1, 0); PG8_LDB(B1, 1, 1); PG8_SCHED; PG8_LDA(At, 1, 0); PG8_STAGE(PG8_SA(0, 1), a2, cA10, cA11);
;             PG8_WAIT_V(8); PG8_WAIT_L(0); PG8_BAR; PG8_MMA(0, 0, At, B0); PG8_MMA(0, 1, At, B1); PG8_BAR; PG8_SCHED;
;             PG8_LDA(At, 1, 1); PG8_STAGE(PG8_SB(1, 0), b3, vB0, vB1); PG8_STAGE(PG8_SB(1, 1), b3 + hstepB, vB0, vB1); PG8_STAGE(PG8_SA(1, 0), a3, cA00, cA01);
;             PG8_WAIT_V(8); PG8_WAIT_L(0); PG8_BAR; PG8_MMA(1, 0, At, B0); PG8_MMA(1, 1, At, B1); PG8_BAR; PG8_SCHED;
;         }
;         if constexpr (Prob::FP8) asm volatile("s_nop 7\n\ts_nop 7\n\ts_nop 7" ::: "memory");
;         if (wr == 0) PG8_BAR;
	s_setprio 1
	s_waitcnt lgkmcnt(0)
	v_mfma_f32_16x16x128_f8f6f4 v[156:159], v[0:7], v[200:207], v[156:159]
	v_mfma_f32_16x16x128_f8f6f4 v[144:147], v[8:15], v[200:207], v[144:147]
	v_mfma_f32_16x16x128_f8f6f4 v[140:143], v[0:7], v[208:215], v[140:143]
	v_mfma_f32_16x16x128_f8f6f4 v[132:135], v[8:15], v[208:215], v[132:135]
	v_mfma_f32_16x16x128_f8f6f4 v[124:127], v[0:7], v[216:223], v[124:127]
	v_mfma_f32_16x16x128_f8f6f4 v[116:119], v[8:15], v[216:223], v[116:119]
	v_mfma_f32_16x16x128_f8f6f4 v[108:111], v[0:7], v[224:231], v[108:111]
	v_mfma_f32_16x16x128_f8f6f4 v[100:103], v[8:15], v[224:231], v[100:103]
	v_mfma_f32_16x16x128_f8f6f4 v[152:155], v[16:23], v[200:207], v[152:155]
	v_mfma_f32_16x16x128_f8f6f4 v[148:151], v[24:31], v[200:207], v[148:151]
	v_mfma_f32_16x16x128_f8f6f4 v[136:139], v[16:23], v[208:215], v[136:139]
	v_mfma_f32_16x16x128_f8f6f4 v[128:131], v[24:31], v[208:215], v[128:131]
	v_mfma_f32_16x16x128_f8f6f4 v[120:123], v[16:23], v[216:223], v[120:123]
	v_mfma_f32_16x16x128_f8f6f4 v[112:115], v[24:31], v[216:223], v[112:115]
	v_mfma_f32_16x16x128_f8f6f4 v[104:107], v[16:23], v[224:231], v[104:107]
	v_mfma_f32_16x16x128_f8f6f4 v[96:99], v[24:31], v[224:231], v[96:99]
	s_setprio 0
	s_barrier
	s_add_i32 s34, s60, s97
	v_lshl_add_u64 v[182:183], v[182:183], 0, s[14:15]
	s_mov_b32 m0, s34
	ds_read_b128 v[200:203], v196 offset:49152
	ds_read_b128 v[204:207], v196 offset:50176
	ds_read_b128 v[208:211], v196 offset:51200
	ds_read_b128 v[212:215], v196 offset:52224
	ds_read_b128 v[216:219], v196 offset:53248
	ds_read_b128 v[220:223], v196 offset:54272
	ds_read_b128 v[224:227], v196 offset:55296
	ds_read_b128 v[228:231], v196 offset:56320
	global_load_lds_dwordx4 v[182:183], off
	s_add_i32 m0, s34, 0x2000
	s_add_u32 s30, s30, 0x40080
	v_lshl_add_u64 v[182:183], v[184:185], 0, s[14:15]
	s_addc_u32 s31, s31, 0
	s_add_i32 s34, s61, s97
	global_load_lds_dwordx4 v[182:183], off
	v_lshl_add_u64 v[182:183], s[30:31], 0, v[162:163]
	s_mov_b32 m0, s34
	s_nop 0
	global_load_lds_dwordx4 v[182:183], off
	v_lshl_add_u64 v[182:183], s[30:31], 0, v[160:161]
	s_add_i32 m0, s34, 0x2000
	s_nop 0
	global_load_lds_dwordx4 v[182:183], off
	v_lshl_add_u64 v[182:183], v[186:187], 0, s[14:15]
	s_mov_b32 m0, s48
	s_nop 0
	global_load_lds_dwordx4 v[182:183], off
	v_lshl_add_u64 v[182:183], v[188:189], 0, s[14:15]
	s_mov_b32 m0, s49
	s_nop 0
	global_load_lds_dwordx4 v[182:183], off
	s_waitcnt vmcnt(8)
	s_waitcnt lgkmcnt(0)
	s_barrier
	s_setprio 1
	s_waitcnt lgkmcnt(0)
	v_mfma_f32_16x16x128_f8f6f4 v[92:95], v[0:7], v[200:207], v[92:95]
	v_mfma_f32_16x16x128_f8f6f4 v[84:87], v[8:15], v[200:207], v[84:87]
	v_mfma_f32_16x16x128_f8f6f4 v[76:79], v[0:7], v[208:215], v[76:79]
	v_mfma_f32_16x16x128_f8f6f4 v[68:71], v[8:15], v[208:215], v[68:71]
	v_mfma_f32_16x16x128_f8f6f4 v[60:63], v[0:7], v[216:223], v[60:63]
	v_mfma_f32_16x16x128_f8f6f4 v[52:55], v[8:15], v[216:223], v[52:55]
	v_mfma_f32_16x16x128_f8f6f4 v[44:47], v[0:7], v[224:231], v[44:47]
	v_mfma_f32_16x16x128_f8f6f4 v[36:39], v[8:15], v[224:231], v[36:39]
	v_mfma_f32_16x16x128_f8f6f4 v[88:91], v[16:23], v[200:207], v[88:91]
	v_mfma_f32_16x16x128_f8f6f4 v[80:83], v[24:31], v[200:207], v[80:83]
	v_mfma_f32_16x16x128_f8f6f4 v[72:75], v[16:23], v[208:215], v[72:75]
	v_mfma_f32_16x16x128_f8f6f4 v[64:67], v[24:31], v[208:215], v[64:67]
	v_mfma_f32_16x16x128_f8f6f4 v[56:59], v[16:23], v[216:223], v[56:59]
	v_mfma_f32_16x16x128_f8f6f4 v[48:51], v[24:31], v[216:223], v[48:51]
	v_mfma_f32_16x16x128_f8f6f4 v[40:43], v[16:23], v[224:231], v[40:43]
	v_mfma_f32_16x16x128_f8f6f4 v[32:35], v[24:31], v[224:231], v[32:35]
	s_setprio 0
	s_barrier
	s_add_i32 s59, s59, 2
	s_add_u32 s10, s10, 0x100
	s_addc_u32 s11, s11, 0
	s_add_u32 s56, s56, 0x100
	s_addc_u32 s58, s58, 0
	s_cmp_gt_u32 s59, 13
	s_cbranch_scc0 .LBB0_1248
	v_readlane_b32 s10, v254, 27
	v_readlane_b32 s11, v254, 28
	s_and_b64 vcc, exec, s[10:11]
	s_cbranch_vccz .LBB0_1251
	s_barrier

; #define PG8_STAGE(bufoff, gbase, o0, o1) do { \
;         __builtin_amdgcn_global_load_lds((const unsigned*)((const char*)(gbase) + (o0)), (LAS unsigned*)(lds + (bufoff) + ldsw), 16, 0, 0); \
;         __builtin_amdgcn_global_load_lds((const unsigned*)((const char*)(gbase) + (o1)), (LAS unsigned*)(lds + (bufoff) + ldsw + 8192), 16, 0, 0); } while (0)
; #define PG8_LDA(dst, b, h) do { _Pragma("unroll") for (int m = 0; m < 4; ++m) _Pragma("unroll") for (int k = 0; k < 2; ++k) dst[m][k] = *(const LAS bf16x8*)(lds + PG8_SA(b, h) + aoff + m * 2048 + k * 1024); } while (0)
; #define PG8_LDB(dst, b, h) do { _Pragma("unroll") for (int n = 0; n < 2; ++n) _Pragma("unroll") for (int k = 0; k < 2; ++k) dst[n][k] = *(const LAS bf16x8*)(lds + PG8_SB(b, h) + boff + n * 2048 + k * 1024); } while (0)
; #define PG8_WAIT_V(n) asm volatile("s_waitcnt vmcnt(" #n ")" ::: "memory")
; #define PG8_WAIT_L(n) asm volatile("s_waitcnt lgkmcnt(" #n ")" ::: "memory")
; #define PG8_BAR __builtin_amdgcn_s_barrier()
; #define PG8_SCHED __builtin_amdgcn_sched_barrier(0)
; template <class Epi, class Sched, class Prob>
; __device__ __forceinline__ void gemm_phase(LAS unsigned char* lds, LAS unsigned char* lds_epi, const Prob g, const Sched& S, const Epi& E, int wid) {
;     ...
;             PG8_LDB(B0, 0, 0); PG8_LDB(B1, 0, 1); PG8_SCHED; PG8_LDA(At, 0, 0); PG8_STAGE(PG8_SA(1, 1), a1, cA10, cA11);
;             PG8_WAIT_V(8); PG8_WAIT_L(0); PG8_BAR; PG8_MMA(0, 0, At, B0); PG8_MMA(0, 1, At, B1); PG8_BAR; PG8_SCHED;
;             PG8_LDA(At, 0, 1); PG8_STAGE(PG8_SB(0, 0), b2, vB0, vB1); PG8_STAGE(PG8_SB(0, 1), b2 + hstepB, vB0, vB1); PG8_STAGE(PG8_SA(0, 0), a2, cA00, cA01);
;             PG8_WAIT_V(8); PG8_WAIT_L(0); PG8_BAR; PG8_MMA(1, 0, At, B0); PG8_MMA(1, 1, At, B1); PG8_BAR; PG8_SCHED;
.LBB0_1336:
	v_add_u32_e32 v146, s55, v149
	ds_read_b128 v[156:159], v146
	ds_read_b128 v[160:163], v146 offset:1024
	ds_read_b128 v[164:167], v146 offset:2048
	ds_read_b128 v[168:171], v146 offset:3072
	v_add_u32_e32 v146, s56, v149
	ds_read_b128 v[172:175], v146
	ds_read_b128 v[176:179], v146 offset:1024
	ds_read_b128 v[180:183], v146 offset:2048
	ds_read_b128 v[184:187], v146 offset:3072
	s_add_u32 s30, s28, 0x80
	s_addc_u32 s31, s29, 0
	s_cmpk_eq_i32 s62, 0x6c
	s_cselect_b32 s35, s25, s31
	s_cselect_b32 s34, s24, s30
	s_cselect_b32 s31, s27, s61
	s_cselect_b32 s30, s26, s60
	v_lshl_add_u64 v[146:147], s[28:29], 0, v[140:141]
	s_add_i32 m0, s47, 0xc000
	ds_read_b128 v[188:191], v153
	ds_read_b128 v[192:195], v153 offset:1024
	ds_read_b128 v[196:199], v153 offset:2048
	ds_read_b128 v[200:203], v153 offset:3072
	ds_read_b128 v[204:207], v153 offset:4096
	ds_read_b128 v[208:211], v153 offset:5120
	ds_read_b128 v[212:215], v153 offset:6144
	ds_read_b128 v[216:219], v153 offset:7168
	global_load_lds_dwordx4 v[146:147], off
	v_lshl_add_u64 v[146:147], s[28:29], 0, v[142:143]
	s_add_i32 m0, s47, 0xe000
	s_nop 0
	global_load_lds_dwordx4 v[146:147], off
	s_waitcnt vmcnt(8)
	s_waitcnt lgkmcnt(0)
	s_barrier
	s_setprio 1
	s_waitcnt lgkmcnt(0)
	v_mfma_f32_16x16x32_bf16 v[120:123], v[156:159], v[188:191], v[120:123]
	v_mfma_f32_16x16x32_bf16 v[112:115], v[164:167], v[188:191], v[112:115]
	v_mfma_f32_16x16x32_bf16 v[104:107], v[156:159], v[196:199], v[104:107]
	v_mfma_f32_16x16x32_bf16 v[96:99], v[164:167], v[196:199], v[96:99]
	v_mfma_f32_16x16x32_bf16 v[88:91], v[156:159], v[204:207], v[88:91]
	v_mfma_f32_16x16x32_bf16 v[80:83], v[164:167], v[204:207], v[80:83]
	v_mfma_f32_16x16x32_bf16 v[72:75], v[156:159], v[212:215], v[72:75]
	v_mfma_f32_16x16x32_bf16 v[64:67], v[164:167], v[212:215], v[64:67]
	v_mfma_f32_16x16x32_bf16 v[120:123], v[160:163], v[192:195], v[120:123]
	v_mfma_f32_16x16x32_bf16 v[112:115], v[168:171], v[192:195], v[112:115]
	v_mfma_f32_16x16x32_bf16 v[104:107], v[160:163], v[200:203], v[104:107]
	v_mfma_f32_16x16x32_bf16 v[96:99], v[168:171], v[200:203], v[96:99]
	v_mfma_f32_16x16x32_bf16 v[88:91], v[160:163], v[208:211], v[88:91]
	v_mfma_f32_16x16x32_bf16 v[80:83], v[168:171], v[208:211], v[80:83]
	v_mfma_f32_16x16x32_bf16 v[72:75], v[160:163], v[216:219], v[72:75]
	v_mfma_f32_16x16x32_bf16 v[64:67], v[168:171], v[216:219], v[64:67]
	v_mfma_f32_16x16x32_bf16 v[124:127], v[172:175], v[188:191], v[124:127]
	v_mfma_f32_16x16x32_bf16 v[116:119], v[180:183], v[188:191], v[116:119]
	v_mfma_f32_16x16x32_bf16 v[108:111], v[172:175], v[196:199], v[108:111]
	v_mfma_f32_16x16x32_bf16 v[100:103], v[180:183], v[196:199], v[100:103]
	v_mfma_f32_16x16x32_bf16 v[92:95], v[172:175], v[204:207], v[92:95]
	v_mfma_f32_16x16x32_bf16 v[84:87], v[180:183], v[204:207], v[84:87]
	v_mfma_f32_16x16x32_bf16 v[76:79], v[172:175], v[212:215], v[76:79]
	v_mfma_f32_16x16x32_bf16 v[68:71], v[180:183], v[212:215], v[68:71]
	v_mfma_f32_16x16x32_bf16 v[124:127], v[176:179], v[192:195], v[124:127]
	v_mfma_f32_16x16x32_bf16 v[116:119], v[184:187], v[192:195], v[116:119]
	v_mfma_f32_16x16x32_bf16 v[108:111], v[176:179], v[200:203], v[108:111]
	v_mfma_f32_16x16x32_bf16 v[100:103], v[184:187], v[200:203], v[100:103]
	v_mfma_f32_16x16x32_bf16 v[92:95], v[176:179], v[208:211], v[92:95]
	v_mfma_f32_16x16x32_bf16 v[84:87], v[184:187], v[208:211], v[84:87]
	v_mfma_f32_16x16x32_bf16 v[76:79], v[176:179], v[216:219], v[76:79]
	v_mfma_f32_16x16x32_bf16 v[68:71], v[184:187], v[216:219], v[68:71]
	s_setprio 0
	s_barrier
	s_add_i32 s63, s55, s97
	v_lshl_add_u64 v[146:147], s[30:31], 0, v[130:131]
	s_mov_b32 m0, s63
	ds_read_b128 v[188:191], v153 offset:16384
	ds_read_b128 v[192:195], v153 offset:17408
	ds_read_b128 v[196:199], v153 offset:18432
	ds_read_b128 v[200:203], v153 offset:19456
	ds_read_b128 v[204:207], v153 offset:20480
	ds_read_b128 v[208:211], v153 offset:21504
	ds_read_b128 v[212:215], v153 offset:22528
	ds_read_b128 v[216:219], v153 offset:23552
	global_load_lds_dwordx4 v[146:147], off
	s_add_i32 m0, s63, 0x2000
	s_add_u32 s64, s30, 0x1c0000
	v_lshl_add_u64 v[220:221], s[30:31], 0, v[128:129]
	s_addc_u32 s65, s31, 0
	s_add_i32 s63, s56, s97
	global_load_lds_dwordx4 v[220:221], off
	v_lshl_add_u64 v[222:223], s[64:65], 0, v[130:131]
	s_mov_b32 m0, s63
	v_lshl_add_u64 v[224:225], s[34:35], 0, v[128:129]
	global_load_lds_dwordx4 v[222:223], off
	v_lshl_add_u64 v[222:223], s[64:65], 0, v[128:129]
	s_add_i32 m0, s63, 0x2000
	s_nop 0
	global_load_lds_dwordx4 v[222:223], off
	v_lshl_add_u64 v[222:223], s[34:35], 0, v[130:131]
	s_mov_b32 m0, s47
	s_nop 0
	global_load_lds_dwordx4 v[222:223], off
	s_mov_b32 m0, s48
	s_nop 0
	global_load_lds_dwordx4 v[224:225], off
	s_waitcnt vmcnt(8)
	s_waitcnt lgkmcnt(0)
	s_barrier
; #define PG8_STAGE(bufoff, gbase, o0, o1) do { \
;         __builtin_amdgcn_global_load_lds((const unsigned*)((const char*)(gbase) + (o0)), (LAS unsigned*)(lds + (bufoff) + ldsw), 16, 0, 0); \
;         __builtin_amdgcn_global_load_lds((const unsigned*)((const char*)(gbase) + (o1)), (LAS unsigned*)(lds + (bufoff) + ldsw + 8192), 16, 0, 0); } while (0)
; #define PG8_LDA(dst, b, h) do { _Pragma("unroll") for (int m = 0; m < 4; ++m) _Pragma("unroll") for (int k = 0; k < 2; ++k) dst[m][k] = *(const LAS bf16x8*)(lds + PG8_SA(b, h) + aoff + m * 2048 + k * 1024); } while (0)
; #define PG8_LDB(dst, b, h) do { _Pragma("unroll") for (int n = 0; n < 2; ++n) _Pragma("unroll") for (int k = 0; k < 2; ++k) dst[n][k] = *(const LAS bf16x8*)(lds + PG8_SB(b, h) + boff + n * 2048 + k * 1024); } while (0)
; #define PG8_WAIT_V(n) asm volatile("s_waitcnt vmcnt(" #n ")" ::: "memory")
; #define PG8_WAIT_L(n) asm volatile("s_waitcnt lgkmcnt(" #n ")" ::: "memory")
; #define PG8_BAR __builtin_amdgcn_s_barrier()
; #define PG8_SCHED __builtin_amdgcn_sched_barrier(0)
; template <class Epi, class Sched, class Prob>
; __device__ __forceinline__ void gemm_phase(LAS unsigned char* lds, LAS unsigned char* lds_epi, const Prob g, const Sched& S, const Epi& E, int wid) {
;     ...
;             PG8_WAIT_V(8); PG8_WAIT_L(0); PG8_BAR; PG8_MMA(1, 0, At, B0); PG8_MMA(1, 1, At, B1); PG8_BAR; PG8_SCHED;
;             PG8_LDB(B0, 1, 0); PG8_LDB(B1, 1, 1); PG8_SCHED; PG8_LDA(At, 1, 0); PG8_STAGE(PG8_SA(0, 1), a2, cA10, cA11);
;             PG8_WAIT_V(8); PG8_WAIT_L(0); PG8_BAR; PG8_MMA(0, 0, At, B0); PG8_MMA(0, 1, At, B1); PG8_BAR; PG8_SCHED;
	s_setprio 1
	s_waitcnt lgkmcnt(0)
	v_mfma_f32_16x16x32_bf16 v[56:59], v[156:159], v[188:191], v[56:59]
	v_mfma_f32_16x16x32_bf16 v[48:51], v[164:167], v[188:191], v[48:51]
	v_mfma_f32_16x16x32_bf16 v[40:43], v[156:159], v[196:199], v[40:43]
	v_mfma_f32_16x16x32_bf16 v[32:35], v[164:167], v[196:199], v[32:35]
	v_mfma_f32_16x16x32_bf16 v[20:23], v[156:159], v[204:207], v[20:23]
	v_mfma_f32_16x16x32_bf16 v[8:11], v[164:167], v[204:207], v[8:11]
	v_mfma_f32_16x16x32_bf16 v[4:7], v[156:159], v[212:215], v[4:7]
	v_mfma_f32_16x16x32_bf16 v[0:3], v[164:167], v[212:215], v[0:3]
	v_mfma_f32_16x16x32_bf16 v[56:59], v[160:163], v[192:195], v[56:59]
	v_mfma_f32_16x16x32_bf16 v[48:51], v[168:171], v[192:195], v[48:51]
	v_mfma_f32_16x16x32_bf16 v[40:43], v[160:163], v[200:203], v[40:43]
	v_mfma_f32_16x16x32_bf16 v[32:35], v[168:171], v[200:203], v[32:35]
	v_mfma_f32_16x16x32_bf16 v[20:23], v[160:163], v[208:211], v[20:23]
	v_mfma_f32_16x16x32_bf16 v[8:11], v[168:171], v[208:211], v[8:11]
	v_mfma_f32_16x16x32_bf16 v[4:7], v[160:163], v[216:219], v[4:7]
	v_mfma_f32_16x16x32_bf16 v[0:3], v[168:171], v[216:219], v[0:3]
	v_mfma_f32_16x16x32_bf16 v[60:63], v[172:175], v[188:191], v[60:63]
	v_mfma_f32_16x16x32_bf16 v[52:55], v[180:183], v[188:191], v[52:55]
	v_mfma_f32_16x16x32_bf16 v[44:47], v[172:175], v[196:199], v[44:47]
	v_mfma_f32_16x16x32_bf16 v[36:39], v[180:183], v[196:199], v[36:39]
	v_mfma_f32_16x16x32_bf16 v[28:31], v[172:175], v[204:207], v[28:31]
	v_mfma_f32_16x16x32_bf16 v[16:19], v[180:183], v[204:207], v[16:19]
	v_mfma_f32_16x16x32_bf16 v[24:27], v[172:175], v[212:215], v[24:27]
	v_mfma_f32_16x16x32_bf16 v[12:15], v[180:183], v[212:215], v[12:15]
	v_mfma_f32_16x16x32_bf16 v[60:63], v[176:179], v[192:195], v[60:63]
	v_mfma_f32_16x16x32_bf16 v[52:55], v[184:187], v[192:195], v[52:55]
	v_mfma_f32_16x16x32_bf16 v[44:47], v[176:179], v[200:203], v[44:47]
	v_mfma_f32_16x16x32_bf16 v[36:39], v[184:187], v[200:203], v[36:39]
	v_mfma_f32_16x16x32_bf16 v[28:31], v[176:179], v[208:211], v[28:31]
	v_mfma_f32_16x16x32_bf16 v[16:19], v[184:187], v[208:211], v[16:19]
	v_mfma_f32_16x16x32_bf16 v[24:27], v[176:179], v[216:219], v[24:27]
	v_mfma_f32_16x16x32_bf16 v[12:15], v[184:187], v[216:219], v[12:15]
	s_setprio 0
	s_barrier
	s_add_i32 s63, 0, 0x18000
	s_add_i32 s64, 0, 0x1c000
	v_add_u32_e32 v168, s63, v149
	v_add_u32_e32 v184, s64, v149
	ds_read_b128 v[156:159], v168
	ds_read_b128 v[160:163], v168 offset:1024
	ds_read_b128 v[164:167], v168 offset:2048
	ds_read_b128 v[168:171], v168 offset:3072
	ds_read_b128 v[172:175], v184
	ds_read_b128 v[176:179], v184 offset:1024
	ds_read_b128 v[180:183], v184 offset:2048
	ds_read_b128 v[184:187], v184 offset:3072
	s_mov_b32 m0, s49
	v_lshl_add_u64 v[226:227], s[34:35], 0, v[132:133]
	ds_read_b128 v[188:191], v153 offset:32768
	ds_read_b128 v[192:195], v153 offset:33792
	ds_read_b128 v[196:199], v153 offset:34816
	ds_read_b128 v[200:203], v153 offset:35840
	ds_read_b128 v[204:207], v153 offset:36864
	ds_read_b128 v[208:211], v153 offset:37888
	ds_read_b128 v[212:215], v153 offset:38912
	ds_read_b128 v[216:219], v153 offset:39936
	global_load_lds_dwordx4 v[226:227], off
	v_lshl_add_u64 v[226:227], s[34:35], 0, v[134:135]
	s_mov_b32 m0, s50
	s_nop 0
	global_load_lds_dwordx4 v[226:227], off
	s_waitcnt vmcnt(8)
	s_waitcnt lgkmcnt(0)
	s_barrier
	s_setprio 1
	s_waitcnt lgkmcnt(0)
	v_mfma_f32_16x16x32_bf16 v[120:123], v[156:159], v[188:191], v[120:123]
	v_mfma_f32_16x16x32_bf16 v[112:115], v[164:167], v[188:191], v[112:115]
	v_mfma_f32_16x16x32_bf16 v[104:107], v[156:159], v[196:199], v[104:107]
	v_mfma_f32_16x16x32_bf16 v[96:99], v[164:167], v[196:199], v[96:99]
	v_mfma_f32_16x16x32_bf16 v[88:91], v[156:159], v[204:207], v[88:91]
	v_mfma_f32_16x16x32_bf16 v[80:83], v[164:167], v[204:207], v[80:83]
	v_mfma_f32_16x16x32_bf16 v[72:75], v[156:159], v[212:215], v[72:75]
	v_mfma_f32_16x16x32_bf16 v[64:67], v[164:167], v[212:215], v[64:67]
	v_mfma_f32_16x16x32_bf16 v[120:123], v[160:163], v[192:195], v[120:123]
	v_mfma_f32_16x16x32_bf16 v[112:115], v[168:171], v[192:195], v[112:115]
	v_mfma_f32_16x16x32_bf16 v[104:107], v[160:163], v[200:203], v[104:107]
	v_mfma_f32_16x16x32_bf16 v[96:99], v[168:171], v[200:203], v[96:99]
	v_mfma_f32_16x16x32_bf16 v[88:91], v[160:163], v[208:211], v[88:91]
	v_mfma_f32_16x16x32_bf16 v[80:83], v[168:171], v[208:211], v[80:83]
	v_mfma_f32_16x16x32_bf16 v[72:75], v[160:163], v[216:219], v[72:75]
	v_mfma_f32_16x16x32_bf16 v[64:67], v[168:171], v[216:219], v[64:67]
	v_mfma_f32_16x16x32_bf16 v[124:127], v[172:175], v[188:191], v[124:127]
	v_mfma_f32_16x16x32_bf16 v[116:119], v[180:183], v[188:191], v[116:119]
	v_mfma_f32_16x16x32_bf16 v[108:111], v[172:175], v[196:199], v[108:111]
	v_mfma_f32_16x16x32_bf16 v[100:103], v[180:183], v[196:199], v[100:103]
	v_mfma_f32_16x16x32_bf16 v[92:95], v[172:175], v[204:207], v[92:95]
	v_mfma_f32_16x16x32_bf16 v[84:87], v[180:183], v[204:207], v[84:87]
	v_mfma_f32_16x16x32_bf16 v[76:79], v[172:175], v[212:215], v[76:79]
	v_mfma_f32_16x16x32_bf16 v[68:71], v[180:183], v[212:215], v[68:71]
	v_mfma_f32_16x16x32_bf16 v[124:127], v[176:179], v[192:195], v[124:127]
	v_mfma_f32_16x16x32_bf16 v[116:119], v[184:187], v[192:195], v[116:119]
	v_mfma_f32_16x16x32_bf16 v[108:111], v[176:179], v[200:203], v[108:111]
	v_mfma_f32_16x16x32_bf16 v[100:103], v[184:187], v[200:203], v[100:103]
	v_mfma_f32_16x16x32_bf16 v[92:95], v[176:179], v[208:211], v[92:95]
	v_mfma_f32_16x16x32_bf16 v[84:87], v[184:187], v[208:211], v[84:87]
	v_mfma_f32_16x16x32_bf16 v[76:79], v[176:179], v[216:219], v[76:79]
	v_mfma_f32_16x16x32_bf16 v[68:71], v[184:187], v[216:219], v[68:71]
	s_setprio 0
	s_barrier
; #define PG8_STAGE(bufoff, gbase, o0, o1) do { \
;         __builtin_amdgcn_global_load_lds((const unsigned*)((const char*)(gbase) + (o0)), (LAS unsigned*)(lds + (bufoff) + ldsw), 16, 0, 0); \
;         __builtin_amdgcn_global_load_lds((const unsigned*)((const char*)(gbase) + (o1)), (LAS unsigned*)(lds + (bufoff) + ldsw + 8192), 16, 0, 0); } while (0)
; #define PG8_LDA(dst, b, h) do { _Pragma("unroll") for (int m = 0; m < 4; ++m) _Pragma("unroll") for (int k = 0; k < 2; ++k) dst[m][k] = *(const LAS bf16x8*)(lds + PG8_SA(b, h) + aoff + m * 2048 + k * 1024); } while (0)
; #define PG8_WAIT_V(n) asm volatile("s_waitcnt vmcnt(" #n ")" ::: "memory")
; #define PG8_WAIT_L(n) asm volatile("s_waitcnt lgkmcnt(" #n ")" ::: "memory")
; #define PG8_BAR __builtin_amdgcn_s_barrier()
; #define PG8_SCHED __builtin_amdgcn_sched_barrier(0)
; template <class Epi, class Sched, class Prob>
; __device__ __forceinline__ void gemm_phase(LAS unsigned char* lds, LAS unsigned char* lds_epi, const Prob g, const Sched& S, const Epi& E, int wid) {
;     ...
;             PG8_LDA(At, 1, 1); PG8_STAGE(PG8_SB(1, 0), b3, vB0, vB1); PG8_STAGE(PG8_SB(1, 1), b3 + hstepB, vB0, vB1); PG8_STAGE(PG8_SA(1, 0), a3, cA00, cA01);
;             PG8_WAIT_V(8); PG8_WAIT_L(0); PG8_BAR; PG8_MMA(1, 0, At, B0); PG8_MMA(1, 1, At, B1); PG8_BAR; PG8_SCHED;
;         }
;         if constexpr (Prob::FP8) asm volatile("s_nop 7\n\ts_nop 7\n\ts_nop 7" ::: "memory");
;         if (wr == 0) PG8_BAR;
	s_add_i32 s34, s63, s97
	v_lshl_add_u64 v[146:147], v[146:147], 0, s[16:17]
	s_mov_b32 m0, s34
	ds_read_b128 v[188:191], v153 offset:49152
	ds_read_b128 v[192:195], v153 offset:50176
	ds_read_b128 v[196:199], v153 offset:51200
	ds_read_b128 v[200:203], v153 offset:52224
	ds_read_b128 v[204:207], v153 offset:53248
	ds_read_b128 v[208:211], v153 offset:54272
	ds_read_b128 v[212:215], v153 offset:55296
	ds_read_b128 v[216:219], v153 offset:56320
	global_load_lds_dwordx4 v[146:147], off
	s_add_i32 m0, s34, 0x2000
	s_add_u32 s30, s30, 0x1c0080
	v_lshl_add_u64 v[146:147], v[220:221], 0, s[16:17]
	s_addc_u32 s31, s31, 0
	s_add_i32 s34, s64, s97
	global_load_lds_dwordx4 v[146:147], off
	v_lshl_add_u64 v[146:147], s[30:31], 0, v[130:131]
	s_mov_b32 m0, s34
	s_nop 0
	global_load_lds_dwordx4 v[146:147], off
	v_lshl_add_u64 v[146:147], s[30:31], 0, v[128:129]
	s_add_i32 m0, s34, 0x2000
	s_nop 0
	global_load_lds_dwordx4 v[146:147], off
	v_lshl_add_u64 v[146:147], v[222:223], 0, s[16:17]
	s_mov_b32 m0, s53
	s_nop 0
	global_load_lds_dwordx4 v[146:147], off
	v_lshl_add_u64 v[146:147], v[224:225], 0, s[16:17]
	s_mov_b32 m0, s54
	s_nop 0
	global_load_lds_dwordx4 v[146:147], off
	s_waitcnt vmcnt(8)
	s_waitcnt lgkmcnt(0)
	s_barrier
	s_setprio 1
	s_waitcnt lgkmcnt(0)
	v_mfma_f32_16x16x32_bf16 v[56:59], v[156:159], v[188:191], v[56:59]
	v_mfma_f32_16x16x32_bf16 v[48:51], v[164:167], v[188:191], v[48:51]
	v_mfma_f32_16x16x32_bf16 v[40:43], v[156:159], v[196:199], v[40:43]
	v_mfma_f32_16x16x32_bf16 v[32:35], v[164:167], v[196:199], v[32:35]
	v_mfma_f32_16x16x32_bf16 v[20:23], v[156:159], v[204:207], v[20:23]
	v_mfma_f32_16x16x32_bf16 v[8:11], v[164:167], v[204:207], v[8:11]
	v_mfma_f32_16x16x32_bf16 v[4:7], v[156:159], v[212:215], v[4:7]
	v_mfma_f32_16x16x32_bf16 v[0:3], v[164:167], v[212:215], v[0:3]
	v_mfma_f32_16x16x32_bf16 v[56:59], v[160:163], v[192:195], v[56:59]
	v_mfma_f32_16x16x32_bf16 v[48:51], v[168:171], v[192:195], v[48:51]
	v_mfma_f32_16x16x32_bf16 v[40:43], v[160:163], v[200:203], v[40:43]
	v_mfma_f32_16x16x32_bf16 v[32:35], v[168:171], v[200:203], v[32:35]
	v_mfma_f32_16x16x32_bf16 v[20:23], v[160:163], v[208:211], v[20:23]
	v_mfma_f32_16x16x32_bf16 v[8:11], v[168:171], v[208:211], v[8:11]
	v_mfma_f32_16x16x32_bf16 v[4:7], v[160:163], v[216:219], v[4:7]
	v_mfma_f32_16x16x32_bf16 v[0:3], v[168:171], v[216:219], v[0:3]
	v_mfma_f32_16x16x32_bf16 v[60:63], v[172:175], v[188:191], v[60:63]
	v_mfma_f32_16x16x32_bf16 v[52:55], v[180:183], v[188:191], v[52:55]
	v_mfma_f32_16x16x32_bf16 v[44:47], v[172:175], v[196:199], v[44:47]
	v_mfma_f32_16x16x32_bf16 v[36:39], v[180:183], v[196:199], v[36:39]
	v_mfma_f32_16x16x32_bf16 v[28:31], v[172:175], v[204:207], v[28:31]
	v_mfma_f32_16x16x32_bf16 v[16:19], v[180:183], v[204:207], v[16:19]
	v_mfma_f32_16x16x32_bf16 v[24:27], v[172:175], v[212:215], v[24:27]
	v_mfma_f32_16x16x32_bf16 v[12:15], v[180:183], v[212:215], v[12:15]
	v_mfma_f32_16x16x32_bf16 v[60:63], v[176:179], v[192:195], v[60:63]
	v_mfma_f32_16x16x32_bf16 v[52:55], v[184:187], v[192:195], v[52:55]
	v_mfma_f32_16x16x32_bf16 v[44:47], v[176:179], v[200:203], v[44:47]
	v_mfma_f32_16x16x32_bf16 v[36:39], v[184:187], v[200:203], v[36:39]
	v_mfma_f32_16x16x32_bf16 v[28:31], v[176:179], v[208:211], v[28:31]
	v_mfma_f32_16x16x32_bf16 v[16:19], v[184:187], v[208:211], v[16:19]
	v_mfma_f32_16x16x32_bf16 v[24:27], v[176:179], v[216:219], v[24:27]
	v_mfma_f32_16x16x32_bf16 v[12:15], v[184:187], v[216:219], v[12:15]
	s_setprio 0
	s_barrier
	s_add_i32 s62, s62, 2
	s_add_u32 s28, s28, 0x100
	s_addc_u32 s29, s29, 0
	s_add_u32 s60, s60, 0x100
	s_addc_u32 s61, s61, 0
	s_cmpk_gt_u32 s62, 0x6d
	s_cbranch_scc0 .LBB0_1336
	v_readlane_b32 s28, v254, 27
	v_readlane_b32 s29, v254, 28
	s_and_b64 vcc, exec, s[28:29]
	s_cbranch_vccz .LBB0_1339
	s_barrier

; #define PG8_STAGE(bufoff, gbase, o0, o1) do { \
;         __builtin_amdgcn_global_load_lds((const unsigned*)((const char*)(gbase) + (o0)), (LAS unsigned*)(lds + (bufoff) + ldsw), 16, 0, 0); \
;         __builtin_amdgcn_global_load_lds((const unsigned*)((const char*)(gbase) + (o1)), (LAS unsigned*)(lds + (bufoff) + ldsw + 8192), 16, 0, 0); } while (0)
; #define PG8_LDA(dst, b, h) do { _Pragma("unroll") for (int m = 0; m < 4; ++m) _Pragma("unroll") for (int k = 0; k < 2; ++k) dst[m][k] = *(const LAS bf16x8*)(lds + PG8_SA(b, h) + aoff + m * 2048 + k * 1024); } while (0)
; #define PG8_LDB(dst, b, h) do { _Pragma("unroll") for (int n = 0; n < 2; ++n) _Pragma("unroll") for (int k = 0; k < 2; ++k) dst[n][k] = *(const LAS bf16x8*)(lds + PG8_SB(b, h) + boff + n * 2048 + k * 1024); } while (0)
; #define PG8_WAIT_V(n) asm volatile("s_waitcnt vmcnt(" #n ")" ::: "memory")
; #define PG8_WAIT_L(n) asm volatile("s_waitcnt lgkmcnt(" #n ")" ::: "memory")
; #define PG8_BAR __builtin_amdgcn_s_barrier()
; #define PG8_SCHED __builtin_amdgcn_sched_barrier(0)
; template <class Epi, class Sched, class Prob>
; __device__ __forceinline__ void gemm_phase(LAS unsigned char* lds, LAS unsigned char* lds_epi, const Prob g, const Sched& S, const Epi& E, int wid) {
;     ...
;         const bool has_next = S.next(ui + 1, nxt);
;         const char* nA = has_next ? g.a_base(nxt) : cA; const char* nB = has_next ? g.b_base(nxt) : cB;
; _Pragma("clang loop unroll(disable)")
;         for (int t = 0; t < nt; t += 2) {
;             const bool last = (t == nt - 2);
;             const char* a1 = cA + (size_t)(t + 1) * kstep;
;             const char* a2 = last ? nA : cA + (size_t)(t + 2) * kstep; const char* b2 = last ? nB : cB + (size_t)(t + 2) * kstep;
;             const char* a3 = a2 + kstep; const char* b3 = b2 + kstep;
;             PG8_LDB(B0, 0, 0); PG8_LDB(B1, 0, 1); PG8_SCHED; PG8_LDA(At, 0, 0); PG8_STAGE(PG8_SA(1, 1), a1, cA10, cA11);
;             PG8_WAIT_V(8); PG8_WAIT_L(0); PG8_BAR; PG8_MMA(0, 0, At, B0); PG8_MMA(0, 1, At, B1); PG8_BAR; PG8_SCHED;
;             PG8_LDA(At, 0, 1); PG8_STAGE(PG8_SB(0, 0), b2, vB0, vB1); PG8_STAGE(PG8_SB(0, 1), b2 + hstepB, vB0, vB1); PG8_STAGE(PG8_SA(0, 0), a2, cA00, cA01);
;             PG8_WAIT_V(8); PG8_WAIT_L(0); PG8_BAR; PG8_MMA(1, 0, At, B0); PG8_MMA(1, 1, At, B1); PG8_BAR; PG8_SCHED;
.LBB0_1433:
	s_ashr_i32 s17, s16, 31
	s_lshl_b64 s[40:41], s[16:17], 20
	s_add_u32 s40, s58, s40
	s_addc_u32 s41, s59, s41
	s_and_b64 s[42:43], s[36:37], exec
	s_cselect_b32 s17, s41, s11
	s_cselect_b32 s52, s40, s10
	s_ashr_i32 s35, s34, 31
	s_lshl_b64 s[42:43], s[34:35], 20
	s_add_u32 s42, s60, s42
	s_addc_u32 s43, s61, s43
	s_and_b64 s[48:49], s[36:37], exec
	s_cselect_b32 s35, s43, s47
	s_cselect_b32 s53, s42, s46
	s_add_u32 s54, s46, 0x100
	v_mov_b32_e32 v0, 0
	s_addc_u32 s55, s47, 0
	s_mov_b32 s87, -2
	ds_read_b128 v[146:149], v240
	ds_read_b128 v[150:153], v240 offset:1024
	ds_read_b128 v[154:157], v240 offset:2048
	ds_read_b128 v[158:161], v240 offset:3072
	ds_read_b128 v[162:165], v241
	ds_read_b128 v[166:169], v241 offset:1024
	ds_read_b128 v[170:173], v241 offset:2048
	ds_read_b128 v[174:177], v241 offset:3072
	s_add_u32 s46, s10, 0x100
	s_addc_u32 s47, s11, 0
	s_cmp_eq_u32 s87, 28
	s_cselect_b32 s51, s17, s47
	s_cselect_b32 s50, s52, s46
	s_cselect_b32 s49, s35, s55
	s_cselect_b32 s48, s53, s54
	v_lshl_add_u64 v[210:211], s[10:11], 0, v[142:143]
	s_add_i32 m0, s62, 0xc000
	ds_read_b128 v[178:181], v242
	ds_read_b128 v[182:185], v242 offset:1024
	ds_read_b128 v[186:189], v242 offset:2048
	ds_read_b128 v[190:193], v242 offset:3072
	ds_read_b128 v[194:197], v242 offset:4096
	ds_read_b128 v[198:201], v242 offset:5120
	ds_read_b128 v[202:205], v242 offset:6144
	ds_read_b128 v[206:209], v242 offset:7168
	global_load_lds_dwordx4 v[210:211], off
	v_lshl_add_u64 v[210:211], s[10:11], 0, v[140:141]
	s_add_i32 m0, s62, 0xe000
	s_nop 0
	global_load_lds_dwordx4 v[210:211], off
	s_waitcnt vmcnt(8)
	s_waitcnt lgkmcnt(0)
	s_barrier
	s_setprio 1
	s_waitcnt lgkmcnt(0)
	v_mfma_f32_16x16x32_bf16 v[124:127], v[146:149], v[178:181], 0
	v_mfma_f32_16x16x32_bf16 v[120:123], v[154:157], v[178:181], 0
	v_mfma_f32_16x16x32_bf16 v[116:119], v[146:149], v[186:189], 0
	v_mfma_f32_16x16x32_bf16 v[112:115], v[154:157], v[186:189], 0
	v_mfma_f32_16x16x32_bf16 v[108:111], v[146:149], v[194:197], 0
	v_mfma_f32_16x16x32_bf16 v[100:103], v[154:157], v[194:197], 0
	v_mfma_f32_16x16x32_bf16 v[92:95], v[146:149], v[202:205], 0
	v_mfma_f32_16x16x32_bf16 v[84:87], v[154:157], v[202:205], 0
	v_mfma_f32_16x16x32_bf16 v[124:127], v[150:153], v[182:185], v[124:127]
	v_mfma_f32_16x16x32_bf16 v[120:123], v[158:161], v[182:185], v[120:123]
	v_mfma_f32_16x16x32_bf16 v[116:119], v[150:153], v[190:193], v[116:119]
	v_mfma_f32_16x16x32_bf16 v[112:115], v[158:161], v[190:193], v[112:115]
	v_mfma_f32_16x16x32_bf16 v[108:111], v[150:153], v[198:201], v[108:111]
	v_mfma_f32_16x16x32_bf16 v[100:103], v[158:161], v[198:201], v[100:103]
	v_mfma_f32_16x16x32_bf16 v[92:95], v[150:153], v[206:209], v[92:95]
	v_mfma_f32_16x16x32_bf16 v[84:87], v[158:161], v[206:209], v[84:87]
	v_mfma_f32_16x16x32_bf16 v[104:107], v[162:165], v[178:181], 0
	v_mfma_f32_16x16x32_bf16 v[96:99], v[170:173], v[178:181], 0
	v_mfma_f32_16x16x32_bf16 v[88:91], v[162:165], v[186:189], 0
	v_mfma_f32_16x16x32_bf16 v[80:83], v[170:173], v[186:189], 0
	v_mfma_f32_16x16x32_bf16 v[76:79], v[162:165], v[194:197], 0
	v_mfma_f32_16x16x32_bf16 v[72:75], v[170:173], v[194:197], 0
	v_mfma_f32_16x16x32_bf16 v[68:71], v[162:165], v[202:205], 0
	v_mfma_f32_16x16x32_bf16 v[64:67], v[170:173], v[202:205], 0
	v_mfma_f32_16x16x32_bf16 v[104:107], v[166:169], v[182:185], v[104:107]
	v_mfma_f32_16x16x32_bf16 v[96:99], v[174:177], v[182:185], v[96:99]
	v_mfma_f32_16x16x32_bf16 v[88:91], v[166:169], v[190:193], v[88:91]
	v_mfma_f32_16x16x32_bf16 v[80:83], v[174:177], v[190:193], v[80:83]
	v_mfma_f32_16x16x32_bf16 v[76:79], v[166:169], v[198:201], v[76:79]
	v_mfma_f32_16x16x32_bf16 v[72:75], v[174:177], v[198:201], v[72:75]
	v_mfma_f32_16x16x32_bf16 v[68:71], v[166:169], v[206:209], v[68:71]
	v_mfma_f32_16x16x32_bf16 v[64:67], v[174:177], v[206:209], v[64:67]
	s_setprio 0
	s_barrier
	s_add_i32 s10, s80, s97
	v_lshl_add_u64 v[210:211], s[48:49], 0, v[128:129]
	s_mov_b32 m0, s10
	ds_read_b128 v[178:181], v242 offset:16384
	ds_read_b128 v[182:185], v242 offset:17408
	ds_read_b128 v[186:189], v242 offset:18432
	ds_read_b128 v[190:193], v242 offset:19456
	ds_read_b128 v[194:197], v242 offset:20480
	ds_read_b128 v[198:201], v242 offset:21504
	ds_read_b128 v[202:205], v242 offset:22528
	ds_read_b128 v[206:209], v242 offset:23552
	global_load_lds_dwordx4 v[210:211], off
	s_add_i32 m0, s10, 0x2000
	s_add_u32 s10, s48, 0x80000
	v_lshl_add_u64 v[212:213], s[48:49], 0, v[130:131]
	s_addc_u32 s11, s49, 0
	s_add_i32 s88, s81, s97
	global_load_lds_dwordx4 v[212:213], off
	v_lshl_add_u64 v[214:215], s[10:11], 0, v[128:129]
	s_mov_b32 m0, s88
	v_lshl_add_u64 v[216:217], s[50:51], 0, v[136:137]
	global_load_lds_dwordx4 v[214:215], off
	v_lshl_add_u64 v[214:215], s[10:11], 0, v[130:131]
	s_add_i32 m0, s88, 0x2000
	s_nop 0
	global_load_lds_dwordx4 v[214:215], off
	v_lshl_add_u64 v[214:215], s[50:51], 0, v[132:133]
	s_mov_b32 m0, s62
	s_nop 0
	global_load_lds_dwordx4 v[214:215], off
	s_mov_b32 m0, s63
	s_nop 0
	global_load_lds_dwordx4 v[216:217], off
	s_waitcnt vmcnt(8)
	s_waitcnt lgkmcnt(0)
	s_barrier
; #define PG8_STAGE(bufoff, gbase, o0, o1) do { \
;         __builtin_amdgcn_global_load_lds((const unsigned*)((const char*)(gbase) + (o0)), (LAS unsigned*)(lds + (bufoff) + ldsw), 16, 0, 0); \
;         __builtin_amdgcn_global_load_lds((const unsigned*)((const char*)(gbase) + (o1)), (LAS unsigned*)(lds + (bufoff) + ldsw + 8192), 16, 0, 0); } while (0)
; #define PG8_LDA(dst, b, h) do { _Pragma("unroll") for (int m = 0; m < 4; ++m) _Pragma("unroll") for (int k = 0; k < 2; ++k) dst[m][k] = *(const LAS bf16x8*)(lds + PG8_SA(b, h) + aoff + m * 2048 + k * 1024); } while (0)
; #define PG8_LDB(dst, b, h) do { _Pragma("unroll") for (int n = 0; n < 2; ++n) _Pragma("unroll") for (int k = 0; k < 2; ++k) dst[n][k] = *(const LAS bf16x8*)(lds + PG8_SB(b, h) + boff + n * 2048 + k * 1024); } while (0)
; #define PG8_WAIT_V(n) asm volatile("s_waitcnt vmcnt(" #n ")" ::: "memory")
; #define PG8_WAIT_L(n) asm volatile("s_waitcnt lgkmcnt(" #n ")" ::: "memory")
; #define PG8_BAR __builtin_amdgcn_s_barrier()
; #define PG8_SCHED __builtin_amdgcn_sched_barrier(0)
; template <class Epi, class Sched, class Prob>
; __device__ __forceinline__ void gemm_phase(LAS unsigned char* lds, LAS unsigned char* lds_epi, const Prob g, const Sched& S, const Epi& E, int wid) {
;     ...
;             PG8_WAIT_V(8); PG8_WAIT_L(0); PG8_BAR; PG8_MMA(1, 0, At, B0); PG8_MMA(1, 1, At, B1); PG8_BAR; PG8_SCHED;
;             PG8_LDB(B0, 1, 0); PG8_LDB(B1, 1, 1); PG8_SCHED; PG8_LDA(At, 1, 0); PG8_STAGE(PG8_SA(0, 1), a2, cA10, cA11);
;             PG8_WAIT_V(8); PG8_WAIT_L(0); PG8_BAR; PG8_MMA(0, 0, At, B0); PG8_MMA(0, 1, At, B1); PG8_BAR; PG8_SCHED;
	s_setprio 1
	s_waitcnt lgkmcnt(0)
	v_mfma_f32_16x16x32_bf16 v[60:63], v[146:149], v[178:181], 0
	v_mfma_f32_16x16x32_bf16 v[56:59], v[154:157], v[178:181], 0
	v_mfma_f32_16x16x32_bf16 v[52:55], v[146:149], v[186:189], 0
	v_mfma_f32_16x16x32_bf16 v[48:51], v[154:157], v[186:189], 0
	v_mfma_f32_16x16x32_bf16 v[36:39], v[146:149], v[194:197], 0
	v_mfma_f32_16x16x32_bf16 v[32:35], v[154:157], v[194:197], 0
	v_mfma_f32_16x16x32_bf16 v[20:23], v[146:149], v[202:205], 0
	v_mfma_f32_16x16x32_bf16 v[16:19], v[154:157], v[202:205], 0
	v_mfma_f32_16x16x32_bf16 v[60:63], v[150:153], v[182:185], v[60:63]
	v_mfma_f32_16x16x32_bf16 v[56:59], v[158:161], v[182:185], v[56:59]
	v_mfma_f32_16x16x32_bf16 v[52:55], v[150:153], v[190:193], v[52:55]
	v_mfma_f32_16x16x32_bf16 v[48:51], v[158:161], v[190:193], v[48:51]
	v_mfma_f32_16x16x32_bf16 v[36:39], v[150:153], v[198:201], v[36:39]
	v_mfma_f32_16x16x32_bf16 v[32:35], v[158:161], v[198:201], v[32:35]
	v_mfma_f32_16x16x32_bf16 v[20:23], v[150:153], v[206:209], v[20:23]
	v_mfma_f32_16x16x32_bf16 v[16:19], v[158:161], v[206:209], v[16:19]
	v_mfma_f32_16x16x32_bf16 v[44:47], v[162:165], v[178:181], 0
	v_mfma_f32_16x16x32_bf16 v[40:43], v[170:173], v[178:181], 0
	v_mfma_f32_16x16x32_bf16 v[28:31], v[162:165], v[186:189], 0
	v_mfma_f32_16x16x32_bf16 v[24:27], v[170:173], v[186:189], 0
	v_mfma_f32_16x16x32_bf16 v[12:15], v[162:165], v[194:197], 0
	v_mfma_f32_16x16x32_bf16 v[8:11], v[170:173], v[194:197], 0
	v_mfma_f32_16x16x32_bf16 v[4:7], v[162:165], v[202:205], 0
	v_mfma_f32_16x16x32_bf16 v[0:3], v[170:173], v[202:205], 0
	v_mfma_f32_16x16x32_bf16 v[44:47], v[166:169], v[182:185], v[44:47]
	v_mfma_f32_16x16x32_bf16 v[40:43], v[174:177], v[182:185], v[40:43]
	v_mfma_f32_16x16x32_bf16 v[28:31], v[166:169], v[190:193], v[28:31]
	v_mfma_f32_16x16x32_bf16 v[24:27], v[174:177], v[190:193], v[24:27]
	v_mfma_f32_16x16x32_bf16 v[12:15], v[166:169], v[198:201], v[12:15]
	v_mfma_f32_16x16x32_bf16 v[8:11], v[174:177], v[198:201], v[8:11]
	v_mfma_f32_16x16x32_bf16 v[4:7], v[166:169], v[206:209], v[4:7]
	v_mfma_f32_16x16x32_bf16 v[0:3], v[174:177], v[206:209], v[0:3]
	s_setprio 0
	s_barrier
	s_add_i32 s10, 0, 0x18000
	s_add_i32 s88, 0, 0x1c000
	v_add_u32_e32 v158, s10, v239
	v_add_u32_e32 v174, s88, v239
	ds_read_b128 v[146:149], v158
	ds_read_b128 v[150:153], v158 offset:1024
	ds_read_b128 v[154:157], v158 offset:2048
	ds_read_b128 v[158:161], v158 offset:3072
	ds_read_b128 v[162:165], v174
	ds_read_b128 v[166:169], v174 offset:1024
	ds_read_b128 v[170:173], v174 offset:2048
	ds_read_b128 v[174:177], v174 offset:3072
	s_mov_b32 m0, s64
	v_lshl_add_u64 v[218:219], s[50:51], 0, v[134:135]
	ds_read_b128 v[178:181], v242 offset:32768
	ds_read_b128 v[182:185], v242 offset:33792
	ds_read_b128 v[186:189], v242 offset:34816
	ds_read_b128 v[190:193], v242 offset:35840
	ds_read_b128 v[194:197], v242 offset:36864
	ds_read_b128 v[198:201], v242 offset:37888
	ds_read_b128 v[202:205], v242 offset:38912
	ds_read_b128 v[206:209], v242 offset:39936
	global_load_lds_dwordx4 v[218:219], off
	v_lshl_add_u64 v[218:219], s[50:51], 0, v[138:139]
	s_mov_b32 m0, s65
	s_nop 0
	global_load_lds_dwordx4 v[218:219], off
	s_waitcnt vmcnt(8)
	s_waitcnt lgkmcnt(0)
	s_barrier
	s_setprio 1
	s_waitcnt lgkmcnt(0)
	v_mfma_f32_16x16x32_bf16 v[124:127], v[146:149], v[178:181], v[124:127]
	v_mfma_f32_16x16x32_bf16 v[120:123], v[154:157], v[178:181], v[120:123]
	v_mfma_f32_16x16x32_bf16 v[116:119], v[146:149], v[186:189], v[116:119]
	v_mfma_f32_16x16x32_bf16 v[112:115], v[154:157], v[186:189], v[112:115]
	v_mfma_f32_16x16x32_bf16 v[108:111], v[146:149], v[194:197], v[108:111]
	v_mfma_f32_16x16x32_bf16 v[100:103], v[154:157], v[194:197], v[100:103]
	v_mfma_f32_16x16x32_bf16 v[92:95], v[146:149], v[202:205], v[92:95]
	v_mfma_f32_16x16x32_bf16 v[84:87], v[154:157], v[202:205], v[84:87]
	v_mfma_f32_16x16x32_bf16 v[124:127], v[150:153], v[182:185], v[124:127]
	v_mfma_f32_16x16x32_bf16 v[120:123], v[158:161], v[182:185], v[120:123]
	v_mfma_f32_16x16x32_bf16 v[116:119], v[150:153], v[190:193], v[116:119]
	v_mfma_f32_16x16x32_bf16 v[112:115], v[158:161], v[190:193], v[112:115]
	v_mfma_f32_16x16x32_bf16 v[108:111], v[150:153], v[198:201], v[108:111]
	v_mfma_f32_16x16x32_bf16 v[100:103], v[158:161], v[198:201], v[100:103]
	v_mfma_f32_16x16x32_bf16 v[92:95], v[150:153], v[206:209], v[92:95]
	v_mfma_f32_16x16x32_bf16 v[84:87], v[158:161], v[206:209], v[84:87]
	v_mfma_f32_16x16x32_bf16 v[104:107], v[162:165], v[178:181], v[104:107]
	v_mfma_f32_16x16x32_bf16 v[96:99], v[170:173], v[178:181], v[96:99]
	v_mfma_f32_16x16x32_bf16 v[88:91], v[162:165], v[186:189], v[88:91]
	v_mfma_f32_16x16x32_bf16 v[80:83], v[170:173], v[186:189], v[80:83]
	v_mfma_f32_16x16x32_bf16 v[76:79], v[162:165], v[194:197], v[76:79]
	v_mfma_f32_16x16x32_bf16 v[72:75], v[170:173], v[194:197], v[72:75]
	v_mfma_f32_16x16x32_bf16 v[68:71], v[162:165], v[202:205], v[68:71]
	v_mfma_f32_16x16x32_bf16 v[64:67], v[170:173], v[202:205], v[64:67]
	v_mfma_f32_16x16x32_bf16 v[104:107], v[166:169], v[182:185], v[104:107]
	v_mfma_f32_16x16x32_bf16 v[96:99], v[174:177], v[182:185], v[96:99]
	v_mfma_f32_16x16x32_bf16 v[88:91], v[166:169], v[190:193], v[88:91]
	v_mfma_f32_16x16x32_bf16 v[80:83], v[174:177], v[190:193], v[80:83]
	v_mfma_f32_16x16x32_bf16 v[76:79], v[166:169], v[198:201], v[76:79]
	v_mfma_f32_16x16x32_bf16 v[72:75], v[174:177], v[198:201], v[72:75]
	v_mfma_f32_16x16x32_bf16 v[68:71], v[166:169], v[206:209], v[68:71]
	v_mfma_f32_16x16x32_bf16 v[64:67], v[174:177], v[206:209], v[64:67]
	s_setprio 0
	s_barrier
; #define PG8_STAGE(bufoff, gbase, o0, o1) do { \
;         __builtin_amdgcn_global_load_lds((const unsigned*)((const char*)(gbase) + (o0)), (LAS unsigned*)(lds + (bufoff) + ldsw), 16, 0, 0); \
;         __builtin_amdgcn_global_load_lds((const unsigned*)((const char*)(gbase) + (o1)), (LAS unsigned*)(lds + (bufoff) + ldsw + 8192), 16, 0, 0); } while (0)
; #define PG8_LDA(dst, b, h) do { _Pragma("unroll") for (int m = 0; m < 4; ++m) _Pragma("unroll") for (int k = 0; k < 2; ++k) dst[m][k] = *(const LAS bf16x8*)(lds + PG8_SA(b, h) + aoff + m * 2048 + k * 1024); } while (0)
; #define PG8_LDB(dst, b, h) do { _Pragma("unroll") for (int n = 0; n < 2; ++n) _Pragma("unroll") for (int k = 0; k < 2; ++k) dst[n][k] = *(const LAS bf16x8*)(lds + PG8_SB(b, h) + boff + n * 2048 + k * 1024); } while (0)
; template <class Epi, class Sched, class Prob>
; __device__ __forceinline__ void gemm_phase(LAS unsigned char* lds, LAS unsigned char* lds_epi, const Prob g, const Sched& S, const Epi& E, int wid) {
;     ...
;         for (int t = 0; t < nt; t += 2) {
;             const bool last = (t == nt - 2);
;             const char* a1 = cA + (size_t)(t + 1) * kstep;
;             const char* a2 = last ? nA : cA + (size_t)(t + 2) * kstep; const char* b2 = last ? nB : cB + (size_t)(t + 2) * kstep;
;             const char* a3 = a2 + kstep; const char* b3 = b2 + kstep;
;             PG8_LDB(B0, 0, 0); PG8_LDB(B1, 0, 1); PG8_SCHED; PG8_LDA(At, 0, 0); PG8_STAGE(PG8_SA(1, 1), a1, cA10, cA11);
;             PG8_WAIT_V(8); PG8_WAIT_L(0); PG8_BAR; PG8_MMA(0, 0, At, B0); PG8_MMA(0, 1, At, B1); PG8_BAR; PG8_SCHED;
;             PG8_LDA(At, 0, 1); PG8_STAGE(PG8_SB(0, 0), b2, vB0, vB1); PG8_STAGE(PG8_SB(0, 1), b2 + hstepB, vB0, vB1); PG8_STAGE(PG8_SA(0, 0), a2, cA00, cA01);
;             PG8_WAIT_V(8); PG8_WAIT_L(0); PG8_BAR; PG8_MMA(1, 0, At, B0); PG8_MMA(1, 1, At, B1); PG8_BAR; PG8_SCHED;
;             PG8_LDB(B0, 1, 0); PG8_LDB(B1, 1, 1); PG8_SCHED; PG8_LDA(At, 1, 0); PG8_STAGE(PG8_SA(0, 1), a2, cA10, cA11);
;             PG8_WAIT_V(8); PG8_WAIT_L(0); PG8_BAR; PG8_MMA(0, 0, At, B0); PG8_MMA(0, 1, At, B1); PG8_BAR; PG8_SCHED;
;             PG8_LDA(At, 1, 1); PG8_STAGE(PG8_SB(1, 0), b3, vB0, vB1); PG8_STAGE(PG8_SB(1, 1), b3 + hstepB, vB0, vB1); PG8_STAGE(PG8_SA(1, 0), a3, cA00, cA01);
;             PG8_WAIT_V(8); PG8_WAIT_L(0); PG8_BAR; PG8_MMA(1, 0, At, B0); PG8_MMA(1, 1, At, B1); PG8_BAR; PG8_SCHED;
	s_add_i32 s10, s10, s97
	v_lshl_add_u64 v[210:211], v[210:211], 0, s[24:25]
	s_mov_b32 m0, s10
	ds_read_b128 v[178:181], v242 offset:49152
	ds_read_b128 v[182:185], v242 offset:50176
	ds_read_b128 v[186:189], v242 offset:51200
	ds_read_b128 v[190:193], v242 offset:52224
	ds_read_b128 v[194:197], v242 offset:53248
	ds_read_b128 v[198:201], v242 offset:54272
	ds_read_b128 v[202:205], v242 offset:55296
	ds_read_b128 v[206:209], v242 offset:56320
	global_load_lds_dwordx4 v[210:211], off
	s_add_i32 m0, s10, 0x2000
	s_add_u32 s10, s48, 0x80080
	v_lshl_add_u64 v[210:211], v[212:213], 0, s[24:25]
	s_addc_u32 s11, s49, 0
	s_add_i32 s48, s88, s97
	global_load_lds_dwordx4 v[210:211], off
	v_lshl_add_u64 v[210:211], s[10:11], 0, v[128:129]
	s_mov_b32 m0, s48
	s_nop 0
	global_load_lds_dwordx4 v[210:211], off
	v_lshl_add_u64 v[210:211], s[10:11], 0, v[130:131]
	s_add_i32 m0, s48, 0x2000
	s_nop 0
	global_load_lds_dwordx4 v[210:211], off
	v_lshl_add_u64 v[210:211], v[214:215], 0, s[24:25]
	s_mov_b32 m0, s78
	s_nop 0
	global_load_lds_dwordx4 v[210:211], off
	v_lshl_add_u64 v[210:211], v[216:217], 0, s[24:25]
	s_mov_b32 m0, s79
	s_nop 0
	global_load_lds_dwordx4 v[210:211], off
	s_waitcnt vmcnt(8)
	s_waitcnt lgkmcnt(0)
	s_barrier
	s_setprio 1
	s_waitcnt lgkmcnt(0)
	v_mfma_f32_16x16x32_bf16 v[60:63], v[146:149], v[178:181], v[60:63]
	v_mfma_f32_16x16x32_bf16 v[56:59], v[154:157], v[178:181], v[56:59]
	v_mfma_f32_16x16x32_bf16 v[52:55], v[146:149], v[186:189], v[52:55]
	v_mfma_f32_16x16x32_bf16 v[48:51], v[154:157], v[186:189], v[48:51]
	v_mfma_f32_16x16x32_bf16 v[36:39], v[146:149], v[194:197], v[36:39]
	v_mfma_f32_16x16x32_bf16 v[32:35], v[154:157], v[194:197], v[32:35]
	v_mfma_f32_16x16x32_bf16 v[20:23], v[146:149], v[202:205], v[20:23]
	v_mfma_f32_16x16x32_bf16 v[16:19], v[154:157], v[202:205], v[16:19]
	v_mfma_f32_16x16x32_bf16 v[60:63], v[150:153], v[182:185], v[60:63]
	v_mfma_f32_16x16x32_bf16 v[56:59], v[158:161], v[182:185], v[56:59]
	v_mfma_f32_16x16x32_bf16 v[52:55], v[150:153], v[190:193], v[52:55]
	v_mfma_f32_16x16x32_bf16 v[48:51], v[158:161], v[190:193], v[48:51]
	v_mfma_f32_16x16x32_bf16 v[36:39], v[150:153], v[198:201], v[36:39]
	v_mfma_f32_16x16x32_bf16 v[32:35], v[158:161], v[198:201], v[32:35]
	v_mfma_f32_16x16x32_bf16 v[20:23], v[150:153], v[206:209], v[20:23]
	v_mfma_f32_16x16x32_bf16 v[16:19], v[158:161], v[206:209], v[16:19]
	v_mfma_f32_16x16x32_bf16 v[44:47], v[162:165], v[178:181], v[44:47]
	v_mfma_f32_16x16x32_bf16 v[40:43], v[170:173], v[178:181], v[40:43]
	v_mfma_f32_16x16x32_bf16 v[28:31], v[162:165], v[186:189], v[28:31]
	v_mfma_f32_16x16x32_bf16 v[24:27], v[170:173], v[186:189], v[24:27]
	v_mfma_f32_16x16x32_bf16 v[12:15], v[162:165], v[194:197], v[12:15]
	v_mfma_f32_16x16x32_bf16 v[8:11], v[170:173], v[194:197], v[8:11]
	v_mfma_f32_16x16x32_bf16 v[4:7], v[162:165], v[202:205], v[4:7]
	v_mfma_f32_16x16x32_bf16 v[0:3], v[170:173], v[202:205], v[0:3]
	v_mfma_f32_16x16x32_bf16 v[44:47], v[166:169], v[182:185], v[44:47]
	v_mfma_f32_16x16x32_bf16 v[40:43], v[174:177], v[182:185], v[40:43]
	v_mfma_f32_16x16x32_bf16 v[28:31], v[166:169], v[190:193], v[28:31]
	v_mfma_f32_16x16x32_bf16 v[24:27], v[174:177], v[190:193], v[24:27]
	v_mfma_f32_16x16x32_bf16 v[12:15], v[166:169], v[198:201], v[12:15]
	v_mfma_f32_16x16x32_bf16 v[8:11], v[174:177], v[198:201], v[8:11]
	v_mfma_f32_16x16x32_bf16 v[4:7], v[166:169], v[206:209], v[4:7]
	v_mfma_f32_16x16x32_bf16 v[0:3], v[174:177], v[206:209], v[0:3]
	s_setprio 0
	s_barrier
	s_add_i32 s87, s87, 2
	s_add_u32 s54, s54, 0x100
	s_addc_u32 s55, s55, 0
	s_cmp_gt_u32 s87, 29
	s_mov_b64 s[10:11], s[46:47]
.LBB0_1434:
	ds_read_b128 v[146:149], v240
	ds_read_b128 v[150:153], v240 offset:1024
	ds_read_b128 v[154:157], v240 offset:2048
	ds_read_b128 v[158:161], v240 offset:3072
	ds_read_b128 v[162:165], v241
	ds_read_b128 v[166:169], v241 offset:1024
	ds_read_b128 v[170:173], v241 offset:2048
	ds_read_b128 v[174:177], v241 offset:3072
	s_add_u32 s46, s10, 0x100
	s_addc_u32 s47, s11, 0
	s_cmp_eq_u32 s87, 28
	s_cselect_b32 s51, s17, s47
	s_cselect_b32 s50, s52, s46
	s_cselect_b32 s49, s35, s55
	s_cselect_b32 s48, s53, s54
	v_lshl_add_u64 v[210:211], s[10:11], 0, v[142:143]
	s_add_i32 m0, s62, 0xc000
	ds_read_b128 v[178:181], v242
	ds_read_b128 v[182:185], v242 offset:1024
	ds_read_b128 v[186:189], v242 offset:2048
	ds_read_b128 v[190:193], v242 offset:3072
	ds_read_b128 v[194:197], v242 offset:4096
	ds_read_b128 v[198:201], v242 offset:5120
	ds_read_b128 v[202:205], v242 offset:6144
	ds_read_b128 v[206:209], v242 offset:7168
	global_load_lds_dwordx4 v[210:211], off
	v_lshl_add_u64 v[210:211], s[10:11], 0, v[140:141]
	s_add_i32 m0, s62, 0xe000
	s_nop 0
	global_load_lds_dwordx4 v[210:211], off
	s_waitcnt vmcnt(8)
	s_waitcnt lgkmcnt(0)
	s_barrier
; #define PG8_STAGE(bufoff, gbase, o0, o1) do { \
;         __builtin_amdgcn_global_load_lds((const unsigned*)((const char*)(gbase) + (o0)), (LAS unsigned*)(lds + (bufoff) + ldsw), 16, 0, 0); \
;         __builtin_amdgcn_global_load_lds((const unsigned*)((const char*)(gbase) + (o1)), (LAS unsigned*)(lds + (bufoff) + ldsw + 8192), 16, 0, 0); } while (0)
; #define PG8_LDA(dst, b, h) do { _Pragma("unroll") for (int m = 0; m < 4; ++m) _Pragma("unroll") for (int k = 0; k < 2; ++k) dst[m][k] = *(const LAS bf16x8*)(lds + PG8_SA(b, h) + aoff + m * 2048 + k * 1024); } while (0)
; #define PG8_WAIT_V(n) asm volatile("s_waitcnt vmcnt(" #n ")" ::: "memory")
; #define PG8_WAIT_L(n) asm volatile("s_waitcnt lgkmcnt(" #n ")" ::: "memory")
; #define PG8_BAR __builtin_amdgcn_s_barrier()
; #define PG8_SCHED __builtin_amdgcn_sched_barrier(0)
; template <class Epi, class Sched, class Prob>
; __device__ __forceinline__ void gemm_phase(LAS unsigned char* lds, LAS unsigned char* lds_epi, const Prob g, const Sched& S, const Epi& E, int wid) {
;     ...
;             PG8_WAIT_V(8); PG8_WAIT_L(0); PG8_BAR; PG8_MMA(0, 0, At, B0); PG8_MMA(0, 1, At, B1); PG8_BAR; PG8_SCHED;
;             PG8_LDA(At, 0, 1); PG8_STAGE(PG8_SB(0, 0), b2, vB0, vB1); PG8_STAGE(PG8_SB(0, 1), b2 + hstepB, vB0, vB1); PG8_STAGE(PG8_SA(0, 0), a2, cA00, cA01);
;             PG8_WAIT_V(8); PG8_WAIT_L(0); PG8_BAR; PG8_MMA(1, 0, At, B0); PG8_MMA(1, 1, At, B1); PG8_BAR; PG8_SCHED;
	s_setprio 1
	s_waitcnt lgkmcnt(0)
	v_mfma_f32_16x16x32_bf16 v[124:127], v[146:149], v[178:181], v[124:127]
	v_mfma_f32_16x16x32_bf16 v[120:123], v[154:157], v[178:181], v[120:123]
	v_mfma_f32_16x16x32_bf16 v[116:119], v[146:149], v[186:189], v[116:119]
	v_mfma_f32_16x16x32_bf16 v[112:115], v[154:157], v[186:189], v[112:115]
	v_mfma_f32_16x16x32_bf16 v[108:111], v[146:149], v[194:197], v[108:111]
	v_mfma_f32_16x16x32_bf16 v[100:103], v[154:157], v[194:197], v[100:103]
	v_mfma_f32_16x16x32_bf16 v[92:95], v[146:149], v[202:205], v[92:95]
	v_mfma_f32_16x16x32_bf16 v[84:87], v[154:157], v[202:205], v[84:87]
	v_mfma_f32_16x16x32_bf16 v[124:127], v[150:153], v[182:185], v[124:127]
	v_mfma_f32_16x16x32_bf16 v[120:123], v[158:161], v[182:185], v[120:123]
	v_mfma_f32_16x16x32_bf16 v[116:119], v[150:153], v[190:193], v[116:119]
	v_mfma_f32_16x16x32_bf16 v[112:115], v[158:161], v[190:193], v[112:115]
	v_mfma_f32_16x16x32_bf16 v[108:111], v[150:153], v[198:201], v[108:111]
	v_mfma_f32_16x16x32_bf16 v[100:103], v[158:161], v[198:201], v[100:103]
	v_mfma_f32_16x16x32_bf16 v[92:95], v[150:153], v[206:209], v[92:95]
	v_mfma_f32_16x16x32_bf16 v[84:87], v[158:161], v[206:209], v[84:87]
	v_mfma_f32_16x16x32_bf16 v[104:107], v[162:165], v[178:181], v[104:107]
	v_mfma_f32_16x16x32_bf16 v[96:99], v[170:173], v[178:181], v[96:99]
	v_mfma_f32_16x16x32_bf16 v[88:91], v[162:165], v[186:189], v[88:91]
	v_mfma_f32_16x16x32_bf16 v[80:83], v[170:173], v[186:189], v[80:83]
	v_mfma_f32_16x16x32_bf16 v[76:79], v[162:165], v[194:197], v[76:79]
	v_mfma_f32_16x16x32_bf16 v[72:75], v[170:173], v[194:197], v[72:75]
	v_mfma_f32_16x16x32_bf16 v[68:71], v[162:165], v[202:205], v[68:71]
	v_mfma_f32_16x16x32_bf16 v[64:67], v[170:173], v[202:205], v[64:67]
	v_mfma_f32_16x16x32_bf16 v[104:107], v[166:169], v[182:185], v[104:107]
	v_mfma_f32_16x16x32_bf16 v[96:99], v[174:177], v[182:185], v[96:99]
	v_mfma_f32_16x16x32_bf16 v[88:91], v[166:169], v[190:193], v[88:91]
	v_mfma_f32_16x16x32_bf16 v[80:83], v[174:177], v[190:193], v[80:83]
	v_mfma_f32_16x16x32_bf16 v[76:79], v[166:169], v[198:201], v[76:79]
	v_mfma_f32_16x16x32_bf16 v[72:75], v[174:177], v[198:201], v[72:75]
	v_mfma_f32_16x16x32_bf16 v[68:71], v[166:169], v[206:209], v[68:71]
	v_mfma_f32_16x16x32_bf16 v[64:67], v[174:177], v[206:209], v[64:67]
	s_setprio 0
	s_barrier
	s_add_i32 s10, s80, s97
	v_lshl_add_u64 v[210:211], s[48:49], 0, v[128:129]
	s_mov_b32 m0, s10
	ds_read_b128 v[178:181], v242 offset:16384
	ds_read_b128 v[182:185], v242 offset:17408
	ds_read_b128 v[186:189], v242 offset:18432
	ds_read_b128 v[190:193], v242 offset:19456
	ds_read_b128 v[194:197], v242 offset:20480
	ds_read_b128 v[198:201], v242 offset:21504
	ds_read_b128 v[202:205], v242 offset:22528
	ds_read_b128 v[206:209], v242 offset:23552
	global_load_lds_dwordx4 v[210:211], off
	s_add_i32 m0, s10, 0x2000
	s_add_u32 s10, s48, 0x80000
	v_lshl_add_u64 v[212:213], s[48:49], 0, v[130:131]
	s_addc_u32 s11, s49, 0
	s_add_i32 s88, s81, s97
	global_load_lds_dwordx4 v[212:213], off
	v_lshl_add_u64 v[214:215], s[10:11], 0, v[128:129]
	s_mov_b32 m0, s88
	v_lshl_add_u64 v[216:217], s[50:51], 0, v[136:137]
	global_load_lds_dwordx4 v[214:215], off
	v_lshl_add_u64 v[214:215], s[10:11], 0, v[130:131]
	s_add_i32 m0, s88, 0x2000
	s_nop 0
	global_load_lds_dwordx4 v[214:215], off
	v_lshl_add_u64 v[214:215], s[50:51], 0, v[132:133]
	s_mov_b32 m0, s62
	s_nop 0
	global_load_lds_dwordx4 v[214:215], off
	s_mov_b32 m0, s63
	s_nop 0
	global_load_lds_dwordx4 v[216:217], off
	s_waitcnt vmcnt(8)
	s_waitcnt lgkmcnt(0)
	s_barrier
	s_setprio 1
	s_waitcnt lgkmcnt(0)
	v_mfma_f32_16x16x32_bf16 v[60:63], v[146:149], v[178:181], v[60:63]
	v_mfma_f32_16x16x32_bf16 v[56:59], v[154:157], v[178:181], v[56:59]
	v_mfma_f32_16x16x32_bf16 v[52:55], v[146:149], v[186:189], v[52:55]
	v_mfma_f32_16x16x32_bf16 v[48:51], v[154:157], v[186:189], v[48:51]
	v_mfma_f32_16x16x32_bf16 v[36:39], v[146:149], v[194:197], v[36:39]
	v_mfma_f32_16x16x32_bf16 v[32:35], v[154:157], v[194:197], v[32:35]
	v_mfma_f32_16x16x32_bf16 v[20:23], v[146:149], v[202:205], v[20:23]
	v_mfma_f32_16x16x32_bf16 v[16:19], v[154:157], v[202:205], v[16:19]
	v_mfma_f32_16x16x32_bf16 v[60:63], v[150:153], v[182:185], v[60:63]
	v_mfma_f32_16x16x32_bf16 v[56:59], v[158:161], v[182:185], v[56:59]
	v_mfma_f32_16x16x32_bf16 v[52:55], v[150:153], v[190:193], v[52:55]
	v_mfma_f32_16x16x32_bf16 v[48:51], v[158:161], v[190:193], v[48:51]
	v_mfma_f32_16x16x32_bf16 v[36:39], v[150:153], v[198:201], v[36:39]
	v_mfma_f32_16x16x32_bf16 v[32:35], v[158:161], v[198:201], v[32:35]
	v_mfma_f32_16x16x32_bf16 v[20:23], v[150:153], v[206:209], v[20:23]
	v_mfma_f32_16x16x32_bf16 v[16:19], v[158:161], v[206:209], v[16:19]
	v_mfma_f32_16x16x32_bf16 v[44:47], v[162:165], v[178:181], v[44:47]
	v_mfma_f32_16x16x32_bf16 v[40:43], v[170:173], v[178:181], v[40:43]
	v_mfma_f32_16x16x32_bf16 v[28:31], v[162:165], v[186:189], v[28:31]
	v_mfma_f32_16x16x32_bf16 v[24:27], v[170:173], v[186:189], v[24:27]
	v_mfma_f32_16x16x32_bf16 v[12:15], v[162:165], v[194:197], v[12:15]
	v_mfma_f32_16x16x32_bf16 v[8:11], v[170:173], v[194:197], v[8:11]
	v_mfma_f32_16x16x32_bf16 v[4:7], v[162:165], v[202:205], v[4:7]
	v_mfma_f32_16x16x32_bf16 v[0:3], v[170:173], v[202:205], v[0:3]
	v_mfma_f32_16x16x32_bf16 v[44:47], v[166:169], v[182:185], v[44:47]
	v_mfma_f32_16x16x32_bf16 v[40:43], v[174:177], v[182:185], v[40:43]
	v_mfma_f32_16x16x32_bf16 v[28:31], v[166:169], v[190:193], v[28:31]
	v_mfma_f32_16x16x32_bf16 v[24:27], v[174:177], v[190:193], v[24:27]
	v_mfma_f32_16x16x32_bf16 v[12:15], v[166:169], v[198:201], v[12:15]
	v_mfma_f32_16x16x32_bf16 v[8:11], v[174:177], v[198:201], v[8:11]
	v_mfma_f32_16x16x32_bf16 v[4:7], v[166:169], v[206:209], v[4:7]
	v_mfma_f32_16x16x32_bf16 v[0:3], v[174:177], v[206:209], v[0:3]
	s_setprio 0
	s_barrier
; #define PG8_STAGE(bufoff, gbase, o0, o1) do { \
;         __builtin_amdgcn_global_load_lds((const unsigned*)((const char*)(gbase) + (o0)), (LAS unsigned*)(lds + (bufoff) + ldsw), 16, 0, 0); \
;         __builtin_amdgcn_global_load_lds((const unsigned*)((const char*)(gbase) + (o1)), (LAS unsigned*)(lds + (bufoff) + ldsw + 8192), 16, 0, 0); } while (0)
; #define PG8_LDA(dst, b, h) do { _Pragma("unroll") for (int m = 0; m < 4; ++m) _Pragma("unroll") for (int k = 0; k < 2; ++k) dst[m][k] = *(const LAS bf16x8*)(lds + PG8_SA(b, h) + aoff + m * 2048 + k * 1024); } while (0)
; #define PG8_LDB(dst, b, h) do { _Pragma("unroll") for (int n = 0; n < 2; ++n) _Pragma("unroll") for (int k = 0; k < 2; ++k) dst[n][k] = *(const LAS bf16x8*)(lds + PG8_SB(b, h) + boff + n * 2048 + k * 1024); } while (0)
; #define PG8_WAIT_V(n) asm volatile("s_waitcnt vmcnt(" #n ")" ::: "memory")
; #define PG8_WAIT_L(n) asm volatile("s_waitcnt lgkmcnt(" #n ")" ::: "memory")
; #define PG8_BAR __builtin_amdgcn_s_barrier()
; #define PG8_SCHED __builtin_amdgcn_sched_barrier(0)
; template <class Epi, class Sched, class Prob>
; __device__ __forceinline__ void gemm_phase(LAS unsigned char* lds, LAS unsigned char* lds_epi, const Prob g, const Sched& S, const Epi& E, int wid) {
;     ...
;             PG8_LDB(B0, 1, 0); PG8_LDB(B1, 1, 1); PG8_SCHED; PG8_LDA(At, 1, 0); PG8_STAGE(PG8_SA(0, 1), a2, cA10, cA11);
;             PG8_WAIT_V(8); PG8_WAIT_L(0); PG8_BAR; PG8_MMA(0, 0, At, B0); PG8_MMA(0, 1, At, B1); PG8_BAR; PG8_SCHED;
	s_add_i32 s10, 0, 0x18000
	s_add_i32 s88, 0, 0x1c000
	v_add_u32_e32 v158, s10, v239
	v_add_u32_e32 v174, s88, v239
	ds_read_b128 v[146:149], v158
	ds_read_b128 v[150:153], v158 offset:1024
	ds_read_b128 v[154:157], v158 offset:2048
	ds_read_b128 v[158:161], v158 offset:3072
	ds_read_b128 v[162:165], v174
	ds_read_b128 v[166:169], v174 offset:1024
	ds_read_b128 v[170:173], v174 offset:2048
	ds_read_b128 v[174:177], v174 offset:3072
	s_mov_b32 m0, s64
	v_lshl_add_u64 v[218:219], s[50:51], 0, v[134:135]
	ds_read_b128 v[178:181], v242 offset:32768
	ds_read_b128 v[182:185], v242 offset:33792
	ds_read_b128 v[186:189], v242 offset:34816
	ds_read_b128 v[190:193], v242 offset:35840
	ds_read_b128 v[194:197], v242 offset:36864
	ds_read_b128 v[198:201], v242 offset:37888
	ds_read_b128 v[202:205], v242 offset:38912
	ds_read_b128 v[206:209], v242 offset:39936
	global_load_lds_dwordx4 v[218:219], off
	v_lshl_add_u64 v[218:219], s[50:51], 0, v[138:139]
	s_mov_b32 m0, s65
	s_nop 0
	global_load_lds_dwordx4 v[218:219], off
	s_waitcnt vmcnt(8)
	s_waitcnt lgkmcnt(0)
	s_barrier
	s_setprio 1
	s_waitcnt lgkmcnt(0)
	v_mfma_f32_16x16x32_bf16 v[124:127], v[146:149], v[178:181], v[124:127]
	v_mfma_f32_16x16x32_bf16 v[120:123], v[154:157], v[178:181], v[120:123]
	v_mfma_f32_16x16x32_bf16 v[116:119], v[146:149], v[186:189], v[116:119]
	v_mfma_f32_16x16x32_bf16 v[112:115], v[154:157], v[186:189], v[112:115]
	v_mfma_f32_16x16x32_bf16 v[108:111], v[146:149], v[194:197], v[108:111]
	v_mfma_f32_16x16x32_bf16 v[100:103], v[154:157], v[194:197], v[100:103]
	v_mfma_f32_16x16x32_bf16 v[92:95], v[146:149], v[202:205], v[92:95]
	v_mfma_f32_16x16x32_bf16 v[84:87], v[154:157], v[202:205], v[84:87]
	v_mfma_f32_16x16x32_bf16 v[124:127], v[150:153], v[182:185], v[124:127]
	v_mfma_f32_16x16x32_bf16 v[120:123], v[158:161], v[182:185], v[120:123]
	v_mfma_f32_16x16x32_bf16 v[116:119], v[150:153], v[190:193], v[116:119]
	v_mfma_f32_16x16x32_bf16 v[112:115], v[158:161], v[190:193], v[112:115]
	v_mfma_f32_16x16x32_bf16 v[108:111], v[150:153], v[198:201], v[108:111]
	v_mfma_f32_16x16x32_bf16 v[100:103], v[158:161], v[198:201], v[100:103]
	v_mfma_f32_16x16x32_bf16 v[92:95], v[150:153], v[206:209], v[92:95]
	v_mfma_f32_16x16x32_bf16 v[84:87], v[158:161], v[206:209], v[84:87]
	v_mfma_f32_16x16x32_bf16 v[104:107], v[162:165], v[178:181], v[104:107]
	v_mfma_f32_16x16x32_bf16 v[96:99], v[170:173], v[178:181], v[96:99]
	v_mfma_f32_16x16x32_bf16 v[88:91], v[162:165], v[186:189], v[88:91]
	v_mfma_f32_16x16x32_bf16 v[80:83], v[170:173], v[186:189], v[80:83]
	v_mfma_f32_16x16x32_bf16 v[76:79], v[162:165], v[194:197], v[76:79]
	v_mfma_f32_16x16x32_bf16 v[72:75], v[170:173], v[194:197], v[72:75]
	v_mfma_f32_16x16x32_bf16 v[68:71], v[162:165], v[202:205], v[68:71]
	v_mfma_f32_16x16x32_bf16 v[64:67], v[170:173], v[202:205], v[64:67]
	v_mfma_f32_16x16x32_bf16 v[104:107], v[166:169], v[182:185], v[104:107]
	v_mfma_f32_16x16x32_bf16 v[96:99], v[174:177], v[182:185], v[96:99]
	v_mfma_f32_16x16x32_bf16 v[88:91], v[166:169], v[190:193], v[88:91]
	v_mfma_f32_16x16x32_bf16 v[80:83], v[174:177], v[190:193], v[80:83]
	v_mfma_f32_16x16x32_bf16 v[76:79], v[166:169], v[198:201], v[76:79]
	v_mfma_f32_16x16x32_bf16 v[72:75], v[174:177], v[198:201], v[72:75]
	v_mfma_f32_16x16x32_bf16 v[68:71], v[166:169], v[206:209], v[68:71]
	v_mfma_f32_16x16x32_bf16 v[64:67], v[174:177], v[206:209], v[64:67]
	s_setprio 0
	s_barrier
; #define PG8_STAGE(bufoff, gbase, o0, o1) do { \
;         __builtin_amdgcn_global_load_lds((const unsigned*)((const char*)(gbase) + (o0)), (LAS unsigned*)(lds + (bufoff) + ldsw), 16, 0, 0); \
;         __builtin_amdgcn_global_load_lds((const unsigned*)((const char*)(gbase) + (o1)), (LAS unsigned*)(lds + (bufoff) + ldsw + 8192), 16, 0, 0); } while (0)
; #define PG8_LDA(dst, b, h) do { _Pragma("unroll") for (int m = 0; m < 4; ++m) _Pragma("unroll") for (int k = 0; k < 2; ++k) dst[m][k] = *(const LAS bf16x8*)(lds + PG8_SA(b, h) + aoff + m * 2048 + k * 1024); } while (0)
; #define PG8_WAIT_V(n) asm volatile("s_waitcnt vmcnt(" #n ")" ::: "memory")
; #define PG8_WAIT_L(n) asm volatile("s_waitcnt lgkmcnt(" #n ")" ::: "memory")
; #define PG8_BAR __builtin_amdgcn_s_barrier()
; #define PG8_SCHED __builtin_amdgcn_sched_barrier(0)
; template <class Epi, class Sched, class Prob>
; __device__ __forceinline__ void gemm_phase(LAS unsigned char* lds, LAS unsigned char* lds_epi, const Prob g, const Sched& S, const Epi& E, int wid) {
;     ...
;             PG8_LDA(At, 1, 1); PG8_STAGE(PG8_SB(1, 0), b3, vB0, vB1); PG8_STAGE(PG8_SB(1, 1), b3 + hstepB, vB0, vB1); PG8_STAGE(PG8_SA(1, 0), a3, cA00, cA01);
;             PG8_WAIT_V(8); PG8_WAIT_L(0); PG8_BAR; PG8_MMA(1, 0, At, B0); PG8_MMA(1, 1, At, B1); PG8_BAR; PG8_SCHED;
;         }
;         if constexpr (Prob::FP8) asm volatile("s_nop 7\n\ts_nop 7\n\ts_nop 7" ::: "memory");
;         if (wr == 0) PG8_BAR;
	s_add_i32 s10, s10, s97
	v_lshl_add_u64 v[210:211], v[210:211], 0, s[24:25]
	s_mov_b32 m0, s10
	ds_read_b128 v[178:181], v242 offset:49152
	ds_read_b128 v[182:185], v242 offset:50176
	ds_read_b128 v[186:189], v242 offset:51200
	ds_read_b128 v[190:193], v242 offset:52224
	ds_read_b128 v[194:197], v242 offset:53248
	ds_read_b128 v[198:201], v242 offset:54272
	ds_read_b128 v[202:205], v242 offset:55296
	ds_read_b128 v[206:209], v242 offset:56320
	global_load_lds_dwordx4 v[210:211], off
	s_add_i32 m0, s10, 0x2000
	s_add_u32 s10, s48, 0x80080
	v_lshl_add_u64 v[210:211], v[212:213], 0, s[24:25]
	s_addc_u32 s11, s49, 0
	s_add_i32 s48, s88, s97
	global_load_lds_dwordx4 v[210:211], off
	v_lshl_add_u64 v[210:211], s[10:11], 0, v[128:129]
	s_mov_b32 m0, s48
	s_nop 0
	global_load_lds_dwordx4 v[210:211], off
	v_lshl_add_u64 v[210:211], s[10:11], 0, v[130:131]
	s_add_i32 m0, s48, 0x2000
	s_nop 0
	global_load_lds_dwordx4 v[210:211], off
	v_lshl_add_u64 v[210:211], v[214:215], 0, s[24:25]
	s_mov_b32 m0, s78
	s_nop 0
	global_load_lds_dwordx4 v[210:211], off
	v_lshl_add_u64 v[210:211], v[216:217], 0, s[24:25]
	s_mov_b32 m0, s79
	s_nop 0
	global_load_lds_dwordx4 v[210:211], off
	s_waitcnt vmcnt(8)
	s_waitcnt lgkmcnt(0)
	s_barrier
	s_setprio 1
	s_waitcnt lgkmcnt(0)
	v_mfma_f32_16x16x32_bf16 v[60:63], v[146:149], v[178:181], v[60:63]
	v_mfma_f32_16x16x32_bf16 v[56:59], v[154:157], v[178:181], v[56:59]
	v_mfma_f32_16x16x32_bf16 v[52:55], v[146:149], v[186:189], v[52:55]
	v_mfma_f32_16x16x32_bf16 v[48:51], v[154:157], v[186:189], v[48:51]
	v_mfma_f32_16x16x32_bf16 v[36:39], v[146:149], v[194:197], v[36:39]
	v_mfma_f32_16x16x32_bf16 v[32:35], v[154:157], v[194:197], v[32:35]
	v_mfma_f32_16x16x32_bf16 v[20:23], v[146:149], v[202:205], v[20:23]
	v_mfma_f32_16x16x32_bf16 v[16:19], v[154:157], v[202:205], v[16:19]
	v_mfma_f32_16x16x32_bf16 v[60:63], v[150:153], v[182:185], v[60:63]
	v_mfma_f32_16x16x32_bf16 v[56:59], v[158:161], v[182:185], v[56:59]
	v_mfma_f32_16x16x32_bf16 v[52:55], v[150:153], v[190:193], v[52:55]
	v_mfma_f32_16x16x32_bf16 v[48:51], v[158:161], v[190:193], v[48:51]
	v_mfma_f32_16x16x32_bf16 v[36:39], v[150:153], v[198:201], v[36:39]
	v_mfma_f32_16x16x32_bf16 v[32:35], v[158:161], v[198:201], v[32:35]
	v_mfma_f32_16x16x32_bf16 v[20:23], v[150:153], v[206:209], v[20:23]
	v_mfma_f32_16x16x32_bf16 v[16:19], v[158:161], v[206:209], v[16:19]
	v_mfma_f32_16x16x32_bf16 v[44:47], v[162:165], v[178:181], v[44:47]
	v_mfma_f32_16x16x32_bf16 v[40:43], v[170:173], v[178:181], v[40:43]
	v_mfma_f32_16x16x32_bf16 v[28:31], v[162:165], v[186:189], v[28:31]
	v_mfma_f32_16x16x32_bf16 v[24:27], v[170:173], v[186:189], v[24:27]
	v_mfma_f32_16x16x32_bf16 v[12:15], v[162:165], v[194:197], v[12:15]
	v_mfma_f32_16x16x32_bf16 v[8:11], v[170:173], v[194:197], v[8:11]
	v_mfma_f32_16x16x32_bf16 v[4:7], v[162:165], v[202:205], v[4:7]
	v_mfma_f32_16x16x32_bf16 v[0:3], v[170:173], v[202:205], v[0:3]
	v_mfma_f32_16x16x32_bf16 v[44:47], v[166:169], v[182:185], v[44:47]
	v_mfma_f32_16x16x32_bf16 v[40:43], v[174:177], v[182:185], v[40:43]
	v_mfma_f32_16x16x32_bf16 v[28:31], v[166:169], v[190:193], v[28:31]
	v_mfma_f32_16x16x32_bf16 v[24:27], v[174:177], v[190:193], v[24:27]
	v_mfma_f32_16x16x32_bf16 v[12:15], v[166:169], v[198:201], v[12:15]
	v_mfma_f32_16x16x32_bf16 v[8:11], v[174:177], v[198:201], v[8:11]
	v_mfma_f32_16x16x32_bf16 v[4:7], v[166:169], v[206:209], v[4:7]
	v_mfma_f32_16x16x32_bf16 v[0:3], v[174:177], v[206:209], v[0:3]
	s_setprio 0
	s_barrier
	s_add_i32 s87, s87, 2
	s_add_u32 s54, s54, 0x100
	s_addc_u32 s55, s55, 0
	s_cmp_gt_u32 s87, 29
	s_mov_b64 s[10:11], s[46:47]
	s_cbranch_scc0 .LBB0_1434
	v_readlane_b32 s10, v254, 27
	v_readlane_b32 s11, v254, 28
	s_and_b64 vcc, exec, s[10:11]
	s_cbranch_vccz .LBB0_1437
	s_barrier

; #define PG8_STAGE(bufoff, gbase, o0, o1) do { \
;         __builtin_amdgcn_global_load_lds((const unsigned*)((const char*)(gbase) + (o0)), (LAS unsigned*)(lds + (bufoff) + ldsw), 16, 0, 0); \
;         __builtin_amdgcn_global_load_lds((const unsigned*)((const char*)(gbase) + (o1)), (LAS unsigned*)(lds + (bufoff) + ldsw + 8192), 16, 0, 0); } while (0)
; #define PG8_LDA(dst, b, h) do { _Pragma("unroll") for (int m = 0; m < 4; ++m) _Pragma("unroll") for (int k = 0; k < 2; ++k) dst[m][k] = *(const LAS bf16x8*)(lds + PG8_SA(b, h) + aoff + m * 2048 + k * 1024); } while (0)
; #define PG8_LDB(dst, b, h) do { _Pragma("unroll") for (int n = 0; n < 2; ++n) _Pragma("unroll") for (int k = 0; k < 2; ++k) dst[n][k] = *(const LAS bf16x8*)(lds + PG8_SB(b, h) + boff + n * 2048 + k * 1024); } while (0)
; #define PG8_WAIT_V(n) asm volatile("s_waitcnt vmcnt(" #n ")" ::: "memory")
; #define PG8_WAIT_L(n) asm volatile("s_waitcnt lgkmcnt(" #n ")" ::: "memory")
; #define PG8_BAR __builtin_amdgcn_s_barrier()
; #define PG8_SCHED __builtin_amdgcn_sched_barrier(0)
; template <class Epi, class Sched, class Prob>
; __device__ __forceinline__ void gemm_phase(LAS unsigned char* lds, LAS unsigned char* lds_epi, const Prob g, const Sched& S, const Epi& E, int wid) {
;     ...
;         const bool has_next = S.next(ui + 1, nxt);
;         const char* nA = has_next ? g.a_base(nxt) : cA; const char* nB = has_next ? g.b_base(nxt) : cB;
; _Pragma("clang loop unroll(disable)")
;         for (int t = 0; t < nt; t += 2) {
;             const bool last = (t == nt - 2);
;             const char* a1 = cA + (size_t)(t + 1) * kstep;
;             const char* a2 = last ? nA : cA + (size_t)(t + 2) * kstep; const char* b2 = last ? nB : cB + (size_t)(t + 2) * kstep;
;             const char* a3 = a2 + kstep; const char* b3 = b2 + kstep;
;             PG8_LDB(B0, 0, 0); PG8_LDB(B1, 0, 1); PG8_SCHED; PG8_LDA(At, 0, 0); PG8_STAGE(PG8_SA(1, 1), a1, cA10, cA11);
;             PG8_WAIT_V(8); PG8_WAIT_L(0); PG8_BAR; PG8_MMA(0, 0, At, B0); PG8_MMA(0, 1, At, B1); PG8_BAR; PG8_SCHED;
;             PG8_LDA(At, 0, 1); PG8_STAGE(PG8_SB(0, 0), b2, vB0, vB1); PG8_STAGE(PG8_SB(0, 1), b2 + hstepB, vB0, vB1); PG8_STAGE(PG8_SA(0, 0), a2, cA00, cA01);
;             PG8_WAIT_V(8); PG8_WAIT_L(0); PG8_BAR; PG8_MMA(1, 0, At, B0); PG8_MMA(1, 1, At, B1); PG8_BAR; PG8_SCHED;
.LBB0_1594:
	s_ashr_i32 s65, s64, 31
	s_lshl_b64 s[14:15], s[64:65], 20
	s_add_u32 s17, s40, s14
	s_addc_u32 s19, s41, s15
	s_ashr_i32 s14, s62, 1
	s_ashr_i32 s15, s14, 31
	s_lshl_b64 s[14:15], s[14:15], 9
	s_add_u32 s68, s17, s14
	s_addc_u32 s69, s19, s15
	s_and_b64 s[14:15], s[66:67], exec
	s_cselect_b32 s17, s69, s9
	s_cselect_b32 s19, s68, s8
	s_ashr_i32 s63, s62, 31
	s_lshl_b64 s[14:15], s[62:63], 17
	s_add_u32 s70, s33, s14
	s_addc_u32 s71, s76, s15
	s_and_b64 s[14:15], s[66:67], exec
	v_mov_b32_e32 v0, 0
	s_cselect_b32 s26, s71, s11
	s_cselect_b32 s27, s70, s10
	s_mov_b64 s[20:21], -1
	s_mov_b64 s[14:15], 0
	s_add_u32 s24, s8, s14
	s_addc_u32 s25, s9, s15
	s_add_u32 s22, s24, 0x100
	s_addc_u32 s23, s25, 0
	v_cndmask_b32_e64 v56, 0, 1, s[20:21]
	s_and_b64 s[20:21], s[12:13], exec
	s_cselect_b32 s20, s19, s22
	s_cselect_b32 s21, s17, s23
	s_add_u32 s14, s10, s14
	s_addc_u32 s15, s11, s15
	s_add_u32 s14, s14, 0x100
	v_cmp_ne_u32_e32 vcc, 1, v56
	ds_read_b128 v[56:59], v221
	ds_read_b128 v[68:71], v221 offset:1024
	ds_read_b128 v[72:75], v221 offset:2048
	ds_read_b128 v[88:91], v221 offset:3072
	ds_read_b128 v[100:103], v222
	ds_read_b128 v[104:107], v222 offset:1024
	ds_read_b128 v[166:169], v222 offset:2048
	ds_read_b128 v[170:173], v222 offset:3072
	s_addc_u32 s15, s15, 0
	s_and_b64 s[12:13], s[12:13], exec
	s_cselect_b32 s15, s26, s15
	s_cselect_b32 s14, s27, s14
	s_add_i32 s65, s85, s97
	s_add_i32 m0, s77, 0xc000
	s_add_i32 s72, s77, 0xe000
	s_add_i32 s36, s65, 0x2000
	s_add_u32 s22, s14, 0x10000
	s_addc_u32 s23, s15, 0
	s_add_i32 s35, 0, 0x18000
	s_add_i32 s63, s86, s97
	s_add_i32 s31, s35, s97
	s_add_i32 s37, s63, 0x2000
	s_add_i32 s34, 0, 0x1c000
	s_add_i32 s29, s31, 0x2000
	s_add_u32 s12, s14, 0x10080
	s_addc_u32 s13, s15, 0
	s_add_i32 s30, s34, s97
	s_add_i32 s28, s30, 0x2000
	v_lshl_add_u64 v[206:207], s[24:25], 0, v[158:159]
	v_lshl_add_u64 v[206:207], v[206:207], 0, s[54:55]
	ds_read_b128 v[174:177], v223
	ds_read_b128 v[178:181], v223 offset:1024
	ds_read_b128 v[182:185], v223 offset:2048
	ds_read_b128 v[186:189], v223 offset:3072
	ds_read_b128 v[190:193], v223 offset:4096
	ds_read_b128 v[194:197], v223 offset:5120
	ds_read_b128 v[198:201], v223 offset:6144
	ds_read_b128 v[202:205], v223 offset:7168
	global_load_lds_dwordx4 v[206:207], off
	v_lshl_add_u64 v[206:207], s[24:25], 0, v[162:163]
	v_lshl_add_u64 v[206:207], v[206:207], 0, s[54:55]
	s_mov_b32 m0, s72
	s_nop 0
	global_load_lds_dwordx4 v[206:207], off
	s_waitcnt vmcnt(8)
	s_waitcnt lgkmcnt(0)
	s_barrier
	s_setprio 1
	s_waitcnt lgkmcnt(0)
	v_mfma_f32_16x16x32_bf16 v[148:151], v[56:59], v[174:177], 0
	v_mfma_f32_16x16x32_bf16 v[116:119], v[72:75], v[174:177], 0
	v_mfma_f32_16x16x32_bf16 v[144:147], v[56:59], v[182:185], 0
	v_mfma_f32_16x16x32_bf16 v[112:115], v[72:75], v[182:185], 0
	v_mfma_f32_16x16x32_bf16 v[140:143], v[56:59], v[190:193], 0
	v_mfma_f32_16x16x32_bf16 v[108:111], v[72:75], v[190:193], 0
	v_mfma_f32_16x16x32_bf16 v[136:139], v[56:59], v[198:201], 0
	v_mfma_f32_16x16x32_bf16 v[96:99], v[72:75], v[198:201], 0
	v_mfma_f32_16x16x32_bf16 v[148:151], v[68:71], v[178:181], v[148:151]
	v_mfma_f32_16x16x32_bf16 v[116:119], v[88:91], v[178:181], v[116:119]
	v_mfma_f32_16x16x32_bf16 v[144:147], v[68:71], v[186:189], v[144:147]
	v_mfma_f32_16x16x32_bf16 v[112:115], v[88:91], v[186:189], v[112:115]
	v_mfma_f32_16x16x32_bf16 v[140:143], v[68:71], v[194:197], v[140:143]
	v_mfma_f32_16x16x32_bf16 v[108:111], v[88:91], v[194:197], v[108:111]
	v_mfma_f32_16x16x32_bf16 v[136:139], v[68:71], v[202:205], v[136:139]
	v_mfma_f32_16x16x32_bf16 v[96:99], v[88:91], v[202:205], v[96:99]
	v_mfma_f32_16x16x32_bf16 v[132:135], v[100:103], v[174:177], 0
	v_mfma_f32_16x16x32_bf16 v[92:95], v[166:169], v[174:177], 0
	v_mfma_f32_16x16x32_bf16 v[128:131], v[100:103], v[182:185], 0
	v_mfma_f32_16x16x32_bf16 v[84:87], v[166:169], v[182:185], 0
	v_mfma_f32_16x16x32_bf16 v[124:127], v[100:103], v[190:193], 0
	v_mfma_f32_16x16x32_bf16 v[80:83], v[166:169], v[190:193], 0
	v_mfma_f32_16x16x32_bf16 v[120:123], v[100:103], v[198:201], 0
	v_mfma_f32_16x16x32_bf16 v[76:79], v[166:169], v[198:201], 0
	v_mfma_f32_16x16x32_bf16 v[132:135], v[104:107], v[178:181], v[132:135]
	v_mfma_f32_16x16x32_bf16 v[92:95], v[170:173], v[178:181], v[92:95]
	v_mfma_f32_16x16x32_bf16 v[128:131], v[104:107], v[186:189], v[128:131]
	v_mfma_f32_16x16x32_bf16 v[84:87], v[170:173], v[186:189], v[84:87]
	v_mfma_f32_16x16x32_bf16 v[124:127], v[104:107], v[194:197], v[124:127]
	v_mfma_f32_16x16x32_bf16 v[80:83], v[170:173], v[194:197], v[80:83]
	v_mfma_f32_16x16x32_bf16 v[120:123], v[104:107], v[202:205], v[120:123]
	v_mfma_f32_16x16x32_bf16 v[76:79], v[170:173], v[202:205], v[76:79]
	s_setprio 0
	s_barrier
	s_mov_b32 m0, s65
	v_lshl_add_u64 v[206:207], s[14:15], 0, v[152:153]
	ds_read_b128 v[174:177], v223 offset:16384
	ds_read_b128 v[178:181], v223 offset:17408
	ds_read_b128 v[182:185], v223 offset:18432
	ds_read_b128 v[186:189], v223 offset:19456
	ds_read_b128 v[190:193], v223 offset:20480
	ds_read_b128 v[194:197], v223 offset:21504
	ds_read_b128 v[198:201], v223 offset:22528
	ds_read_b128 v[202:205], v223 offset:23552
	global_load_lds_dwordx4 v[206:207], off
	v_lshl_add_u64 v[208:209], s[14:15], 0, v[154:155]
	s_mov_b32 m0, s36
	v_lshl_add_u64 v[210:211], s[22:23], 0, v[152:153]
	global_load_lds_dwordx4 v[208:209], off
	s_mov_b32 m0, s63
	v_lshl_add_u64 v[212:213], s[20:21], 0, v[160:161]
	global_load_lds_dwordx4 v[210:211], off
	v_lshl_add_u64 v[210:211], s[22:23], 0, v[154:155]
	s_mov_b32 m0, s37
	s_nop 0
	global_load_lds_dwordx4 v[210:211], off
	v_lshl_add_u64 v[210:211], s[20:21], 0, v[156:157]
	s_mov_b32 m0, s77
	s_nop 0
	global_load_lds_dwordx4 v[210:211], off
	s_mov_b32 m0, s78
	s_nop 0
	global_load_lds_dwordx4 v[212:213], off
	s_waitcnt vmcnt(8)
	s_waitcnt lgkmcnt(0)
	s_barrier
; #define PG8_STAGE(bufoff, gbase, o0, o1) do { \
;         __builtin_amdgcn_global_load_lds((const unsigned*)((const char*)(gbase) + (o0)), (LAS unsigned*)(lds + (bufoff) + ldsw), 16, 0, 0); \
;         __builtin_amdgcn_global_load_lds((const unsigned*)((const char*)(gbase) + (o1)), (LAS unsigned*)(lds + (bufoff) + ldsw + 8192), 16, 0, 0); } while (0)
; #define PG8_LDA(dst, b, h) do { _Pragma("unroll") for (int m = 0; m < 4; ++m) _Pragma("unroll") for (int k = 0; k < 2; ++k) dst[m][k] = *(const LAS bf16x8*)(lds + PG8_SA(b, h) + aoff + m * 2048 + k * 1024); } while (0)
; #define PG8_LDB(dst, b, h) do { _Pragma("unroll") for (int n = 0; n < 2; ++n) _Pragma("unroll") for (int k = 0; k < 2; ++k) dst[n][k] = *(const LAS bf16x8*)(lds + PG8_SB(b, h) + boff + n * 2048 + k * 1024); } while (0)
; #define PG8_WAIT_V(n) asm volatile("s_waitcnt vmcnt(" #n ")" ::: "memory")
; #define PG8_WAIT_L(n) asm volatile("s_waitcnt lgkmcnt(" #n ")" ::: "memory")
; #define PG8_BAR __builtin_amdgcn_s_barrier()
; #define PG8_SCHED __builtin_amdgcn_sched_barrier(0)
; template <class Epi, class Sched, class Prob>
; __device__ __forceinline__ void gemm_phase(LAS unsigned char* lds, LAS unsigned char* lds_epi, const Prob g, const Sched& S, const Epi& E, int wid) {
;     ...
;             PG8_WAIT_V(8); PG8_WAIT_L(0); PG8_BAR; PG8_MMA(1, 0, At, B0); PG8_MMA(1, 1, At, B1); PG8_BAR; PG8_SCHED;
;             PG8_LDB(B0, 1, 0); PG8_LDB(B1, 1, 1); PG8_SCHED; PG8_LDA(At, 1, 0); PG8_STAGE(PG8_SA(0, 1), a2, cA10, cA11);
;             PG8_WAIT_V(8); PG8_WAIT_L(0); PG8_BAR; PG8_MMA(0, 0, At, B0); PG8_MMA(0, 1, At, B1); PG8_BAR; PG8_SCHED;
	s_setprio 1
	s_waitcnt lgkmcnt(0)
	v_mfma_f32_16x16x32_bf16 v[64:67], v[56:59], v[174:177], 0
	v_mfma_f32_16x16x32_bf16 v[28:31], v[72:75], v[174:177], 0
	v_mfma_f32_16x16x32_bf16 v[60:63], v[56:59], v[182:185], 0
	v_mfma_f32_16x16x32_bf16 v[24:27], v[72:75], v[182:185], 0
	v_mfma_f32_16x16x32_bf16 v[52:55], v[56:59], v[190:193], 0
	v_mfma_f32_16x16x32_bf16 v[20:23], v[72:75], v[190:193], 0
	v_mfma_f32_16x16x32_bf16 v[48:51], v[56:59], v[198:201], 0
	v_mfma_f32_16x16x32_bf16 v[16:19], v[72:75], v[198:201], 0
	v_mfma_f32_16x16x32_bf16 v[64:67], v[68:71], v[178:181], v[64:67]
	v_mfma_f32_16x16x32_bf16 v[28:31], v[88:91], v[178:181], v[28:31]
	v_mfma_f32_16x16x32_bf16 v[60:63], v[68:71], v[186:189], v[60:63]
	v_mfma_f32_16x16x32_bf16 v[24:27], v[88:91], v[186:189], v[24:27]
	v_mfma_f32_16x16x32_bf16 v[52:55], v[68:71], v[194:197], v[52:55]
	v_mfma_f32_16x16x32_bf16 v[20:23], v[88:91], v[194:197], v[20:23]
	v_mfma_f32_16x16x32_bf16 v[48:51], v[68:71], v[202:205], v[48:51]
	v_mfma_f32_16x16x32_bf16 v[16:19], v[88:91], v[202:205], v[16:19]
	v_mfma_f32_16x16x32_bf16 v[44:47], v[100:103], v[174:177], 0
	v_mfma_f32_16x16x32_bf16 v[12:15], v[166:169], v[174:177], 0
	v_mfma_f32_16x16x32_bf16 v[40:43], v[100:103], v[182:185], 0
	v_mfma_f32_16x16x32_bf16 v[8:11], v[166:169], v[182:185], 0
	v_mfma_f32_16x16x32_bf16 v[36:39], v[100:103], v[190:193], 0
	v_mfma_f32_16x16x32_bf16 v[4:7], v[166:169], v[190:193], 0
	v_mfma_f32_16x16x32_bf16 v[32:35], v[100:103], v[198:201], 0
	v_mfma_f32_16x16x32_bf16 v[0:3], v[166:169], v[198:201], 0
	v_mfma_f32_16x16x32_bf16 v[44:47], v[104:107], v[178:181], v[44:47]
	v_mfma_f32_16x16x32_bf16 v[12:15], v[170:173], v[178:181], v[12:15]
	v_mfma_f32_16x16x32_bf16 v[40:43], v[104:107], v[186:189], v[40:43]
	v_mfma_f32_16x16x32_bf16 v[8:11], v[170:173], v[186:189], v[8:11]
	v_mfma_f32_16x16x32_bf16 v[36:39], v[104:107], v[194:197], v[36:39]
	v_mfma_f32_16x16x32_bf16 v[4:7], v[170:173], v[194:197], v[4:7]
	v_mfma_f32_16x16x32_bf16 v[32:35], v[104:107], v[202:205], v[32:35]
	v_mfma_f32_16x16x32_bf16 v[0:3], v[170:173], v[202:205], v[0:3]
	s_setprio 0
	s_barrier
	v_add_u32_e32 v88, s35, v220
	v_add_u32_e32 v170, s34, v220
	ds_read_b128 v[56:59], v88
	ds_read_b128 v[68:71], v88 offset:1024
	ds_read_b128 v[72:75], v88 offset:2048
	ds_read_b128 v[88:91], v88 offset:3072
	ds_read_b128 v[100:103], v170
	ds_read_b128 v[104:107], v170 offset:1024
	ds_read_b128 v[166:169], v170 offset:2048
	ds_read_b128 v[170:173], v170 offset:3072
	s_mov_b32 m0, s79
	v_lshl_add_u64 v[214:215], s[20:21], 0, v[158:159]
	ds_read_b128 v[174:177], v223 offset:32768
	ds_read_b128 v[178:181], v223 offset:33792
	ds_read_b128 v[182:185], v223 offset:34816
	ds_read_b128 v[186:189], v223 offset:35840
	ds_read_b128 v[190:193], v223 offset:36864
	ds_read_b128 v[194:197], v223 offset:37888
	ds_read_b128 v[198:201], v223 offset:38912
	ds_read_b128 v[202:205], v223 offset:39936
	global_load_lds_dwordx4 v[214:215], off
	v_lshl_add_u64 v[214:215], s[20:21], 0, v[162:163]
	s_mov_b32 m0, s80
	s_nop 0
	global_load_lds_dwordx4 v[214:215], off
	s_waitcnt vmcnt(8)
	s_waitcnt lgkmcnt(0)
	s_barrier
	s_setprio 1
	s_waitcnt lgkmcnt(0)
	v_mfma_f32_16x16x32_bf16 v[148:151], v[56:59], v[174:177], v[148:151]
	v_mfma_f32_16x16x32_bf16 v[116:119], v[72:75], v[174:177], v[116:119]
	v_mfma_f32_16x16x32_bf16 v[144:147], v[56:59], v[182:185], v[144:147]
	v_mfma_f32_16x16x32_bf16 v[112:115], v[72:75], v[182:185], v[112:115]
	v_mfma_f32_16x16x32_bf16 v[140:143], v[56:59], v[190:193], v[140:143]
	v_mfma_f32_16x16x32_bf16 v[108:111], v[72:75], v[190:193], v[108:111]
	v_mfma_f32_16x16x32_bf16 v[136:139], v[56:59], v[198:201], v[136:139]
	v_mfma_f32_16x16x32_bf16 v[96:99], v[72:75], v[198:201], v[96:99]
	v_mfma_f32_16x16x32_bf16 v[148:151], v[68:71], v[178:181], v[148:151]
	v_mfma_f32_16x16x32_bf16 v[116:119], v[88:91], v[178:181], v[116:119]
	v_mfma_f32_16x16x32_bf16 v[144:147], v[68:71], v[186:189], v[144:147]
	v_mfma_f32_16x16x32_bf16 v[112:115], v[88:91], v[186:189], v[112:115]
	v_mfma_f32_16x16x32_bf16 v[140:143], v[68:71], v[194:197], v[140:143]
	v_mfma_f32_16x16x32_bf16 v[108:111], v[88:91], v[194:197], v[108:111]
	v_mfma_f32_16x16x32_bf16 v[136:139], v[68:71], v[202:205], v[136:139]
	v_mfma_f32_16x16x32_bf16 v[96:99], v[88:91], v[202:205], v[96:99]
	v_mfma_f32_16x16x32_bf16 v[132:135], v[100:103], v[174:177], v[132:135]
	v_mfma_f32_16x16x32_bf16 v[92:95], v[166:169], v[174:177], v[92:95]
	v_mfma_f32_16x16x32_bf16 v[128:131], v[100:103], v[182:185], v[128:131]
	v_mfma_f32_16x16x32_bf16 v[84:87], v[166:169], v[182:185], v[84:87]
	v_mfma_f32_16x16x32_bf16 v[124:127], v[100:103], v[190:193], v[124:127]
	v_mfma_f32_16x16x32_bf16 v[80:83], v[166:169], v[190:193], v[80:83]
	v_mfma_f32_16x16x32_bf16 v[120:123], v[100:103], v[198:201], v[120:123]
	v_mfma_f32_16x16x32_bf16 v[76:79], v[166:169], v[198:201], v[76:79]
	v_mfma_f32_16x16x32_bf16 v[132:135], v[104:107], v[178:181], v[132:135]
	v_mfma_f32_16x16x32_bf16 v[92:95], v[170:173], v[178:181], v[92:95]
	v_mfma_f32_16x16x32_bf16 v[128:131], v[104:107], v[186:189], v[128:131]
	v_mfma_f32_16x16x32_bf16 v[84:87], v[170:173], v[186:189], v[84:87]
	v_mfma_f32_16x16x32_bf16 v[124:127], v[104:107], v[194:197], v[124:127]
	v_mfma_f32_16x16x32_bf16 v[80:83], v[170:173], v[194:197], v[80:83]
	v_mfma_f32_16x16x32_bf16 v[120:123], v[104:107], v[202:205], v[120:123]
	v_mfma_f32_16x16x32_bf16 v[76:79], v[170:173], v[202:205], v[76:79]
	s_setprio 0
	s_barrier
; #define PG8_STAGE(bufoff, gbase, o0, o1) do { \
;         __builtin_amdgcn_global_load_lds((const unsigned*)((const char*)(gbase) + (o0)), (LAS unsigned*)(lds + (bufoff) + ldsw), 16, 0, 0); \
;         __builtin_amdgcn_global_load_lds((const unsigned*)((const char*)(gbase) + (o1)), (LAS unsigned*)(lds + (bufoff) + ldsw + 8192), 16, 0, 0); } while (0)
; #define PG8_LDA(dst, b, h) do { _Pragma("unroll") for (int m = 0; m < 4; ++m) _Pragma("unroll") for (int k = 0; k < 2; ++k) dst[m][k] = *(const LAS bf16x8*)(lds + PG8_SA(b, h) + aoff + m * 2048 + k * 1024); } while (0)
; #define PG8_LDB(dst, b, h) do { _Pragma("unroll") for (int n = 0; n < 2; ++n) _Pragma("unroll") for (int k = 0; k < 2; ++k) dst[n][k] = *(const LAS bf16x8*)(lds + PG8_SB(b, h) + boff + n * 2048 + k * 1024); } while (0)
; template <class Epi, class Sched, class Prob>
; __device__ __forceinline__ void gemm_phase(LAS unsigned char* lds, LAS unsigned char* lds_epi, const Prob g, const Sched& S, const Epi& E, int wid) {
;     ...
;         for (int t = 0; t < nt; t += 2) {
;             const bool last = (t == nt - 2);
;             const char* a1 = cA + (size_t)(t + 1) * kstep;
;             const char* a2 = last ? nA : cA + (size_t)(t + 2) * kstep; const char* b2 = last ? nB : cB + (size_t)(t + 2) * kstep;
;             const char* a3 = a2 + kstep; const char* b3 = b2 + kstep;
;             PG8_LDB(B0, 0, 0); PG8_LDB(B1, 0, 1); PG8_SCHED; PG8_LDA(At, 0, 0); PG8_STAGE(PG8_SA(1, 1), a1, cA10, cA11);
;             PG8_WAIT_V(8); PG8_WAIT_L(0); PG8_BAR; PG8_MMA(0, 0, At, B0); PG8_MMA(0, 1, At, B1); PG8_BAR; PG8_SCHED;
;             PG8_LDA(At, 0, 1); PG8_STAGE(PG8_SB(0, 0), b2, vB0, vB1); PG8_STAGE(PG8_SB(0, 1), b2 + hstepB, vB0, vB1); PG8_STAGE(PG8_SA(0, 0), a2, cA00, cA01);
;             PG8_WAIT_V(8); PG8_WAIT_L(0); PG8_BAR; PG8_MMA(1, 0, At, B0); PG8_MMA(1, 1, At, B1); PG8_BAR; PG8_SCHED;
;             PG8_LDB(B0, 1, 0); PG8_LDB(B1, 1, 1); PG8_SCHED; PG8_LDA(At, 1, 0); PG8_STAGE(PG8_SA(0, 1), a2, cA10, cA11);
;             PG8_WAIT_V(8); PG8_WAIT_L(0); PG8_BAR; PG8_MMA(0, 0, At, B0); PG8_MMA(0, 1, At, B1); PG8_BAR; PG8_SCHED;
;             PG8_LDA(At, 1, 1); PG8_STAGE(PG8_SB(1, 0), b3, vB0, vB1); PG8_STAGE(PG8_SB(1, 1), b3 + hstepB, vB0, vB1); PG8_STAGE(PG8_SA(1, 0), a3, cA00, cA01);
;             PG8_WAIT_V(8); PG8_WAIT_L(0); PG8_BAR; PG8_MMA(1, 0, At, B0); PG8_MMA(1, 1, At, B1); PG8_BAR; PG8_SCHED;
	s_mov_b32 m0, s31
	v_lshl_add_u64 v[206:207], v[206:207], 0, s[54:55]
	ds_read_b128 v[174:177], v223 offset:49152
	ds_read_b128 v[178:181], v223 offset:50176
	ds_read_b128 v[182:185], v223 offset:51200
	ds_read_b128 v[186:189], v223 offset:52224
	ds_read_b128 v[190:193], v223 offset:53248
	ds_read_b128 v[194:197], v223 offset:54272
	ds_read_b128 v[198:201], v223 offset:55296
	ds_read_b128 v[202:205], v223 offset:56320
	global_load_lds_dwordx4 v[206:207], off
	v_lshl_add_u64 v[206:207], v[208:209], 0, s[54:55]
	s_mov_b32 m0, s29
	s_nop 0
	global_load_lds_dwordx4 v[206:207], off
	v_lshl_add_u64 v[206:207], s[12:13], 0, v[152:153]
	s_mov_b32 m0, s30
	s_nop 0
	global_load_lds_dwordx4 v[206:207], off
	v_lshl_add_u64 v[206:207], s[12:13], 0, v[154:155]
	s_mov_b32 m0, s28
	s_nop 0
	global_load_lds_dwordx4 v[206:207], off
	v_lshl_add_u64 v[206:207], v[210:211], 0, s[54:55]
	s_mov_b32 m0, s83
	s_nop 0
	global_load_lds_dwordx4 v[206:207], off
	v_lshl_add_u64 v[206:207], v[212:213], 0, s[54:55]
	s_mov_b32 m0, s84
	s_nop 0
	global_load_lds_dwordx4 v[206:207], off
	s_waitcnt vmcnt(8)
	s_waitcnt lgkmcnt(0)
	s_barrier
	s_setprio 1
	s_waitcnt lgkmcnt(0)
	v_mfma_f32_16x16x32_bf16 v[64:67], v[56:59], v[174:177], v[64:67]
	v_mfma_f32_16x16x32_bf16 v[28:31], v[72:75], v[174:177], v[28:31]
	v_mfma_f32_16x16x32_bf16 v[60:63], v[56:59], v[182:185], v[60:63]
	v_mfma_f32_16x16x32_bf16 v[24:27], v[72:75], v[182:185], v[24:27]
	v_mfma_f32_16x16x32_bf16 v[52:55], v[56:59], v[190:193], v[52:55]
	v_mfma_f32_16x16x32_bf16 v[20:23], v[72:75], v[190:193], v[20:23]
	v_mfma_f32_16x16x32_bf16 v[48:51], v[56:59], v[198:201], v[48:51]
	v_mfma_f32_16x16x32_bf16 v[16:19], v[72:75], v[198:201], v[16:19]
	v_mfma_f32_16x16x32_bf16 v[64:67], v[68:71], v[178:181], v[64:67]
	v_mfma_f32_16x16x32_bf16 v[28:31], v[88:91], v[178:181], v[28:31]
	v_mfma_f32_16x16x32_bf16 v[60:63], v[68:71], v[186:189], v[60:63]
	v_mfma_f32_16x16x32_bf16 v[24:27], v[88:91], v[186:189], v[24:27]
	v_mfma_f32_16x16x32_bf16 v[52:55], v[68:71], v[194:197], v[52:55]
	v_mfma_f32_16x16x32_bf16 v[20:23], v[88:91], v[194:197], v[20:23]
	v_mfma_f32_16x16x32_bf16 v[48:51], v[68:71], v[202:205], v[48:51]
	v_mfma_f32_16x16x32_bf16 v[16:19], v[88:91], v[202:205], v[16:19]
	v_mfma_f32_16x16x32_bf16 v[44:47], v[100:103], v[174:177], v[44:47]
	v_mfma_f32_16x16x32_bf16 v[12:15], v[166:169], v[174:177], v[12:15]
	v_mfma_f32_16x16x32_bf16 v[40:43], v[100:103], v[182:185], v[40:43]
	v_mfma_f32_16x16x32_bf16 v[8:11], v[166:169], v[182:185], v[8:11]
	v_mfma_f32_16x16x32_bf16 v[36:39], v[100:103], v[190:193], v[36:39]
	v_mfma_f32_16x16x32_bf16 v[4:7], v[166:169], v[190:193], v[4:7]
	v_mfma_f32_16x16x32_bf16 v[32:35], v[100:103], v[198:201], v[32:35]
	v_mfma_f32_16x16x32_bf16 v[0:3], v[166:169], v[198:201], v[0:3]
	v_mfma_f32_16x16x32_bf16 v[44:47], v[104:107], v[178:181], v[44:47]
	v_mfma_f32_16x16x32_bf16 v[12:15], v[170:173], v[178:181], v[12:15]
	v_mfma_f32_16x16x32_bf16 v[40:43], v[104:107], v[186:189], v[40:43]
	v_mfma_f32_16x16x32_bf16 v[8:11], v[170:173], v[186:189], v[8:11]
	v_mfma_f32_16x16x32_bf16 v[36:39], v[104:107], v[194:197], v[36:39]
	v_mfma_f32_16x16x32_bf16 v[4:7], v[170:173], v[194:197], v[4:7]
	v_mfma_f32_16x16x32_bf16 v[32:35], v[104:107], v[202:205], v[32:35]
	v_mfma_f32_16x16x32_bf16 v[0:3], v[170:173], v[202:205], v[0:3]
	s_setprio 0
	s_barrier
	s_mov_b64 s[20:21], 0
	s_mov_b64 s[12:13], -1
	s_mov_b64 s[14:15], 0x100
.LBB0_1595:
	s_add_u32 s24, s8, s14
	s_addc_u32 s25, s9, s15
	s_add_u32 s22, s24, 0x100
	s_addc_u32 s23, s25, 0
	v_cndmask_b32_e64 v56, 0, 1, s[20:21]
	s_and_b64 s[20:21], s[12:13], exec
	s_cselect_b32 s20, s19, s22
	s_cselect_b32 s21, s17, s23
	s_add_u32 s14, s10, s14
	s_addc_u32 s15, s11, s15
	s_add_u32 s14, s14, 0x100
	v_cmp_ne_u32_e32 vcc, 1, v56
	ds_read_b128 v[56:59], v221
	ds_read_b128 v[68:71], v221 offset:1024
	ds_read_b128 v[72:75], v221 offset:2048
	ds_read_b128 v[88:91], v221 offset:3072
	ds_read_b128 v[100:103], v222
	ds_read_b128 v[104:107], v222 offset:1024
	ds_read_b128 v[166:169], v222 offset:2048
	ds_read_b128 v[170:173], v222 offset:3072
	s_addc_u32 s15, s15, 0
	s_and_b64 s[12:13], s[12:13], exec
	s_cselect_b32 s15, s26, s15
	s_cselect_b32 s14, s27, s14
	s_add_i32 s65, s85, s97
	s_add_i32 m0, s77, 0xc000
	s_add_i32 s72, s77, 0xe000
	s_add_i32 s36, s65, 0x2000
	s_add_u32 s22, s14, 0x10000
	s_addc_u32 s23, s15, 0
	s_add_i32 s35, 0, 0x18000
	s_add_i32 s63, s86, s97
	s_add_i32 s31, s35, s97
	s_add_i32 s37, s63, 0x2000
	s_add_i32 s34, 0, 0x1c000
	s_add_i32 s29, s31, 0x2000
	s_add_u32 s12, s14, 0x10080
	s_addc_u32 s13, s15, 0
	s_add_i32 s30, s34, s97
	s_add_i32 s28, s30, 0x2000
	v_lshl_add_u64 v[206:207], s[24:25], 0, v[158:159]
	v_lshl_add_u64 v[206:207], v[206:207], 0, s[54:55]
	ds_read_b128 v[174:177], v223
	ds_read_b128 v[178:181], v223 offset:1024
	ds_read_b128 v[182:185], v223 offset:2048
	ds_read_b128 v[186:189], v223 offset:3072
	ds_read_b128 v[190:193], v223 offset:4096
	ds_read_b128 v[194:197], v223 offset:5120
	ds_read_b128 v[198:201], v223 offset:6144
	ds_read_b128 v[202:205], v223 offset:7168
	global_load_lds_dwordx4 v[206:207], off
	v_lshl_add_u64 v[206:207], s[24:25], 0, v[162:163]
	v_lshl_add_u64 v[206:207], v[206:207], 0, s[54:55]
	s_mov_b32 m0, s72
	s_nop 0
	global_load_lds_dwordx4 v[206:207], off
	s_waitcnt vmcnt(8)
	s_waitcnt lgkmcnt(0)
	s_barrier
; #define PG8_STAGE(bufoff, gbase, o0, o1) do { \
;         __builtin_amdgcn_global_load_lds((const unsigned*)((const char*)(gbase) + (o0)), (LAS unsigned*)(lds + (bufoff) + ldsw), 16, 0, 0); \
;         __builtin_amdgcn_global_load_lds((const unsigned*)((const char*)(gbase) + (o1)), (LAS unsigned*)(lds + (bufoff) + ldsw + 8192), 16, 0, 0); } while (0)
; #define PG8_LDA(dst, b, h) do { _Pragma("unroll") for (int m = 0; m < 4; ++m) _Pragma("unroll") for (int k = 0; k < 2; ++k) dst[m][k] = *(const LAS bf16x8*)(lds + PG8_SA(b, h) + aoff + m * 2048 + k * 1024); } while (0)
; #define PG8_LDB(dst, b, h) do { _Pragma("unroll") for (int n = 0; n < 2; ++n) _Pragma("unroll") for (int k = 0; k < 2; ++k) dst[n][k] = *(const LAS bf16x8*)(lds + PG8_SB(b, h) + boff + n * 2048 + k * 1024); } while (0)
; #define PG8_WAIT_V(n) asm volatile("s_waitcnt vmcnt(" #n ")" ::: "memory")
; #define PG8_WAIT_L(n) asm volatile("s_waitcnt lgkmcnt(" #n ")" ::: "memory")
; #define PG8_BAR __builtin_amdgcn_s_barrier()
; #define PG8_SCHED __builtin_amdgcn_sched_barrier(0)
; template <class Epi, class Sched, class Prob>
; __device__ __forceinline__ void gemm_phase(LAS unsigned char* lds, LAS unsigned char* lds_epi, const Prob g, const Sched& S, const Epi& E, int wid) {
;     ...
;             PG8_LDB(B0, 0, 0); PG8_LDB(B1, 0, 1); PG8_SCHED; PG8_LDA(At, 0, 0); PG8_STAGE(PG8_SA(1, 1), a1, cA10, cA11);
;             PG8_WAIT_V(8); PG8_WAIT_L(0); PG8_BAR; PG8_MMA(0, 0, At, B0); PG8_MMA(0, 1, At, B1); PG8_BAR; PG8_SCHED;
;             PG8_LDA(At, 0, 1); PG8_STAGE(PG8_SB(0, 0), b2, vB0, vB1); PG8_STAGE(PG8_SB(0, 1), b2 + hstepB, vB0, vB1); PG8_STAGE(PG8_SA(0, 0), a2, cA00, cA01);
;             PG8_WAIT_V(8); PG8_WAIT_L(0); PG8_BAR; PG8_MMA(1, 0, At, B0); PG8_MMA(1, 1, At, B1); PG8_BAR; PG8_SCHED;
	s_setprio 1
	s_waitcnt lgkmcnt(0)
	v_mfma_f32_16x16x32_bf16 v[148:151], v[56:59], v[174:177], v[148:151]
	v_mfma_f32_16x16x32_bf16 v[116:119], v[72:75], v[174:177], v[116:119]
	v_mfma_f32_16x16x32_bf16 v[144:147], v[56:59], v[182:185], v[144:147]
	v_mfma_f32_16x16x32_bf16 v[112:115], v[72:75], v[182:185], v[112:115]
	v_mfma_f32_16x16x32_bf16 v[140:143], v[56:59], v[190:193], v[140:143]
	v_mfma_f32_16x16x32_bf16 v[108:111], v[72:75], v[190:193], v[108:111]
	v_mfma_f32_16x16x32_bf16 v[136:139], v[56:59], v[198:201], v[136:139]
	v_mfma_f32_16x16x32_bf16 v[96:99], v[72:75], v[198:201], v[96:99]
	v_mfma_f32_16x16x32_bf16 v[148:151], v[68:71], v[178:181], v[148:151]
	v_mfma_f32_16x16x32_bf16 v[116:119], v[88:91], v[178:181], v[116:119]
	v_mfma_f32_16x16x32_bf16 v[144:147], v[68:71], v[186:189], v[144:147]
	v_mfma_f32_16x16x32_bf16 v[112:115], v[88:91], v[186:189], v[112:115]
	v_mfma_f32_16x16x32_bf16 v[140:143], v[68:71], v[194:197], v[140:143]
	v_mfma_f32_16x16x32_bf16 v[108:111], v[88:91], v[194:197], v[108:111]
	v_mfma_f32_16x16x32_bf16 v[136:139], v[68:71], v[202:205], v[136:139]
	v_mfma_f32_16x16x32_bf16 v[96:99], v[88:91], v[202:205], v[96:99]
	v_mfma_f32_16x16x32_bf16 v[132:135], v[100:103], v[174:177], v[132:135]
	v_mfma_f32_16x16x32_bf16 v[92:95], v[166:169], v[174:177], v[92:95]
	v_mfma_f32_16x16x32_bf16 v[128:131], v[100:103], v[182:185], v[128:131]
	v_mfma_f32_16x16x32_bf16 v[84:87], v[166:169], v[182:185], v[84:87]
	v_mfma_f32_16x16x32_bf16 v[124:127], v[100:103], v[190:193], v[124:127]
	v_mfma_f32_16x16x32_bf16 v[80:83], v[166:169], v[190:193], v[80:83]
	v_mfma_f32_16x16x32_bf16 v[120:123], v[100:103], v[198:201], v[120:123]
	v_mfma_f32_16x16x32_bf16 v[76:79], v[166:169], v[198:201], v[76:79]
	v_mfma_f32_16x16x32_bf16 v[132:135], v[104:107], v[178:181], v[132:135]
	v_mfma_f32_16x16x32_bf16 v[92:95], v[170:173], v[178:181], v[92:95]
	v_mfma_f32_16x16x32_bf16 v[128:131], v[104:107], v[186:189], v[128:131]
	v_mfma_f32_16x16x32_bf16 v[84:87], v[170:173], v[186:189], v[84:87]
	v_mfma_f32_16x16x32_bf16 v[124:127], v[104:107], v[194:197], v[124:127]
	v_mfma_f32_16x16x32_bf16 v[80:83], v[170:173], v[194:197], v[80:83]
	v_mfma_f32_16x16x32_bf16 v[120:123], v[104:107], v[202:205], v[120:123]
	v_mfma_f32_16x16x32_bf16 v[76:79], v[170:173], v[202:205], v[76:79]
	s_setprio 0
	s_barrier
	s_mov_b32 m0, s65
	v_lshl_add_u64 v[206:207], s[14:15], 0, v[152:153]
	ds_read_b128 v[174:177], v223 offset:16384
	ds_read_b128 v[178:181], v223 offset:17408
	ds_read_b128 v[182:185], v223 offset:18432
	ds_read_b128 v[186:189], v223 offset:19456
	ds_read_b128 v[190:193], v223 offset:20480
	ds_read_b128 v[194:197], v223 offset:21504
	ds_read_b128 v[198:201], v223 offset:22528
	ds_read_b128 v[202:205], v223 offset:23552
	global_load_lds_dwordx4 v[206:207], off
	v_lshl_add_u64 v[208:209], s[14:15], 0, v[154:155]
	s_mov_b32 m0, s36
	v_lshl_add_u64 v[210:211], s[22:23], 0, v[152:153]
	global_load_lds_dwordx4 v[208:209], off
	s_mov_b32 m0, s63
	v_lshl_add_u64 v[212:213], s[20:21], 0, v[160:161]
	global_load_lds_dwordx4 v[210:211], off
	v_lshl_add_u64 v[210:211], s[22:23], 0, v[154:155]
	s_mov_b32 m0, s37
	s_nop 0
	global_load_lds_dwordx4 v[210:211], off
	v_lshl_add_u64 v[210:211], s[20:21], 0, v[156:157]
	s_mov_b32 m0, s77
	s_nop 0
	global_load_lds_dwordx4 v[210:211], off
	s_mov_b32 m0, s78
	s_nop 0
	global_load_lds_dwordx4 v[212:213], off
	s_waitcnt vmcnt(8)
	s_waitcnt lgkmcnt(0)
	s_barrier
	s_setprio 1
	s_waitcnt lgkmcnt(0)
	v_mfma_f32_16x16x32_bf16 v[64:67], v[56:59], v[174:177], v[64:67]
	v_mfma_f32_16x16x32_bf16 v[28:31], v[72:75], v[174:177], v[28:31]
	v_mfma_f32_16x16x32_bf16 v[60:63], v[56:59], v[182:185], v[60:63]
	v_mfma_f32_16x16x32_bf16 v[24:27], v[72:75], v[182:185], v[24:27]
	v_mfma_f32_16x16x32_bf16 v[52:55], v[56:59], v[190:193], v[52:55]
	v_mfma_f32_16x16x32_bf16 v[20:23], v[72:75], v[190:193], v[20:23]
	v_mfma_f32_16x16x32_bf16 v[48:51], v[56:59], v[198:201], v[48:51]
	v_mfma_f32_16x16x32_bf16 v[16:19], v[72:75], v[198:201], v[16:19]
	v_mfma_f32_16x16x32_bf16 v[64:67], v[68:71], v[178:181], v[64:67]
	v_mfma_f32_16x16x32_bf16 v[28:31], v[88:91], v[178:181], v[28:31]
	v_mfma_f32_16x16x32_bf16 v[60:63], v[68:71], v[186:189], v[60:63]
	v_mfma_f32_16x16x32_bf16 v[24:27], v[88:91], v[186:189], v[24:27]
	v_mfma_f32_16x16x32_bf16 v[52:55], v[68:71], v[194:197], v[52:55]
	v_mfma_f32_16x16x32_bf16 v[20:23], v[88:91], v[194:197], v[20:23]
	v_mfma_f32_16x16x32_bf16 v[48:51], v[68:71], v[202:205], v[48:51]
	v_mfma_f32_16x16x32_bf16 v[16:19], v[88:91], v[202:205], v[16:19]
	v_mfma_f32_16x16x32_bf16 v[44:47], v[100:103], v[174:177], v[44:47]
	v_mfma_f32_16x16x32_bf16 v[12:15], v[166:169], v[174:177], v[12:15]
	v_mfma_f32_16x16x32_bf16 v[40:43], v[100:103], v[182:185], v[40:43]
	v_mfma_f32_16x16x32_bf16 v[8:11], v[166:169], v[182:185], v[8:11]
	v_mfma_f32_16x16x32_bf16 v[36:39], v[100:103], v[190:193], v[36:39]
	v_mfma_f32_16x16x32_bf16 v[4:7], v[166:169], v[190:193], v[4:7]
	v_mfma_f32_16x16x32_bf16 v[32:35], v[100:103], v[198:201], v[32:35]
	v_mfma_f32_16x16x32_bf16 v[0:3], v[166:169], v[198:201], v[0:3]
	v_mfma_f32_16x16x32_bf16 v[44:47], v[104:107], v[178:181], v[44:47]
	v_mfma_f32_16x16x32_bf16 v[12:15], v[170:173], v[178:181], v[12:15]
	v_mfma_f32_16x16x32_bf16 v[40:43], v[104:107], v[186:189], v[40:43]
	v_mfma_f32_16x16x32_bf16 v[8:11], v[170:173], v[186:189], v[8:11]
	v_mfma_f32_16x16x32_bf16 v[36:39], v[104:107], v[194:197], v[36:39]
	v_mfma_f32_16x16x32_bf16 v[4:7], v[170:173], v[194:197], v[4:7]
	v_mfma_f32_16x16x32_bf16 v[32:35], v[104:107], v[202:205], v[32:35]
	v_mfma_f32_16x16x32_bf16 v[0:3], v[170:173], v[202:205], v[0:3]
	s_setprio 0
	s_barrier
; #define PG8_STAGE(bufoff, gbase, o0, o1) do { \
;         __builtin_amdgcn_global_load_lds((const unsigned*)((const char*)(gbase) + (o0)), (LAS unsigned*)(lds + (bufoff) + ldsw), 16, 0, 0); \
;         __builtin_amdgcn_global_load_lds((const unsigned*)((const char*)(gbase) + (o1)), (LAS unsigned*)(lds + (bufoff) + ldsw + 8192), 16, 0, 0); } while (0)
; #define PG8_LDA(dst, b, h) do { _Pragma("unroll") for (int m = 0; m < 4; ++m) _Pragma("unroll") for (int k = 0; k < 2; ++k) dst[m][k] = *(const LAS bf16x8*)(lds + PG8_SA(b, h) + aoff + m * 2048 + k * 1024); } while (0)
; #define PG8_LDB(dst, b, h) do { _Pragma("unroll") for (int n = 0; n < 2; ++n) _Pragma("unroll") for (int k = 0; k < 2; ++k) dst[n][k] = *(const LAS bf16x8*)(lds + PG8_SB(b, h) + boff + n * 2048 + k * 1024); } while (0)
; #define PG8_WAIT_V(n) asm volatile("s_waitcnt vmcnt(" #n ")" ::: "memory")
; #define PG8_WAIT_L(n) asm volatile("s_waitcnt lgkmcnt(" #n ")" ::: "memory")
; #define PG8_BAR __builtin_amdgcn_s_barrier()
; #define PG8_SCHED __builtin_amdgcn_sched_barrier(0)
; template <class Epi, class Sched, class Prob>
; __device__ __forceinline__ void gemm_phase(LAS unsigned char* lds, LAS unsigned char* lds_epi, const Prob g, const Sched& S, const Epi& E, int wid) {
;     ...
;             PG8_LDB(B0, 1, 0); PG8_LDB(B1, 1, 1); PG8_SCHED; PG8_LDA(At, 1, 0); PG8_STAGE(PG8_SA(0, 1), a2, cA10, cA11);
;             PG8_WAIT_V(8); PG8_WAIT_L(0); PG8_BAR; PG8_MMA(0, 0, At, B0); PG8_MMA(0, 1, At, B1); PG8_BAR; PG8_SCHED;
;             PG8_LDA(At, 1, 1); PG8_STAGE(PG8_SB(1, 0), b3, vB0, vB1); PG8_STAGE(PG8_SB(1, 1), b3 + hstepB, vB0, vB1); PG8_STAGE(PG8_SA(1, 0), a3, cA00, cA01);
;             PG8_WAIT_V(8); PG8_WAIT_L(0); PG8_BAR; PG8_MMA(1, 0, At, B0); PG8_MMA(1, 1, At, B1); PG8_BAR; PG8_SCHED;
;         }
;         if constexpr (Prob::FP8) asm volatile("s_nop 7\n\ts_nop 7\n\ts_nop 7" ::: "memory");
;         if (wr == 0) PG8_BAR;
	v_add_u32_e32 v88, s35, v220
	v_add_u32_e32 v170, s34, v220
	ds_read_b128 v[56:59], v88
	ds_read_b128 v[68:71], v88 offset:1024
	ds_read_b128 v[72:75], v88 offset:2048
	ds_read_b128 v[88:91], v88 offset:3072
	ds_read_b128 v[100:103], v170
	ds_read_b128 v[104:107], v170 offset:1024
	ds_read_b128 v[166:169], v170 offset:2048
	ds_read_b128 v[170:173], v170 offset:3072
	s_mov_b32 m0, s79
	v_lshl_add_u64 v[214:215], s[20:21], 0, v[158:159]
	ds_read_b128 v[174:177], v223 offset:32768
	ds_read_b128 v[178:181], v223 offset:33792
	ds_read_b128 v[182:185], v223 offset:34816
	ds_read_b128 v[186:189], v223 offset:35840
	ds_read_b128 v[190:193], v223 offset:36864
	ds_read_b128 v[194:197], v223 offset:37888
	ds_read_b128 v[198:201], v223 offset:38912
	ds_read_b128 v[202:205], v223 offset:39936
	global_load_lds_dwordx4 v[214:215], off
	v_lshl_add_u64 v[214:215], s[20:21], 0, v[162:163]
	s_mov_b32 m0, s80
	s_nop 0
	global_load_lds_dwordx4 v[214:215], off
	s_waitcnt vmcnt(8)
	s_waitcnt lgkmcnt(0)
	s_barrier
	s_setprio 1
	s_waitcnt lgkmcnt(0)
	v_mfma_f32_16x16x32_bf16 v[148:151], v[56:59], v[174:177], v[148:151]
	v_mfma_f32_16x16x32_bf16 v[116:119], v[72:75], v[174:177], v[116:119]
	v_mfma_f32_16x16x32_bf16 v[144:147], v[56:59], v[182:185], v[144:147]
	v_mfma_f32_16x16x32_bf16 v[112:115], v[72:75], v[182:185], v[112:115]
	v_mfma_f32_16x16x32_bf16 v[140:143], v[56:59], v[190:193], v[140:143]
	v_mfma_f32_16x16x32_bf16 v[108:111], v[72:75], v[190:193], v[108:111]
	v_mfma_f32_16x16x32_bf16 v[136:139], v[56:59], v[198:201], v[136:139]
	v_mfma_f32_16x16x32_bf16 v[96:99], v[72:75], v[198:201], v[96:99]
	v_mfma_f32_16x16x32_bf16 v[148:151], v[68:71], v[178:181], v[148:151]
	v_mfma_f32_16x16x32_bf16 v[116:119], v[88:91], v[178:181], v[116:119]
	v_mfma_f32_16x16x32_bf16 v[144:147], v[68:71], v[186:189], v[144:147]
	v_mfma_f32_16x16x32_bf16 v[112:115], v[88:91], v[186:189], v[112:115]
	v_mfma_f32_16x16x32_bf16 v[140:143], v[68:71], v[194:197], v[140:143]
	v_mfma_f32_16x16x32_bf16 v[108:111], v[88:91], v[194:197], v[108:111]
	v_mfma_f32_16x16x32_bf16 v[136:139], v[68:71], v[202:205], v[136:139]
	v_mfma_f32_16x16x32_bf16 v[96:99], v[88:91], v[202:205], v[96:99]
	v_mfma_f32_16x16x32_bf16 v[132:135], v[100:103], v[174:177], v[132:135]
	v_mfma_f32_16x16x32_bf16 v[92:95], v[166:169], v[174:177], v[92:95]
	v_mfma_f32_16x16x32_bf16 v[128:131], v[100:103], v[182:185], v[128:131]
	v_mfma_f32_16x16x32_bf16 v[84:87], v[166:169], v[182:185], v[84:87]
	v_mfma_f32_16x16x32_bf16 v[124:127], v[100:103], v[190:193], v[124:127]
	v_mfma_f32_16x16x32_bf16 v[80:83], v[166:169], v[190:193], v[80:83]
	v_mfma_f32_16x16x32_bf16 v[120:123], v[100:103], v[198:201], v[120:123]
	v_mfma_f32_16x16x32_bf16 v[76:79], v[166:169], v[198:201], v[76:79]
	v_mfma_f32_16x16x32_bf16 v[132:135], v[104:107], v[178:181], v[132:135]
	v_mfma_f32_16x16x32_bf16 v[92:95], v[170:173], v[178:181], v[92:95]
	v_mfma_f32_16x16x32_bf16 v[128:131], v[104:107], v[186:189], v[128:131]
	v_mfma_f32_16x16x32_bf16 v[84:87], v[170:173], v[186:189], v[84:87]
	v_mfma_f32_16x16x32_bf16 v[124:127], v[104:107], v[194:197], v[124:127]
	v_mfma_f32_16x16x32_bf16 v[80:83], v[170:173], v[194:197], v[80:83]
	v_mfma_f32_16x16x32_bf16 v[120:123], v[104:107], v[202:205], v[120:123]
	v_mfma_f32_16x16x32_bf16 v[76:79], v[170:173], v[202:205], v[76:79]
	s_setprio 0
	s_barrier
	s_mov_b32 m0, s31
	v_lshl_add_u64 v[206:207], v[206:207], 0, s[54:55]
	ds_read_b128 v[174:177], v223 offset:49152
	ds_read_b128 v[178:181], v223 offset:50176
	ds_read_b128 v[182:185], v223 offset:51200
	ds_read_b128 v[186:189], v223 offset:52224
	ds_read_b128 v[190:193], v223 offset:53248
	ds_read_b128 v[194:197], v223 offset:54272
	ds_read_b128 v[198:201], v223 offset:55296
	ds_read_b128 v[202:205], v223 offset:56320
	global_load_lds_dwordx4 v[206:207], off
	v_lshl_add_u64 v[206:207], v[208:209], 0, s[54:55]
	s_mov_b32 m0, s29
	s_nop 0
	global_load_lds_dwordx4 v[206:207], off
	v_lshl_add_u64 v[206:207], s[12:13], 0, v[152:153]
	s_mov_b32 m0, s30
	s_nop 0
	global_load_lds_dwordx4 v[206:207], off
	v_lshl_add_u64 v[206:207], s[12:13], 0, v[154:155]
	s_mov_b32 m0, s28
	s_nop 0
	global_load_lds_dwordx4 v[206:207], off
	v_lshl_add_u64 v[206:207], v[210:211], 0, s[54:55]
	s_mov_b32 m0, s83
	s_nop 0
	global_load_lds_dwordx4 v[206:207], off
	v_lshl_add_u64 v[206:207], v[212:213], 0, s[54:55]
	s_mov_b32 m0, s84
	s_nop 0
	global_load_lds_dwordx4 v[206:207], off
	s_waitcnt vmcnt(8)
	s_waitcnt lgkmcnt(0)
	s_barrier
	s_setprio 1
	s_waitcnt lgkmcnt(0)
	v_mfma_f32_16x16x32_bf16 v[64:67], v[56:59], v[174:177], v[64:67]
	v_mfma_f32_16x16x32_bf16 v[28:31], v[72:75], v[174:177], v[28:31]
	v_mfma_f32_16x16x32_bf16 v[60:63], v[56:59], v[182:185], v[60:63]
	v_mfma_f32_16x16x32_bf16 v[24:27], v[72:75], v[182:185], v[24:27]
	v_mfma_f32_16x16x32_bf16 v[52:55], v[56:59], v[190:193], v[52:55]
	v_mfma_f32_16x16x32_bf16 v[20:23], v[72:75], v[190:193], v[20:23]
	v_mfma_f32_16x16x32_bf16 v[48:51], v[56:59], v[198:201], v[48:51]
	v_mfma_f32_16x16x32_bf16 v[16:19], v[72:75], v[198:201], v[16:19]
	v_mfma_f32_16x16x32_bf16 v[64:67], v[68:71], v[178:181], v[64:67]
	v_mfma_f32_16x16x32_bf16 v[28:31], v[88:91], v[178:181], v[28:31]
	v_mfma_f32_16x16x32_bf16 v[60:63], v[68:71], v[186:189], v[60:63]
	v_mfma_f32_16x16x32_bf16 v[24:27], v[88:91], v[186:189], v[24:27]
	v_mfma_f32_16x16x32_bf16 v[52:55], v[68:71], v[194:197], v[52:55]
	v_mfma_f32_16x16x32_bf16 v[20:23], v[88:91], v[194:197], v[20:23]
	v_mfma_f32_16x16x32_bf16 v[48:51], v[68:71], v[202:205], v[48:51]
	v_mfma_f32_16x16x32_bf16 v[16:19], v[88:91], v[202:205], v[16:19]
	v_mfma_f32_16x16x32_bf16 v[44:47], v[100:103], v[174:177], v[44:47]
	v_mfma_f32_16x16x32_bf16 v[12:15], v[166:169], v[174:177], v[12:15]
	v_mfma_f32_16x16x32_bf16 v[40:43], v[100:103], v[182:185], v[40:43]
	v_mfma_f32_16x16x32_bf16 v[8:11], v[166:169], v[182:185], v[8:11]
	v_mfma_f32_16x16x32_bf16 v[36:39], v[100:103], v[190:193], v[36:39]
	v_mfma_f32_16x16x32_bf16 v[4:7], v[166:169], v[190:193], v[4:7]
	v_mfma_f32_16x16x32_bf16 v[32:35], v[100:103], v[198:201], v[32:35]
	v_mfma_f32_16x16x32_bf16 v[0:3], v[166:169], v[198:201], v[0:3]
	v_mfma_f32_16x16x32_bf16 v[44:47], v[104:107], v[178:181], v[44:47]
	v_mfma_f32_16x16x32_bf16 v[12:15], v[170:173], v[178:181], v[12:15]
	v_mfma_f32_16x16x32_bf16 v[40:43], v[104:107], v[186:189], v[40:43]
	v_mfma_f32_16x16x32_bf16 v[8:11], v[170:173], v[186:189], v[8:11]
	v_mfma_f32_16x16x32_bf16 v[36:39], v[104:107], v[194:197], v[36:39]
	v_mfma_f32_16x16x32_bf16 v[4:7], v[170:173], v[194:197], v[4:7]
	v_mfma_f32_16x16x32_bf16 v[32:35], v[104:107], v[202:205], v[32:35]
	v_mfma_f32_16x16x32_bf16 v[0:3], v[170:173], v[202:205], v[0:3]
	s_setprio 0
	s_barrier
	s_mov_b64 s[20:21], 0
	s_mov_b64 s[12:13], -1
	s_mov_b64 s[14:15], 0x100
	s_cbranch_vccz .LBB0_1595
	v_readlane_b32 s8, v254, 27
	v_readlane_b32 s9, v254, 28
	s_and_b64 vcc, exec, s[8:9]
	s_cbranch_vccz .LBB0_1598
	s_barrier

; #define PG8_STAGE(bufoff, gbase, o0, o1) do { \
;         __builtin_amdgcn_global_load_lds((const unsigned*)((const char*)(gbase) + (o0)), (LAS unsigned*)(lds + (bufoff) + ldsw), 16, 0, 0); \
;         __builtin_amdgcn_global_load_lds((const unsigned*)((const char*)(gbase) + (o1)), (LAS unsigned*)(lds + (bufoff) + ldsw + 8192), 16, 0, 0); } while (0)
; #define PG8_LDA(dst, b, h) do { _Pragma("unroll") for (int m = 0; m < 4; ++m) _Pragma("unroll") for (int k = 0; k < 2; ++k) dst[m][k] = *(const LAS bf16x8*)(lds + PG8_SA(b, h) + aoff + m * 2048 + k * 1024); } while (0)
; #define PG8_LDB(dst, b, h) do { _Pragma("unroll") for (int n = 0; n < 2; ++n) _Pragma("unroll") for (int k = 0; k < 2; ++k) dst[n][k] = *(const LAS bf16x8*)(lds + PG8_SB(b, h) + boff + n * 2048 + k * 1024); } while (0)
; #define PG8_WAIT_V(n) asm volatile("s_waitcnt vmcnt(" #n ")" ::: "memory")
; #define PG8_WAIT_L(n) asm volatile("s_waitcnt lgkmcnt(" #n ")" ::: "memory")
; #define PG8_BAR __builtin_amdgcn_s_barrier()
; #define PG8_SCHED __builtin_amdgcn_sched_barrier(0)
; template <class Epi, class Sched, class Prob>
; __device__ __forceinline__ void gemm_phase(LAS unsigned char* lds, LAS unsigned char* lds_epi, const Prob g, const Sched& S, const Epi& E, int wid) {
;     ...
;         for (int t = 0; t < nt; t += 2) {
;             const bool last = (t == nt - 2);
;             const char* a1 = cA + (size_t)(t + 1) * kstep;
;             const char* a2 = last ? nA : cA + (size_t)(t + 2) * kstep; const char* b2 = last ? nB : cB + (size_t)(t + 2) * kstep;
;             const char* a3 = a2 + kstep; const char* b3 = b2 + kstep;
;             PG8_LDB(B0, 0, 0); PG8_LDB(B1, 0, 1); PG8_SCHED; PG8_LDA(At, 0, 0); PG8_STAGE(PG8_SA(1, 1), a1, cA10, cA11);
;             PG8_WAIT_V(8); PG8_WAIT_L(0); PG8_BAR; PG8_MMA(0, 0, At, B0); PG8_MMA(0, 1, At, B1); PG8_BAR; PG8_SCHED;
;             PG8_LDA(At, 0, 1); PG8_STAGE(PG8_SB(0, 0), b2, vB0, vB1); PG8_STAGE(PG8_SB(0, 1), b2 + hstepB, vB0, vB1); PG8_STAGE(PG8_SA(0, 0), a2, cA00, cA01);
;             PG8_WAIT_V(8); PG8_WAIT_L(0); PG8_BAR; PG8_MMA(1, 0, At, B0); PG8_MMA(1, 1, At, B1); PG8_BAR; PG8_SCHED;
.LBB0_1749:
	v_add_u32_e32 v160, s51, v145
	v_add_u32_e32 v176, s52, v145
	ds_read_b128 v[148:151], v160
	ds_read_b128 v[152:155], v160 offset:1024
	ds_read_b128 v[156:159], v160 offset:2048
	ds_read_b128 v[160:163], v160 offset:3072
	ds_read_b128 v[164:167], v176
	ds_read_b128 v[168:171], v176 offset:1024
	ds_read_b128 v[172:175], v176 offset:2048
	ds_read_b128 v[176:179], v176 offset:3072
	s_add_u32 s28, s26, 0x80
	s_addc_u32 s29, s27, 0
	s_cmp_eq_u32 s57, 28
	s_cselect_b32 s35, s17, s29
	s_cselect_b32 s34, s19, s28
	s_cselect_b32 s29, s15, s56
	s_cselect_b32 s28, s54, s55
	v_lshl_add_u64 v[212:213], s[26:27], 0, v[140:141]
	s_add_i32 m0, s21, 0xc000
	ds_read_b128 v[180:183], v147
	ds_read_b128 v[184:187], v147 offset:1024
	ds_read_b128 v[188:191], v147 offset:2048
	ds_read_b128 v[192:195], v147 offset:3072
	ds_read_b128 v[196:199], v147 offset:4096
	ds_read_b128 v[200:203], v147 offset:5120
	ds_read_b128 v[204:207], v147 offset:6144
	ds_read_b128 v[208:211], v147 offset:7168
	global_load_lds_dwordx4 v[212:213], off
	v_lshl_add_u64 v[212:213], s[26:27], 0, v[138:139]
	s_add_i32 m0, s21, 0xe000
	s_nop 0
	global_load_lds_dwordx4 v[212:213], off
	s_waitcnt vmcnt(8)
	s_waitcnt lgkmcnt(0)
	s_barrier
	s_setprio 1
	s_waitcnt lgkmcnt(0)
	v_mfma_f32_16x16x32_bf16 v[12:15], v[148:151], v[180:183], v[12:15]
	v_mfma_f32_16x16x32_bf16 v[28:31], v[156:159], v[180:183], v[28:31]
	v_mfma_f32_16x16x32_bf16 v[8:11], v[148:151], v[188:191], v[8:11]
	v_mfma_f32_16x16x32_bf16 v[24:27], v[156:159], v[188:191], v[24:27]
	v_mfma_f32_16x16x32_bf16 v[4:7], v[148:151], v[196:199], v[4:7]
	v_mfma_f32_16x16x32_bf16 v[20:23], v[156:159], v[196:199], v[20:23]
	v_mfma_f32_16x16x32_bf16 v[0:3], v[148:151], v[204:207], v[0:3]
	v_mfma_f32_16x16x32_bf16 v[16:19], v[156:159], v[204:207], v[16:19]
	v_mfma_f32_16x16x32_bf16 v[12:15], v[152:155], v[184:187], v[12:15]
	v_mfma_f32_16x16x32_bf16 v[28:31], v[160:163], v[184:187], v[28:31]
	v_mfma_f32_16x16x32_bf16 v[8:11], v[152:155], v[192:195], v[8:11]
	v_mfma_f32_16x16x32_bf16 v[24:27], v[160:163], v[192:195], v[24:27]
	v_mfma_f32_16x16x32_bf16 v[4:7], v[152:155], v[200:203], v[4:7]
	v_mfma_f32_16x16x32_bf16 v[20:23], v[160:163], v[200:203], v[20:23]
	v_mfma_f32_16x16x32_bf16 v[0:3], v[152:155], v[208:211], v[0:3]
	v_mfma_f32_16x16x32_bf16 v[16:19], v[160:163], v[208:211], v[16:19]
	v_mfma_f32_16x16x32_bf16 v[44:47], v[164:167], v[180:183], v[44:47]
	v_mfma_f32_16x16x32_bf16 v[68:71], v[172:175], v[180:183], v[68:71]
	v_mfma_f32_16x16x32_bf16 v[40:43], v[164:167], v[188:191], v[40:43]
	v_mfma_f32_16x16x32_bf16 v[64:67], v[172:175], v[188:191], v[64:67]
	v_mfma_f32_16x16x32_bf16 v[36:39], v[164:167], v[196:199], v[36:39]
	v_mfma_f32_16x16x32_bf16 v[60:63], v[172:175], v[196:199], v[60:63]
	v_mfma_f32_16x16x32_bf16 v[32:35], v[164:167], v[204:207], v[32:35]
	v_mfma_f32_16x16x32_bf16 v[56:59], v[172:175], v[204:207], v[56:59]
	v_mfma_f32_16x16x32_bf16 v[44:47], v[168:171], v[184:187], v[44:47]
	v_mfma_f32_16x16x32_bf16 v[68:71], v[176:179], v[184:187], v[68:71]
	v_mfma_f32_16x16x32_bf16 v[40:43], v[168:171], v[192:195], v[40:43]
	v_mfma_f32_16x16x32_bf16 v[64:67], v[176:179], v[192:195], v[64:67]
	v_mfma_f32_16x16x32_bf16 v[36:39], v[168:171], v[200:203], v[36:39]
	v_mfma_f32_16x16x32_bf16 v[60:63], v[176:179], v[200:203], v[60:63]
	v_mfma_f32_16x16x32_bf16 v[32:35], v[168:171], v[208:211], v[32:35]
	v_mfma_f32_16x16x32_bf16 v[56:59], v[176:179], v[208:211], v[56:59]
	s_setprio 0
	s_barrier
	s_add_i32 s58, s51, s97
	v_lshl_add_u64 v[212:213], s[28:29], 0, v[130:131]
	s_mov_b32 m0, s58
	ds_read_b128 v[180:183], v147 offset:16384
	ds_read_b128 v[184:187], v147 offset:17408
	ds_read_b128 v[188:191], v147 offset:18432
	ds_read_b128 v[192:195], v147 offset:19456
	ds_read_b128 v[196:199], v147 offset:20480
	ds_read_b128 v[200:203], v147 offset:21504
	ds_read_b128 v[204:207], v147 offset:22528
	ds_read_b128 v[208:211], v147 offset:23552
	global_load_lds_dwordx4 v[212:213], off
	s_add_i32 m0, s58, 0x2000
	s_add_u32 s58, s28, 0x80000
	v_lshl_add_u64 v[214:215], s[28:29], 0, v[128:129]
	s_addc_u32 s59, s29, 0
	s_add_i32 s60, s52, s97
	global_load_lds_dwordx4 v[214:215], off
	v_lshl_add_u64 v[216:217], s[58:59], 0, v[130:131]
	s_mov_b32 m0, s60
	v_lshl_add_u64 v[218:219], s[34:35], 0, v[128:129]
	global_load_lds_dwordx4 v[216:217], off
	v_lshl_add_u64 v[216:217], s[58:59], 0, v[128:129]
	s_add_i32 m0, s60, 0x2000
	s_nop 0
	global_load_lds_dwordx4 v[216:217], off
	v_lshl_add_u64 v[216:217], s[34:35], 0, v[130:131]
	s_mov_b32 m0, s21
	s_nop 0
	global_load_lds_dwordx4 v[216:217], off
	s_mov_b32 m0, s46
	s_nop 0
	global_load_lds_dwordx4 v[218:219], off
	s_waitcnt vmcnt(8)
	s_waitcnt lgkmcnt(0)
	s_barrier
; #define PG8_STAGE(bufoff, gbase, o0, o1) do { \
;         __builtin_amdgcn_global_load_lds((const unsigned*)((const char*)(gbase) + (o0)), (LAS unsigned*)(lds + (bufoff) + ldsw), 16, 0, 0); \
;         __builtin_amdgcn_global_load_lds((const unsigned*)((const char*)(gbase) + (o1)), (LAS unsigned*)(lds + (bufoff) + ldsw + 8192), 16, 0, 0); } while (0)
; #define PG8_LDA(dst, b, h) do { _Pragma("unroll") for (int m = 0; m < 4; ++m) _Pragma("unroll") for (int k = 0; k < 2; ++k) dst[m][k] = *(const LAS bf16x8*)(lds + PG8_SA(b, h) + aoff + m * 2048 + k * 1024); } while (0)
; #define PG8_LDB(dst, b, h) do { _Pragma("unroll") for (int n = 0; n < 2; ++n) _Pragma("unroll") for (int k = 0; k < 2; ++k) dst[n][k] = *(const LAS bf16x8*)(lds + PG8_SB(b, h) + boff + n * 2048 + k * 1024); } while (0)
; #define PG8_WAIT_V(n) asm volatile("s_waitcnt vmcnt(" #n ")" ::: "memory")
; #define PG8_WAIT_L(n) asm volatile("s_waitcnt lgkmcnt(" #n ")" ::: "memory")
; #define PG8_BAR __builtin_amdgcn_s_barrier()
; #define PG8_SCHED __builtin_amdgcn_sched_barrier(0)
; template <class Epi, class Sched, class Prob>
; __device__ __forceinline__ void gemm_phase(LAS unsigned char* lds, LAS unsigned char* lds_epi, const Prob g, const Sched& S, const Epi& E, int wid) {
;     ...
;             PG8_WAIT_V(8); PG8_WAIT_L(0); PG8_BAR; PG8_MMA(1, 0, At, B0); PG8_MMA(1, 1, At, B1); PG8_BAR; PG8_SCHED;
;             PG8_LDB(B0, 1, 0); PG8_LDB(B1, 1, 1); PG8_SCHED; PG8_LDA(At, 1, 0); PG8_STAGE(PG8_SA(0, 1), a2, cA10, cA11);
;             PG8_WAIT_V(8); PG8_WAIT_L(0); PG8_BAR; PG8_MMA(0, 0, At, B0); PG8_MMA(0, 1, At, B1); PG8_BAR; PG8_SCHED;
;             PG8_LDA(At, 1, 1); PG8_STAGE(PG8_SB(1, 0), b3, vB0, vB1); PG8_STAGE(PG8_SB(1, 1), b3 + hstepB, vB0, vB1); PG8_STAGE(PG8_SA(1, 0), a3, cA00, cA01);
	s_setprio 1
	s_waitcnt lgkmcnt(0)
	v_mfma_f32_16x16x32_bf16 v[52:55], v[148:151], v[180:183], v[52:55]
	v_mfma_f32_16x16x32_bf16 v[76:79], v[156:159], v[180:183], v[76:79]
	v_mfma_f32_16x16x32_bf16 v[48:51], v[148:151], v[188:191], v[48:51]
	v_mfma_f32_16x16x32_bf16 v[72:75], v[156:159], v[188:191], v[72:75]
	v_mfma_f32_16x16x32_bf16 v[100:103], v[148:151], v[196:199], v[100:103]
	v_mfma_f32_16x16x32_bf16 v[108:111], v[156:159], v[196:199], v[108:111]
	v_mfma_f32_16x16x32_bf16 v[96:99], v[148:151], v[204:207], v[96:99]
	v_mfma_f32_16x16x32_bf16 v[104:107], v[156:159], v[204:207], v[104:107]
	v_mfma_f32_16x16x32_bf16 v[52:55], v[152:155], v[184:187], v[52:55]
	v_mfma_f32_16x16x32_bf16 v[76:79], v[160:163], v[184:187], v[76:79]
	v_mfma_f32_16x16x32_bf16 v[48:51], v[152:155], v[192:195], v[48:51]
	v_mfma_f32_16x16x32_bf16 v[72:75], v[160:163], v[192:195], v[72:75]
	v_mfma_f32_16x16x32_bf16 v[100:103], v[152:155], v[200:203], v[100:103]
	v_mfma_f32_16x16x32_bf16 v[108:111], v[160:163], v[200:203], v[108:111]
	v_mfma_f32_16x16x32_bf16 v[96:99], v[152:155], v[208:211], v[96:99]
	v_mfma_f32_16x16x32_bf16 v[104:107], v[160:163], v[208:211], v[104:107]
	v_mfma_f32_16x16x32_bf16 v[84:87], v[164:167], v[180:183], v[84:87]
	v_mfma_f32_16x16x32_bf16 v[92:95], v[172:175], v[180:183], v[92:95]
	v_mfma_f32_16x16x32_bf16 v[80:83], v[164:167], v[188:191], v[80:83]
	v_mfma_f32_16x16x32_bf16 v[88:91], v[172:175], v[188:191], v[88:91]
	v_mfma_f32_16x16x32_bf16 v[116:119], v[164:167], v[196:199], v[116:119]
	v_mfma_f32_16x16x32_bf16 v[124:127], v[172:175], v[196:199], v[124:127]
	v_mfma_f32_16x16x32_bf16 v[112:115], v[164:167], v[204:207], v[112:115]
	v_mfma_f32_16x16x32_bf16 v[120:123], v[172:175], v[204:207], v[120:123]
	v_mfma_f32_16x16x32_bf16 v[84:87], v[168:171], v[184:187], v[84:87]
	v_mfma_f32_16x16x32_bf16 v[92:95], v[176:179], v[184:187], v[92:95]
	v_mfma_f32_16x16x32_bf16 v[80:83], v[168:171], v[192:195], v[80:83]
	v_mfma_f32_16x16x32_bf16 v[88:91], v[176:179], v[192:195], v[88:91]
	v_mfma_f32_16x16x32_bf16 v[116:119], v[168:171], v[200:203], v[116:119]
	v_mfma_f32_16x16x32_bf16 v[124:127], v[176:179], v[200:203], v[124:127]
	v_mfma_f32_16x16x32_bf16 v[112:115], v[168:171], v[208:211], v[112:115]
	v_mfma_f32_16x16x32_bf16 v[120:123], v[176:179], v[208:211], v[120:123]
	s_setprio 0
	s_barrier
	s_add_i32 s58, 0, 0x18000
	s_add_i32 s59, 0, 0x1c000
	v_add_u32_e32 v160, s58, v145
	v_add_u32_e32 v176, s59, v145
	ds_read_b128 v[148:151], v160
	ds_read_b128 v[152:155], v160 offset:1024
	ds_read_b128 v[156:159], v160 offset:2048
	ds_read_b128 v[160:163], v160 offset:3072
	ds_read_b128 v[164:167], v176
	ds_read_b128 v[168:171], v176 offset:1024
	ds_read_b128 v[172:175], v176 offset:2048
	ds_read_b128 v[176:179], v176 offset:3072
	s_mov_b32 m0, s47
	v_lshl_add_u64 v[220:221], s[34:35], 0, v[132:133]
	ds_read_b128 v[180:183], v147 offset:32768
	ds_read_b128 v[184:187], v147 offset:33792
	ds_read_b128 v[188:191], v147 offset:34816
	ds_read_b128 v[192:195], v147 offset:35840
	ds_read_b128 v[196:199], v147 offset:36864
	ds_read_b128 v[200:203], v147 offset:37888
	ds_read_b128 v[204:207], v147 offset:38912
	ds_read_b128 v[208:211], v147 offset:39936
	global_load_lds_dwordx4 v[220:221], off
	v_lshl_add_u64 v[220:221], s[34:35], 0, v[134:135]
	s_mov_b32 m0, s48
	s_nop 0
	global_load_lds_dwordx4 v[220:221], off
	s_waitcnt vmcnt(8)
	s_waitcnt lgkmcnt(0)
	s_barrier
	s_setprio 1
	s_waitcnt lgkmcnt(0)
	v_mfma_f32_16x16x32_bf16 v[12:15], v[148:151], v[180:183], v[12:15]
	v_mfma_f32_16x16x32_bf16 v[28:31], v[156:159], v[180:183], v[28:31]
	v_mfma_f32_16x16x32_bf16 v[8:11], v[148:151], v[188:191], v[8:11]
	v_mfma_f32_16x16x32_bf16 v[24:27], v[156:159], v[188:191], v[24:27]
	v_mfma_f32_16x16x32_bf16 v[4:7], v[148:151], v[196:199], v[4:7]
	v_mfma_f32_16x16x32_bf16 v[20:23], v[156:159], v[196:199], v[20:23]
	v_mfma_f32_16x16x32_bf16 v[0:3], v[148:151], v[204:207], v[0:3]
	v_mfma_f32_16x16x32_bf16 v[16:19], v[156:159], v[204:207], v[16:19]
	v_mfma_f32_16x16x32_bf16 v[12:15], v[152:155], v[184:187], v[12:15]
	v_mfma_f32_16x16x32_bf16 v[28:31], v[160:163], v[184:187], v[28:31]
	v_mfma_f32_16x16x32_bf16 v[8:11], v[152:155], v[192:195], v[8:11]
	v_mfma_f32_16x16x32_bf16 v[24:27], v[160:163], v[192:195], v[24:27]
	v_mfma_f32_16x16x32_bf16 v[4:7], v[152:155], v[200:203], v[4:7]
	v_mfma_f32_16x16x32_bf16 v[20:23], v[160:163], v[200:203], v[20:23]
	v_mfma_f32_16x16x32_bf16 v[0:3], v[152:155], v[208:211], v[0:3]
	v_mfma_f32_16x16x32_bf16 v[16:19], v[160:163], v[208:211], v[16:19]
	v_mfma_f32_16x16x32_bf16 v[44:47], v[164:167], v[180:183], v[44:47]
	v_mfma_f32_16x16x32_bf16 v[68:71], v[172:175], v[180:183], v[68:71]
	v_mfma_f32_16x16x32_bf16 v[40:43], v[164:167], v[188:191], v[40:43]
	v_mfma_f32_16x16x32_bf16 v[64:67], v[172:175], v[188:191], v[64:67]
	v_mfma_f32_16x16x32_bf16 v[36:39], v[164:167], v[196:199], v[36:39]
	v_mfma_f32_16x16x32_bf16 v[60:63], v[172:175], v[196:199], v[60:63]
	v_mfma_f32_16x16x32_bf16 v[32:35], v[164:167], v[204:207], v[32:35]
	v_mfma_f32_16x16x32_bf16 v[56:59], v[172:175], v[204:207], v[56:59]
	v_mfma_f32_16x16x32_bf16 v[44:47], v[168:171], v[184:187], v[44:47]
	v_mfma_f32_16x16x32_bf16 v[68:71], v[176:179], v[184:187], v[68:71]
	v_mfma_f32_16x16x32_bf16 v[40:43], v[168:171], v[192:195], v[40:43]
	v_mfma_f32_16x16x32_bf16 v[64:67], v[176:179], v[192:195], v[64:67]
	v_mfma_f32_16x16x32_bf16 v[36:39], v[168:171], v[200:203], v[36:39]
	v_mfma_f32_16x16x32_bf16 v[60:63], v[176:179], v[200:203], v[60:63]
	v_mfma_f32_16x16x32_bf16 v[32:35], v[168:171], v[208:211], v[32:35]
	v_mfma_f32_16x16x32_bf16 v[56:59], v[176:179], v[208:211], v[56:59]
	s_setprio 0
	s_barrier
; #define PG8_STAGE(bufoff, gbase, o0, o1) do { \
;         __builtin_amdgcn_global_load_lds((const unsigned*)((const char*)(gbase) + (o0)), (LAS unsigned*)(lds + (bufoff) + ldsw), 16, 0, 0); \
;         __builtin_amdgcn_global_load_lds((const unsigned*)((const char*)(gbase) + (o1)), (LAS unsigned*)(lds + (bufoff) + ldsw + 8192), 16, 0, 0); } while (0)
; #define PG8_LDA(dst, b, h) do { _Pragma("unroll") for (int m = 0; m < 4; ++m) _Pragma("unroll") for (int k = 0; k < 2; ++k) dst[m][k] = *(const LAS bf16x8*)(lds + PG8_SA(b, h) + aoff + m * 2048 + k * 1024); } while (0)
; #define PG8_WAIT_V(n) asm volatile("s_waitcnt vmcnt(" #n ")" ::: "memory")
; #define PG8_WAIT_L(n) asm volatile("s_waitcnt lgkmcnt(" #n ")" ::: "memory")
; #define PG8_BAR __builtin_amdgcn_s_barrier()
; #define PG8_SCHED __builtin_amdgcn_sched_barrier(0)
; template <class Epi, class Sched, class Prob>
; __device__ __forceinline__ void gemm_phase(LAS unsigned char* lds, LAS unsigned char* lds_epi, const Prob g, const Sched& S, const Epi& E, int wid) {
;     ...
;             PG8_LDA(At, 1, 1); PG8_STAGE(PG8_SB(1, 0), b3, vB0, vB1); PG8_STAGE(PG8_SB(1, 1), b3 + hstepB, vB0, vB1); PG8_STAGE(PG8_SA(1, 0), a3, cA00, cA01);
;             PG8_WAIT_V(8); PG8_WAIT_L(0); PG8_BAR; PG8_MMA(1, 0, At, B0); PG8_MMA(1, 1, At, B1); PG8_BAR; PG8_SCHED;
;         }
;         if constexpr (Prob::FP8) asm volatile("s_nop 7\n\ts_nop 7\n\ts_nop 7" ::: "memory");
;         if (wr == 0) PG8_BAR;
	s_add_i32 s34, s58, s97
	v_lshl_add_u64 v[212:213], v[212:213], 0, s[8:9]
	s_mov_b32 m0, s34
	ds_read_b128 v[180:183], v147 offset:49152
	ds_read_b128 v[184:187], v147 offset:50176
	ds_read_b128 v[188:191], v147 offset:51200
	ds_read_b128 v[192:195], v147 offset:52224
	ds_read_b128 v[196:199], v147 offset:53248
	ds_read_b128 v[200:203], v147 offset:54272
	ds_read_b128 v[204:207], v147 offset:55296
	ds_read_b128 v[208:211], v147 offset:56320
	global_load_lds_dwordx4 v[212:213], off
	s_add_i32 m0, s34, 0x2000
	s_add_u32 s28, s28, 0x80080
	v_lshl_add_u64 v[212:213], v[214:215], 0, s[8:9]
	s_addc_u32 s29, s29, 0
	s_add_i32 s34, s59, s97
	global_load_lds_dwordx4 v[212:213], off
	v_lshl_add_u64 v[212:213], s[28:29], 0, v[130:131]
	s_mov_b32 m0, s34
	s_nop 0
	global_load_lds_dwordx4 v[212:213], off
	v_lshl_add_u64 v[212:213], s[28:29], 0, v[128:129]
	s_add_i32 m0, s34, 0x2000
	s_nop 0
	global_load_lds_dwordx4 v[212:213], off
	v_lshl_add_u64 v[212:213], v[216:217], 0, s[8:9]
	s_mov_b32 m0, s49
	s_nop 0
	global_load_lds_dwordx4 v[212:213], off
	v_lshl_add_u64 v[212:213], v[218:219], 0, s[8:9]
	s_mov_b32 m0, s50
	s_nop 0
	global_load_lds_dwordx4 v[212:213], off
	s_waitcnt vmcnt(8)
	s_waitcnt lgkmcnt(0)
	s_barrier
	s_setprio 1
	s_waitcnt lgkmcnt(0)
	v_mfma_f32_16x16x32_bf16 v[52:55], v[148:151], v[180:183], v[52:55]
	v_mfma_f32_16x16x32_bf16 v[76:79], v[156:159], v[180:183], v[76:79]
	v_mfma_f32_16x16x32_bf16 v[48:51], v[148:151], v[188:191], v[48:51]
	v_mfma_f32_16x16x32_bf16 v[72:75], v[156:159], v[188:191], v[72:75]
	v_mfma_f32_16x16x32_bf16 v[100:103], v[148:151], v[196:199], v[100:103]
	v_mfma_f32_16x16x32_bf16 v[108:111], v[156:159], v[196:199], v[108:111]
	v_mfma_f32_16x16x32_bf16 v[96:99], v[148:151], v[204:207], v[96:99]
	v_mfma_f32_16x16x32_bf16 v[104:107], v[156:159], v[204:207], v[104:107]
	v_mfma_f32_16x16x32_bf16 v[52:55], v[152:155], v[184:187], v[52:55]
	v_mfma_f32_16x16x32_bf16 v[76:79], v[160:163], v[184:187], v[76:79]
	v_mfma_f32_16x16x32_bf16 v[48:51], v[152:155], v[192:195], v[48:51]
	v_mfma_f32_16x16x32_bf16 v[72:75], v[160:163], v[192:195], v[72:75]
	v_mfma_f32_16x16x32_bf16 v[100:103], v[152:155], v[200:203], v[100:103]
	v_mfma_f32_16x16x32_bf16 v[108:111], v[160:163], v[200:203], v[108:111]
	v_mfma_f32_16x16x32_bf16 v[96:99], v[152:155], v[208:211], v[96:99]
	v_mfma_f32_16x16x32_bf16 v[104:107], v[160:163], v[208:211], v[104:107]
	v_mfma_f32_16x16x32_bf16 v[84:87], v[164:167], v[180:183], v[84:87]
	v_mfma_f32_16x16x32_bf16 v[92:95], v[172:175], v[180:183], v[92:95]
	v_mfma_f32_16x16x32_bf16 v[80:83], v[164:167], v[188:191], v[80:83]
	v_mfma_f32_16x16x32_bf16 v[88:91], v[172:175], v[188:191], v[88:91]
	v_mfma_f32_16x16x32_bf16 v[116:119], v[164:167], v[196:199], v[116:119]
	v_mfma_f32_16x16x32_bf16 v[124:127], v[172:175], v[196:199], v[124:127]
	v_mfma_f32_16x16x32_bf16 v[112:115], v[164:167], v[204:207], v[112:115]
	v_mfma_f32_16x16x32_bf16 v[120:123], v[172:175], v[204:207], v[120:123]
	v_mfma_f32_16x16x32_bf16 v[84:87], v[168:171], v[184:187], v[84:87]
	v_mfma_f32_16x16x32_bf16 v[92:95], v[176:179], v[184:187], v[92:95]
	v_mfma_f32_16x16x32_bf16 v[80:83], v[168:171], v[192:195], v[80:83]
	v_mfma_f32_16x16x32_bf16 v[88:91], v[176:179], v[192:195], v[88:91]
	v_mfma_f32_16x16x32_bf16 v[116:119], v[168:171], v[200:203], v[116:119]
	v_mfma_f32_16x16x32_bf16 v[124:127], v[176:179], v[200:203], v[124:127]
	v_mfma_f32_16x16x32_bf16 v[112:115], v[168:171], v[208:211], v[112:115]
	v_mfma_f32_16x16x32_bf16 v[120:123], v[176:179], v[208:211], v[120:123]
	s_setprio 0
	s_barrier
	s_add_i32 s57, s57, 2
	s_add_u32 s26, s26, 0x100
	s_addc_u32 s27, s27, 0
	s_add_u32 s55, s55, 0x100
	s_addc_u32 s56, s56, 0
	s_cmp_gt_u32 s57, 29
	s_cbranch_scc0 .LBB0_1749
	v_readlane_b32 s26, v254, 27
	v_readlane_b32 s27, v254, 28
	s_and_b64 vcc, exec, s[26:27]
	s_cbranch_vccz .LBB0_1752
	s_barrier

; #define PG8_STAGE(bufoff, gbase, o0, o1) do { \
;         __builtin_amdgcn_global_load_lds((const unsigned*)((const char*)(gbase) + (o0)), (LAS unsigned*)(lds + (bufoff) + ldsw), 16, 0, 0); \
;         __builtin_amdgcn_global_load_lds((const unsigned*)((const char*)(gbase) + (o1)), (LAS unsigned*)(lds + (bufoff) + ldsw + 8192), 16, 0, 0); } while (0)
; #define PG8_LDA(dst, b, h) do { _Pragma("unroll") for (int m = 0; m < 4; ++m) _Pragma("unroll") for (int k = 0; k < 2; ++k) dst[m][k] = *(const LAS bf16x8*)(lds + PG8_SA(b, h) + aoff + m * 2048 + k * 1024); } while (0)
; template <class Epi, class Sched, class Prob>
; __device__ __forceinline__ void gemm_phase(LAS unsigned char* lds, LAS unsigned char* lds_epi, const Prob g, const Sched& S, const Epi& E, int wid) {
;     ...
;         const bool has_next = S.next(ui + 1, nxt);
;         const char* nA = has_next ? g.a_base(nxt) : cA; const char* nB = has_next ? g.b_base(nxt) : cB;
; _Pragma("clang loop unroll(disable)")
;         for (int t = 0; t < nt; t += 2) {
;             const bool last = (t == nt - 2);
;             const char* a1 = cA + (size_t)(t + 1) * kstep;
;             const char* a2 = last ? nA : cA + (size_t)(t + 2) * kstep; const char* b2 = last ? nB : cB + (size_t)(t + 2) * kstep;
;             const char* a3 = a2 + kstep; const char* b3 = b2 + kstep;
;             PG8_LDB(B0, 0, 0); PG8_LDB(B1, 0, 1); PG8_SCHED; PG8_LDA(At, 0, 0); PG8_STAGE(PG8_SA(1, 1), a1, cA10, cA11);
;             PG8_WAIT_V(8); PG8_WAIT_L(0); PG8_BAR; PG8_MMA(0, 0, At, B0); PG8_MMA(0, 1, At, B1); PG8_BAR; PG8_SCHED;
;             PG8_LDA(At, 0, 1); PG8_STAGE(PG8_SB(0, 0), b2, vB0, vB1); PG8_STAGE(PG8_SB(0, 1), b2 + hstepB, vB0, vB1); PG8_STAGE(PG8_SA(0, 0), a2, cA00, cA01);
;             PG8_WAIT_V(8); PG8_WAIT_L(0); PG8_BAR; PG8_MMA(1, 0, At, B0); PG8_MMA(1, 1, At, B1); PG8_BAR; PG8_SCHED;
;             PG8_LDB(B0, 1, 0); PG8_LDB(B1, 1, 1); PG8_SCHED; PG8_LDA(At, 1, 0); PG8_STAGE(PG8_SA(0, 1), a2, cA10, cA11);
;             PG8_WAIT_V(8); PG8_WAIT_L(0); PG8_BAR; PG8_MMA(0, 0, At, B0); PG8_MMA(0, 1, At, B1); PG8_BAR; PG8_SCHED;
;             PG8_LDA(At, 1, 1); PG8_STAGE(PG8_SB(1, 0), b3, vB0, vB1); PG8_STAGE(PG8_SB(1, 1), b3 + hstepB, vB0, vB1); PG8_STAGE(PG8_SA(1, 0), a3, cA00, cA01);
;             PG8_WAIT_V(8); PG8_WAIT_L(0); PG8_BAR; PG8_MMA(1, 0, At, B0); PG8_MMA(1, 1, At, B1); PG8_BAR; PG8_SCHED;
.LBB0_2090:
	s_ashr_i32 s11, s10, 31
	s_lshl_b64 s[30:31], s[10:11], 19
	s_add_u32 s30, s51, s30
	s_addc_u32 s31, s52, s31
	s_and_b64 s[40:41], s[40:41], exec
	s_cselect_b32 s11, s31, s37
	s_cselect_b32 s29, s30, s36
	s_add_u32 s36, s36, 0x80
	v_mov_b32_e32 v32, 0
	s_addc_u32 s37, s37, 0
	v_lshl_add_u64 v[182:183], v[0:1], 0, s[22:23]
	s_mov_b32 s69, -2
	ds_read_b128 v[24:27], v199
	ds_read_b128 v[28:31], v199 offset:1024
	ds_read_b128 v[16:19], v199 offset:2048
	ds_read_b128 v[20:23], v199 offset:3072
	ds_read_b128 v[8:11], v200
	ds_read_b128 v[12:15], v200 offset:1024
	ds_read_b128 v[0:3], v200 offset:2048
	ds_read_b128 v[4:7], v200 offset:3072
	s_add_u32 s40, s36, 0x80
	s_addc_u32 s41, s37, 0
	s_cmp_eq_u32 s69, 12
	s_cselect_b64 vcc, -1, 0
	s_cselect_b32 s41, s11, s41
	s_cselect_b32 s40, s29, s40
	v_cndmask_b32_e32 v185, v183, v181, vcc
	v_cndmask_b32_e32 v184, v182, v180, vcc
	v_lshl_add_u64 v[228:229], s[36:37], 0, v[176:177]
	s_add_i32 m0, s35, 0xc000
	ds_read_b128 v[186:189], v201
	ds_read_b128 v[190:193], v201 offset:1024
	ds_read_b128 v[204:207], v201 offset:2048
	ds_read_b128 v[208:211], v201 offset:3072
	ds_read_b128 v[212:215], v201 offset:4096
	ds_read_b128 v[216:219], v201 offset:5120
	ds_read_b128 v[220:223], v201 offset:6144
	ds_read_b128 v[224:227], v201 offset:7168
	global_load_lds_dwordx4 v[228:229], off
	v_lshl_add_u64 v[228:229], s[36:37], 0, v[174:175]
	s_add_i32 m0, s35, 0xe000
	s_nop 0
	global_load_lds_dwordx4 v[228:229], off
	s_waitcnt vmcnt(8)
	s_waitcnt lgkmcnt(0)
	s_barrier
	s_setprio 1
	s_waitcnt lgkmcnt(0)
	v_mfma_f32_16x16x128_f8f6f4 v[156:159], v[24:31], v[186:193], 0
	v_mfma_f32_16x16x128_f8f6f4 v[152:155], v[16:23], v[186:193], 0
	v_mfma_f32_16x16x128_f8f6f4 v[140:143], v[24:31], v[204:211], 0
	v_mfma_f32_16x16x128_f8f6f4 v[136:139], v[16:23], v[204:211], 0
	v_mfma_f32_16x16x128_f8f6f4 v[124:127], v[24:31], v[212:219], 0
	v_mfma_f32_16x16x128_f8f6f4 v[120:123], v[16:23], v[212:219], 0
	v_mfma_f32_16x16x128_f8f6f4 v[108:111], v[24:31], v[220:227], 0
	v_mfma_f32_16x16x128_f8f6f4 v[104:107], v[16:23], v[220:227], 0
	v_mfma_f32_16x16x128_f8f6f4 v[148:151], v[8:15], v[186:193], 0
	v_mfma_f32_16x16x128_f8f6f4 v[144:147], v[0:7], v[186:193], 0
	v_mfma_f32_16x16x128_f8f6f4 v[132:135], v[8:15], v[204:211], 0
	v_mfma_f32_16x16x128_f8f6f4 v[128:131], v[0:7], v[204:211], 0
	v_mfma_f32_16x16x128_f8f6f4 v[116:119], v[8:15], v[212:219], 0
	v_mfma_f32_16x16x128_f8f6f4 v[112:115], v[0:7], v[212:219], 0
	v_mfma_f32_16x16x128_f8f6f4 v[100:103], v[8:15], v[220:227], 0
	v_mfma_f32_16x16x128_f8f6f4 v[96:99], v[0:7], v[220:227], 0
	s_setprio 0
	s_barrier
	s_add_i32 s70, s63, s97
	v_lshl_add_u64 v[186:187], v[184:185], 0, v[160:161]
	s_mov_b32 m0, s70
	ds_read_b128 v[204:207], v201 offset:16384
	ds_read_b128 v[208:211], v201 offset:17408
	ds_read_b128 v[212:215], v201 offset:18432
	ds_read_b128 v[216:219], v201 offset:19456
	ds_read_b128 v[220:223], v201 offset:20480
	ds_read_b128 v[224:227], v201 offset:21504
	ds_read_b128 v[228:231], v201 offset:22528
	ds_read_b128 v[232:235], v201 offset:23552
	global_load_lds_dwordx4 v[186:187], off
	v_lshl_add_u64 v[188:189], v[184:185], 0, v[162:163]
	s_add_i32 m0, s70, 0x2000
	v_lshl_add_u64 v[190:191], v[184:185], 0, s[12:13]
	s_add_i32 s70, s64, s97
	global_load_lds_dwordx4 v[188:189], off
	v_lshl_add_u64 v[192:193], v[190:191], 0, v[160:161]
	s_mov_b32 m0, s70
	v_lshl_add_u64 v[190:191], v[190:191], 0, v[162:163]
	global_load_lds_dwordx4 v[192:193], off
	s_add_i32 m0, s70, 0x2000
	v_lshl_add_u64 v[192:193], s[40:41], 0, v[168:169]
	global_load_lds_dwordx4 v[190:191], off
	v_lshl_add_u64 v[190:191], s[40:41], 0, v[164:165]
	s_mov_b32 m0, s35
	s_nop 0
	global_load_lds_dwordx4 v[190:191], off
	s_mov_b32 m0, s58
	s_nop 0
	global_load_lds_dwordx4 v[192:193], off
	s_waitcnt vmcnt(8)
	s_waitcnt lgkmcnt(0)
	s_barrier
	s_setprio 1
	s_waitcnt lgkmcnt(0)
	v_mfma_f32_16x16x128_f8f6f4 v[92:95], v[24:31], v[204:211], 0
	v_mfma_f32_16x16x128_f8f6f4 v[88:91], v[16:23], v[204:211], 0
	v_mfma_f32_16x16x128_f8f6f4 v[76:79], v[24:31], v[212:219], 0
	v_mfma_f32_16x16x128_f8f6f4 v[72:75], v[16:23], v[212:219], 0
	v_mfma_f32_16x16x128_f8f6f4 v[60:63], v[24:31], v[220:227], 0
	v_mfma_f32_16x16x128_f8f6f4 v[56:59], v[16:23], v[220:227], 0
	v_mfma_f32_16x16x128_f8f6f4 v[44:47], v[24:31], v[228:235], 0
	v_mfma_f32_16x16x128_f8f6f4 v[40:43], v[16:23], v[228:235], 0
	v_mfma_f32_16x16x128_f8f6f4 v[84:87], v[8:15], v[204:211], 0
	v_mfma_f32_16x16x128_f8f6f4 v[80:83], v[0:7], v[204:211], 0
	v_mfma_f32_16x16x128_f8f6f4 v[68:71], v[8:15], v[212:219], 0
	v_mfma_f32_16x16x128_f8f6f4 v[64:67], v[0:7], v[212:219], 0
	v_mfma_f32_16x16x128_f8f6f4 v[52:55], v[8:15], v[220:227], 0
	v_mfma_f32_16x16x128_f8f6f4 v[48:51], v[0:7], v[220:227], 0
	v_mfma_f32_16x16x128_f8f6f4 v[36:39], v[8:15], v[228:235], 0
	v_mfma_f32_16x16x128_f8f6f4 v[32:35], v[0:7], v[228:235], 0
	s_setprio 0
	s_barrier
	s_add_i32 s70, 0, 0x18000
	s_add_i32 s71, 0, 0x1c000
	v_add_u32_e32 v12, s70, v195
	v_add_u32_e32 v28, s71, v195
	ds_read_b128 v[0:3], v12
	ds_read_b128 v[4:7], v12 offset:1024
	ds_read_b128 v[8:11], v12 offset:2048
	ds_read_b128 v[12:15], v12 offset:3072
	ds_read_b128 v[16:19], v28
	ds_read_b128 v[20:23], v28 offset:1024
	ds_read_b128 v[24:27], v28 offset:2048
	ds_read_b128 v[28:31], v28 offset:3072
	s_mov_b32 m0, s59
	v_lshl_add_u64 v[236:237], s[40:41], 0, v[166:167]
	ds_read_b128 v[204:207], v201 offset:32768
	ds_read_b128 v[208:211], v201 offset:33792
	ds_read_b128 v[212:215], v201 offset:34816
	ds_read_b128 v[216:219], v201 offset:35840
	ds_read_b128 v[220:223], v201 offset:36864
	ds_read_b128 v[224:227], v201 offset:37888
	ds_read_b128 v[228:231], v201 offset:38912
	ds_read_b128 v[232:235], v201 offset:39936
	global_load_lds_dwordx4 v[236:237], off
	v_lshl_add_u64 v[236:237], s[40:41], 0, v[170:171]
	s_mov_b32 m0, s60
	s_nop 0
	global_load_lds_dwordx4 v[236:237], off
	s_waitcnt vmcnt(8)
	s_waitcnt lgkmcnt(0)
	s_barrier
; #define PG8_STAGE(bufoff, gbase, o0, o1) do { \
;         __builtin_amdgcn_global_load_lds((const unsigned*)((const char*)(gbase) + (o0)), (LAS unsigned*)(lds + (bufoff) + ldsw), 16, 0, 0); \
;         __builtin_amdgcn_global_load_lds((const unsigned*)((const char*)(gbase) + (o1)), (LAS unsigned*)(lds + (bufoff) + ldsw + 8192), 16, 0, 0); } while (0)
; #define PG8_LDA(dst, b, h) do { _Pragma("unroll") for (int m = 0; m < 4; ++m) _Pragma("unroll") for (int k = 0; k < 2; ++k) dst[m][k] = *(const LAS bf16x8*)(lds + PG8_SA(b, h) + aoff + m * 2048 + k * 1024); } while (0)
; #define PG8_LDB(dst, b, h) do { _Pragma("unroll") for (int n = 0; n < 2; ++n) _Pragma("unroll") for (int k = 0; k < 2; ++k) dst[n][k] = *(const LAS bf16x8*)(lds + PG8_SB(b, h) + boff + n * 2048 + k * 1024); } while (0)
; #define PG8_WAIT_V(n) asm volatile("s_waitcnt vmcnt(" #n ")" ::: "memory")
; #define PG8_WAIT_L(n) asm volatile("s_waitcnt lgkmcnt(" #n ")" ::: "memory")
; #define PG8_BAR __builtin_amdgcn_s_barrier()
; #define PG8_SCHED __builtin_amdgcn_sched_barrier(0)
; template <class Epi, class Sched, class Prob>
; __device__ __forceinline__ void gemm_phase(LAS unsigned char* lds, LAS unsigned char* lds_epi, const Prob g, const Sched& S, const Epi& E, int wid) {
;     ...
;             PG8_LDB(B0, 0, 0); PG8_LDB(B1, 0, 1); PG8_SCHED; PG8_LDA(At, 0, 0); PG8_STAGE(PG8_SA(1, 1), a1, cA10, cA11);
;             PG8_WAIT_V(8); PG8_WAIT_L(0); PG8_BAR; PG8_MMA(0, 0, At, B0); PG8_MMA(0, 1, At, B1); PG8_BAR; PG8_SCHED;
;             PG8_LDA(At, 0, 1); PG8_STAGE(PG8_SB(0, 0), b2, vB0, vB1); PG8_STAGE(PG8_SB(0, 1), b2 + hstepB, vB0, vB1); PG8_STAGE(PG8_SA(0, 0), a2, cA00, cA01);
;             PG8_WAIT_V(8); PG8_WAIT_L(0); PG8_BAR; PG8_MMA(1, 0, At, B0); PG8_MMA(1, 1, At, B1); PG8_BAR; PG8_SCHED;
;             PG8_LDB(B0, 1, 0); PG8_LDB(B1, 1, 1); PG8_SCHED; PG8_LDA(At, 1, 0); PG8_STAGE(PG8_SA(0, 1), a2, cA10, cA11);
;             PG8_WAIT_V(8); PG8_WAIT_L(0); PG8_BAR; PG8_MMA(0, 0, At, B0); PG8_MMA(0, 1, At, B1); PG8_BAR; PG8_SCHED;
;             PG8_LDA(At, 1, 1); PG8_STAGE(PG8_SB(1, 0), b3, vB0, vB1); PG8_STAGE(PG8_SB(1, 1), b3 + hstepB, vB0, vB1); PG8_STAGE(PG8_SA(1, 0), a3, cA00, cA01);
;             PG8_WAIT_V(8); PG8_WAIT_L(0); PG8_BAR; PG8_MMA(1, 0, At, B0); PG8_MMA(1, 1, At, B1); PG8_BAR; PG8_SCHED;
	s_setprio 1
	s_waitcnt lgkmcnt(0)
	v_mfma_f32_16x16x128_f8f6f4 v[156:159], v[0:7], v[204:211], v[156:159]
	v_mfma_f32_16x16x128_f8f6f4 v[152:155], v[8:15], v[204:211], v[152:155]
	v_mfma_f32_16x16x128_f8f6f4 v[140:143], v[0:7], v[212:219], v[140:143]
	v_mfma_f32_16x16x128_f8f6f4 v[136:139], v[8:15], v[212:219], v[136:139]
	v_mfma_f32_16x16x128_f8f6f4 v[124:127], v[0:7], v[220:227], v[124:127]
	v_mfma_f32_16x16x128_f8f6f4 v[120:123], v[8:15], v[220:227], v[120:123]
	v_mfma_f32_16x16x128_f8f6f4 v[108:111], v[0:7], v[228:235], v[108:111]
	v_mfma_f32_16x16x128_f8f6f4 v[104:107], v[8:15], v[228:235], v[104:107]
	v_mfma_f32_16x16x128_f8f6f4 v[148:151], v[16:23], v[204:211], v[148:151]
	v_mfma_f32_16x16x128_f8f6f4 v[144:147], v[24:31], v[204:211], v[144:147]
	v_mfma_f32_16x16x128_f8f6f4 v[132:135], v[16:23], v[212:219], v[132:135]
	v_mfma_f32_16x16x128_f8f6f4 v[128:131], v[24:31], v[212:219], v[128:131]
	v_mfma_f32_16x16x128_f8f6f4 v[116:119], v[16:23], v[220:227], v[116:119]
	v_mfma_f32_16x16x128_f8f6f4 v[112:115], v[24:31], v[220:227], v[112:115]
	v_mfma_f32_16x16x128_f8f6f4 v[100:103], v[16:23], v[228:235], v[100:103]
	v_mfma_f32_16x16x128_f8f6f4 v[96:99], v[24:31], v[228:235], v[96:99]
	s_setprio 0
	s_barrier
	s_add_i32 s40, s70, s97
	v_lshl_add_u64 v[186:187], v[186:187], 0, s[18:19]
	s_mov_b32 m0, s40
	ds_read_b128 v[204:207], v201 offset:49152
	ds_read_b128 v[208:211], v201 offset:50176
	ds_read_b128 v[212:215], v201 offset:51200
	ds_read_b128 v[216:219], v201 offset:52224
	ds_read_b128 v[220:223], v201 offset:53248
	ds_read_b128 v[224:227], v201 offset:54272
	ds_read_b128 v[228:231], v201 offset:55296
	ds_read_b128 v[232:235], v201 offset:56320
	global_load_lds_dwordx4 v[186:187], off
	v_lshl_add_u64 v[186:187], v[188:189], 0, s[18:19]
	s_add_i32 m0, s40, 0x2000
	v_lshl_add_u64 v[184:185], v[184:185], 0, s[20:21]
	s_add_i32 s40, s71, s97
	global_load_lds_dwordx4 v[186:187], off
	v_lshl_add_u64 v[186:187], v[184:185], 0, v[160:161]
	s_mov_b32 m0, s40
	v_lshl_add_u64 v[184:185], v[184:185], 0, v[162:163]
	global_load_lds_dwordx4 v[186:187], off
	s_add_i32 m0, s40, 0x2000
	s_nop 0
	global_load_lds_dwordx4 v[184:185], off
	v_lshl_add_u64 v[184:185], v[190:191], 0, s[18:19]
	s_mov_b32 m0, s61
	s_nop 0
	global_load_lds_dwordx4 v[184:185], off
	v_lshl_add_u64 v[184:185], v[192:193], 0, s[18:19]
	s_mov_b32 m0, s62
	s_nop 0
	global_load_lds_dwordx4 v[184:185], off
	s_waitcnt vmcnt(8)
	s_waitcnt lgkmcnt(0)
	s_barrier
	s_setprio 1
	s_waitcnt lgkmcnt(0)
	v_mfma_f32_16x16x128_f8f6f4 v[92:95], v[0:7], v[204:211], v[92:95]
	v_mfma_f32_16x16x128_f8f6f4 v[88:91], v[8:15], v[204:211], v[88:91]
	v_mfma_f32_16x16x128_f8f6f4 v[76:79], v[0:7], v[212:219], v[76:79]
	v_mfma_f32_16x16x128_f8f6f4 v[72:75], v[8:15], v[212:219], v[72:75]
	v_mfma_f32_16x16x128_f8f6f4 v[60:63], v[0:7], v[220:227], v[60:63]
	v_mfma_f32_16x16x128_f8f6f4 v[56:59], v[8:15], v[220:227], v[56:59]
	v_mfma_f32_16x16x128_f8f6f4 v[44:47], v[0:7], v[228:235], v[44:47]
	v_mfma_f32_16x16x128_f8f6f4 v[40:43], v[8:15], v[228:235], v[40:43]
	v_mfma_f32_16x16x128_f8f6f4 v[84:87], v[16:23], v[204:211], v[84:87]
	v_mfma_f32_16x16x128_f8f6f4 v[80:83], v[24:31], v[204:211], v[80:83]
	v_mfma_f32_16x16x128_f8f6f4 v[68:71], v[16:23], v[212:219], v[68:71]
	v_mfma_f32_16x16x128_f8f6f4 v[64:67], v[24:31], v[212:219], v[64:67]
	v_mfma_f32_16x16x128_f8f6f4 v[52:55], v[16:23], v[220:227], v[52:55]
	v_mfma_f32_16x16x128_f8f6f4 v[48:51], v[24:31], v[220:227], v[48:51]
	v_mfma_f32_16x16x128_f8f6f4 v[36:39], v[16:23], v[228:235], v[36:39]
	v_mfma_f32_16x16x128_f8f6f4 v[32:35], v[24:31], v[228:235], v[32:35]
	s_setprio 0
	s_barrier
	s_add_i32 s69, s69, 2
	s_add_u32 s36, s36, 0x100
	s_addc_u32 s37, s37, 0
	s_cmp_gt_u32 s69, 13
	v_lshl_add_u64 v[182:183], v[182:183], 0, s[22:23]
.LBB0_2091:
	ds_read_b128 v[24:27], v199
	ds_read_b128 v[28:31], v199 offset:1024
	ds_read_b128 v[16:19], v199 offset:2048
	ds_read_b128 v[20:23], v199 offset:3072
	ds_read_b128 v[8:11], v200
	ds_read_b128 v[12:15], v200 offset:1024
	ds_read_b128 v[0:3], v200 offset:2048
	ds_read_b128 v[4:7], v200 offset:3072
	s_add_u32 s40, s36, 0x80
	s_addc_u32 s41, s37, 0
	s_cmp_eq_u32 s69, 12
	s_cselect_b64 vcc, -1, 0
	s_cselect_b32 s41, s11, s41
	s_cselect_b32 s40, s29, s40
	v_cndmask_b32_e32 v185, v183, v181, vcc
	v_cndmask_b32_e32 v184, v182, v180, vcc
	v_lshl_add_u64 v[228:229], s[36:37], 0, v[176:177]
	s_add_i32 m0, s35, 0xc000
	ds_read_b128 v[186:189], v201
	ds_read_b128 v[190:193], v201 offset:1024
	ds_read_b128 v[204:207], v201 offset:2048
	ds_read_b128 v[208:211], v201 offset:3072
	ds_read_b128 v[212:215], v201 offset:4096
	ds_read_b128 v[216:219], v201 offset:5120
	ds_read_b128 v[220:223], v201 offset:6144
	ds_read_b128 v[224:227], v201 offset:7168
	global_load_lds_dwordx4 v[228:229], off
	v_lshl_add_u64 v[228:229], s[36:37], 0, v[174:175]
	s_add_i32 m0, s35, 0xe000
	s_nop 0
	global_load_lds_dwordx4 v[228:229], off
	s_waitcnt vmcnt(8)
	s_waitcnt lgkmcnt(0)
	s_barrier
	s_setprio 1
	s_waitcnt lgkmcnt(0)
	v_mfma_f32_16x16x128_f8f6f4 v[156:159], v[24:31], v[186:193], v[156:159]
	v_mfma_f32_16x16x128_f8f6f4 v[152:155], v[16:23], v[186:193], v[152:155]
	v_mfma_f32_16x16x128_f8f6f4 v[140:143], v[24:31], v[204:211], v[140:143]
	v_mfma_f32_16x16x128_f8f6f4 v[136:139], v[16:23], v[204:211], v[136:139]
	v_mfma_f32_16x16x128_f8f6f4 v[124:127], v[24:31], v[212:219], v[124:127]
	v_mfma_f32_16x16x128_f8f6f4 v[120:123], v[16:23], v[212:219], v[120:123]
	v_mfma_f32_16x16x128_f8f6f4 v[108:111], v[24:31], v[220:227], v[108:111]
	v_mfma_f32_16x16x128_f8f6f4 v[104:107], v[16:23], v[220:227], v[104:107]
	v_mfma_f32_16x16x128_f8f6f4 v[148:151], v[8:15], v[186:193], v[148:151]
	v_mfma_f32_16x16x128_f8f6f4 v[144:147], v[0:7], v[186:193], v[144:147]
	v_mfma_f32_16x16x128_f8f6f4 v[132:135], v[8:15], v[204:211], v[132:135]
	v_mfma_f32_16x16x128_f8f6f4 v[128:131], v[0:7], v[204:211], v[128:131]
	v_mfma_f32_16x16x128_f8f6f4 v[116:119], v[8:15], v[212:219], v[116:119]
	v_mfma_f32_16x16x128_f8f6f4 v[112:115], v[0:7], v[212:219], v[112:115]
	v_mfma_f32_16x16x128_f8f6f4 v[100:103], v[8:15], v[220:227], v[100:103]
	v_mfma_f32_16x16x128_f8f6f4 v[96:99], v[0:7], v[220:227], v[96:99]
	s_setprio 0
	s_barrier
; #define PG8_STAGE(bufoff, gbase, o0, o1) do { \
;         __builtin_amdgcn_global_load_lds((const unsigned*)((const char*)(gbase) + (o0)), (LAS unsigned*)(lds + (bufoff) + ldsw), 16, 0, 0); \
;         __builtin_amdgcn_global_load_lds((const unsigned*)((const char*)(gbase) + (o1)), (LAS unsigned*)(lds + (bufoff) + ldsw + 8192), 16, 0, 0); } while (0)
; #define PG8_LDA(dst, b, h) do { _Pragma("unroll") for (int m = 0; m < 4; ++m) _Pragma("unroll") for (int k = 0; k < 2; ++k) dst[m][k] = *(const LAS bf16x8*)(lds + PG8_SA(b, h) + aoff + m * 2048 + k * 1024); } while (0)
; #define PG8_LDB(dst, b, h) do { _Pragma("unroll") for (int n = 0; n < 2; ++n) _Pragma("unroll") for (int k = 0; k < 2; ++k) dst[n][k] = *(const LAS bf16x8*)(lds + PG8_SB(b, h) + boff + n * 2048 + k * 1024); } while (0)
; #define PG8_WAIT_V(n) asm volatile("s_waitcnt vmcnt(" #n ")" ::: "memory")
; #define PG8_WAIT_L(n) asm volatile("s_waitcnt lgkmcnt(" #n ")" ::: "memory")
; #define PG8_BAR __builtin_amdgcn_s_barrier()
; #define PG8_SCHED __builtin_amdgcn_sched_barrier(0)
; template <class Epi, class Sched, class Prob>
; __device__ __forceinline__ void gemm_phase(LAS unsigned char* lds, LAS unsigned char* lds_epi, const Prob g, const Sched& S, const Epi& E, int wid) {
;     ...
;             PG8_LDA(At, 0, 1); PG8_STAGE(PG8_SB(0, 0), b2, vB0, vB1); PG8_STAGE(PG8_SB(0, 1), b2 + hstepB, vB0, vB1); PG8_STAGE(PG8_SA(0, 0), a2, cA00, cA01);
;             PG8_WAIT_V(8); PG8_WAIT_L(0); PG8_BAR; PG8_MMA(1, 0, At, B0); PG8_MMA(1, 1, At, B1); PG8_BAR; PG8_SCHED;
;             PG8_LDB(B0, 1, 0); PG8_LDB(B1, 1, 1); PG8_SCHED; PG8_LDA(At, 1, 0); PG8_STAGE(PG8_SA(0, 1), a2, cA10, cA11);
;             PG8_WAIT_V(8); PG8_WAIT_L(0); PG8_BAR; PG8_MMA(0, 0, At, B0); PG8_MMA(0, 1, At, B1); PG8_BAR; PG8_SCHED;
	s_add_i32 s70, s63, s97
	v_lshl_add_u64 v[186:187], v[184:185], 0, v[160:161]
	s_mov_b32 m0, s70
	ds_read_b128 v[204:207], v201 offset:16384
	ds_read_b128 v[208:211], v201 offset:17408
	ds_read_b128 v[212:215], v201 offset:18432
	ds_read_b128 v[216:219], v201 offset:19456
	ds_read_b128 v[220:223], v201 offset:20480
	ds_read_b128 v[224:227], v201 offset:21504
	ds_read_b128 v[228:231], v201 offset:22528
	ds_read_b128 v[232:235], v201 offset:23552
	global_load_lds_dwordx4 v[186:187], off
	v_lshl_add_u64 v[188:189], v[184:185], 0, v[162:163]
	s_add_i32 m0, s70, 0x2000
	v_lshl_add_u64 v[190:191], v[184:185], 0, s[12:13]
	s_add_i32 s70, s64, s97
	global_load_lds_dwordx4 v[188:189], off
	v_lshl_add_u64 v[192:193], v[190:191], 0, v[160:161]
	s_mov_b32 m0, s70
	v_lshl_add_u64 v[190:191], v[190:191], 0, v[162:163]
	global_load_lds_dwordx4 v[192:193], off
	s_add_i32 m0, s70, 0x2000
	v_lshl_add_u64 v[192:193], s[40:41], 0, v[168:169]
	global_load_lds_dwordx4 v[190:191], off
	v_lshl_add_u64 v[190:191], s[40:41], 0, v[164:165]
	s_mov_b32 m0, s35
	s_nop 0
	global_load_lds_dwordx4 v[190:191], off
	s_mov_b32 m0, s58
	s_nop 0
	global_load_lds_dwordx4 v[192:193], off
	s_waitcnt vmcnt(8)
	s_waitcnt lgkmcnt(0)
	s_barrier
	s_setprio 1
	s_waitcnt lgkmcnt(0)
	v_mfma_f32_16x16x128_f8f6f4 v[92:95], v[24:31], v[204:211], v[92:95]
	v_mfma_f32_16x16x128_f8f6f4 v[88:91], v[16:23], v[204:211], v[88:91]
	v_mfma_f32_16x16x128_f8f6f4 v[76:79], v[24:31], v[212:219], v[76:79]
	v_mfma_f32_16x16x128_f8f6f4 v[72:75], v[16:23], v[212:219], v[72:75]
	v_mfma_f32_16x16x128_f8f6f4 v[60:63], v[24:31], v[220:227], v[60:63]
	v_mfma_f32_16x16x128_f8f6f4 v[56:59], v[16:23], v[220:227], v[56:59]
	v_mfma_f32_16x16x128_f8f6f4 v[44:47], v[24:31], v[228:235], v[44:47]
	v_mfma_f32_16x16x128_f8f6f4 v[40:43], v[16:23], v[228:235], v[40:43]
	v_mfma_f32_16x16x128_f8f6f4 v[84:87], v[8:15], v[204:211], v[84:87]
	v_mfma_f32_16x16x128_f8f6f4 v[80:83], v[0:7], v[204:211], v[80:83]
	v_mfma_f32_16x16x128_f8f6f4 v[68:71], v[8:15], v[212:219], v[68:71]
	v_mfma_f32_16x16x128_f8f6f4 v[64:67], v[0:7], v[212:219], v[64:67]
	v_mfma_f32_16x16x128_f8f6f4 v[52:55], v[8:15], v[220:227], v[52:55]
	v_mfma_f32_16x16x128_f8f6f4 v[48:51], v[0:7], v[220:227], v[48:51]
	v_mfma_f32_16x16x128_f8f6f4 v[36:39], v[8:15], v[228:235], v[36:39]
	v_mfma_f32_16x16x128_f8f6f4 v[32:35], v[0:7], v[228:235], v[32:35]
	s_setprio 0
	s_barrier
	s_add_i32 s70, 0, 0x18000
	s_add_i32 s71, 0, 0x1c000
	v_add_u32_e32 v12, s70, v195
	v_add_u32_e32 v28, s71, v195
	ds_read_b128 v[0:3], v12
	ds_read_b128 v[4:7], v12 offset:1024
	ds_read_b128 v[8:11], v12 offset:2048
	ds_read_b128 v[12:15], v12 offset:3072
	ds_read_b128 v[16:19], v28
	ds_read_b128 v[20:23], v28 offset:1024
	ds_read_b128 v[24:27], v28 offset:2048
	ds_read_b128 v[28:31], v28 offset:3072
	s_mov_b32 m0, s59
	v_lshl_add_u64 v[236:237], s[40:41], 0, v[166:167]
	ds_read_b128 v[204:207], v201 offset:32768
	ds_read_b128 v[208:211], v201 offset:33792
	ds_read_b128 v[212:215], v201 offset:34816
	ds_read_b128 v[216:219], v201 offset:35840
	ds_read_b128 v[220:223], v201 offset:36864
	ds_read_b128 v[224:227], v201 offset:37888
	ds_read_b128 v[228:231], v201 offset:38912
	ds_read_b128 v[232:235], v201 offset:39936
	global_load_lds_dwordx4 v[236:237], off
	v_lshl_add_u64 v[236:237], s[40:41], 0, v[170:171]
	s_mov_b32 m0, s60
	s_nop 0
	global_load_lds_dwordx4 v[236:237], off
	s_waitcnt vmcnt(8)
	s_waitcnt lgkmcnt(0)
	s_barrier
; #define PG8_STAGE(bufoff, gbase, o0, o1) do { \
;         __builtin_amdgcn_global_load_lds((const unsigned*)((const char*)(gbase) + (o0)), (LAS unsigned*)(lds + (bufoff) + ldsw), 16, 0, 0); \
;         __builtin_amdgcn_global_load_lds((const unsigned*)((const char*)(gbase) + (o1)), (LAS unsigned*)(lds + (bufoff) + ldsw + 8192), 16, 0, 0); } while (0)
; #define PG8_LDA(dst, b, h) do { _Pragma("unroll") for (int m = 0; m < 4; ++m) _Pragma("unroll") for (int k = 0; k < 2; ++k) dst[m][k] = *(const LAS bf16x8*)(lds + PG8_SA(b, h) + aoff + m * 2048 + k * 1024); } while (0)
; #define PG8_WAIT_V(n) asm volatile("s_waitcnt vmcnt(" #n ")" ::: "memory")
; #define PG8_WAIT_L(n) asm volatile("s_waitcnt lgkmcnt(" #n ")" ::: "memory")
; #define PG8_BAR __builtin_amdgcn_s_barrier()
; #define PG8_SCHED __builtin_amdgcn_sched_barrier(0)
; template <class Epi, class Sched, class Prob>
; __device__ __forceinline__ void gemm_phase(LAS unsigned char* lds, LAS unsigned char* lds_epi, const Prob g, const Sched& S, const Epi& E, int wid) {
;     ...
;             PG8_WAIT_V(8); PG8_WAIT_L(0); PG8_BAR; PG8_MMA(0, 0, At, B0); PG8_MMA(0, 1, At, B1); PG8_BAR; PG8_SCHED;
;             PG8_LDA(At, 1, 1); PG8_STAGE(PG8_SB(1, 0), b3, vB0, vB1); PG8_STAGE(PG8_SB(1, 1), b3 + hstepB, vB0, vB1); PG8_STAGE(PG8_SA(1, 0), a3, cA00, cA01);
;             PG8_WAIT_V(8); PG8_WAIT_L(0); PG8_BAR; PG8_MMA(1, 0, At, B0); PG8_MMA(1, 1, At, B1); PG8_BAR; PG8_SCHED;
;         }
;         if constexpr (Prob::FP8) asm volatile("s_nop 7\n\ts_nop 7\n\ts_nop 7" ::: "memory");
;         if (wr == 0) PG8_BAR;
	s_setprio 1
	s_waitcnt lgkmcnt(0)
	v_mfma_f32_16x16x128_f8f6f4 v[156:159], v[0:7], v[204:211], v[156:159]
	v_mfma_f32_16x16x128_f8f6f4 v[152:155], v[8:15], v[204:211], v[152:155]
	v_mfma_f32_16x16x128_f8f6f4 v[140:143], v[0:7], v[212:219], v[140:143]
	v_mfma_f32_16x16x128_f8f6f4 v[136:139], v[8:15], v[212:219], v[136:139]
	v_mfma_f32_16x16x128_f8f6f4 v[124:127], v[0:7], v[220:227], v[124:127]
	v_mfma_f32_16x16x128_f8f6f4 v[120:123], v[8:15], v[220:227], v[120:123]
	v_mfma_f32_16x16x128_f8f6f4 v[108:111], v[0:7], v[228:235], v[108:111]
	v_mfma_f32_16x16x128_f8f6f4 v[104:107], v[8:15], v[228:235], v[104:107]
	v_mfma_f32_16x16x128_f8f6f4 v[148:151], v[16:23], v[204:211], v[148:151]
	v_mfma_f32_16x16x128_f8f6f4 v[144:147], v[24:31], v[204:211], v[144:147]
	v_mfma_f32_16x16x128_f8f6f4 v[132:135], v[16:23], v[212:219], v[132:135]
	v_mfma_f32_16x16x128_f8f6f4 v[128:131], v[24:31], v[212:219], v[128:131]
	v_mfma_f32_16x16x128_f8f6f4 v[116:119], v[16:23], v[220:227], v[116:119]
	v_mfma_f32_16x16x128_f8f6f4 v[112:115], v[24:31], v[220:227], v[112:115]
	v_mfma_f32_16x16x128_f8f6f4 v[100:103], v[16:23], v[228:235], v[100:103]
	v_mfma_f32_16x16x128_f8f6f4 v[96:99], v[24:31], v[228:235], v[96:99]
	s_setprio 0
	s_barrier
	s_add_i32 s40, s70, s97
	v_lshl_add_u64 v[186:187], v[186:187], 0, s[18:19]
	s_mov_b32 m0, s40
	ds_read_b128 v[204:207], v201 offset:49152
	ds_read_b128 v[208:211], v201 offset:50176
	ds_read_b128 v[212:215], v201 offset:51200
	ds_read_b128 v[216:219], v201 offset:52224
	ds_read_b128 v[220:223], v201 offset:53248
	ds_read_b128 v[224:227], v201 offset:54272
	ds_read_b128 v[228:231], v201 offset:55296
	ds_read_b128 v[232:235], v201 offset:56320
	global_load_lds_dwordx4 v[186:187], off
	v_lshl_add_u64 v[186:187], v[188:189], 0, s[18:19]
	s_add_i32 m0, s40, 0x2000
	v_lshl_add_u64 v[184:185], v[184:185], 0, s[20:21]
	s_add_i32 s40, s71, s97
	global_load_lds_dwordx4 v[186:187], off
	v_lshl_add_u64 v[186:187], v[184:185], 0, v[160:161]
	s_mov_b32 m0, s40
	v_lshl_add_u64 v[184:185], v[184:185], 0, v[162:163]
	global_load_lds_dwordx4 v[186:187], off
	s_add_i32 m0, s40, 0x2000
	s_nop 0
	global_load_lds_dwordx4 v[184:185], off
	v_lshl_add_u64 v[184:185], v[190:191], 0, s[18:19]
	s_mov_b32 m0, s61
	s_nop 0
	global_load_lds_dwordx4 v[184:185], off
	v_lshl_add_u64 v[184:185], v[192:193], 0, s[18:19]
	s_mov_b32 m0, s62
	s_nop 0
	global_load_lds_dwordx4 v[184:185], off
	s_waitcnt vmcnt(8)
	s_waitcnt lgkmcnt(0)
	s_barrier
	s_setprio 1
	s_waitcnt lgkmcnt(0)
	v_mfma_f32_16x16x128_f8f6f4 v[92:95], v[0:7], v[204:211], v[92:95]
	v_mfma_f32_16x16x128_f8f6f4 v[88:91], v[8:15], v[204:211], v[88:91]
	v_mfma_f32_16x16x128_f8f6f4 v[76:79], v[0:7], v[212:219], v[76:79]
	v_mfma_f32_16x16x128_f8f6f4 v[72:75], v[8:15], v[212:219], v[72:75]
	v_mfma_f32_16x16x128_f8f6f4 v[60:63], v[0:7], v[220:227], v[60:63]
	v_mfma_f32_16x16x128_f8f6f4 v[56:59], v[8:15], v[220:227], v[56:59]
	v_mfma_f32_16x16x128_f8f6f4 v[44:47], v[0:7], v[228:235], v[44:47]
	v_mfma_f32_16x16x128_f8f6f4 v[40:43], v[8:15], v[228:235], v[40:43]
	v_mfma_f32_16x16x128_f8f6f4 v[84:87], v[16:23], v[204:211], v[84:87]
	v_mfma_f32_16x16x128_f8f6f4 v[80:83], v[24:31], v[204:211], v[80:83]
	v_mfma_f32_16x16x128_f8f6f4 v[68:71], v[16:23], v[212:219], v[68:71]
	v_mfma_f32_16x16x128_f8f6f4 v[64:67], v[24:31], v[212:219], v[64:67]
	v_mfma_f32_16x16x128_f8f6f4 v[52:55], v[16:23], v[220:227], v[52:55]
	v_mfma_f32_16x16x128_f8f6f4 v[48:51], v[24:31], v[220:227], v[48:51]
	v_mfma_f32_16x16x128_f8f6f4 v[36:39], v[16:23], v[228:235], v[36:39]
	v_mfma_f32_16x16x128_f8f6f4 v[32:35], v[24:31], v[228:235], v[32:35]
	s_setprio 0
	s_barrier
	s_add_i32 s69, s69, 2
	s_add_u32 s36, s36, 0x100
	s_addc_u32 s37, s37, 0
	s_cmp_gt_u32 s69, 13
	v_lshl_add_u64 v[182:183], v[182:183], 0, s[22:23]
	s_cbranch_scc0 .LBB0_2091
	v_readlane_b32 s36, v254, 27
	v_readlane_b32 s37, v254, 28
	s_and_b64 vcc, exec, s[36:37]
	s_cbranch_vccz .LBB0_2094
	s_barrier

; #define PG8_STAGE(bufoff, gbase, o0, o1) do { \
;         __builtin_amdgcn_global_load_lds((const unsigned*)((const char*)(gbase) + (o0)), (LAS unsigned*)(lds + (bufoff) + ldsw), 16, 0, 0); \
;         __builtin_amdgcn_global_load_lds((const unsigned*)((const char*)(gbase) + (o1)), (LAS unsigned*)(lds + (bufoff) + ldsw + 8192), 16, 0, 0); } while (0)
; #define PG8_LDA(dst, b, h) do { _Pragma("unroll") for (int m = 0; m < 4; ++m) _Pragma("unroll") for (int k = 0; k < 2; ++k) dst[m][k] = *(const LAS bf16x8*)(lds + PG8_SA(b, h) + aoff + m * 2048 + k * 1024); } while (0)
; template <class Epi, class Sched, class Prob>
; __device__ __forceinline__ void gemm_phase(LAS unsigned char* lds, LAS unsigned char* lds_epi, const Prob g, const Sched& S, const Epi& E, int wid) {
;     ...
;         const bool has_next = S.next(ui + 1, nxt);
;         const char* nA = has_next ? g.a_base(nxt) : cA; const char* nB = has_next ? g.b_base(nxt) : cB;
; _Pragma("clang loop unroll(disable)")
;         for (int t = 0; t < nt; t += 2) {
;             const bool last = (t == nt - 2);
;             const char* a1 = cA + (size_t)(t + 1) * kstep;
;             const char* a2 = last ? nA : cA + (size_t)(t + 2) * kstep; const char* b2 = last ? nB : cB + (size_t)(t + 2) * kstep;
;             const char* a3 = a2 + kstep; const char* b3 = b2 + kstep;
;             PG8_LDB(B0, 0, 0); PG8_LDB(B1, 0, 1); PG8_SCHED; PG8_LDA(At, 0, 0); PG8_STAGE(PG8_SA(1, 1), a1, cA10, cA11);
;             PG8_WAIT_V(8); PG8_WAIT_L(0); PG8_BAR; PG8_MMA(0, 0, At, B0); PG8_MMA(0, 1, At, B1); PG8_BAR; PG8_SCHED;
;             PG8_LDA(At, 0, 1); PG8_STAGE(PG8_SB(0, 0), b2, vB0, vB1); PG8_STAGE(PG8_SB(0, 1), b2 + hstepB, vB0, vB1); PG8_STAGE(PG8_SA(0, 0), a2, cA00, cA01);
;             PG8_WAIT_V(8); PG8_WAIT_L(0); PG8_BAR; PG8_MMA(1, 0, At, B0); PG8_MMA(1, 1, At, B1); PG8_BAR; PG8_SCHED;
;             PG8_LDB(B0, 1, 0); PG8_LDB(B1, 1, 1); PG8_SCHED; PG8_LDA(At, 1, 0); PG8_STAGE(PG8_SA(0, 1), a2, cA10, cA11);
;             PG8_WAIT_V(8); PG8_WAIT_L(0); PG8_BAR; PG8_MMA(0, 0, At, B0); PG8_MMA(0, 1, At, B1); PG8_BAR; PG8_SCHED;
;             PG8_LDA(At, 1, 1); PG8_STAGE(PG8_SB(1, 0), b3, vB0, vB1); PG8_STAGE(PG8_SB(1, 1), b3 + hstepB, vB0, vB1); PG8_STAGE(PG8_SA(1, 0), a3, cA00, cA01);
;             PG8_WAIT_V(8); PG8_WAIT_L(0); PG8_BAR; PG8_MMA(1, 0, At, B0); PG8_MMA(1, 1, At, B1); PG8_BAR; PG8_SCHED;
.LBB0_2172:
	s_add_u32 s36, s36, 0x80
	v_mov_b32_e32 v32, 0
	s_addc_u32 s37, s37, 0
	v_lshl_add_u64 v[186:187], v[0:1], 0, s[22:23]
	s_mov_b32 s64, -2
	ds_read_b128 v[24:27], v161
	ds_read_b128 v[28:31], v161 offset:1024
	ds_read_b128 v[16:19], v161 offset:2048
	ds_read_b128 v[20:23], v161 offset:3072
	ds_read_b128 v[8:11], v207
	ds_read_b128 v[12:15], v207 offset:1024
	ds_read_b128 v[0:3], v207 offset:2048
	ds_read_b128 v[4:7], v207 offset:3072
	s_add_u32 s40, s36, 0x80
	s_addc_u32 s41, s37, 0
	s_cmp_eq_u32 s64, 52
	s_cselect_b64 vcc, -1, 0
	s_cselect_b32 s41, s31, s41
	s_cselect_b32 s40, s30, s40
	v_cndmask_b32_e32 v189, v187, v185, vcc
	v_cndmask_b32_e32 v188, v186, v184, vcc
	v_lshl_add_u64 v[212:213], s[36:37], 0, v[182:183]
	s_add_i32 m0, s33, 0xc000
	ds_read_b128 v[190:193], v208
	ds_read_b128 v[194:197], v208 offset:1024
	ds_read_b128 v[216:219], v208 offset:2048
	ds_read_b128 v[220:223], v208 offset:3072
	ds_read_b128 v[224:227], v208 offset:4096
	ds_read_b128 v[228:231], v208 offset:5120
	ds_read_b128 v[238:241], v208 offset:6144
	ds_read_b128 v[242:245], v208 offset:7168
	global_load_lds_dwordx4 v[212:213], off
	v_lshl_add_u64 v[212:213], s[36:37], 0, v[180:181]
	s_add_i32 m0, s33, 0xe000
	s_nop 0
	global_load_lds_dwordx4 v[212:213], off
	s_waitcnt vmcnt(8)
	s_waitcnt lgkmcnt(0)
	s_barrier
	s_setprio 1
	s_waitcnt lgkmcnt(0)
	v_mfma_f32_16x16x128_f8f6f4 v[156:159], v[24:31], v[190:197], 0
	v_mfma_f32_16x16x128_f8f6f4 v[152:155], v[16:23], v[190:197], 0
	v_mfma_f32_16x16x128_f8f6f4 v[140:143], v[24:31], v[216:223], 0
	v_mfma_f32_16x16x128_f8f6f4 v[136:139], v[16:23], v[216:223], 0
	v_mfma_f32_16x16x128_f8f6f4 v[124:127], v[24:31], v[224:231], 0
	v_mfma_f32_16x16x128_f8f6f4 v[120:123], v[16:23], v[224:231], 0
	v_mfma_f32_16x16x128_f8f6f4 v[108:111], v[24:31], v[238:245], 0
	v_mfma_f32_16x16x128_f8f6f4 v[104:107], v[16:23], v[238:245], 0
	v_mfma_f32_16x16x128_f8f6f4 v[148:151], v[8:15], v[190:197], 0
	v_mfma_f32_16x16x128_f8f6f4 v[144:147], v[0:7], v[190:197], 0
	v_mfma_f32_16x16x128_f8f6f4 v[132:135], v[8:15], v[216:223], 0
	v_mfma_f32_16x16x128_f8f6f4 v[128:131], v[0:7], v[216:223], 0
	v_mfma_f32_16x16x128_f8f6f4 v[116:119], v[8:15], v[224:231], 0
	v_mfma_f32_16x16x128_f8f6f4 v[112:115], v[0:7], v[224:231], 0
	v_mfma_f32_16x16x128_f8f6f4 v[100:103], v[8:15], v[238:245], 0
	v_mfma_f32_16x16x128_f8f6f4 v[96:99], v[0:7], v[238:245], 0
	s_setprio 0
	s_barrier
	s_add_i32 s65, s58, s97
	v_lshl_add_u64 v[190:191], v[188:189], 0, v[162:163]
	s_mov_b32 m0, s65
	ds_read_b128 v[216:219], v208 offset:16384
	ds_read_b128 v[220:223], v208 offset:17408
	ds_read_b128 v[224:227], v208 offset:18432
	ds_read_b128 v[228:231], v208 offset:19456
	ds_read_b128 v[238:241], v208 offset:20480
	ds_read_b128 v[242:245], v208 offset:21504
	ds_read_b128 v[246:249], v208 offset:22528
	ds_read_b128 v[250:253], v208 offset:23552
	global_load_lds_dwordx4 v[190:191], off
	v_lshl_add_u64 v[192:193], v[188:189], 0, v[164:165]
	s_add_i32 m0, s65, 0x2000
	v_lshl_add_u64 v[194:195], v[188:189], 0, s[16:17]
	s_add_i32 s65, s59, s97
	global_load_lds_dwordx4 v[192:193], off
	v_lshl_add_u64 v[196:197], v[194:195], 0, v[162:163]
	s_mov_b32 m0, s65
	v_lshl_add_u64 v[194:195], v[194:195], 0, v[164:165]
	global_load_lds_dwordx4 v[196:197], off
	s_add_i32 m0, s65, 0x2000
	v_lshl_add_u64 v[196:197], s[40:41], 0, v[174:175]
	global_load_lds_dwordx4 v[194:195], off
	v_lshl_add_u64 v[194:195], s[40:41], 0, v[170:171]
	s_mov_b32 m0, s33
	s_nop 0
	global_load_lds_dwordx4 v[194:195], off
	s_mov_b32 m0, s35
	s_nop 0
	global_load_lds_dwordx4 v[196:197], off
	s_waitcnt vmcnt(8)
	s_waitcnt lgkmcnt(0)
	s_barrier
	s_setprio 1
	s_waitcnt lgkmcnt(0)
	v_mfma_f32_16x16x128_f8f6f4 v[92:95], v[24:31], v[216:223], 0
	v_mfma_f32_16x16x128_f8f6f4 v[88:91], v[16:23], v[216:223], 0
	v_mfma_f32_16x16x128_f8f6f4 v[76:79], v[24:31], v[224:231], 0
	v_mfma_f32_16x16x128_f8f6f4 v[72:75], v[16:23], v[224:231], 0
	v_mfma_f32_16x16x128_f8f6f4 v[60:63], v[24:31], v[238:245], 0
	v_mfma_f32_16x16x128_f8f6f4 v[56:59], v[16:23], v[238:245], 0
	v_mfma_f32_16x16x128_f8f6f4 v[44:47], v[24:31], v[246:253], 0
	v_mfma_f32_16x16x128_f8f6f4 v[40:43], v[16:23], v[246:253], 0
	v_mfma_f32_16x16x128_f8f6f4 v[84:87], v[8:15], v[216:223], 0
	v_mfma_f32_16x16x128_f8f6f4 v[80:83], v[0:7], v[216:223], 0
	v_mfma_f32_16x16x128_f8f6f4 v[68:71], v[8:15], v[224:231], 0
	v_mfma_f32_16x16x128_f8f6f4 v[64:67], v[0:7], v[224:231], 0
	v_mfma_f32_16x16x128_f8f6f4 v[52:55], v[8:15], v[238:245], 0
	v_mfma_f32_16x16x128_f8f6f4 v[48:51], v[0:7], v[238:245], 0
	v_mfma_f32_16x16x128_f8f6f4 v[36:39], v[8:15], v[246:253], 0
	v_mfma_f32_16x16x128_f8f6f4 v[32:35], v[0:7], v[246:253], 0
	s_setprio 0
	s_barrier
	s_add_i32 s65, 0, 0x18000
	s_add_i32 s66, 0, 0x1c000
	v_add_u32_e32 v12, s65, v204
	v_add_u32_e32 v28, s66, v204
	ds_read_b128 v[0:3], v12
	ds_read_b128 v[4:7], v12 offset:1024
	ds_read_b128 v[8:11], v12 offset:2048
	ds_read_b128 v[12:15], v12 offset:3072
	ds_read_b128 v[16:19], v28
	ds_read_b128 v[20:23], v28 offset:1024
	ds_read_b128 v[24:27], v28 offset:2048
	ds_read_b128 v[28:31], v28 offset:3072
	s_mov_b32 m0, s48
	v_lshl_add_u64 v[212:213], s[40:41], 0, v[172:173]
	ds_read_b128 v[216:219], v208 offset:32768
	ds_read_b128 v[220:223], v208 offset:33792
	ds_read_b128 v[224:227], v208 offset:34816
	ds_read_b128 v[228:231], v208 offset:35840
	ds_read_b128 v[238:241], v208 offset:36864
	ds_read_b128 v[242:245], v208 offset:37888
	ds_read_b128 v[246:249], v208 offset:38912
	ds_read_b128 v[250:253], v208 offset:39936
	global_load_lds_dwordx4 v[212:213], off
	v_lshl_add_u64 v[212:213], s[40:41], 0, v[176:177]
	s_mov_b32 m0, s52
	s_nop 0
	global_load_lds_dwordx4 v[212:213], off
	s_waitcnt vmcnt(8)
	s_waitcnt lgkmcnt(0)
	s_barrier
; #define PG8_STAGE(bufoff, gbase, o0, o1) do { \
;         __builtin_amdgcn_global_load_lds((const unsigned*)((const char*)(gbase) + (o0)), (LAS unsigned*)(lds + (bufoff) + ldsw), 16, 0, 0); \
;         __builtin_amdgcn_global_load_lds((const unsigned*)((const char*)(gbase) + (o1)), (LAS unsigned*)(lds + (bufoff) + ldsw + 8192), 16, 0, 0); } while (0)
; #define PG8_LDA(dst, b, h) do { _Pragma("unroll") for (int m = 0; m < 4; ++m) _Pragma("unroll") for (int k = 0; k < 2; ++k) dst[m][k] = *(const LAS bf16x8*)(lds + PG8_SA(b, h) + aoff + m * 2048 + k * 1024); } while (0)
; #define PG8_LDB(dst, b, h) do { _Pragma("unroll") for (int n = 0; n < 2; ++n) _Pragma("unroll") for (int k = 0; k < 2; ++k) dst[n][k] = *(const LAS bf16x8*)(lds + PG8_SB(b, h) + boff + n * 2048 + k * 1024); } while (0)
; #define PG8_WAIT_V(n) asm volatile("s_waitcnt vmcnt(" #n ")" ::: "memory")
; #define PG8_WAIT_L(n) asm volatile("s_waitcnt lgkmcnt(" #n ")" ::: "memory")
; #define PG8_BAR __builtin_amdgcn_s_barrier()
; #define PG8_SCHED __builtin_amdgcn_sched_barrier(0)
; template <class Epi, class Sched, class Prob>
; __device__ __forceinline__ void gemm_phase(LAS unsigned char* lds, LAS unsigned char* lds_epi, const Prob g, const Sched& S, const Epi& E, int wid) {
;     ...
;             PG8_LDB(B0, 0, 0); PG8_LDB(B1, 0, 1); PG8_SCHED; PG8_LDA(At, 0, 0); PG8_STAGE(PG8_SA(1, 1), a1, cA10, cA11);
;             PG8_WAIT_V(8); PG8_WAIT_L(0); PG8_BAR; PG8_MMA(0, 0, At, B0); PG8_MMA(0, 1, At, B1); PG8_BAR; PG8_SCHED;
;             PG8_LDA(At, 0, 1); PG8_STAGE(PG8_SB(0, 0), b2, vB0, vB1); PG8_STAGE(PG8_SB(0, 1), b2 + hstepB, vB0, vB1); PG8_STAGE(PG8_SA(0, 0), a2, cA00, cA01);
;             PG8_WAIT_V(8); PG8_WAIT_L(0); PG8_BAR; PG8_MMA(1, 0, At, B0); PG8_MMA(1, 1, At, B1); PG8_BAR; PG8_SCHED;
;             PG8_LDB(B0, 1, 0); PG8_LDB(B1, 1, 1); PG8_SCHED; PG8_LDA(At, 1, 0); PG8_STAGE(PG8_SA(0, 1), a2, cA10, cA11);
;             PG8_WAIT_V(8); PG8_WAIT_L(0); PG8_BAR; PG8_MMA(0, 0, At, B0); PG8_MMA(0, 1, At, B1); PG8_BAR; PG8_SCHED;
;             PG8_LDA(At, 1, 1); PG8_STAGE(PG8_SB(1, 0), b3, vB0, vB1); PG8_STAGE(PG8_SB(1, 1), b3 + hstepB, vB0, vB1); PG8_STAGE(PG8_SA(1, 0), a3, cA00, cA01);
;             PG8_WAIT_V(8); PG8_WAIT_L(0); PG8_BAR; PG8_MMA(1, 0, At, B0); PG8_MMA(1, 1, At, B1); PG8_BAR; PG8_SCHED;
	s_setprio 1
	s_waitcnt lgkmcnt(0)
	v_mfma_f32_16x16x128_f8f6f4 v[156:159], v[0:7], v[216:223], v[156:159]
	v_mfma_f32_16x16x128_f8f6f4 v[152:155], v[8:15], v[216:223], v[152:155]
	v_mfma_f32_16x16x128_f8f6f4 v[140:143], v[0:7], v[224:231], v[140:143]
	v_mfma_f32_16x16x128_f8f6f4 v[136:139], v[8:15], v[224:231], v[136:139]
	v_mfma_f32_16x16x128_f8f6f4 v[124:127], v[0:7], v[238:245], v[124:127]
	v_mfma_f32_16x16x128_f8f6f4 v[120:123], v[8:15], v[238:245], v[120:123]
	v_mfma_f32_16x16x128_f8f6f4 v[108:111], v[0:7], v[246:253], v[108:111]
	v_mfma_f32_16x16x128_f8f6f4 v[104:107], v[8:15], v[246:253], v[104:107]
	v_mfma_f32_16x16x128_f8f6f4 v[148:151], v[16:23], v[216:223], v[148:151]
	v_mfma_f32_16x16x128_f8f6f4 v[144:147], v[24:31], v[216:223], v[144:147]
	v_mfma_f32_16x16x128_f8f6f4 v[132:135], v[16:23], v[224:231], v[132:135]
	v_mfma_f32_16x16x128_f8f6f4 v[128:131], v[24:31], v[224:231], v[128:131]
	v_mfma_f32_16x16x128_f8f6f4 v[116:119], v[16:23], v[238:245], v[116:119]
	v_mfma_f32_16x16x128_f8f6f4 v[112:115], v[24:31], v[238:245], v[112:115]
	v_mfma_f32_16x16x128_f8f6f4 v[100:103], v[16:23], v[246:253], v[100:103]
	v_mfma_f32_16x16x128_f8f6f4 v[96:99], v[24:31], v[246:253], v[96:99]
	s_setprio 0
	s_barrier
	s_add_i32 s40, s65, s97
	v_lshl_add_u64 v[190:191], v[190:191], 0, s[18:19]
	s_mov_b32 m0, s40
	ds_read_b128 v[216:219], v208 offset:49152
	ds_read_b128 v[220:223], v208 offset:50176
	ds_read_b128 v[224:227], v208 offset:51200
	ds_read_b128 v[228:231], v208 offset:52224
	ds_read_b128 v[238:241], v208 offset:53248
	ds_read_b128 v[242:245], v208 offset:54272
	ds_read_b128 v[246:249], v208 offset:55296
	ds_read_b128 v[250:253], v208 offset:56320
	global_load_lds_dwordx4 v[190:191], off
	v_lshl_add_u64 v[190:191], v[192:193], 0, s[18:19]
	s_add_i32 m0, s40, 0x2000
	v_lshl_add_u64 v[188:189], v[188:189], 0, s[20:21]
	s_add_i32 s40, s66, s97
	global_load_lds_dwordx4 v[190:191], off
	v_lshl_add_u64 v[190:191], v[188:189], 0, v[162:163]
	s_mov_b32 m0, s40
	v_lshl_add_u64 v[188:189], v[188:189], 0, v[164:165]
	global_load_lds_dwordx4 v[190:191], off
	s_add_i32 m0, s40, 0x2000
	s_nop 0
	global_load_lds_dwordx4 v[188:189], off
	v_lshl_add_u64 v[188:189], v[194:195], 0, s[18:19]
	s_mov_b32 m0, s54
	s_nop 0
	global_load_lds_dwordx4 v[188:189], off
	v_lshl_add_u64 v[188:189], v[196:197], 0, s[18:19]
	s_mov_b32 m0, s55
	s_nop 0
	global_load_lds_dwordx4 v[188:189], off
	s_waitcnt vmcnt(8)
	s_waitcnt lgkmcnt(0)
	s_barrier
	s_setprio 1
	s_waitcnt lgkmcnt(0)
	v_mfma_f32_16x16x128_f8f6f4 v[92:95], v[0:7], v[216:223], v[92:95]
	v_mfma_f32_16x16x128_f8f6f4 v[88:91], v[8:15], v[216:223], v[88:91]
	v_mfma_f32_16x16x128_f8f6f4 v[76:79], v[0:7], v[224:231], v[76:79]
	v_mfma_f32_16x16x128_f8f6f4 v[72:75], v[8:15], v[224:231], v[72:75]
	v_mfma_f32_16x16x128_f8f6f4 v[60:63], v[0:7], v[238:245], v[60:63]
	v_mfma_f32_16x16x128_f8f6f4 v[56:59], v[8:15], v[238:245], v[56:59]
	v_mfma_f32_16x16x128_f8f6f4 v[44:47], v[0:7], v[246:253], v[44:47]
	v_mfma_f32_16x16x128_f8f6f4 v[40:43], v[8:15], v[246:253], v[40:43]
	v_mfma_f32_16x16x128_f8f6f4 v[84:87], v[16:23], v[216:223], v[84:87]
	v_mfma_f32_16x16x128_f8f6f4 v[80:83], v[24:31], v[216:223], v[80:83]
	v_mfma_f32_16x16x128_f8f6f4 v[68:71], v[16:23], v[224:231], v[68:71]
	v_mfma_f32_16x16x128_f8f6f4 v[64:67], v[24:31], v[224:231], v[64:67]
	v_mfma_f32_16x16x128_f8f6f4 v[52:55], v[16:23], v[238:245], v[52:55]
	v_mfma_f32_16x16x128_f8f6f4 v[48:51], v[24:31], v[238:245], v[48:51]
	v_mfma_f32_16x16x128_f8f6f4 v[36:39], v[16:23], v[246:253], v[36:39]
	v_mfma_f32_16x16x128_f8f6f4 v[32:35], v[24:31], v[246:253], v[32:35]
	s_setprio 0
	s_barrier
	s_add_i32 s64, s64, 2
	s_add_u32 s36, s36, 0x100
	s_addc_u32 s37, s37, 0
	s_cmp_gt_u32 s64, 53
	v_lshl_add_u64 v[186:187], v[186:187], 0, s[22:23]
.LBB0_2173:
	ds_read_b128 v[24:27], v161
	ds_read_b128 v[28:31], v161 offset:1024
	ds_read_b128 v[16:19], v161 offset:2048
	ds_read_b128 v[20:23], v161 offset:3072
	ds_read_b128 v[8:11], v207
	ds_read_b128 v[12:15], v207 offset:1024
	ds_read_b128 v[0:3], v207 offset:2048
	ds_read_b128 v[4:7], v207 offset:3072
	s_add_u32 s40, s36, 0x80
	s_addc_u32 s41, s37, 0
	s_cmp_eq_u32 s64, 52
	s_cselect_b64 vcc, -1, 0
	s_cselect_b32 s41, s31, s41
	s_cselect_b32 s40, s30, s40
	v_cndmask_b32_e32 v189, v187, v185, vcc
	v_cndmask_b32_e32 v188, v186, v184, vcc
	v_lshl_add_u64 v[212:213], s[36:37], 0, v[182:183]
	s_add_i32 m0, s33, 0xc000
	ds_read_b128 v[190:193], v208
	ds_read_b128 v[194:197], v208 offset:1024
	ds_read_b128 v[216:219], v208 offset:2048
	ds_read_b128 v[220:223], v208 offset:3072
	ds_read_b128 v[224:227], v208 offset:4096
	ds_read_b128 v[228:231], v208 offset:5120
	ds_read_b128 v[238:241], v208 offset:6144
	ds_read_b128 v[242:245], v208 offset:7168
	global_load_lds_dwordx4 v[212:213], off
	v_lshl_add_u64 v[212:213], s[36:37], 0, v[180:181]
	s_add_i32 m0, s33, 0xe000
	s_nop 0
	global_load_lds_dwordx4 v[212:213], off
	s_waitcnt vmcnt(8)
	s_waitcnt lgkmcnt(0)
	s_barrier
	s_setprio 1
	s_waitcnt lgkmcnt(0)
	v_mfma_f32_16x16x128_f8f6f4 v[156:159], v[24:31], v[190:197], v[156:159]
	v_mfma_f32_16x16x128_f8f6f4 v[152:155], v[16:23], v[190:197], v[152:155]
	v_mfma_f32_16x16x128_f8f6f4 v[140:143], v[24:31], v[216:223], v[140:143]
	v_mfma_f32_16x16x128_f8f6f4 v[136:139], v[16:23], v[216:223], v[136:139]
	v_mfma_f32_16x16x128_f8f6f4 v[124:127], v[24:31], v[224:231], v[124:127]
	v_mfma_f32_16x16x128_f8f6f4 v[120:123], v[16:23], v[224:231], v[120:123]
	v_mfma_f32_16x16x128_f8f6f4 v[108:111], v[24:31], v[238:245], v[108:111]
	v_mfma_f32_16x16x128_f8f6f4 v[104:107], v[16:23], v[238:245], v[104:107]
	v_mfma_f32_16x16x128_f8f6f4 v[148:151], v[8:15], v[190:197], v[148:151]
	v_mfma_f32_16x16x128_f8f6f4 v[144:147], v[0:7], v[190:197], v[144:147]
	v_mfma_f32_16x16x128_f8f6f4 v[132:135], v[8:15], v[216:223], v[132:135]
	v_mfma_f32_16x16x128_f8f6f4 v[128:131], v[0:7], v[216:223], v[128:131]
	v_mfma_f32_16x16x128_f8f6f4 v[116:119], v[8:15], v[224:231], v[116:119]
	v_mfma_f32_16x16x128_f8f6f4 v[112:115], v[0:7], v[224:231], v[112:115]
	v_mfma_f32_16x16x128_f8f6f4 v[100:103], v[8:15], v[238:245], v[100:103]
	v_mfma_f32_16x16x128_f8f6f4 v[96:99], v[0:7], v[238:245], v[96:99]
	s_setprio 0
	s_barrier
; #define PG8_STAGE(bufoff, gbase, o0, o1) do { \
;         __builtin_amdgcn_global_load_lds((const unsigned*)((const char*)(gbase) + (o0)), (LAS unsigned*)(lds + (bufoff) + ldsw), 16, 0, 0); \
;         __builtin_amdgcn_global_load_lds((const unsigned*)((const char*)(gbase) + (o1)), (LAS unsigned*)(lds + (bufoff) + ldsw + 8192), 16, 0, 0); } while (0)
; #define PG8_LDA(dst, b, h) do { _Pragma("unroll") for (int m = 0; m < 4; ++m) _Pragma("unroll") for (int k = 0; k < 2; ++k) dst[m][k] = *(const LAS bf16x8*)(lds + PG8_SA(b, h) + aoff + m * 2048 + k * 1024); } while (0)
; #define PG8_LDB(dst, b, h) do { _Pragma("unroll") for (int n = 0; n < 2; ++n) _Pragma("unroll") for (int k = 0; k < 2; ++k) dst[n][k] = *(const LAS bf16x8*)(lds + PG8_SB(b, h) + boff + n * 2048 + k * 1024); } while (0)
; #define PG8_WAIT_V(n) asm volatile("s_waitcnt vmcnt(" #n ")" ::: "memory")
; #define PG8_WAIT_L(n) asm volatile("s_waitcnt lgkmcnt(" #n ")" ::: "memory")
; #define PG8_BAR __builtin_amdgcn_s_barrier()
; #define PG8_SCHED __builtin_amdgcn_sched_barrier(0)
; template <class Epi, class Sched, class Prob>
; __device__ __forceinline__ void gemm_phase(LAS unsigned char* lds, LAS unsigned char* lds_epi, const Prob g, const Sched& S, const Epi& E, int wid) {
;     ...
;             PG8_LDA(At, 0, 1); PG8_STAGE(PG8_SB(0, 0), b2, vB0, vB1); PG8_STAGE(PG8_SB(0, 1), b2 + hstepB, vB0, vB1); PG8_STAGE(PG8_SA(0, 0), a2, cA00, cA01);
;             PG8_WAIT_V(8); PG8_WAIT_L(0); PG8_BAR; PG8_MMA(1, 0, At, B0); PG8_MMA(1, 1, At, B1); PG8_BAR; PG8_SCHED;
;             PG8_LDB(B0, 1, 0); PG8_LDB(B1, 1, 1); PG8_SCHED; PG8_LDA(At, 1, 0); PG8_STAGE(PG8_SA(0, 1), a2, cA10, cA11);
;             PG8_WAIT_V(8); PG8_WAIT_L(0); PG8_BAR; PG8_MMA(0, 0, At, B0); PG8_MMA(0, 1, At, B1); PG8_BAR; PG8_SCHED;
	s_add_i32 s65, s58, s97
	v_lshl_add_u64 v[190:191], v[188:189], 0, v[162:163]
	s_mov_b32 m0, s65
	ds_read_b128 v[216:219], v208 offset:16384
	ds_read_b128 v[220:223], v208 offset:17408
	ds_read_b128 v[224:227], v208 offset:18432
	ds_read_b128 v[228:231], v208 offset:19456
	ds_read_b128 v[238:241], v208 offset:20480
	ds_read_b128 v[242:245], v208 offset:21504
	ds_read_b128 v[246:249], v208 offset:22528
	ds_read_b128 v[250:253], v208 offset:23552
	global_load_lds_dwordx4 v[190:191], off
	v_lshl_add_u64 v[192:193], v[188:189], 0, v[164:165]
	s_add_i32 m0, s65, 0x2000
	v_lshl_add_u64 v[194:195], v[188:189], 0, s[16:17]
	s_add_i32 s65, s59, s97
	global_load_lds_dwordx4 v[192:193], off
	v_lshl_add_u64 v[196:197], v[194:195], 0, v[162:163]
	s_mov_b32 m0, s65
	v_lshl_add_u64 v[194:195], v[194:195], 0, v[164:165]
	global_load_lds_dwordx4 v[196:197], off
	s_add_i32 m0, s65, 0x2000
	v_lshl_add_u64 v[196:197], s[40:41], 0, v[174:175]
	global_load_lds_dwordx4 v[194:195], off
	v_lshl_add_u64 v[194:195], s[40:41], 0, v[170:171]
	s_mov_b32 m0, s33
	s_nop 0
	global_load_lds_dwordx4 v[194:195], off
	s_mov_b32 m0, s35
	s_nop 0
	global_load_lds_dwordx4 v[196:197], off
	s_waitcnt vmcnt(8)
	s_waitcnt lgkmcnt(0)
	s_barrier
	s_setprio 1
	s_waitcnt lgkmcnt(0)
	v_mfma_f32_16x16x128_f8f6f4 v[92:95], v[24:31], v[216:223], v[92:95]
	v_mfma_f32_16x16x128_f8f6f4 v[88:91], v[16:23], v[216:223], v[88:91]
	v_mfma_f32_16x16x128_f8f6f4 v[76:79], v[24:31], v[224:231], v[76:79]
	v_mfma_f32_16x16x128_f8f6f4 v[72:75], v[16:23], v[224:231], v[72:75]
	v_mfma_f32_16x16x128_f8f6f4 v[60:63], v[24:31], v[238:245], v[60:63]
	v_mfma_f32_16x16x128_f8f6f4 v[56:59], v[16:23], v[238:245], v[56:59]
	v_mfma_f32_16x16x128_f8f6f4 v[44:47], v[24:31], v[246:253], v[44:47]
	v_mfma_f32_16x16x128_f8f6f4 v[40:43], v[16:23], v[246:253], v[40:43]
	v_mfma_f32_16x16x128_f8f6f4 v[84:87], v[8:15], v[216:223], v[84:87]
	v_mfma_f32_16x16x128_f8f6f4 v[80:83], v[0:7], v[216:223], v[80:83]
	v_mfma_f32_16x16x128_f8f6f4 v[68:71], v[8:15], v[224:231], v[68:71]
	v_mfma_f32_16x16x128_f8f6f4 v[64:67], v[0:7], v[224:231], v[64:67]
	v_mfma_f32_16x16x128_f8f6f4 v[52:55], v[8:15], v[238:245], v[52:55]
	v_mfma_f32_16x16x128_f8f6f4 v[48:51], v[0:7], v[238:245], v[48:51]
	v_mfma_f32_16x16x128_f8f6f4 v[36:39], v[8:15], v[246:253], v[36:39]
	v_mfma_f32_16x16x128_f8f6f4 v[32:35], v[0:7], v[246:253], v[32:35]
	s_setprio 0
	s_barrier
	s_add_i32 s65, 0, 0x18000
	s_add_i32 s66, 0, 0x1c000
	v_add_u32_e32 v12, s65, v204
	v_add_u32_e32 v28, s66, v204
	ds_read_b128 v[0:3], v12
	ds_read_b128 v[4:7], v12 offset:1024
	ds_read_b128 v[8:11], v12 offset:2048
	ds_read_b128 v[12:15], v12 offset:3072
	ds_read_b128 v[16:19], v28
	ds_read_b128 v[20:23], v28 offset:1024
	ds_read_b128 v[24:27], v28 offset:2048
	ds_read_b128 v[28:31], v28 offset:3072
	s_mov_b32 m0, s48
	v_lshl_add_u64 v[212:213], s[40:41], 0, v[172:173]
	ds_read_b128 v[216:219], v208 offset:32768
	ds_read_b128 v[220:223], v208 offset:33792
	ds_read_b128 v[224:227], v208 offset:34816
	ds_read_b128 v[228:231], v208 offset:35840
	ds_read_b128 v[238:241], v208 offset:36864
	ds_read_b128 v[242:245], v208 offset:37888
	ds_read_b128 v[246:249], v208 offset:38912
	ds_read_b128 v[250:253], v208 offset:39936
	global_load_lds_dwordx4 v[212:213], off
	v_lshl_add_u64 v[212:213], s[40:41], 0, v[176:177]
	s_mov_b32 m0, s52
	s_nop 0
	global_load_lds_dwordx4 v[212:213], off
	s_waitcnt vmcnt(8)
	s_waitcnt lgkmcnt(0)
	s_barrier
; #define PG8_STAGE(bufoff, gbase, o0, o1) do { \
;         __builtin_amdgcn_global_load_lds((const unsigned*)((const char*)(gbase) + (o0)), (LAS unsigned*)(lds + (bufoff) + ldsw), 16, 0, 0); \
;         __builtin_amdgcn_global_load_lds((const unsigned*)((const char*)(gbase) + (o1)), (LAS unsigned*)(lds + (bufoff) + ldsw + 8192), 16, 0, 0); } while (0)
; #define PG8_LDA(dst, b, h) do { _Pragma("unroll") for (int m = 0; m < 4; ++m) _Pragma("unroll") for (int k = 0; k < 2; ++k) dst[m][k] = *(const LAS bf16x8*)(lds + PG8_SA(b, h) + aoff + m * 2048 + k * 1024); } while (0)
; #define PG8_WAIT_V(n) asm volatile("s_waitcnt vmcnt(" #n ")" ::: "memory")
; #define PG8_WAIT_L(n) asm volatile("s_waitcnt lgkmcnt(" #n ")" ::: "memory")
; #define PG8_BAR __builtin_amdgcn_s_barrier()
; #define PG8_SCHED __builtin_amdgcn_sched_barrier(0)
; template <class Epi, class Sched, class Prob>
; __device__ __forceinline__ void gemm_phase(LAS unsigned char* lds, LAS unsigned char* lds_epi, const Prob g, const Sched& S, const Epi& E, int wid) {
;     ...
;             PG8_WAIT_V(8); PG8_WAIT_L(0); PG8_BAR; PG8_MMA(0, 0, At, B0); PG8_MMA(0, 1, At, B1); PG8_BAR; PG8_SCHED;
;             PG8_LDA(At, 1, 1); PG8_STAGE(PG8_SB(1, 0), b3, vB0, vB1); PG8_STAGE(PG8_SB(1, 1), b3 + hstepB, vB0, vB1); PG8_STAGE(PG8_SA(1, 0), a3, cA00, cA01);
;             PG8_WAIT_V(8); PG8_WAIT_L(0); PG8_BAR; PG8_MMA(1, 0, At, B0); PG8_MMA(1, 1, At, B1); PG8_BAR; PG8_SCHED;
;         }
;         if constexpr (Prob::FP8) asm volatile("s_nop 7\n\ts_nop 7\n\ts_nop 7" ::: "memory");
;         if (wr == 0) PG8_BAR;
	s_setprio 1
	s_waitcnt lgkmcnt(0)
	v_mfma_f32_16x16x128_f8f6f4 v[156:159], v[0:7], v[216:223], v[156:159]
	v_mfma_f32_16x16x128_f8f6f4 v[152:155], v[8:15], v[216:223], v[152:155]
	v_mfma_f32_16x16x128_f8f6f4 v[140:143], v[0:7], v[224:231], v[140:143]
	v_mfma_f32_16x16x128_f8f6f4 v[136:139], v[8:15], v[224:231], v[136:139]
	v_mfma_f32_16x16x128_f8f6f4 v[124:127], v[0:7], v[238:245], v[124:127]
	v_mfma_f32_16x16x128_f8f6f4 v[120:123], v[8:15], v[238:245], v[120:123]
	v_mfma_f32_16x16x128_f8f6f4 v[108:111], v[0:7], v[246:253], v[108:111]
	v_mfma_f32_16x16x128_f8f6f4 v[104:107], v[8:15], v[246:253], v[104:107]
	v_mfma_f32_16x16x128_f8f6f4 v[148:151], v[16:23], v[216:223], v[148:151]
	v_mfma_f32_16x16x128_f8f6f4 v[144:147], v[24:31], v[216:223], v[144:147]
	v_mfma_f32_16x16x128_f8f6f4 v[132:135], v[16:23], v[224:231], v[132:135]
	v_mfma_f32_16x16x128_f8f6f4 v[128:131], v[24:31], v[224:231], v[128:131]
	v_mfma_f32_16x16x128_f8f6f4 v[116:119], v[16:23], v[238:245], v[116:119]
	v_mfma_f32_16x16x128_f8f6f4 v[112:115], v[24:31], v[238:245], v[112:115]
	v_mfma_f32_16x16x128_f8f6f4 v[100:103], v[16:23], v[246:253], v[100:103]
	v_mfma_f32_16x16x128_f8f6f4 v[96:99], v[24:31], v[246:253], v[96:99]
	s_setprio 0
	s_barrier
	s_add_i32 s40, s65, s97
	v_lshl_add_u64 v[190:191], v[190:191], 0, s[18:19]
	s_mov_b32 m0, s40
	ds_read_b128 v[216:219], v208 offset:49152
	ds_read_b128 v[220:223], v208 offset:50176
	ds_read_b128 v[224:227], v208 offset:51200
	ds_read_b128 v[228:231], v208 offset:52224
	ds_read_b128 v[238:241], v208 offset:53248
	ds_read_b128 v[242:245], v208 offset:54272
	ds_read_b128 v[246:249], v208 offset:55296
	ds_read_b128 v[250:253], v208 offset:56320
	global_load_lds_dwordx4 v[190:191], off
	v_lshl_add_u64 v[190:191], v[192:193], 0, s[18:19]
	s_add_i32 m0, s40, 0x2000
	v_lshl_add_u64 v[188:189], v[188:189], 0, s[20:21]
	s_add_i32 s40, s66, s97
	global_load_lds_dwordx4 v[190:191], off
	v_lshl_add_u64 v[190:191], v[188:189], 0, v[162:163]
	s_mov_b32 m0, s40
	v_lshl_add_u64 v[188:189], v[188:189], 0, v[164:165]
	global_load_lds_dwordx4 v[190:191], off
	s_add_i32 m0, s40, 0x2000
	s_nop 0
	global_load_lds_dwordx4 v[188:189], off
	v_lshl_add_u64 v[188:189], v[194:195], 0, s[18:19]
	s_mov_b32 m0, s54
	s_nop 0
	global_load_lds_dwordx4 v[188:189], off
	v_lshl_add_u64 v[188:189], v[196:197], 0, s[18:19]
	s_mov_b32 m0, s55
	s_nop 0
	global_load_lds_dwordx4 v[188:189], off
	s_waitcnt vmcnt(8)
	s_waitcnt lgkmcnt(0)
	s_barrier
	s_setprio 1
	s_waitcnt lgkmcnt(0)
	v_mfma_f32_16x16x128_f8f6f4 v[92:95], v[0:7], v[216:223], v[92:95]
	v_mfma_f32_16x16x128_f8f6f4 v[88:91], v[8:15], v[216:223], v[88:91]
	v_mfma_f32_16x16x128_f8f6f4 v[76:79], v[0:7], v[224:231], v[76:79]
	v_mfma_f32_16x16x128_f8f6f4 v[72:75], v[8:15], v[224:231], v[72:75]
	v_mfma_f32_16x16x128_f8f6f4 v[60:63], v[0:7], v[238:245], v[60:63]
	v_mfma_f32_16x16x128_f8f6f4 v[56:59], v[8:15], v[238:245], v[56:59]
	v_mfma_f32_16x16x128_f8f6f4 v[44:47], v[0:7], v[246:253], v[44:47]
	v_mfma_f32_16x16x128_f8f6f4 v[40:43], v[8:15], v[246:253], v[40:43]
	v_mfma_f32_16x16x128_f8f6f4 v[84:87], v[16:23], v[216:223], v[84:87]
	v_mfma_f32_16x16x128_f8f6f4 v[80:83], v[24:31], v[216:223], v[80:83]
	v_mfma_f32_16x16x128_f8f6f4 v[68:71], v[16:23], v[224:231], v[68:71]
	v_mfma_f32_16x16x128_f8f6f4 v[64:67], v[24:31], v[224:231], v[64:67]
	v_mfma_f32_16x16x128_f8f6f4 v[52:55], v[16:23], v[238:245], v[52:55]
	v_mfma_f32_16x16x128_f8f6f4 v[48:51], v[24:31], v[238:245], v[48:51]
	v_mfma_f32_16x16x128_f8f6f4 v[36:39], v[16:23], v[246:253], v[36:39]
	v_mfma_f32_16x16x128_f8f6f4 v[32:35], v[24:31], v[246:253], v[32:35]
	s_setprio 0
	s_barrier
	s_add_i32 s64, s64, 2
	s_add_u32 s36, s36, 0x100
	s_addc_u32 s37, s37, 0
	s_cmp_gt_u32 s64, 53
	v_lshl_add_u64 v[186:187], v[186:187], 0, s[22:23]
	s_cbranch_scc0 .LBB0_2173
	s_nop 7
	s_nop 7
	s_nop 7
	v_readlane_b32 s36, v254, 27
	v_readlane_b32 s37, v254, 28
	s_and_b64 vcc, exec, s[36:37]
	s_cbranch_vccz .LBB0_2176
	s_barrier

; #define PG8_STAGE(bufoff, gbase, o0, o1) do { \
;         __builtin_amdgcn_global_load_lds((const unsigned*)((const char*)(gbase) + (o0)), (LAS unsigned*)(lds + (bufoff) + ldsw), 16, 0, 0); \
;         __builtin_amdgcn_global_load_lds((const unsigned*)((const char*)(gbase) + (o1)), (LAS unsigned*)(lds + (bufoff) + ldsw + 8192), 16, 0, 0); } while (0)
; #define PG8_LDA(dst, b, h) do { _Pragma("unroll") for (int m = 0; m < 4; ++m) _Pragma("unroll") for (int k = 0; k < 2; ++k) dst[m][k] = *(const LAS bf16x8*)(lds + PG8_SA(b, h) + aoff + m * 2048 + k * 1024); } while (0)
; #define PG8_LDB(dst, b, h) do { _Pragma("unroll") for (int n = 0; n < 2; ++n) _Pragma("unroll") for (int k = 0; k < 2; ++k) dst[n][k] = *(const LAS bf16x8*)(lds + PG8_SB(b, h) + boff + n * 2048 + k * 1024); } while (0)
; #define PG8_WAIT_V(n) asm volatile("s_waitcnt vmcnt(" #n ")" ::: "memory")
; #define PG8_WAIT_L(n) asm volatile("s_waitcnt lgkmcnt(" #n ")" ::: "memory")
; #define PG8_BAR __builtin_amdgcn_s_barrier()
; #define PG8_SCHED __builtin_amdgcn_sched_barrier(0)
; template <class Epi, class Sched, class Prob>
; __device__ __forceinline__ void gemm_phase(LAS unsigned char* lds, LAS unsigned char* lds_epi, const Prob g, const Sched& S, const Epi& E, int wid) {
;     ...
;         for (int t = 0; t < nt; t += 2) {
;             const bool last = (t == nt - 2);
;             const char* a1 = cA + (size_t)(t + 1) * kstep;
;             const char* a2 = last ? nA : cA + (size_t)(t + 2) * kstep; const char* b2 = last ? nB : cB + (size_t)(t + 2) * kstep;
;             const char* a3 = a2 + kstep; const char* b3 = b2 + kstep;
;             PG8_LDB(B0, 0, 0); PG8_LDB(B1, 0, 1); PG8_SCHED; PG8_LDA(At, 0, 0); PG8_STAGE(PG8_SA(1, 1), a1, cA10, cA11);
;             PG8_WAIT_V(8); PG8_WAIT_L(0); PG8_BAR; PG8_MMA(0, 0, At, B0); PG8_MMA(0, 1, At, B1); PG8_BAR; PG8_SCHED;
;             PG8_LDA(At, 0, 1); PG8_STAGE(PG8_SB(0, 0), b2, vB0, vB1); PG8_STAGE(PG8_SB(0, 1), b2 + hstepB, vB0, vB1); PG8_STAGE(PG8_SA(0, 0), a2, cA00, cA01);
;             PG8_WAIT_V(8); PG8_WAIT_L(0); PG8_BAR; PG8_MMA(1, 0, At, B0); PG8_MMA(1, 1, At, B1); PG8_BAR; PG8_SCHED;
;             PG8_LDB(B0, 1, 0); PG8_LDB(B1, 1, 1); PG8_SCHED; PG8_LDA(At, 1, 0); PG8_STAGE(PG8_SA(0, 1), a2, cA10, cA11);
;             PG8_WAIT_V(8); PG8_WAIT_L(0); PG8_BAR; PG8_MMA(0, 0, At, B0); PG8_MMA(0, 1, At, B1); PG8_BAR; PG8_SCHED;
.LBB0_2191:
	ds_read_b128 v[24:27], v161
	ds_read_b128 v[28:31], v161 offset:1024
	ds_read_b128 v[16:19], v161 offset:2048
	ds_read_b128 v[20:23], v161 offset:3072
	ds_read_b128 v[8:11], v186
	ds_read_b128 v[12:15], v186 offset:1024
	ds_read_b128 v[0:3], v186 offset:2048
	ds_read_b128 v[4:7], v186 offset:3072
	s_add_u32 s18, s14, s16
	s_addc_u32 s19, s15, s17
	s_add_u32 s18, s18, 0x41000100
	s_addc_u32 s19, s19, 0
	s_add_u32 s47, s31, s16
	s_addc_u32 s48, s33, s17
	s_cmpk_eq_i32 s16, 0x600
	s_cselect_b32 s21, s5, s19
	s_cselect_b32 s20, s4, s18
	s_cselect_b32 s19, s11, s48
	s_cselect_b32 s18, s10, s47
	s_mov_b32 m0, s35
	v_lshl_add_u64 v[208:209], v[176:177], 0, s[16:17]
	ds_read_b128 v[178:181], v187
	ds_read_b128 v[182:185], v187 offset:1024
	ds_read_b128 v[190:193], v187 offset:2048
	ds_read_b128 v[194:197], v187 offset:3072
	ds_read_b128 v[200:203], v187 offset:4096
	ds_read_b128 v[204:207], v187 offset:5120
	ds_read_b128 v[216:219], v187 offset:6144
	ds_read_b128 v[220:223], v187 offset:7168
	global_load_lds_dwordx4 v[208:209], off
	v_lshl_add_u64 v[208:209], v[174:175], 0, s[16:17]
	s_mov_b32 m0, s36
	s_nop 0
	global_load_lds_dwordx4 v[208:209], off
	s_waitcnt vmcnt(8)
	s_waitcnt lgkmcnt(0)
	s_barrier
	s_setprio 1
	s_waitcnt lgkmcnt(0)
	v_mfma_f32_16x16x128_f8f6f4 v[156:159], v[24:31], v[178:185], v[156:159]
	v_mfma_f32_16x16x128_f8f6f4 v[152:155], v[16:23], v[178:185], v[152:155]
	v_mfma_f32_16x16x128_f8f6f4 v[148:151], v[24:31], v[190:197], v[148:151]
	v_mfma_f32_16x16x128_f8f6f4 v[144:147], v[16:23], v[190:197], v[144:147]
	v_mfma_f32_16x16x128_f8f6f4 v[140:143], v[24:31], v[200:207], v[140:143]
	v_mfma_f32_16x16x128_f8f6f4 v[136:139], v[16:23], v[200:207], v[136:139]
	v_mfma_f32_16x16x128_f8f6f4 v[132:135], v[24:31], v[216:223], v[132:135]
	v_mfma_f32_16x16x128_f8f6f4 v[128:131], v[16:23], v[216:223], v[128:131]
	v_mfma_f32_16x16x128_f8f6f4 v[124:127], v[8:15], v[178:185], v[124:127]
	v_mfma_f32_16x16x128_f8f6f4 v[120:123], v[0:7], v[178:185], v[120:123]
	v_mfma_f32_16x16x128_f8f6f4 v[116:119], v[8:15], v[190:197], v[116:119]
	v_mfma_f32_16x16x128_f8f6f4 v[112:115], v[0:7], v[190:197], v[112:115]
	v_mfma_f32_16x16x128_f8f6f4 v[108:111], v[8:15], v[200:207], v[108:111]
	v_mfma_f32_16x16x128_f8f6f4 v[104:107], v[0:7], v[200:207], v[104:107]
	v_mfma_f32_16x16x128_f8f6f4 v[100:103], v[8:15], v[216:223], v[100:103]
	v_mfma_f32_16x16x128_f8f6f4 v[96:99], v[0:7], v[216:223], v[96:99]
	s_setprio 0
	s_barrier
	s_mov_b32 m0, s37
	v_lshl_add_u64 v[178:179], s[18:19], 0, v[162:163]
	s_add_u32 s48, s18, 0xe0000
	ds_read_b128 v[190:193], v187 offset:16384
	ds_read_b128 v[194:197], v187 offset:17408
	ds_read_b128 v[200:203], v187 offset:18432
	ds_read_b128 v[204:207], v187 offset:19456
	ds_read_b128 v[216:219], v187 offset:20480
	ds_read_b128 v[220:223], v187 offset:21504
	ds_read_b128 v[224:227], v187 offset:22528
	ds_read_b128 v[228:231], v187 offset:23552
	global_load_lds_dwordx4 v[178:179], off
	v_lshl_add_u64 v[180:181], s[18:19], 0, v[164:165]
	s_mov_b32 m0, s40
	s_addc_u32 s49, s19, 0
	global_load_lds_dwordx4 v[180:181], off
	v_lshl_add_u64 v[182:183], s[48:49], 0, v[162:163]
	s_mov_b32 m0, s41
	v_lshl_add_u64 v[184:185], s[20:21], 0, v[168:169]
	global_load_lds_dwordx4 v[182:183], off
	v_lshl_add_u64 v[182:183], s[48:49], 0, v[164:165]
	s_mov_b32 m0, s42
	s_nop 0
	global_load_lds_dwordx4 v[182:183], off
	v_lshl_add_u64 v[182:183], s[20:21], 0, v[166:167]
	s_mov_b32 m0, s25
	s_nop 0
	global_load_lds_dwordx4 v[182:183], off
	s_mov_b32 m0, s26
	s_nop 0
	global_load_lds_dwordx4 v[184:185], off
	s_waitcnt vmcnt(8)
	s_waitcnt lgkmcnt(0)
	s_barrier
	s_setprio 1
	s_waitcnt lgkmcnt(0)
	v_mfma_f32_16x16x128_f8f6f4 v[92:95], v[24:31], v[190:197], v[92:95]
	v_mfma_f32_16x16x128_f8f6f4 v[88:91], v[16:23], v[190:197], v[88:91]
	v_mfma_f32_16x16x128_f8f6f4 v[84:87], v[24:31], v[200:207], v[84:87]
	v_mfma_f32_16x16x128_f8f6f4 v[80:83], v[16:23], v[200:207], v[80:83]
	v_mfma_f32_16x16x128_f8f6f4 v[76:79], v[24:31], v[216:223], v[76:79]
	v_mfma_f32_16x16x128_f8f6f4 v[72:75], v[16:23], v[216:223], v[72:75]
	v_mfma_f32_16x16x128_f8f6f4 v[68:71], v[24:31], v[224:231], v[68:71]
	v_mfma_f32_16x16x128_f8f6f4 v[64:67], v[16:23], v[224:231], v[64:67]
	v_mfma_f32_16x16x128_f8f6f4 v[60:63], v[8:15], v[190:197], v[60:63]
	v_mfma_f32_16x16x128_f8f6f4 v[56:59], v[0:7], v[190:197], v[56:59]
	v_mfma_f32_16x16x128_f8f6f4 v[52:55], v[8:15], v[200:207], v[52:55]
	v_mfma_f32_16x16x128_f8f6f4 v[48:51], v[0:7], v[200:207], v[48:51]
	v_mfma_f32_16x16x128_f8f6f4 v[44:47], v[8:15], v[216:223], v[44:47]
	v_mfma_f32_16x16x128_f8f6f4 v[40:43], v[0:7], v[216:223], v[40:43]
	v_mfma_f32_16x16x128_f8f6f4 v[36:39], v[8:15], v[224:231], v[36:39]
	v_mfma_f32_16x16x128_f8f6f4 v[32:35], v[0:7], v[224:231], v[32:35]
	s_setprio 0
	s_barrier
; #define PG8_STAGE(bufoff, gbase, o0, o1) do { \
;         __builtin_amdgcn_global_load_lds((const unsigned*)((const char*)(gbase) + (o0)), (LAS unsigned*)(lds + (bufoff) + ldsw), 16, 0, 0); \
;         __builtin_amdgcn_global_load_lds((const unsigned*)((const char*)(gbase) + (o1)), (LAS unsigned*)(lds + (bufoff) + ldsw + 8192), 16, 0, 0); } while (0)
; #define PG8_LDA(dst, b, h) do { _Pragma("unroll") for (int m = 0; m < 4; ++m) _Pragma("unroll") for (int k = 0; k < 2; ++k) dst[m][k] = *(const LAS bf16x8*)(lds + PG8_SA(b, h) + aoff + m * 2048 + k * 1024); } while (0)
; #define PG8_LDB(dst, b, h) do { _Pragma("unroll") for (int n = 0; n < 2; ++n) _Pragma("unroll") for (int k = 0; k < 2; ++k) dst[n][k] = *(const LAS bf16x8*)(lds + PG8_SB(b, h) + boff + n * 2048 + k * 1024); } while (0)
; #define PG8_WAIT_V(n) asm volatile("s_waitcnt vmcnt(" #n ")" ::: "memory")
; #define PG8_WAIT_L(n) asm volatile("s_waitcnt lgkmcnt(" #n ")" ::: "memory")
; #define PG8_BAR __builtin_amdgcn_s_barrier()
; #define PG8_SCHED __builtin_amdgcn_sched_barrier(0)
; template <class Epi, class Sched, class Prob>
; __device__ __forceinline__ void gemm_phase(LAS unsigned char* lds, LAS unsigned char* lds_epi, const Prob g, const Sched& S, const Epi& E, int wid) {
;     ...
;             PG8_LDB(B0, 1, 0); PG8_LDB(B1, 1, 1); PG8_SCHED; PG8_LDA(At, 1, 0); PG8_STAGE(PG8_SA(0, 1), a2, cA10, cA11);
;             PG8_WAIT_V(8); PG8_WAIT_L(0); PG8_BAR; PG8_MMA(0, 0, At, B0); PG8_MMA(0, 1, At, B1); PG8_BAR; PG8_SCHED;
;             PG8_LDA(At, 1, 1); PG8_STAGE(PG8_SB(1, 0), b3, vB0, vB1); PG8_STAGE(PG8_SB(1, 1), b3 + hstepB, vB0, vB1); PG8_STAGE(PG8_SA(1, 0), a3, cA00, cA01);
;             PG8_WAIT_V(8); PG8_WAIT_L(0); PG8_BAR; PG8_MMA(1, 0, At, B0); PG8_MMA(1, 1, At, B1); PG8_BAR; PG8_SCHED;
;         }
;         if constexpr (Prob::FP8) asm volatile("s_nop 7\n\ts_nop 7\n\ts_nop 7" ::: "memory");
;         if (wr == 0) PG8_BAR;
	ds_read_b128 v[0:3], v188
	ds_read_b128 v[4:7], v188 offset:1024
	ds_read_b128 v[8:11], v188 offset:2048
	ds_read_b128 v[12:15], v188 offset:3072
	ds_read_b128 v[16:19], v189
	ds_read_b128 v[20:23], v189 offset:1024
	ds_read_b128 v[24:27], v189 offset:2048
	ds_read_b128 v[28:31], v189 offset:3072
	s_mov_b32 m0, s27
	v_lshl_add_u64 v[208:209], s[20:21], 0, v[170:171]
	ds_read_b128 v[190:193], v187 offset:32768
	ds_read_b128 v[194:197], v187 offset:33792
	ds_read_b128 v[200:203], v187 offset:34816
	ds_read_b128 v[204:207], v187 offset:35840
	ds_read_b128 v[216:219], v187 offset:36864
	ds_read_b128 v[220:223], v187 offset:37888
	ds_read_b128 v[224:227], v187 offset:38912
	ds_read_b128 v[228:231], v187 offset:39936
	global_load_lds_dwordx4 v[208:209], off
	v_lshl_add_u64 v[208:209], s[20:21], 0, v[172:173]
	s_mov_b32 m0, s28
	s_nop 0
	global_load_lds_dwordx4 v[208:209], off
	s_waitcnt vmcnt(8)
	s_waitcnt lgkmcnt(0)
	s_barrier
	s_setprio 1
	s_waitcnt lgkmcnt(0)
	v_mfma_f32_16x16x128_f8f6f4 v[156:159], v[0:7], v[190:197], v[156:159]
	v_mfma_f32_16x16x128_f8f6f4 v[152:155], v[8:15], v[190:197], v[152:155]
	v_mfma_f32_16x16x128_f8f6f4 v[148:151], v[0:7], v[200:207], v[148:151]
	v_mfma_f32_16x16x128_f8f6f4 v[144:147], v[8:15], v[200:207], v[144:147]
	v_mfma_f32_16x16x128_f8f6f4 v[140:143], v[0:7], v[216:223], v[140:143]
	v_mfma_f32_16x16x128_f8f6f4 v[136:139], v[8:15], v[216:223], v[136:139]
	v_mfma_f32_16x16x128_f8f6f4 v[132:135], v[0:7], v[224:231], v[132:135]
	v_mfma_f32_16x16x128_f8f6f4 v[128:131], v[8:15], v[224:231], v[128:131]
	v_mfma_f32_16x16x128_f8f6f4 v[124:127], v[16:23], v[190:197], v[124:127]
	v_mfma_f32_16x16x128_f8f6f4 v[120:123], v[24:31], v[190:197], v[120:123]
	v_mfma_f32_16x16x128_f8f6f4 v[116:119], v[16:23], v[200:207], v[116:119]
	v_mfma_f32_16x16x128_f8f6f4 v[112:115], v[24:31], v[200:207], v[112:115]
	v_mfma_f32_16x16x128_f8f6f4 v[108:111], v[16:23], v[216:223], v[108:111]
	v_mfma_f32_16x16x128_f8f6f4 v[104:107], v[24:31], v[216:223], v[104:107]
	v_mfma_f32_16x16x128_f8f6f4 v[100:103], v[16:23], v[224:231], v[100:103]
	v_mfma_f32_16x16x128_f8f6f4 v[96:99], v[24:31], v[224:231], v[96:99]
	s_setprio 0
	s_barrier
	s_mov_b32 m0, s43
	v_lshl_add_u64 v[178:179], v[178:179], 0, s[12:13]
	s_add_u32 s18, s18, 0xe0080
	ds_read_b128 v[190:193], v187 offset:49152
	ds_read_b128 v[194:197], v187 offset:50176
	ds_read_b128 v[200:203], v187 offset:51200
	ds_read_b128 v[204:207], v187 offset:52224
	ds_read_b128 v[216:219], v187 offset:53248
	ds_read_b128 v[220:223], v187 offset:54272
	ds_read_b128 v[224:227], v187 offset:55296
	ds_read_b128 v[228:231], v187 offset:56320
	global_load_lds_dwordx4 v[178:179], off
	v_lshl_add_u64 v[178:179], v[180:181], 0, s[12:13]
	s_mov_b32 m0, s44
	s_addc_u32 s19, s19, 0
	global_load_lds_dwordx4 v[178:179], off
	v_lshl_add_u64 v[178:179], s[18:19], 0, v[162:163]
	s_mov_b32 m0, s45
	s_nop 0
	global_load_lds_dwordx4 v[178:179], off
	v_lshl_add_u64 v[178:179], s[18:19], 0, v[164:165]
	s_mov_b32 m0, s46
	s_nop 0
	global_load_lds_dwordx4 v[178:179], off
	v_lshl_add_u64 v[178:179], v[182:183], 0, s[12:13]
	s_mov_b32 m0, s29
	s_nop 0
	global_load_lds_dwordx4 v[178:179], off
	v_lshl_add_u64 v[178:179], v[184:185], 0, s[12:13]
	s_mov_b32 m0, s30
	s_nop 0
	global_load_lds_dwordx4 v[178:179], off
	s_waitcnt vmcnt(8)
	s_waitcnt lgkmcnt(0)
	s_barrier
	s_setprio 1
	s_waitcnt lgkmcnt(0)
	v_mfma_f32_16x16x128_f8f6f4 v[92:95], v[0:7], v[190:197], v[92:95]
	v_mfma_f32_16x16x128_f8f6f4 v[88:91], v[8:15], v[190:197], v[88:91]
	v_mfma_f32_16x16x128_f8f6f4 v[84:87], v[0:7], v[200:207], v[84:87]
	v_mfma_f32_16x16x128_f8f6f4 v[80:83], v[8:15], v[200:207], v[80:83]
	v_mfma_f32_16x16x128_f8f6f4 v[76:79], v[0:7], v[216:223], v[76:79]
	v_mfma_f32_16x16x128_f8f6f4 v[72:75], v[8:15], v[216:223], v[72:75]
	v_mfma_f32_16x16x128_f8f6f4 v[68:71], v[0:7], v[224:231], v[68:71]
	v_mfma_f32_16x16x128_f8f6f4 v[64:67], v[8:15], v[224:231], v[64:67]
	v_mfma_f32_16x16x128_f8f6f4 v[60:63], v[16:23], v[190:197], v[60:63]
	v_mfma_f32_16x16x128_f8f6f4 v[56:59], v[24:31], v[190:197], v[56:59]
	v_mfma_f32_16x16x128_f8f6f4 v[52:55], v[16:23], v[200:207], v[52:55]
	v_mfma_f32_16x16x128_f8f6f4 v[48:51], v[24:31], v[200:207], v[48:51]
	v_mfma_f32_16x16x128_f8f6f4 v[44:47], v[16:23], v[216:223], v[44:47]
	v_mfma_f32_16x16x128_f8f6f4 v[40:43], v[24:31], v[216:223], v[40:43]
	v_mfma_f32_16x16x128_f8f6f4 v[36:39], v[16:23], v[224:231], v[36:39]
	v_mfma_f32_16x16x128_f8f6f4 v[32:35], v[24:31], v[224:231], v[32:35]
	s_setprio 0
	s_barrier
	s_add_i32 s34, s34, 2
	s_add_u32 s16, s16, 0x100
	s_addc_u32 s17, s17, 0
	s_cmp_gt_u32 s34, 11
	s_cbranch_scc0 .LBB0_2191
	s_nop 7
	s_nop 7
	s_nop 7
	v_readlane_b32 s4, v254, 27
	v_readlane_b32 s5, v254, 28
	s_and_b64 vcc, exec, s[4:5]
	s_cbranch_vccz .LBB0_2194
	s_barrier
